# baseline (speedup 1.0000x reference)
_Z7k_stageILi0ELi8EEv8AttnArgsPKDF16_PKfPDF16_iii:
	v_readfirstlane_b32 s94, v0
	s_nop 0
	s_lshr_b32 s94, s94, 6
	s_load_dwordx2 s[80:81], s[0:1], 0x70
	s_load_dwordx2 s[82:83], s[0:1], 0x88
	v_and_b32_e32 v255, 63, v0
	v_lshlrev_b32_e32 v255, 7, v255
	s_load_dwordx4 s[8:11], s[0:1], 0x88
	s_lshl_b32 s4, s2, 4
	s_and_b32 s4, s4, 0x70
	s_lshr_b32 s5, s2, 3
	s_add_i32 s4, s4, s5
	s_lshr_b32 s7, s4, 5
	s_lshl_b32 s6, s4, 1
	s_waitcnt lgkmcnt(0)
	s_mul_i32 s84, s3, s83
	s_add_i32 s84, s84, s82
	s_mul_i32 s84, s84, 0x60000
	s_mul_i32 s85, s94, 0x6000
	s_add_u32 s84, s84, s85
	s_add_u32 s80, s80, s84
	s_addc_u32 s81, s81, 0
	s_lshl_b32 s11, s2, 1
	s_cmp_gt_i32 s10, 0
	v_readfirstlane_b32 s24, v0
	s_cbranch_scc1 .LBB3_2
	s_lshl_b32 s31, s7, 12
	s_ashr_i32 s2, s3, 31
	s_mov_b64 s[4:5], 0
	s_branch .LBB3_3

.LBB3_5:
	s_waitcnt lgkmcnt(0)
	v_cvt_f16_f32_e32 v180, s7
	v_cvt_f16_f32_e32 v182, s6
	v_cvt_f16_f32_e32 v181, s28
	s_waitcnt vmcnt(3)
	v_pk_mul_f16 v183, v182, v184 op_sel_hi:[0,1]
	v_pk_mul_f16 v190, v182, v187 op_sel_hi:[0,1]
	v_pk_mul_f16 v194, v180, v187 op_sel_hi:[0,1]
	v_pk_mul_f16 v198, v181, v187 op_sel_hi:[0,1]
	v_pk_mul_f16 v188, v182, v185 op_sel_hi:[0,1]
	v_pk_mul_f16 v189, v182, v186 op_sel_hi:[0,1]
	v_pk_mul_f16 v191, v180, v184 op_sel_hi:[0,1]
	s_mov_b64 exec, s[64:65]
	buffer_load_dwordx4 v[18:21], v249, s[16:19], 0 offen
	buffer_load_dwordx4 v[6:9], v249, s[16:19], 0 offen offset:512
	s_mov_b64 exec, -1
	v_pk_mul_f16 v192, v180, v185 op_sel_hi:[0,1]
	v_pk_mul_f16 v193, v180, v186 op_sel_hi:[0,1]
	v_pk_mul_f16 v195, v181, v184 op_sel_hi:[0,1]
	v_pk_mul_f16 v196, v181, v185 op_sel_hi:[0,1]
	v_pk_mul_f16 v197, v181, v186 op_sel_hi:[0,1]
	v_pk_fma_f16 v113, v113, v187, v190
	v_pk_fma_f16 v110, v110, v184, v183
	v_pk_fma_f16 v129, v129, v187, v190
	v_pk_fma_f16 v126, v126, v184, v183
	v_pk_fma_f16 v141, v141, v187, v190
	v_pk_fma_f16 v138, v138, v184, v183
	v_pk_fma_f16 v183, v89, v187, v194
	v_pk_fma_f16 v199, v109, v187, v194
	buffer_load_dwordx4 v[30:33], v250, s[16:19], 0 offen offset:512
	buffer_load_dwordx4 v[10:13], v250, s[16:19], 0 offen offset:1024
	v_pk_fma_f16 v194, v125, v187, v194
	v_pk_fma_f16 v203, v53, v187, v198
	v_pk_fma_f16 v207, v69, v187, v198
	v_pk_fma_f16 v187, v97, v187, v198
	v_pk_maximum3_f16 v198, v113, v129, v141
	v_pk_fma_f16 v112, v112, v186, v189
	v_pk_fma_f16 v111, v111, v185, v188
	v_pk_fma_f16 v128, v128, v186, v189
	v_pk_fma_f16 v127, v127, v185, v188
	v_pk_fma_f16 v140, v140, v186, v189
	v_pk_fma_f16 v139, v139, v185, v188
	v_pk_fma_f16 v188, v88, v186, v193
	v_pk_fma_f16 v189, v87, v185, v192
	v_pk_fma_f16 v190, v86, v184, v191
	v_pk_fma_f16 v200, v108, v186, v193
	v_pk_fma_f16 v201, v107, v185, v192
	s_mov_b64 exec, s[66:67]
	buffer_load_dwordx4 v[54:57], v250, s[16:19], 0 offen offset:2048
	buffer_load_dwordx4 v[14:17], v250, s[16:19], 0 offen offset:2560
	s_mov_b64 exec, -1
	v_pk_fma_f16 v202, v106, v184, v191
	v_pk_fma_f16 v193, v124, v186, v193
	v_pk_fma_f16 v192, v123, v185, v192
	v_pk_fma_f16 v191, v122, v184, v191
	v_pk_fma_f16 v204, v52, v186, v197
	v_pk_fma_f16 v205, v51, v185, v196
	v_pk_fma_f16 v206, v50, v184, v195
	v_pk_fma_f16 v208, v68, v186, v197
	v_pk_fma_f16 v209, v67, v185, v196
	v_pk_fma_f16 v210, v66, v184, v195
	v_pk_fma_f16 v186, v96, v186, v197
	v_pk_fma_f16 v185, v95, v185, v196
	v_pk_fma_f16 v184, v94, v184, v195
	v_pk_maximum3_f16 v195, v110, v126, v138
	v_pk_maximum3_f16 v196, v111, v127, v139
	v_pk_maximum3_f16 v197, v112, v128, v140
	v_pk_maximum3_f16 v214, v183, v199, v194
	v_pk_maximum3_f16 v218, v203, v207, v187
	v_pk_maximum3_f16 v211, v190, v202, v191
	v_pk_maximum3_f16 v212, v189, v201, v192
	v_pk_maximum3_f16 v213, v188, v200, v193
	v_pk_maximum3_f16 v215, v206, v210, v184
	v_pk_maximum3_f16 v216, v205, v209, v185
	v_pk_maximum3_f16 v198, v198, v214, v218
	v_pk_maximum3_f16 v217, v204, v208, v186
	v_pk_maximum3_f16 v195, v195, v211, v215
	v_pk_maximum3_f16 v196, v196, v212, v216
	v_pk_maximum3_f16 v197, v197, v213, v217
	v_pk_add_f16 v113, v113, v198 neg_lo:[0,1] neg_hi:[0,1]
	s_mov_b64 exec, s[64:65]
	buffer_load_dwordx4 v[74:77], v251, s[16:19], 0 offen
	buffer_load_dwordx4 v[26:29], v251, s[16:19], 0 offen offset:512
	s_mov_b64 exec, -1
	v_pk_add_f16 v110, v110, v195 neg_lo:[0,1] neg_hi:[0,1]
	v_pk_add_f16 v111, v111, v196 neg_lo:[0,1] neg_hi:[0,1]
	v_pk_add_f16 v112, v112, v197 neg_lo:[0,1] neg_hi:[0,1]
	v_pk_add_f16 v126, v126, v195 neg_lo:[0,1] neg_hi:[0,1]
	v_exp_f16_sdwa v211, v110 dst_sel:WORD_0 dst_unused:UNUSED_PAD src0_sel:WORD_0
	v_exp_f16_sdwa v212, v111 dst_sel:WORD_0 dst_unused:UNUSED_PAD src0_sel:WORD_0
	v_exp_f16_sdwa v213, v112 dst_sel:WORD_0 dst_unused:UNUSED_PAD src0_sel:WORD_0
	v_exp_f16_sdwa v214, v113 dst_sel:WORD_0 dst_unused:UNUSED_PAD src0_sel:WORD_0
	v_exp_f16_sdwa v211, v110 dst_sel:WORD_1 dst_unused:UNUSED_PRESERVE src0_sel:WORD_1
	v_exp_f16_sdwa v212, v111 dst_sel:WORD_1 dst_unused:UNUSED_PRESERVE src0_sel:WORD_1
	v_exp_f16_sdwa v213, v112 dst_sel:WORD_1 dst_unused:UNUSED_PRESERVE src0_sel:WORD_1
	v_exp_f16_sdwa v214, v113 dst_sel:WORD_1 dst_unused:UNUSED_PRESERVE src0_sel:WORD_1
	v_pk_add_f16 v127, v127, v196 neg_lo:[0,1] neg_hi:[0,1]
	v_pk_add_f16 v113, v211, 0
	v_pk_fma_f16 v81, v81, v214, 0
	v_pk_add_f16 v110, v214, 0
	v_pk_add_f16 v111, v213, 0
	v_pk_add_f16 v112, v212, 0
	v_pk_fma_f16 v80, v80, v213, 0
	v_pk_fma_f16 v79, v79, v212, 0
	v_pk_fma_f16 v78, v78, v211, 0
	v_pk_add_f16 v128, v128, v197 neg_lo:[0,1] neg_hi:[0,1]
	buffer_load_dwordx4 v[98:101], v252, s[16:19], 0 offen offset:512
	buffer_load_dwordx4 v[38:41], v252, s[16:19], 0 offen offset:1024
	v_pk_add_f16 v129, v129, v198 neg_lo:[0,1] neg_hi:[0,1]
	v_exp_f16_sdwa v211, v126 dst_sel:WORD_0 dst_unused:UNUSED_PAD src0_sel:WORD_0
	v_exp_f16_sdwa v212, v127 dst_sel:WORD_0 dst_unused:UNUSED_PAD src0_sel:WORD_0
	v_exp_f16_sdwa v213, v128 dst_sel:WORD_0 dst_unused:UNUSED_PAD src0_sel:WORD_0
	v_exp_f16_sdwa v214, v129 dst_sel:WORD_0 dst_unused:UNUSED_PAD src0_sel:WORD_0
	v_exp_f16_sdwa v211, v126 dst_sel:WORD_1 dst_unused:UNUSED_PRESERVE src0_sel:WORD_1
	v_exp_f16_sdwa v212, v127 dst_sel:WORD_1 dst_unused:UNUSED_PRESERVE src0_sel:WORD_1
	v_exp_f16_sdwa v213, v128 dst_sel:WORD_1 dst_unused:UNUSED_PRESERVE src0_sel:WORD_1
	v_exp_f16_sdwa v214, v129 dst_sel:WORD_1 dst_unused:UNUSED_PRESERVE src0_sel:WORD_1
	v_pk_add_f16 v113, v113, v211
	v_pk_fma_f16 v81, v105, v214, v81
	v_pk_add_f16 v105, v141, v198 neg_lo:[0,1] neg_hi:[0,1]
	v_pk_add_f16 v112, v112, v212
	v_pk_add_f16 v111, v111, v213
	v_pk_add_f16 v110, v110, v214
	v_pk_fma_f16 v78, v102, v211, v78
	v_pk_fma_f16 v79, v103, v212, v79
	v_pk_fma_f16 v80, v104, v213, v80
	v_pk_add_f16 v102, v138, v195 neg_lo:[0,1] neg_hi:[0,1]
	v_pk_add_f16 v103, v139, v196 neg_lo:[0,1] neg_hi:[0,1]
	v_pk_add_f16 v104, v140, v197 neg_lo:[0,1] neg_hi:[0,1]
	v_exp_f16_sdwa v126, v102 dst_sel:WORD_0 dst_unused:UNUSED_PAD src0_sel:WORD_0
	v_exp_f16_sdwa v127, v103 dst_sel:WORD_0 dst_unused:UNUSED_PAD src0_sel:WORD_0
	v_exp_f16_sdwa v128, v104 dst_sel:WORD_0 dst_unused:UNUSED_PAD src0_sel:WORD_0
	v_exp_f16_sdwa v129, v105 dst_sel:WORD_0 dst_unused:UNUSED_PAD src0_sel:WORD_0
	v_exp_f16_sdwa v126, v102 dst_sel:WORD_1 dst_unused:UNUSED_PRESERVE src0_sel:WORD_1
	v_exp_f16_sdwa v127, v103 dst_sel:WORD_1 dst_unused:UNUSED_PRESERVE src0_sel:WORD_1
	v_exp_f16_sdwa v128, v104 dst_sel:WORD_1 dst_unused:UNUSED_PRESERVE src0_sel:WORD_1
	v_exp_f16_sdwa v129, v105 dst_sel:WORD_1 dst_unused:UNUSED_PRESERVE src0_sel:WORD_1
	v_pk_add_f16 v105, v113, v126
	v_pk_add_f16 v102, v110, v129
	s_mov_b64 exec, s[66:67]
	buffer_load_dwordx4 v[114:117], v252, s[16:19], 0 offen offset:2048
	buffer_load_dwordx4 v[58:61], v252, s[16:19], 0 offen offset:2560
	s_mov_b64 exec, -1
	v_pk_add_f16 v103, v111, v128
	v_pk_add_f16 v104, v112, v127
	v_pk_fma_f16 v81, v121, v129, v81
	v_pk_fma_f16 v80, v120, v128, v80
	v_pk_fma_f16 v79, v119, v127, v79
	v_pk_fma_f16 v78, v118, v126, v78
	v_pk_add_f16 v110, v190, v195 neg_lo:[0,1] neg_hi:[0,1]
	v_pk_add_f16 v111, v189, v196 neg_lo:[0,1] neg_hi:[0,1]
	v_pk_add_f16 v112, v188, v197 neg_lo:[0,1] neg_hi:[0,1]
	v_pk_add_f16 v113, v183, v198 neg_lo:[0,1] neg_hi:[0,1]
	v_exp_f16_sdwa v118, v110 dst_sel:WORD_0 dst_unused:UNUSED_PAD src0_sel:WORD_0
	v_exp_f16_sdwa v119, v111 dst_sel:WORD_0 dst_unused:UNUSED_PAD src0_sel:WORD_0
	v_exp_f16_sdwa v120, v112 dst_sel:WORD_0 dst_unused:UNUSED_PAD src0_sel:WORD_0
	v_exp_f16_sdwa v121, v113 dst_sel:WORD_0 dst_unused:UNUSED_PAD src0_sel:WORD_0
	v_exp_f16_sdwa v118, v110 dst_sel:WORD_1 dst_unused:UNUSED_PRESERVE src0_sel:WORD_1
	v_exp_f16_sdwa v119, v111 dst_sel:WORD_1 dst_unused:UNUSED_PRESERVE src0_sel:WORD_1
	v_exp_f16_sdwa v120, v112 dst_sel:WORD_1 dst_unused:UNUSED_PRESERVE src0_sel:WORD_1
	v_exp_f16_sdwa v121, v113 dst_sel:WORD_1 dst_unused:UNUSED_PRESERVE src0_sel:WORD_1
	v_pk_add_f16 v110, v202, v195 neg_lo:[0,1] neg_hi:[0,1]
	v_pk_add_f16 v105, v105, v118
	v_pk_add_f16 v104, v104, v119
	v_pk_add_f16 v103, v103, v120
	s_mov_b64 exec, s[76:77]
	buffer_load_dwordx4 v[130:133], v253, s[16:19], 0 offen
	buffer_load_dwordx4 v[70:73], v253, s[16:19], 0 offen offset:512
	s_mov_b64 exec, -1
	v_pk_add_f16 v102, v102, v121
	v_pk_fma_f16 v78, v46, v118, v78
	v_pk_fma_f16 v79, v47, v119, v79
	v_pk_fma_f16 v80, v48, v120, v80
	v_pk_fma_f16 v81, v49, v121, v81
	v_pk_add_f16 v111, v201, v196 neg_lo:[0,1] neg_hi:[0,1]
	v_pk_add_f16 v112, v200, v197 neg_lo:[0,1] neg_hi:[0,1]
	v_pk_add_f16 v113, v199, v198 neg_lo:[0,1] neg_hi:[0,1]
	v_exp_f16_sdwa v118, v110 dst_sel:WORD_0 dst_unused:UNUSED_PAD src0_sel:WORD_0
	v_exp_f16_sdwa v119, v111 dst_sel:WORD_0 dst_unused:UNUSED_PAD src0_sel:WORD_0
	v_exp_f16_sdwa v120, v112 dst_sel:WORD_0 dst_unused:UNUSED_PAD src0_sel:WORD_0
	v_exp_f16_sdwa v121, v113 dst_sel:WORD_0 dst_unused:UNUSED_PAD src0_sel:WORD_0
	v_exp_f16_sdwa v118, v110 dst_sel:WORD_1 dst_unused:UNUSED_PRESERVE src0_sel:WORD_1
	v_exp_f16_sdwa v119, v111 dst_sel:WORD_1 dst_unused:UNUSED_PRESERVE src0_sel:WORD_1
	v_exp_f16_sdwa v120, v112 dst_sel:WORD_1 dst_unused:UNUSED_PRESERVE src0_sel:WORD_1
	v_exp_f16_sdwa v121, v113 dst_sel:WORD_1 dst_unused:UNUSED_PRESERVE src0_sel:WORD_1
	v_pk_add_f16 v110, v191, v195 neg_lo:[0,1] neg_hi:[0,1]
	v_pk_add_f16 v105, v105, v118
	v_pk_add_f16 v102, v102, v121
	v_pk_add_f16 v103, v103, v120
	v_pk_add_f16 v104, v104, v119
	v_pk_fma_f16 v81, v65, v121, v81
	v_pk_fma_f16 v80, v64, v120, v80
	s_mov_b64 exec, s[70:71]
	buffer_load_dwordx4 v[134:137], v254, s[16:19], 0 offen offset:512
	buffer_load_dwordx4 v[90:93], v254, s[16:19], 0 offen offset:1024
	s_mov_b64 exec, -1
	v_pk_fma_f16 v79, v63, v119, v79
	v_pk_fma_f16 v78, v62, v118, v78
	v_pk_add_f16 v111, v192, v196 neg_lo:[0,1] neg_hi:[0,1]
	v_pk_add_f16 v112, v193, v197 neg_lo:[0,1] neg_hi:[0,1]
	v_pk_add_f16 v113, v194, v198 neg_lo:[0,1] neg_hi:[0,1]
	v_exp_f16_sdwa v118, v110 dst_sel:WORD_0 dst_unused:UNUSED_PAD src0_sel:WORD_0
	v_exp_f16_sdwa v119, v111 dst_sel:WORD_0 dst_unused:UNUSED_PAD src0_sel:WORD_0
	v_exp_f16_sdwa v120, v112 dst_sel:WORD_0 dst_unused:UNUSED_PAD src0_sel:WORD_0
	v_exp_f16_sdwa v121, v113 dst_sel:WORD_0 dst_unused:UNUSED_PAD src0_sel:WORD_0
	v_exp_f16_sdwa v118, v110 dst_sel:WORD_1 dst_unused:UNUSED_PRESERVE src0_sel:WORD_1
	v_exp_f16_sdwa v119, v111 dst_sel:WORD_1 dst_unused:UNUSED_PRESERVE src0_sel:WORD_1
	v_exp_f16_sdwa v120, v112 dst_sel:WORD_1 dst_unused:UNUSED_PRESERVE src0_sel:WORD_1
	v_exp_f16_sdwa v121, v113 dst_sel:WORD_1 dst_unused:UNUSED_PRESERVE src0_sel:WORD_1
	v_pk_add_f16 v110, v206, v195 neg_lo:[0,1] neg_hi:[0,1]
	v_pk_add_f16 v105, v105, v118
	v_pk_add_f16 v104, v104, v119
	v_pk_add_f16 v103, v103, v120
	v_pk_add_f16 v102, v102, v121
	v_pk_fma_f16 v78, v82, v118, v78
	v_pk_fma_f16 v79, v83, v119, v79
	v_pk_fma_f16 v80, v84, v120, v80
	v_pk_fma_f16 v81, v85, v121, v81
	s_mov_b64 exec, s[78:79]
	buffer_load_dwordx4 v[142:145], v254, s[16:19], 0 offen offset:2048
	buffer_load_dwordx4 v[2:5], v254, s[16:19], 0 offen offset:2560
	s_mov_b64 exec, -1
	v_pk_add_f16 v111, v205, v196 neg_lo:[0,1] neg_hi:[0,1]
	v_pk_add_f16 v112, v204, v197 neg_lo:[0,1] neg_hi:[0,1]
	v_pk_add_f16 v113, v203, v198 neg_lo:[0,1] neg_hi:[0,1]
	v_exp_f16_sdwa v118, v110 dst_sel:WORD_0 dst_unused:UNUSED_PAD src0_sel:WORD_0
	v_exp_f16_sdwa v119, v111 dst_sel:WORD_0 dst_unused:UNUSED_PAD src0_sel:WORD_0
	v_exp_f16_sdwa v120, v112 dst_sel:WORD_0 dst_unused:UNUSED_PAD src0_sel:WORD_0
	v_exp_f16_sdwa v121, v113 dst_sel:WORD_0 dst_unused:UNUSED_PAD src0_sel:WORD_0
	v_exp_f16_sdwa v118, v110 dst_sel:WORD_1 dst_unused:UNUSED_PRESERVE src0_sel:WORD_1
	v_exp_f16_sdwa v119, v111 dst_sel:WORD_1 dst_unused:UNUSED_PRESERVE src0_sel:WORD_1
	v_exp_f16_sdwa v120, v112 dst_sel:WORD_1 dst_unused:UNUSED_PRESERVE src0_sel:WORD_1
	v_exp_f16_sdwa v121, v113 dst_sel:WORD_1 dst_unused:UNUSED_PRESERVE src0_sel:WORD_1
	v_pk_add_f16 v110, v210, v195 neg_lo:[0,1] neg_hi:[0,1]
	v_pk_add_f16 v105, v105, v118
	v_pk_add_f16 v102, v102, v121
	v_pk_add_f16 v103, v103, v120
	v_pk_add_f16 v104, v104, v119
	v_pk_fma_f16 v81, v25, v121, v81
	v_pk_fma_f16 v80, v24, v120, v80
	v_pk_fma_f16 v79, v23, v119, v79
	v_pk_fma_f16 v78, v22, v118, v78
	v_pk_add_f16 v111, v209, v196 neg_lo:[0,1] neg_hi:[0,1]
	v_pk_add_f16 v112, v208, v197 neg_lo:[0,1] neg_hi:[0,1]
	v_pk_add_f16 v113, v207, v198 neg_lo:[0,1] neg_hi:[0,1]
	v_exp_f16_sdwa v118, v110 dst_sel:WORD_0 dst_unused:UNUSED_PAD src0_sel:WORD_0
	v_exp_f16_sdwa v119, v111 dst_sel:WORD_0 dst_unused:UNUSED_PAD src0_sel:WORD_0
	v_exp_f16_sdwa v120, v112 dst_sel:WORD_0 dst_unused:UNUSED_PAD src0_sel:WORD_0
	v_exp_f16_sdwa v121, v113 dst_sel:WORD_0 dst_unused:UNUSED_PAD src0_sel:WORD_0
	v_exp_f16_sdwa v118, v110 dst_sel:WORD_1 dst_unused:UNUSED_PRESERVE src0_sel:WORD_1
	v_exp_f16_sdwa v119, v111 dst_sel:WORD_1 dst_unused:UNUSED_PRESERVE src0_sel:WORD_1
	v_exp_f16_sdwa v120, v112 dst_sel:WORD_1 dst_unused:UNUSED_PRESERVE src0_sel:WORD_1
	v_exp_f16_sdwa v121, v113 dst_sel:WORD_1 dst_unused:UNUSED_PRESERVE src0_sel:WORD_1
	v_pk_add_f16 v110, v184, v195 neg_lo:[0,1] neg_hi:[0,1]
	v_pk_add_f16 v105, v105, v118
	v_pk_add_f16 v104, v104, v119
	v_pk_add_f16 v103, v103, v120
	v_pk_add_f16 v102, v102, v121
	v_pk_fma_f16 v78, v34, v118, v78
	v_pk_fma_f16 v79, v35, v119, v79
	v_pk_fma_f16 v80, v36, v120, v80
	v_pk_fma_f16 v81, v37, v121, v81
	v_pk_add_f16 v111, v185, v196 neg_lo:[0,1] neg_hi:[0,1]
	v_pk_add_f16 v112, v186, v197 neg_lo:[0,1] neg_hi:[0,1]
	v_pk_add_f16 v113, v187, v198 neg_lo:[0,1] neg_hi:[0,1]
	v_exp_f16_sdwa v118, v110 dst_sel:WORD_0 dst_unused:UNUSED_PAD src0_sel:WORD_0
	v_exp_f16_sdwa v119, v111 dst_sel:WORD_0 dst_unused:UNUSED_PAD src0_sel:WORD_0
	v_exp_f16_sdwa v120, v112 dst_sel:WORD_0 dst_unused:UNUSED_PAD src0_sel:WORD_0
	v_exp_f16_sdwa v121, v113 dst_sel:WORD_0 dst_unused:UNUSED_PAD src0_sel:WORD_0
	v_exp_f16_sdwa v118, v110 dst_sel:WORD_1 dst_unused:UNUSED_PRESERVE src0_sel:WORD_1
	v_exp_f16_sdwa v119, v111 dst_sel:WORD_1 dst_unused:UNUSED_PRESERVE src0_sel:WORD_1
	v_exp_f16_sdwa v120, v112 dst_sel:WORD_1 dst_unused:UNUSED_PRESERVE src0_sel:WORD_1
	v_exp_f16_sdwa v121, v113 dst_sel:WORD_1 dst_unused:UNUSED_PRESERVE src0_sel:WORD_1
	v_pk_add_f16 v105, v105, v118
	v_pk_add_f16 v104, v104, v119
	v_rcp_f16_e32 v110, v105
	v_rcp_f16_sdwa v105, v105 dst_sel:DWORD dst_unused:UNUSED_PAD src0_sel:WORD_1
	v_pk_add_f16 v103, v103, v120
	v_rcp_f16_e32 v111, v104
	v_rcp_f16_sdwa v104, v104 dst_sel:DWORD dst_unused:UNUSED_PAD src0_sel:WORD_1
	v_pk_add_f16 v102, v102, v121
	v_rcp_f16_e32 v112, v103
	v_rcp_f16_sdwa v103, v103 dst_sel:DWORD dst_unused:UNUSED_PAD src0_sel:WORD_1
	v_rcp_f16_e32 v113, v102
	v_rcp_f16_sdwa v102, v102 dst_sel:DWORD dst_unused:UNUSED_PAD src0_sel:WORD_1
	v_pk_fma_f16 v78, v42, v118, v78
	v_pack_b32_f16 v105, v110, v105
	v_pk_fma_f16 v79, v43, v119, v79
	v_pk_mul_f16 v110, v78, v105
	v_pack_b32_f16 v78, v111, v104
	v_pk_fma_f16 v80, v44, v120, v80
	v_pk_mul_f16 v111, v79, v78
	v_pack_b32_f16 v78, v112, v103
	v_pk_fma_f16 v81, v45, v121, v81
	v_pk_mul_f16 v112, v80, v78
	v_pack_b32_f16 v78, v113, v102
	v_pk_mul_f16 v113, v81, v78
	s_waitcnt vmcnt(12)
	v_pk_mul_f16 v78, v182, v154 op_sel_hi:[0,1]
	v_pk_mul_f16 v81, v182, v157 op_sel_hi:[0,1]
	v_pk_mul_f16 v105, v180, v157 op_sel_hi:[0,1]
	v_pk_mul_f16 v121, v181, v157 op_sel_hi:[0,1]
	v_pk_mul_f16 v79, v182, v155 op_sel_hi:[0,1]
	v_pk_mul_f16 v80, v182, v156 op_sel_hi:[0,1]
	v_pk_mul_f16 v102, v180, v154 op_sel_hi:[0,1]
	v_pk_mul_f16 v103, v180, v155 op_sel_hi:[0,1]
	v_pk_mul_f16 v104, v180, v156 op_sel_hi:[0,1]
	v_pk_mul_f16 v118, v181, v154 op_sel_hi:[0,1]
	v_pk_mul_f16 v119, v181, v155 op_sel_hi:[0,1]
	v_pk_mul_f16 v120, v181, v156 op_sel_hi:[0,1]
	v_pk_fma_f16 v89, v89, v157, v81
	v_pk_fma_f16 v86, v86, v154, v78
	v_pk_fma_f16 v109, v109, v157, v81
	v_pk_fma_f16 v106, v106, v154, v78
	v_pk_fma_f16 v81, v125, v157, v81
	v_pk_fma_f16 v78, v122, v154, v78
	v_pk_fma_f16 v122, v53, v157, v105
	v_pk_fma_f16 v126, v69, v157, v105
	v_pk_fma_f16 v105, v97, v157, v105
	v_pk_fma_f16 v138, v21, v157, v121
	v_pk_fma_f16 v183, v33, v157, v121
	v_pk_fma_f16 v121, v57, v157, v121
	v_pk_maximum3_f16 v157, v89, v109, v81
	v_pk_fma_f16 v88, v88, v156, v80
	v_pk_fma_f16 v87, v87, v155, v79
	v_pk_fma_f16 v108, v108, v156, v80
	v_pk_fma_f16 v107, v107, v155, v79
	v_pk_fma_f16 v80, v124, v156, v80
	v_pk_fma_f16 v79, v123, v155, v79
	v_pk_fma_f16 v123, v52, v156, v104
	v_pk_fma_f16 v124, v51, v155, v103
	v_pk_fma_f16 v125, v50, v154, v102
	v_pk_fma_f16 v127, v68, v156, v104
	v_pk_fma_f16 v128, v67, v155, v103
	v_pk_fma_f16 v129, v66, v154, v102
	v_pk_fma_f16 v104, v96, v156, v104
	v_pk_fma_f16 v103, v95, v155, v103
	v_pk_fma_f16 v102, v94, v154, v102
	v_pk_fma_f16 v139, v20, v156, v120
	v_pk_fma_f16 v140, v19, v155, v119
	v_pk_fma_f16 v141, v18, v154, v118
	v_pk_fma_f16 v184, v32, v156, v120
	v_pk_fma_f16 v185, v31, v155, v119
	v_pk_fma_f16 v186, v30, v154, v118
	v_pk_fma_f16 v120, v56, v156, v120
	v_pk_fma_f16 v119, v55, v155, v119
	v_pk_fma_f16 v118, v54, v154, v118
	v_pk_maximum3_f16 v154, v86, v106, v78
	v_pk_maximum3_f16 v155, v87, v107, v79
	v_pk_maximum3_f16 v156, v88, v108, v80
	v_pk_maximum3_f16 v190, v122, v126, v105
	v_pk_maximum3_f16 v194, v138, v183, v121
	v_pk_maximum3_f16 v187, v125, v129, v102
	v_pk_maximum3_f16 v188, v124, v128, v103
	v_pk_maximum3_f16 v189, v123, v127, v104
	v_pk_maximum3_f16 v191, v141, v186, v118
	v_pk_maximum3_f16 v192, v140, v185, v119
	v_pk_maximum3_f16 v157, v157, v190, v194
	v_pk_maximum3_f16 v193, v139, v184, v120
	v_pk_maximum3_f16 v154, v154, v187, v191
	v_pk_maximum3_f16 v155, v155, v188, v192
	v_pk_maximum3_f16 v156, v156, v189, v193
	v_pk_add_f16 v89, v89, v157 neg_lo:[0,1] neg_hi:[0,1]
	v_pk_add_f16 v86, v86, v154 neg_lo:[0,1] neg_hi:[0,1]
	v_pk_add_f16 v87, v87, v155 neg_lo:[0,1] neg_hi:[0,1]
	v_pk_add_f16 v88, v88, v156 neg_lo:[0,1] neg_hi:[0,1]
	v_pk_add_f16 v106, v106, v154 neg_lo:[0,1] neg_hi:[0,1]
	v_exp_f16_sdwa v187, v86 dst_sel:WORD_0 dst_unused:UNUSED_PAD src0_sel:WORD_0
	v_exp_f16_sdwa v188, v87 dst_sel:WORD_0 dst_unused:UNUSED_PAD src0_sel:WORD_0
	v_exp_f16_sdwa v189, v88 dst_sel:WORD_0 dst_unused:UNUSED_PAD src0_sel:WORD_0
	v_exp_f16_sdwa v190, v89 dst_sel:WORD_0 dst_unused:UNUSED_PAD src0_sel:WORD_0
	v_exp_f16_sdwa v187, v86 dst_sel:WORD_1 dst_unused:UNUSED_PRESERVE src0_sel:WORD_1
	v_exp_f16_sdwa v188, v87 dst_sel:WORD_1 dst_unused:UNUSED_PRESERVE src0_sel:WORD_1
	v_exp_f16_sdwa v189, v88 dst_sel:WORD_1 dst_unused:UNUSED_PRESERVE src0_sel:WORD_1
	v_exp_f16_sdwa v190, v89 dst_sel:WORD_1 dst_unused:UNUSED_PRESERVE src0_sel:WORD_1
	v_pk_add_f16 v107, v107, v155 neg_lo:[0,1] neg_hi:[0,1]
	v_pk_add_f16 v89, v187, 0
	v_pk_fma_f16 v49, v49, v190, 0
	v_pk_add_f16 v86, v190, 0
	v_pk_add_f16 v87, v189, 0
	v_pk_add_f16 v88, v188, 0
	v_pk_fma_f16 v48, v48, v189, 0
	v_pk_fma_f16 v47, v47, v188, 0
	v_pk_fma_f16 v46, v46, v187, 0
	v_pk_add_f16 v108, v108, v156 neg_lo:[0,1] neg_hi:[0,1]
	v_pk_add_f16 v109, v109, v157 neg_lo:[0,1] neg_hi:[0,1]
	v_exp_f16_sdwa v187, v106 dst_sel:WORD_0 dst_unused:UNUSED_PAD src0_sel:WORD_0
	v_exp_f16_sdwa v188, v107 dst_sel:WORD_0 dst_unused:UNUSED_PAD src0_sel:WORD_0
	v_exp_f16_sdwa v189, v108 dst_sel:WORD_0 dst_unused:UNUSED_PAD src0_sel:WORD_0
	v_exp_f16_sdwa v190, v109 dst_sel:WORD_0 dst_unused:UNUSED_PAD src0_sel:WORD_0
	v_exp_f16_sdwa v187, v106 dst_sel:WORD_1 dst_unused:UNUSED_PRESERVE src0_sel:WORD_1
	v_exp_f16_sdwa v188, v107 dst_sel:WORD_1 dst_unused:UNUSED_PRESERVE src0_sel:WORD_1
	v_exp_f16_sdwa v189, v108 dst_sel:WORD_1 dst_unused:UNUSED_PRESERVE src0_sel:WORD_1
	v_exp_f16_sdwa v190, v109 dst_sel:WORD_1 dst_unused:UNUSED_PRESERVE src0_sel:WORD_1
	v_pk_add_f16 v89, v89, v187
	v_pk_fma_f16 v49, v65, v190, v49
	v_pk_add_f16 v65, v81, v157 neg_lo:[0,1] neg_hi:[0,1]
	v_pk_add_f16 v88, v88, v188
	v_pk_add_f16 v87, v87, v189
	v_pk_add_f16 v86, v86, v190
	v_pk_fma_f16 v46, v62, v187, v46
	v_pk_fma_f16 v47, v63, v188, v47
	v_pk_fma_f16 v48, v64, v189, v48
	v_pk_add_f16 v62, v78, v154 neg_lo:[0,1] neg_hi:[0,1]
	v_pk_add_f16 v63, v79, v155 neg_lo:[0,1] neg_hi:[0,1]
	v_pk_add_f16 v64, v80, v156 neg_lo:[0,1] neg_hi:[0,1]
	v_exp_f16_sdwa v78, v62 dst_sel:WORD_0 dst_unused:UNUSED_PAD src0_sel:WORD_0
	v_exp_f16_sdwa v79, v63 dst_sel:WORD_0 dst_unused:UNUSED_PAD src0_sel:WORD_0
	v_exp_f16_sdwa v80, v64 dst_sel:WORD_0 dst_unused:UNUSED_PAD src0_sel:WORD_0
	v_exp_f16_sdwa v81, v65 dst_sel:WORD_0 dst_unused:UNUSED_PAD src0_sel:WORD_0
	v_exp_f16_sdwa v78, v62 dst_sel:WORD_1 dst_unused:UNUSED_PRESERVE src0_sel:WORD_1
	v_exp_f16_sdwa v79, v63 dst_sel:WORD_1 dst_unused:UNUSED_PRESERVE src0_sel:WORD_1
	v_exp_f16_sdwa v80, v64 dst_sel:WORD_1 dst_unused:UNUSED_PRESERVE src0_sel:WORD_1
	v_exp_f16_sdwa v81, v65 dst_sel:WORD_1 dst_unused:UNUSED_PRESERVE src0_sel:WORD_1
	v_pk_add_f16 v65, v89, v78
	v_pk_add_f16 v62, v86, v81
	v_pk_add_f16 v63, v87, v80
	v_pk_add_f16 v64, v88, v79
	v_pk_fma_f16 v49, v85, v81, v49
	v_pk_fma_f16 v48, v84, v80, v48
	v_pk_fma_f16 v47, v83, v79, v47
	v_pk_fma_f16 v46, v82, v78, v46
	v_pk_add_f16 v78, v125, v154 neg_lo:[0,1] neg_hi:[0,1]
	v_pk_add_f16 v79, v124, v155 neg_lo:[0,1] neg_hi:[0,1]
	v_pk_add_f16 v80, v123, v156 neg_lo:[0,1] neg_hi:[0,1]
	v_pk_add_f16 v81, v122, v157 neg_lo:[0,1] neg_hi:[0,1]
	v_exp_f16_sdwa v82, v78 dst_sel:WORD_0 dst_unused:UNUSED_PAD src0_sel:WORD_0
	v_exp_f16_sdwa v83, v79 dst_sel:WORD_0 dst_unused:UNUSED_PAD src0_sel:WORD_0
	v_exp_f16_sdwa v84, v80 dst_sel:WORD_0 dst_unused:UNUSED_PAD src0_sel:WORD_0
	v_exp_f16_sdwa v85, v81 dst_sel:WORD_0 dst_unused:UNUSED_PAD src0_sel:WORD_0
	v_exp_f16_sdwa v82, v78 dst_sel:WORD_1 dst_unused:UNUSED_PRESERVE src0_sel:WORD_1
	v_exp_f16_sdwa v83, v79 dst_sel:WORD_1 dst_unused:UNUSED_PRESERVE src0_sel:WORD_1
	v_exp_f16_sdwa v84, v80 dst_sel:WORD_1 dst_unused:UNUSED_PRESERVE src0_sel:WORD_1
	v_exp_f16_sdwa v85, v81 dst_sel:WORD_1 dst_unused:UNUSED_PRESERVE src0_sel:WORD_1
	v_pk_add_f16 v78, v129, v154 neg_lo:[0,1] neg_hi:[0,1]
	v_pk_add_f16 v65, v65, v82
	v_pk_add_f16 v64, v64, v83
	v_pk_add_f16 v63, v63, v84
	v_pk_add_f16 v62, v62, v85
	v_pk_fma_f16 v46, v22, v82, v46
	v_pk_fma_f16 v47, v23, v83, v47
	v_pk_fma_f16 v48, v24, v84, v48
	v_pk_fma_f16 v49, v25, v85, v49
	v_pk_add_f16 v79, v128, v155 neg_lo:[0,1] neg_hi:[0,1]
	v_pk_add_f16 v80, v127, v156 neg_lo:[0,1] neg_hi:[0,1]
	v_pk_add_f16 v81, v126, v157 neg_lo:[0,1] neg_hi:[0,1]
	v_exp_f16_sdwa v82, v78 dst_sel:WORD_0 dst_unused:UNUSED_PAD src0_sel:WORD_0
	v_exp_f16_sdwa v83, v79 dst_sel:WORD_0 dst_unused:UNUSED_PAD src0_sel:WORD_0
	v_exp_f16_sdwa v84, v80 dst_sel:WORD_0 dst_unused:UNUSED_PAD src0_sel:WORD_0
	v_exp_f16_sdwa v85, v81 dst_sel:WORD_0 dst_unused:UNUSED_PAD src0_sel:WORD_0
	v_exp_f16_sdwa v82, v78 dst_sel:WORD_1 dst_unused:UNUSED_PRESERVE src0_sel:WORD_1
	v_exp_f16_sdwa v83, v79 dst_sel:WORD_1 dst_unused:UNUSED_PRESERVE src0_sel:WORD_1
	v_exp_f16_sdwa v84, v80 dst_sel:WORD_1 dst_unused:UNUSED_PRESERVE src0_sel:WORD_1
	v_exp_f16_sdwa v85, v81 dst_sel:WORD_1 dst_unused:UNUSED_PRESERVE src0_sel:WORD_1
	v_pk_add_f16 v78, v102, v154 neg_lo:[0,1] neg_hi:[0,1]
	v_pk_add_f16 v65, v65, v82
	v_pk_add_f16 v62, v62, v85
	v_pk_add_f16 v63, v63, v84
	v_pk_add_f16 v64, v64, v83
	v_pk_fma_f16 v49, v37, v85, v49
	v_pk_fma_f16 v48, v36, v84, v48
	v_pk_fma_f16 v47, v35, v83, v47
	v_pk_fma_f16 v46, v34, v82, v46
	v_pk_add_f16 v79, v103, v155 neg_lo:[0,1] neg_hi:[0,1]
	v_pk_add_f16 v80, v104, v156 neg_lo:[0,1] neg_hi:[0,1]
	v_pk_add_f16 v81, v105, v157 neg_lo:[0,1] neg_hi:[0,1]
	v_exp_f16_sdwa v82, v78 dst_sel:WORD_0 dst_unused:UNUSED_PAD src0_sel:WORD_0
	v_exp_f16_sdwa v83, v79 dst_sel:WORD_0 dst_unused:UNUSED_PAD src0_sel:WORD_0
	v_exp_f16_sdwa v84, v80 dst_sel:WORD_0 dst_unused:UNUSED_PAD src0_sel:WORD_0
	v_exp_f16_sdwa v85, v81 dst_sel:WORD_0 dst_unused:UNUSED_PAD src0_sel:WORD_0
	v_exp_f16_sdwa v82, v78 dst_sel:WORD_1 dst_unused:UNUSED_PRESERVE src0_sel:WORD_1
	v_exp_f16_sdwa v83, v79 dst_sel:WORD_1 dst_unused:UNUSED_PRESERVE src0_sel:WORD_1
	v_exp_f16_sdwa v84, v80 dst_sel:WORD_1 dst_unused:UNUSED_PRESERVE src0_sel:WORD_1
	v_exp_f16_sdwa v85, v81 dst_sel:WORD_1 dst_unused:UNUSED_PRESERVE src0_sel:WORD_1
	v_pk_add_f16 v78, v141, v154 neg_lo:[0,1] neg_hi:[0,1]
	v_pk_add_f16 v65, v65, v82
	v_pk_add_f16 v64, v64, v83
	v_pk_add_f16 v63, v63, v84
	v_pk_add_f16 v62, v62, v85
	v_pk_fma_f16 v46, v42, v82, v46
	v_pk_fma_f16 v47, v43, v83, v47
	v_pk_fma_f16 v48, v44, v84, v48
	v_pk_fma_f16 v49, v45, v85, v49
	v_pk_add_f16 v79, v140, v155 neg_lo:[0,1] neg_hi:[0,1]
	v_pk_add_f16 v80, v139, v156 neg_lo:[0,1] neg_hi:[0,1]
	v_pk_add_f16 v81, v138, v157 neg_lo:[0,1] neg_hi:[0,1]
	v_exp_f16_sdwa v82, v78 dst_sel:WORD_0 dst_unused:UNUSED_PAD src0_sel:WORD_0
	v_exp_f16_sdwa v83, v79 dst_sel:WORD_0 dst_unused:UNUSED_PAD src0_sel:WORD_0
	v_exp_f16_sdwa v84, v80 dst_sel:WORD_0 dst_unused:UNUSED_PAD src0_sel:WORD_0
	v_exp_f16_sdwa v85, v81 dst_sel:WORD_0 dst_unused:UNUSED_PAD src0_sel:WORD_0
	v_exp_f16_sdwa v82, v78 dst_sel:WORD_1 dst_unused:UNUSED_PRESERVE src0_sel:WORD_1
	v_exp_f16_sdwa v83, v79 dst_sel:WORD_1 dst_unused:UNUSED_PRESERVE src0_sel:WORD_1
	v_exp_f16_sdwa v84, v80 dst_sel:WORD_1 dst_unused:UNUSED_PRESERVE src0_sel:WORD_1
	v_exp_f16_sdwa v85, v81 dst_sel:WORD_1 dst_unused:UNUSED_PRESERVE src0_sel:WORD_1
	v_pk_add_f16 v78, v186, v154 neg_lo:[0,1] neg_hi:[0,1]
	v_pk_add_f16 v65, v65, v82
	v_pk_add_f16 v62, v62, v85
	v_pk_add_f16 v63, v63, v84
	v_pk_add_f16 v64, v64, v83
	v_pk_fma_f16 v49, v9, v85, v49
	v_pk_fma_f16 v48, v8, v84, v48
	v_pk_fma_f16 v47, v7, v83, v47
	v_pk_fma_f16 v46, v6, v82, v46
	v_pk_add_f16 v79, v185, v155 neg_lo:[0,1] neg_hi:[0,1]
	v_pk_add_f16 v80, v184, v156 neg_lo:[0,1] neg_hi:[0,1]
	v_pk_add_f16 v81, v183, v157 neg_lo:[0,1] neg_hi:[0,1]
	v_exp_f16_sdwa v82, v78 dst_sel:WORD_0 dst_unused:UNUSED_PAD src0_sel:WORD_0
	v_exp_f16_sdwa v83, v79 dst_sel:WORD_0 dst_unused:UNUSED_PAD src0_sel:WORD_0
	v_exp_f16_sdwa v84, v80 dst_sel:WORD_0 dst_unused:UNUSED_PAD src0_sel:WORD_0
	v_exp_f16_sdwa v85, v81 dst_sel:WORD_0 dst_unused:UNUSED_PAD src0_sel:WORD_0
	v_exp_f16_sdwa v82, v78 dst_sel:WORD_1 dst_unused:UNUSED_PRESERVE src0_sel:WORD_1
	v_exp_f16_sdwa v83, v79 dst_sel:WORD_1 dst_unused:UNUSED_PRESERVE src0_sel:WORD_1
	v_exp_f16_sdwa v84, v80 dst_sel:WORD_1 dst_unused:UNUSED_PRESERVE src0_sel:WORD_1
	v_exp_f16_sdwa v85, v81 dst_sel:WORD_1 dst_unused:UNUSED_PRESERVE src0_sel:WORD_1
	v_pk_add_f16 v78, v118, v154 neg_lo:[0,1] neg_hi:[0,1]
	v_pk_add_f16 v65, v65, v82
	v_pk_add_f16 v64, v64, v83
	v_pk_add_f16 v63, v63, v84
	v_pk_add_f16 v62, v62, v85
	v_pk_fma_f16 v46, v10, v82, v46
	v_pk_fma_f16 v47, v11, v83, v47
	v_pk_fma_f16 v48, v12, v84, v48
	v_pk_fma_f16 v49, v13, v85, v49
	v_pk_add_f16 v79, v119, v155 neg_lo:[0,1] neg_hi:[0,1]
	v_pk_add_f16 v80, v120, v156 neg_lo:[0,1] neg_hi:[0,1]
	v_pk_add_f16 v81, v121, v157 neg_lo:[0,1] neg_hi:[0,1]
	v_exp_f16_sdwa v82, v78 dst_sel:WORD_0 dst_unused:UNUSED_PAD src0_sel:WORD_0
	v_exp_f16_sdwa v83, v79 dst_sel:WORD_0 dst_unused:UNUSED_PAD src0_sel:WORD_0
	v_exp_f16_sdwa v84, v80 dst_sel:WORD_0 dst_unused:UNUSED_PAD src0_sel:WORD_0
	v_exp_f16_sdwa v85, v81 dst_sel:WORD_0 dst_unused:UNUSED_PAD src0_sel:WORD_0
	v_exp_f16_sdwa v82, v78 dst_sel:WORD_1 dst_unused:UNUSED_PRESERVE src0_sel:WORD_1
	v_exp_f16_sdwa v83, v79 dst_sel:WORD_1 dst_unused:UNUSED_PRESERVE src0_sel:WORD_1
	v_exp_f16_sdwa v84, v80 dst_sel:WORD_1 dst_unused:UNUSED_PRESERVE src0_sel:WORD_1
	v_exp_f16_sdwa v85, v81 dst_sel:WORD_1 dst_unused:UNUSED_PRESERVE src0_sel:WORD_1
	v_pk_add_f16 v65, v65, v82
	v_pk_add_f16 v64, v64, v83
	v_rcp_f16_e32 v78, v65
	v_rcp_f16_sdwa v65, v65 dst_sel:DWORD dst_unused:UNUSED_PAD src0_sel:WORD_1
	v_pk_add_f16 v63, v63, v84
	v_rcp_f16_e32 v79, v64
	v_rcp_f16_sdwa v64, v64 dst_sel:DWORD dst_unused:UNUSED_PAD src0_sel:WORD_1
	v_pk_add_f16 v62, v62, v85
	v_rcp_f16_e32 v80, v63
	v_rcp_f16_sdwa v81, v63 dst_sel:DWORD dst_unused:UNUSED_PAD src0_sel:WORD_1
	v_pk_fma_f16 v47, v15, v83, v47
	v_pk_fma_f16 v46, v14, v82, v46
	v_rcp_f16_e32 v82, v62
	v_rcp_f16_sdwa v83, v62 dst_sel:DWORD dst_unused:UNUSED_PAD src0_sel:WORD_1
	v_pack_b32_f16 v62, v78, v65
	v_pk_mul_f16 v62, v46, v62
	v_pack_b32_f16 v46, v79, v64
	v_pk_fma_f16 v48, v16, v84, v48
	v_pk_mul_f16 v63, v47, v46
	v_pack_b32_f16 v46, v80, v81
	v_pk_fma_f16 v49, v17, v85, v49
	v_pk_mul_f16 v64, v48, v46
	v_pack_b32_f16 v46, v82, v83
	v_pk_mul_f16 v65, v49, v46
	s_waitcnt vmcnt(6)
	v_pk_mul_f16 v46, v182, v150 op_sel_hi:[0,1]
	v_pk_mul_f16 v47, v182, v151 op_sel_hi:[0,1]
	v_pk_mul_f16 v48, v182, v152 op_sel_hi:[0,1]
	v_pk_mul_f16 v49, v182, v153 op_sel_hi:[0,1]
	v_pk_mul_f16 v78, v180, v150 op_sel_hi:[0,1]
	v_pk_mul_f16 v82, v181, v150 op_sel_hi:[0,1]
	v_pk_fma_f16 v50, v50, v150, v46
	v_pk_fma_f16 v66, v66, v150, v46
	v_pk_fma_f16 v46, v94, v150, v46
	v_pk_mul_f16 v79, v180, v151 op_sel_hi:[0,1]
	v_pk_maximum3_f16 v118, v50, v66, v46
	v_pk_mul_f16 v80, v180, v152 op_sel_hi:[0,1]
	v_pk_mul_f16 v81, v180, v153 op_sel_hi:[0,1]
	v_pk_mul_f16 v83, v181, v151 op_sel_hi:[0,1]
	v_pk_mul_f16 v84, v181, v152 op_sel_hi:[0,1]
	v_pk_mul_f16 v85, v181, v153 op_sel_hi:[0,1]
	v_pk_fma_f16 v53, v53, v153, v49
	v_pk_fma_f16 v52, v52, v152, v48
	v_pk_fma_f16 v51, v51, v151, v47
	v_pk_fma_f16 v69, v69, v153, v49
	v_pk_fma_f16 v68, v68, v152, v48
	v_pk_fma_f16 v67, v67, v151, v47
	v_pk_fma_f16 v49, v97, v153, v49
	v_pk_fma_f16 v48, v96, v152, v48
	v_pk_fma_f16 v47, v95, v151, v47
	v_pk_fma_f16 v89, v18, v150, v78
	v_pk_fma_f16 v97, v30, v150, v78
	v_pk_fma_f16 v78, v54, v150, v78
	v_pk_fma_f16 v105, v74, v150, v82
	v_pk_fma_f16 v109, v98, v150, v82
	v_pk_fma_f16 v82, v114, v150, v82
	v_pk_maximum3_f16 v119, v51, v67, v47
	v_pk_maximum3_f16 v120, v52, v68, v48
	v_pk_maximum3_f16 v121, v53, v69, v49
	v_pk_maximum3_f16 v122, v89, v97, v78
	v_pk_fma_f16 v86, v21, v153, v81
	v_pk_maximum3_f16 v126, v105, v109, v82
	v_pk_fma_f16 v87, v20, v152, v80
	v_pk_maximum3_f16 v118, v118, v122, v126
	v_pk_fma_f16 v88, v19, v151, v79
	v_pk_fma_f16 v94, v33, v153, v81
	v_pk_fma_f16 v95, v32, v152, v80
	v_pk_fma_f16 v96, v31, v151, v79
	v_pk_fma_f16 v81, v57, v153, v81
	v_pk_fma_f16 v80, v56, v152, v80
	v_pk_fma_f16 v79, v55, v151, v79
	v_pk_fma_f16 v102, v77, v153, v85
	v_pk_fma_f16 v103, v76, v152, v84
	v_pk_fma_f16 v104, v75, v151, v83
	v_pk_fma_f16 v106, v101, v153, v85
	v_pk_fma_f16 v107, v100, v152, v84
	v_pk_fma_f16 v108, v99, v151, v83
	v_pk_fma_f16 v85, v117, v153, v85
	v_pk_fma_f16 v84, v116, v152, v84
	v_pk_fma_f16 v83, v115, v151, v83
	v_pk_maximum3_f16 v123, v88, v96, v79
	v_pk_maximum3_f16 v124, v87, v95, v80
	v_pk_maximum3_f16 v125, v86, v94, v81
	v_pk_maximum3_f16 v128, v103, v107, v84
	v_pk_maximum3_f16 v129, v102, v106, v85
	v_pk_maximum3_f16 v127, v104, v108, v83
	v_pk_maximum3_f16 v119, v119, v123, v127
	v_pk_maximum3_f16 v120, v120, v124, v128
	v_pk_maximum3_f16 v121, v121, v125, v129
	v_pk_add_f16 v50, v50, v118 neg_lo:[0,1] neg_hi:[0,1]
	v_pk_add_f16 v51, v51, v119 neg_lo:[0,1] neg_hi:[0,1]
	v_pk_add_f16 v52, v52, v120 neg_lo:[0,1] neg_hi:[0,1]
	v_pk_add_f16 v53, v53, v121 neg_lo:[0,1] neg_hi:[0,1]
	v_pk_add_f16 v66, v66, v118 neg_lo:[0,1] neg_hi:[0,1]
	v_exp_f16_sdwa v122, v50 dst_sel:WORD_0 dst_unused:UNUSED_PAD src0_sel:WORD_0
	v_exp_f16_sdwa v123, v51 dst_sel:WORD_0 dst_unused:UNUSED_PAD src0_sel:WORD_0
	v_exp_f16_sdwa v124, v52 dst_sel:WORD_0 dst_unused:UNUSED_PAD src0_sel:WORD_0
	v_exp_f16_sdwa v125, v53 dst_sel:WORD_0 dst_unused:UNUSED_PAD src0_sel:WORD_0
	v_exp_f16_sdwa v122, v50 dst_sel:WORD_1 dst_unused:UNUSED_PRESERVE src0_sel:WORD_1
	v_exp_f16_sdwa v123, v51 dst_sel:WORD_1 dst_unused:UNUSED_PRESERVE src0_sel:WORD_1
	v_exp_f16_sdwa v124, v52 dst_sel:WORD_1 dst_unused:UNUSED_PRESERVE src0_sel:WORD_1
	v_exp_f16_sdwa v125, v53 dst_sel:WORD_1 dst_unused:UNUSED_PRESERVE src0_sel:WORD_1
	v_pk_add_f16 v67, v67, v119 neg_lo:[0,1] neg_hi:[0,1]
	v_pk_add_f16 v50, v125, 0
	v_pk_fma_f16 v22, v22, v122, 0
	v_pk_add_f16 v51, v124, 0
	v_pk_add_f16 v52, v123, 0
	v_pk_add_f16 v53, v122, 0
	v_pk_fma_f16 v23, v23, v123, 0
	v_pk_fma_f16 v24, v24, v124, 0
	v_pk_fma_f16 v25, v25, v125, 0
	v_pk_add_f16 v68, v68, v120 neg_lo:[0,1] neg_hi:[0,1]
	v_pk_add_f16 v69, v69, v121 neg_lo:[0,1] neg_hi:[0,1]
	v_exp_f16_sdwa v122, v66 dst_sel:WORD_0 dst_unused:UNUSED_PAD src0_sel:WORD_0
	v_exp_f16_sdwa v123, v67 dst_sel:WORD_0 dst_unused:UNUSED_PAD src0_sel:WORD_0
	v_exp_f16_sdwa v124, v68 dst_sel:WORD_0 dst_unused:UNUSED_PAD src0_sel:WORD_0
	v_exp_f16_sdwa v125, v69 dst_sel:WORD_0 dst_unused:UNUSED_PAD src0_sel:WORD_0
	v_exp_f16_sdwa v122, v66 dst_sel:WORD_1 dst_unused:UNUSED_PRESERVE src0_sel:WORD_1
	v_exp_f16_sdwa v123, v67 dst_sel:WORD_1 dst_unused:UNUSED_PRESERVE src0_sel:WORD_1
	v_exp_f16_sdwa v124, v68 dst_sel:WORD_1 dst_unused:UNUSED_PRESERVE src0_sel:WORD_1
	v_exp_f16_sdwa v125, v69 dst_sel:WORD_1 dst_unused:UNUSED_PRESERVE src0_sel:WORD_1
	s_nop 0
	v_pk_add_f16 v50, v50, v125
	v_pk_fma_f16 v22, v34, v122, v22
	v_pk_add_f16 v34, v46, v118 neg_lo:[0,1] neg_hi:[0,1]
	v_pk_add_f16 v53, v53, v122
	v_pk_add_f16 v52, v52, v123
	v_pk_add_f16 v51, v51, v124
	v_pk_fma_f16 v25, v37, v125, v25
	v_pk_fma_f16 v24, v36, v124, v24
	v_pk_fma_f16 v23, v35, v123, v23
	v_pk_add_f16 v35, v47, v119 neg_lo:[0,1] neg_hi:[0,1]
	v_pk_add_f16 v36, v48, v120 neg_lo:[0,1] neg_hi:[0,1]
	v_pk_add_f16 v37, v49, v121 neg_lo:[0,1] neg_hi:[0,1]
	v_exp_f16_sdwa v46, v34 dst_sel:WORD_0 dst_unused:UNUSED_PAD src0_sel:WORD_0
	v_exp_f16_sdwa v47, v35 dst_sel:WORD_0 dst_unused:UNUSED_PAD src0_sel:WORD_0
	v_exp_f16_sdwa v48, v36 dst_sel:WORD_0 dst_unused:UNUSED_PAD src0_sel:WORD_0
	v_exp_f16_sdwa v49, v37 dst_sel:WORD_0 dst_unused:UNUSED_PAD src0_sel:WORD_0
	v_exp_f16_sdwa v46, v34 dst_sel:WORD_1 dst_unused:UNUSED_PRESERVE src0_sel:WORD_1
	v_exp_f16_sdwa v47, v35 dst_sel:WORD_1 dst_unused:UNUSED_PRESERVE src0_sel:WORD_1
	v_exp_f16_sdwa v48, v36 dst_sel:WORD_1 dst_unused:UNUSED_PRESERVE src0_sel:WORD_1
	v_exp_f16_sdwa v49, v37 dst_sel:WORD_1 dst_unused:UNUSED_PRESERVE src0_sel:WORD_1
	s_nop 0
	v_pk_add_f16 v34, v50, v49
	v_pk_add_f16 v35, v51, v48
	v_pk_add_f16 v36, v52, v47
	v_pk_add_f16 v37, v53, v46
	v_pk_fma_f16 v22, v42, v46, v22
	v_pk_fma_f16 v23, v43, v47, v23
	v_pk_fma_f16 v24, v44, v48, v24
	v_pk_fma_f16 v25, v45, v49, v25
	v_pk_add_f16 v42, v89, v118 neg_lo:[0,1] neg_hi:[0,1]
	v_pk_add_f16 v43, v88, v119 neg_lo:[0,1] neg_hi:[0,1]
	v_pk_add_f16 v44, v87, v120 neg_lo:[0,1] neg_hi:[0,1]
	v_pk_add_f16 v45, v86, v121 neg_lo:[0,1] neg_hi:[0,1]
	v_exp_f16_sdwa v46, v42 dst_sel:WORD_0 dst_unused:UNUSED_PAD src0_sel:WORD_0
	v_exp_f16_sdwa v47, v43 dst_sel:WORD_0 dst_unused:UNUSED_PAD src0_sel:WORD_0
	v_exp_f16_sdwa v48, v44 dst_sel:WORD_0 dst_unused:UNUSED_PAD src0_sel:WORD_0
	v_exp_f16_sdwa v49, v45 dst_sel:WORD_0 dst_unused:UNUSED_PAD src0_sel:WORD_0
	v_exp_f16_sdwa v46, v42 dst_sel:WORD_1 dst_unused:UNUSED_PRESERVE src0_sel:WORD_1
	v_exp_f16_sdwa v47, v43 dst_sel:WORD_1 dst_unused:UNUSED_PRESERVE src0_sel:WORD_1
	v_exp_f16_sdwa v48, v44 dst_sel:WORD_1 dst_unused:UNUSED_PRESERVE src0_sel:WORD_1
	v_exp_f16_sdwa v49, v45 dst_sel:WORD_1 dst_unused:UNUSED_PRESERVE src0_sel:WORD_1
	v_pk_add_f16 v42, v97, v118 neg_lo:[0,1] neg_hi:[0,1]
	v_pk_add_f16 v34, v34, v49
	v_pk_add_f16 v37, v37, v46
	v_pk_add_f16 v36, v36, v47
	v_pk_add_f16 v35, v35, v48
	v_pk_fma_f16 v25, v9, v49, v25
	v_pk_fma_f16 v24, v8, v48, v24
	v_pk_fma_f16 v23, v7, v47, v23
	v_pk_fma_f16 v22, v6, v46, v22
	v_pk_add_f16 v43, v96, v119 neg_lo:[0,1] neg_hi:[0,1]
	v_pk_add_f16 v44, v95, v120 neg_lo:[0,1] neg_hi:[0,1]
	v_pk_add_f16 v45, v94, v121 neg_lo:[0,1] neg_hi:[0,1]
	v_exp_f16_sdwa v46, v42 dst_sel:WORD_0 dst_unused:UNUSED_PAD src0_sel:WORD_0
	v_exp_f16_sdwa v47, v43 dst_sel:WORD_0 dst_unused:UNUSED_PAD src0_sel:WORD_0
	v_exp_f16_sdwa v48, v44 dst_sel:WORD_0 dst_unused:UNUSED_PAD src0_sel:WORD_0
	v_exp_f16_sdwa v49, v45 dst_sel:WORD_0 dst_unused:UNUSED_PAD src0_sel:WORD_0
	v_exp_f16_sdwa v46, v42 dst_sel:WORD_1 dst_unused:UNUSED_PRESERVE src0_sel:WORD_1
	v_exp_f16_sdwa v47, v43 dst_sel:WORD_1 dst_unused:UNUSED_PRESERVE src0_sel:WORD_1
	v_exp_f16_sdwa v48, v44 dst_sel:WORD_1 dst_unused:UNUSED_PRESERVE src0_sel:WORD_1
	v_exp_f16_sdwa v49, v45 dst_sel:WORD_1 dst_unused:UNUSED_PRESERVE src0_sel:WORD_1
	v_pk_add_f16 v42, v78, v118 neg_lo:[0,1] neg_hi:[0,1]
	v_pk_add_f16 v34, v34, v49
	v_pk_add_f16 v35, v35, v48
	v_pk_add_f16 v36, v36, v47
	v_pk_add_f16 v37, v37, v46
	v_pk_fma_f16 v22, v10, v46, v22
	v_pk_fma_f16 v23, v11, v47, v23
	v_pk_fma_f16 v24, v12, v48, v24
	v_pk_fma_f16 v25, v13, v49, v25
	v_pk_add_f16 v43, v79, v119 neg_lo:[0,1] neg_hi:[0,1]
	v_pk_add_f16 v44, v80, v120 neg_lo:[0,1] neg_hi:[0,1]
	v_pk_add_f16 v45, v81, v121 neg_lo:[0,1] neg_hi:[0,1]
	v_exp_f16_sdwa v46, v42 dst_sel:WORD_0 dst_unused:UNUSED_PAD src0_sel:WORD_0
	v_exp_f16_sdwa v47, v43 dst_sel:WORD_0 dst_unused:UNUSED_PAD src0_sel:WORD_0
	v_exp_f16_sdwa v48, v44 dst_sel:WORD_0 dst_unused:UNUSED_PAD src0_sel:WORD_0
	v_exp_f16_sdwa v49, v45 dst_sel:WORD_0 dst_unused:UNUSED_PAD src0_sel:WORD_0
	v_exp_f16_sdwa v46, v42 dst_sel:WORD_1 dst_unused:UNUSED_PRESERVE src0_sel:WORD_1
	v_exp_f16_sdwa v47, v43 dst_sel:WORD_1 dst_unused:UNUSED_PRESERVE src0_sel:WORD_1
	v_exp_f16_sdwa v48, v44 dst_sel:WORD_1 dst_unused:UNUSED_PRESERVE src0_sel:WORD_1
	v_exp_f16_sdwa v49, v45 dst_sel:WORD_1 dst_unused:UNUSED_PRESERVE src0_sel:WORD_1
	v_pk_add_f16 v42, v105, v118 neg_lo:[0,1] neg_hi:[0,1]
	v_pk_add_f16 v34, v34, v49
	v_pk_add_f16 v37, v37, v46
	v_pk_add_f16 v36, v36, v47
	v_pk_add_f16 v35, v35, v48
	v_pk_fma_f16 v25, v17, v49, v25
	v_pk_fma_f16 v24, v16, v48, v24
	v_pk_fma_f16 v23, v15, v47, v23
	v_pk_fma_f16 v22, v14, v46, v22
	v_pk_add_f16 v43, v104, v119 neg_lo:[0,1] neg_hi:[0,1]
	v_pk_add_f16 v44, v103, v120 neg_lo:[0,1] neg_hi:[0,1]
	v_pk_add_f16 v45, v102, v121 neg_lo:[0,1] neg_hi:[0,1]
	v_exp_f16_sdwa v46, v42 dst_sel:WORD_0 dst_unused:UNUSED_PAD src0_sel:WORD_0
	v_exp_f16_sdwa v47, v43 dst_sel:WORD_0 dst_unused:UNUSED_PAD src0_sel:WORD_0
	v_exp_f16_sdwa v48, v44 dst_sel:WORD_0 dst_unused:UNUSED_PAD src0_sel:WORD_0
	v_exp_f16_sdwa v49, v45 dst_sel:WORD_0 dst_unused:UNUSED_PAD src0_sel:WORD_0
	v_exp_f16_sdwa v46, v42 dst_sel:WORD_1 dst_unused:UNUSED_PRESERVE src0_sel:WORD_1
	v_exp_f16_sdwa v47, v43 dst_sel:WORD_1 dst_unused:UNUSED_PRESERVE src0_sel:WORD_1
	v_exp_f16_sdwa v48, v44 dst_sel:WORD_1 dst_unused:UNUSED_PRESERVE src0_sel:WORD_1
	v_exp_f16_sdwa v49, v45 dst_sel:WORD_1 dst_unused:UNUSED_PRESERVE src0_sel:WORD_1
	v_pk_add_f16 v42, v109, v118 neg_lo:[0,1] neg_hi:[0,1]
	v_pk_add_f16 v34, v34, v49
	v_pk_add_f16 v35, v35, v48
	v_pk_add_f16 v36, v36, v47
	v_pk_add_f16 v37, v37, v46
	v_pk_fma_f16 v22, v26, v46, v22
	v_pk_fma_f16 v23, v27, v47, v23
	v_pk_fma_f16 v24, v28, v48, v24
	v_pk_fma_f16 v25, v29, v49, v25
	v_pk_add_f16 v43, v108, v119 neg_lo:[0,1] neg_hi:[0,1]
	v_pk_add_f16 v44, v107, v120 neg_lo:[0,1] neg_hi:[0,1]
	v_pk_add_f16 v45, v106, v121 neg_lo:[0,1] neg_hi:[0,1]
	v_exp_f16_sdwa v46, v42 dst_sel:WORD_0 dst_unused:UNUSED_PAD src0_sel:WORD_0
	v_exp_f16_sdwa v47, v43 dst_sel:WORD_0 dst_unused:UNUSED_PAD src0_sel:WORD_0
	v_exp_f16_sdwa v48, v44 dst_sel:WORD_0 dst_unused:UNUSED_PAD src0_sel:WORD_0
	v_exp_f16_sdwa v49, v45 dst_sel:WORD_0 dst_unused:UNUSED_PAD src0_sel:WORD_0
	v_exp_f16_sdwa v46, v42 dst_sel:WORD_1 dst_unused:UNUSED_PRESERVE src0_sel:WORD_1
	v_exp_f16_sdwa v47, v43 dst_sel:WORD_1 dst_unused:UNUSED_PRESERVE src0_sel:WORD_1
	v_exp_f16_sdwa v48, v44 dst_sel:WORD_1 dst_unused:UNUSED_PRESERVE src0_sel:WORD_1
	v_exp_f16_sdwa v49, v45 dst_sel:WORD_1 dst_unused:UNUSED_PRESERVE src0_sel:WORD_1
	v_pk_add_f16 v42, v82, v118 neg_lo:[0,1] neg_hi:[0,1]
	v_pk_add_f16 v34, v34, v49
	v_pk_add_f16 v37, v37, v46
	v_pk_add_f16 v36, v36, v47
	v_pk_add_f16 v35, v35, v48
	v_pk_fma_f16 v25, v41, v49, v25
	v_pk_fma_f16 v24, v40, v48, v24
	v_pk_fma_f16 v23, v39, v47, v23
	v_pk_fma_f16 v22, v38, v46, v22
	v_pk_add_f16 v43, v83, v119 neg_lo:[0,1] neg_hi:[0,1]
	v_pk_add_f16 v44, v84, v120 neg_lo:[0,1] neg_hi:[0,1]
	v_pk_add_f16 v45, v85, v121 neg_lo:[0,1] neg_hi:[0,1]
	v_exp_f16_sdwa v46, v42 dst_sel:WORD_0 dst_unused:UNUSED_PAD src0_sel:WORD_0
	v_exp_f16_sdwa v47, v43 dst_sel:WORD_0 dst_unused:UNUSED_PAD src0_sel:WORD_0
	v_exp_f16_sdwa v48, v44 dst_sel:WORD_0 dst_unused:UNUSED_PAD src0_sel:WORD_0
	v_exp_f16_sdwa v49, v45 dst_sel:WORD_0 dst_unused:UNUSED_PAD src0_sel:WORD_0
	v_exp_f16_sdwa v46, v42 dst_sel:WORD_1 dst_unused:UNUSED_PRESERVE src0_sel:WORD_1
	v_exp_f16_sdwa v47, v43 dst_sel:WORD_1 dst_unused:UNUSED_PRESERVE src0_sel:WORD_1
	v_exp_f16_sdwa v48, v44 dst_sel:WORD_1 dst_unused:UNUSED_PRESERVE src0_sel:WORD_1
	v_exp_f16_sdwa v49, v45 dst_sel:WORD_1 dst_unused:UNUSED_PRESERVE src0_sel:WORD_1
	s_nop 0
	v_pk_add_f16 v34, v34, v49
	v_pk_add_f16 v35, v35, v48
	v_rcp_f16_e32 v44, v34
	v_rcp_f16_sdwa v34, v34 dst_sel:DWORD dst_unused:UNUSED_PAD src0_sel:WORD_1
	v_pk_add_f16 v36, v36, v47
	v_rcp_f16_e32 v45, v35
	v_rcp_f16_sdwa v35, v35 dst_sel:DWORD dst_unused:UNUSED_PAD src0_sel:WORD_1
	v_pk_add_f16 v37, v37, v46
	v_rcp_f16_e32 v43, v36
	v_rcp_f16_sdwa v36, v36 dst_sel:DWORD dst_unused:UNUSED_PAD src0_sel:WORD_1
	v_rcp_f16_e32 v42, v37
	v_rcp_f16_sdwa v37, v37 dst_sel:DWORD dst_unused:UNUSED_PAD src0_sel:WORD_1
	v_pk_fma_f16 v25, v61, v49, v25
	v_pack_b32_f16 v34, v44, v34
	v_pk_fma_f16 v24, v60, v48, v24
	v_pk_mul_f16 v25, v25, v34
	v_pack_b32_f16 v34, v45, v35
	v_pk_fma_f16 v23, v59, v47, v23
	v_pk_mul_f16 v24, v24, v34
	v_pack_b32_f16 v34, v43, v36
	v_pk_fma_f16 v22, v58, v46, v22
	v_pk_mul_f16 v23, v23, v34
	v_pack_b32_f16 v34, v42, v37
	v_pk_mul_f16 v22, v22, v34
	s_waitcnt vmcnt(0)
	s_cmp_lg_u32 s10, 1
	s_cbranch_scc1 .Lmywp3_2
	s_mov_b64 s[86:87], s[80:81]
	global_load_dword v254, v255, s[86:87]
	s_add_u32 s86, s86, 0x2000
	s_addc_u32 s87, s87, 0
	global_load_dword v254, v255, s[86:87]
	s_add_u32 s86, s86, 0x2000
	s_addc_u32 s87, s87, 0
	global_load_dword v254, v255, s[86:87]
	s_add_u32 s86, s86, 0x2c000
	s_addc_u32 s87, s87, 0
	global_load_dword v254, v255, s[86:87]
	s_add_u32 s86, s86, 0x2000
	s_addc_u32 s87, s87, 0
	global_load_dword v254, v255, s[86:87]
	s_add_u32 s86, s86, 0x2000
	s_addc_u32 s87, s87, 0
	global_load_dword v254, v255, s[86:87]
.Lmywp3_2:
	v_pk_mul_f16 v34, v182, v146 op_sel_hi:[0,1]
	v_pk_mul_f16 v35, v182, v147 op_sel_hi:[0,1]
	v_pk_mul_f16 v36, v182, v148 op_sel_hi:[0,1]
	v_pk_mul_f16 v37, v182, v149 op_sel_hi:[0,1]
	v_pk_mul_f16 v42, v180, v146 op_sel_hi:[0,1]
	v_pk_mul_f16 v43, v180, v147 op_sel_hi:[0,1]
	v_pk_mul_f16 v44, v180, v148 op_sel_hi:[0,1]
	v_pk_mul_f16 v45, v180, v149 op_sel_hi:[0,1]
	v_pk_mul_f16 v46, v181, v146 op_sel_hi:[0,1]
	v_pk_mul_f16 v47, v181, v147 op_sel_hi:[0,1]
	v_pk_mul_f16 v48, v181, v148 op_sel_hi:[0,1]
	v_pk_mul_f16 v49, v181, v149 op_sel_hi:[0,1]
	v_pk_fma_f16 v21, v21, v149, v37
	v_pk_fma_f16 v20, v20, v148, v36
	v_pk_fma_f16 v19, v19, v147, v35
	v_pk_fma_f16 v18, v18, v146, v34
	v_pk_fma_f16 v33, v33, v149, v37
	v_pk_fma_f16 v32, v32, v148, v36
	v_pk_fma_f16 v31, v31, v147, v35
	v_pk_fma_f16 v30, v30, v146, v34
	v_pk_fma_f16 v37, v57, v149, v37
	v_pk_fma_f16 v36, v56, v148, v36
	v_pk_fma_f16 v35, v55, v147, v35
	v_pk_fma_f16 v34, v54, v146, v34
	v_pk_maximum3_f16 v79, v19, v31, v35
	v_pk_maximum3_f16 v80, v20, v32, v36
	v_pk_maximum3_f16 v81, v21, v33, v37
	v_pk_fma_f16 v50, v77, v149, v45
	v_pk_maximum3_f16 v78, v18, v30, v34
	v_pk_fma_f16 v51, v76, v148, v44
	v_pk_fma_f16 v52, v75, v147, v43
	v_pk_fma_f16 v53, v74, v146, v42
	v_pk_fma_f16 v54, v101, v149, v45
	v_pk_fma_f16 v55, v100, v148, v44
	v_pk_fma_f16 v56, v99, v147, v43
	v_pk_fma_f16 v57, v98, v146, v42
	v_pk_fma_f16 v45, v117, v149, v45
	v_pk_fma_f16 v44, v116, v148, v44
	v_pk_fma_f16 v43, v115, v147, v43
	v_pk_fma_f16 v42, v114, v146, v42
	v_pk_fma_f16 v66, v133, v149, v49
	v_pk_fma_f16 v67, v132, v148, v48
	v_pk_fma_f16 v68, v131, v147, v47
	v_pk_fma_f16 v69, v130, v146, v46
	v_pk_fma_f16 v74, v137, v149, v49
	v_pk_fma_f16 v75, v136, v148, v48
	v_pk_fma_f16 v76, v135, v147, v47
	v_pk_fma_f16 v77, v134, v146, v46
	v_pk_fma_f16 v49, v145, v149, v49
	v_pk_fma_f16 v48, v144, v148, v48
	v_pk_fma_f16 v47, v143, v147, v47
	v_pk_fma_f16 v46, v142, v146, v46
	v_pk_maximum3_f16 v82, v53, v57, v42
	v_pk_maximum3_f16 v83, v52, v56, v43
	v_pk_maximum3_f16 v84, v51, v55, v44
	v_pk_maximum3_f16 v85, v50, v54, v45
	v_pk_maximum3_f16 v87, v68, v76, v47
	v_pk_maximum3_f16 v86, v69, v77, v46
	v_pk_maximum3_f16 v88, v67, v75, v48
	v_pk_maximum3_f16 v89, v66, v74, v49
	v_pk_maximum3_f16 v78, v78, v82, v86
	v_pk_maximum3_f16 v79, v79, v83, v87
	v_pk_maximum3_f16 v80, v80, v84, v88
	v_pk_maximum3_f16 v81, v81, v85, v89
	s_nop 0
	v_pk_add_f16 v18, v18, v78 neg_lo:[0,1] neg_hi:[0,1]
	v_pk_add_f16 v19, v19, v79 neg_lo:[0,1] neg_hi:[0,1]
	v_pk_add_f16 v20, v20, v80 neg_lo:[0,1] neg_hi:[0,1]
	v_pk_add_f16 v21, v21, v81 neg_lo:[0,1] neg_hi:[0,1]
	v_pk_add_f16 v30, v30, v78 neg_lo:[0,1] neg_hi:[0,1]
	v_exp_f16_sdwa v82, v18 dst_sel:WORD_0 dst_unused:UNUSED_PAD src0_sel:WORD_0
	v_exp_f16_sdwa v83, v19 dst_sel:WORD_0 dst_unused:UNUSED_PAD src0_sel:WORD_0
	v_exp_f16_sdwa v84, v20 dst_sel:WORD_0 dst_unused:UNUSED_PAD src0_sel:WORD_0
	v_exp_f16_sdwa v85, v21 dst_sel:WORD_0 dst_unused:UNUSED_PAD src0_sel:WORD_0
	v_exp_f16_sdwa v82, v18 dst_sel:WORD_1 dst_unused:UNUSED_PRESERVE src0_sel:WORD_1
	v_exp_f16_sdwa v83, v19 dst_sel:WORD_1 dst_unused:UNUSED_PRESERVE src0_sel:WORD_1
	v_exp_f16_sdwa v84, v20 dst_sel:WORD_1 dst_unused:UNUSED_PRESERVE src0_sel:WORD_1
	v_exp_f16_sdwa v85, v21 dst_sel:WORD_1 dst_unused:UNUSED_PRESERVE src0_sel:WORD_1
	v_pk_add_f16 v31, v31, v79 neg_lo:[0,1] neg_hi:[0,1]
	v_pk_add_f16 v18, v82, 0
	v_pk_add_f16 v19, v83, 0
	v_pk_add_f16 v20, v84, 0
	v_pk_add_f16 v21, v85, 0
	v_pk_fma_f16 v6, v6, v82, 0
	v_pk_fma_f16 v7, v7, v83, 0
	v_pk_fma_f16 v8, v8, v84, 0
	v_pk_fma_f16 v9, v9, v85, 0
	v_pk_add_f16 v32, v32, v80 neg_lo:[0,1] neg_hi:[0,1]
	v_pk_add_f16 v33, v33, v81 neg_lo:[0,1] neg_hi:[0,1]
	v_exp_f16_sdwa v82, v30 dst_sel:WORD_0 dst_unused:UNUSED_PAD src0_sel:WORD_0
	v_exp_f16_sdwa v83, v31 dst_sel:WORD_0 dst_unused:UNUSED_PAD src0_sel:WORD_0
	v_exp_f16_sdwa v84, v32 dst_sel:WORD_0 dst_unused:UNUSED_PAD src0_sel:WORD_0
	v_exp_f16_sdwa v85, v33 dst_sel:WORD_0 dst_unused:UNUSED_PAD src0_sel:WORD_0
	v_exp_f16_sdwa v82, v30 dst_sel:WORD_1 dst_unused:UNUSED_PRESERVE src0_sel:WORD_1
	v_exp_f16_sdwa v83, v31 dst_sel:WORD_1 dst_unused:UNUSED_PRESERVE src0_sel:WORD_1
	v_exp_f16_sdwa v84, v32 dst_sel:WORD_1 dst_unused:UNUSED_PRESERVE src0_sel:WORD_1
	v_exp_f16_sdwa v85, v33 dst_sel:WORD_1 dst_unused:UNUSED_PRESERVE src0_sel:WORD_1
	s_nop 0
	v_pk_add_f16 v21, v21, v85
	v_pk_add_f16 v20, v20, v84
	v_pk_add_f16 v19, v19, v83
	v_pk_add_f16 v18, v18, v82
	v_pk_fma_f16 v9, v13, v85, v9
	v_pk_fma_f16 v8, v12, v84, v8
	v_pk_fma_f16 v7, v11, v83, v7
	v_pk_fma_f16 v6, v10, v82, v6
	v_pk_add_f16 v10, v34, v78 neg_lo:[0,1] neg_hi:[0,1]
	v_pk_add_f16 v11, v35, v79 neg_lo:[0,1] neg_hi:[0,1]
	v_pk_add_f16 v12, v36, v80 neg_lo:[0,1] neg_hi:[0,1]
	v_pk_add_f16 v13, v37, v81 neg_lo:[0,1] neg_hi:[0,1]
	v_exp_f16_sdwa v30, v10 dst_sel:WORD_0 dst_unused:UNUSED_PAD src0_sel:WORD_0
	v_exp_f16_sdwa v31, v11 dst_sel:WORD_0 dst_unused:UNUSED_PAD src0_sel:WORD_0
	v_exp_f16_sdwa v32, v12 dst_sel:WORD_0 dst_unused:UNUSED_PAD src0_sel:WORD_0
	v_exp_f16_sdwa v33, v13 dst_sel:WORD_0 dst_unused:UNUSED_PAD src0_sel:WORD_0
	v_exp_f16_sdwa v30, v10 dst_sel:WORD_1 dst_unused:UNUSED_PRESERVE src0_sel:WORD_1
	v_exp_f16_sdwa v31, v11 dst_sel:WORD_1 dst_unused:UNUSED_PRESERVE src0_sel:WORD_1
	v_exp_f16_sdwa v32, v12 dst_sel:WORD_1 dst_unused:UNUSED_PRESERVE src0_sel:WORD_1
	v_exp_f16_sdwa v33, v13 dst_sel:WORD_1 dst_unused:UNUSED_PRESERVE src0_sel:WORD_1
	v_pk_add_f16 v10, v18, v30
	v_pk_add_f16 v11, v19, v31
	v_pk_add_f16 v12, v20, v32
	v_pk_add_f16 v13, v21, v33
	v_pk_fma_f16 v6, v14, v30, v6
	v_pk_fma_f16 v7, v15, v31, v7
	v_pk_fma_f16 v8, v16, v32, v8
	v_pk_fma_f16 v9, v17, v33, v9
	v_pk_add_f16 v14, v53, v78 neg_lo:[0,1] neg_hi:[0,1]
	v_pk_add_f16 v15, v52, v79 neg_lo:[0,1] neg_hi:[0,1]
	v_pk_add_f16 v16, v51, v80 neg_lo:[0,1] neg_hi:[0,1]
	v_pk_add_f16 v17, v50, v81 neg_lo:[0,1] neg_hi:[0,1]
	v_exp_f16_sdwa v18, v14 dst_sel:WORD_0 dst_unused:UNUSED_PAD src0_sel:WORD_0
	v_exp_f16_sdwa v19, v15 dst_sel:WORD_0 dst_unused:UNUSED_PAD src0_sel:WORD_0
	v_exp_f16_sdwa v20, v16 dst_sel:WORD_0 dst_unused:UNUSED_PAD src0_sel:WORD_0
	v_exp_f16_sdwa v21, v17 dst_sel:WORD_0 dst_unused:UNUSED_PAD src0_sel:WORD_0
	v_exp_f16_sdwa v18, v14 dst_sel:WORD_1 dst_unused:UNUSED_PRESERVE src0_sel:WORD_1
	v_exp_f16_sdwa v19, v15 dst_sel:WORD_1 dst_unused:UNUSED_PRESERVE src0_sel:WORD_1
	v_exp_f16_sdwa v20, v16 dst_sel:WORD_1 dst_unused:UNUSED_PRESERVE src0_sel:WORD_1
	v_exp_f16_sdwa v21, v17 dst_sel:WORD_1 dst_unused:UNUSED_PRESERVE src0_sel:WORD_1
	v_pk_add_f16 v14, v57, v78 neg_lo:[0,1] neg_hi:[0,1]
	v_pk_add_f16 v13, v13, v21
	v_pk_add_f16 v12, v12, v20
	v_pk_add_f16 v11, v11, v19
	v_pk_add_f16 v10, v10, v18
	v_pk_fma_f16 v9, v29, v21, v9
	v_pk_fma_f16 v8, v28, v20, v8
	v_pk_fma_f16 v7, v27, v19, v7
	v_pk_fma_f16 v6, v26, v18, v6
	v_pk_add_f16 v15, v56, v79 neg_lo:[0,1] neg_hi:[0,1]
	v_pk_add_f16 v16, v55, v80 neg_lo:[0,1] neg_hi:[0,1]
	v_pk_add_f16 v17, v54, v81 neg_lo:[0,1] neg_hi:[0,1]
	v_exp_f16_sdwa v18, v14 dst_sel:WORD_0 dst_unused:UNUSED_PAD src0_sel:WORD_0
	v_exp_f16_sdwa v19, v15 dst_sel:WORD_0 dst_unused:UNUSED_PAD src0_sel:WORD_0
	v_exp_f16_sdwa v20, v16 dst_sel:WORD_0 dst_unused:UNUSED_PAD src0_sel:WORD_0
	v_exp_f16_sdwa v21, v17 dst_sel:WORD_0 dst_unused:UNUSED_PAD src0_sel:WORD_0
	v_exp_f16_sdwa v18, v14 dst_sel:WORD_1 dst_unused:UNUSED_PRESERVE src0_sel:WORD_1
	v_exp_f16_sdwa v19, v15 dst_sel:WORD_1 dst_unused:UNUSED_PRESERVE src0_sel:WORD_1
	v_exp_f16_sdwa v20, v16 dst_sel:WORD_1 dst_unused:UNUSED_PRESERVE src0_sel:WORD_1
	v_exp_f16_sdwa v21, v17 dst_sel:WORD_1 dst_unused:UNUSED_PRESERVE src0_sel:WORD_1
	v_pk_add_f16 v14, v42, v78 neg_lo:[0,1] neg_hi:[0,1]
	v_pk_add_f16 v10, v10, v18
	v_pk_add_f16 v11, v11, v19
	v_pk_add_f16 v12, v12, v20
	v_pk_add_f16 v13, v13, v21
	v_pk_fma_f16 v6, v38, v18, v6
	v_pk_fma_f16 v7, v39, v19, v7
	v_pk_fma_f16 v8, v40, v20, v8
	v_pk_fma_f16 v9, v41, v21, v9
	v_pk_add_f16 v15, v43, v79 neg_lo:[0,1] neg_hi:[0,1]
	v_pk_add_f16 v16, v44, v80 neg_lo:[0,1] neg_hi:[0,1]
	v_pk_add_f16 v17, v45, v81 neg_lo:[0,1] neg_hi:[0,1]
	v_exp_f16_sdwa v18, v14 dst_sel:WORD_0 dst_unused:UNUSED_PAD src0_sel:WORD_0
	v_exp_f16_sdwa v19, v15 dst_sel:WORD_0 dst_unused:UNUSED_PAD src0_sel:WORD_0
	v_exp_f16_sdwa v20, v16 dst_sel:WORD_0 dst_unused:UNUSED_PAD src0_sel:WORD_0
	v_exp_f16_sdwa v21, v17 dst_sel:WORD_0 dst_unused:UNUSED_PAD src0_sel:WORD_0
	v_exp_f16_sdwa v18, v14 dst_sel:WORD_1 dst_unused:UNUSED_PRESERVE src0_sel:WORD_1
	v_exp_f16_sdwa v19, v15 dst_sel:WORD_1 dst_unused:UNUSED_PRESERVE src0_sel:WORD_1
	v_exp_f16_sdwa v20, v16 dst_sel:WORD_1 dst_unused:UNUSED_PRESERVE src0_sel:WORD_1
	v_exp_f16_sdwa v21, v17 dst_sel:WORD_1 dst_unused:UNUSED_PRESERVE src0_sel:WORD_1
	v_pk_add_f16 v14, v69, v78 neg_lo:[0,1] neg_hi:[0,1]
	v_pk_add_f16 v13, v13, v21
	v_pk_add_f16 v12, v12, v20
	v_pk_add_f16 v11, v11, v19
	v_pk_add_f16 v10, v10, v18
	v_pk_fma_f16 v9, v61, v21, v9
	v_pk_fma_f16 v8, v60, v20, v8
	v_pk_fma_f16 v7, v59, v19, v7
	v_pk_fma_f16 v6, v58, v18, v6
	v_pk_add_f16 v15, v68, v79 neg_lo:[0,1] neg_hi:[0,1]
	v_pk_add_f16 v16, v67, v80 neg_lo:[0,1] neg_hi:[0,1]
	v_pk_add_f16 v17, v66, v81 neg_lo:[0,1] neg_hi:[0,1]
	v_exp_f16_sdwa v18, v14 dst_sel:WORD_0 dst_unused:UNUSED_PAD src0_sel:WORD_0
	v_exp_f16_sdwa v19, v15 dst_sel:WORD_0 dst_unused:UNUSED_PAD src0_sel:WORD_0
	v_exp_f16_sdwa v20, v16 dst_sel:WORD_0 dst_unused:UNUSED_PAD src0_sel:WORD_0
	v_exp_f16_sdwa v21, v17 dst_sel:WORD_0 dst_unused:UNUSED_PAD src0_sel:WORD_0
	v_exp_f16_sdwa v18, v14 dst_sel:WORD_1 dst_unused:UNUSED_PRESERVE src0_sel:WORD_1
	v_exp_f16_sdwa v19, v15 dst_sel:WORD_1 dst_unused:UNUSED_PRESERVE src0_sel:WORD_1
	v_exp_f16_sdwa v20, v16 dst_sel:WORD_1 dst_unused:UNUSED_PRESERVE src0_sel:WORD_1
	v_exp_f16_sdwa v21, v17 dst_sel:WORD_1 dst_unused:UNUSED_PRESERVE src0_sel:WORD_1
	v_pk_add_f16 v10, v10, v18
	v_pk_add_f16 v11, v11, v19
	v_pk_add_f16 v12, v12, v20
	v_pk_add_f16 v13, v13, v21
	v_pk_fma_f16 v14, v70, v18, v6
	v_pk_fma_f16 v15, v71, v19, v7
	v_pk_fma_f16 v16, v72, v20, v8
	v_pk_fma_f16 v17, v73, v21, v9
	v_pk_add_f16 v6, v77, v78 neg_lo:[0,1] neg_hi:[0,1]
	v_pk_add_f16 v7, v76, v79 neg_lo:[0,1] neg_hi:[0,1]
	v_pk_add_f16 v8, v75, v80 neg_lo:[0,1] neg_hi:[0,1]
	v_pk_add_f16 v9, v74, v81 neg_lo:[0,1] neg_hi:[0,1]
	v_exp_f16_sdwa v18, v6 dst_sel:WORD_0 dst_unused:UNUSED_PAD src0_sel:WORD_0
	v_exp_f16_sdwa v19, v7 dst_sel:WORD_0 dst_unused:UNUSED_PAD src0_sel:WORD_0
	v_exp_f16_sdwa v20, v8 dst_sel:WORD_0 dst_unused:UNUSED_PAD src0_sel:WORD_0
	v_exp_f16_sdwa v21, v9 dst_sel:WORD_0 dst_unused:UNUSED_PAD src0_sel:WORD_0
	v_exp_f16_sdwa v18, v6 dst_sel:WORD_1 dst_unused:UNUSED_PRESERVE src0_sel:WORD_1
	v_exp_f16_sdwa v19, v7 dst_sel:WORD_1 dst_unused:UNUSED_PRESERVE src0_sel:WORD_1
	v_exp_f16_sdwa v20, v8 dst_sel:WORD_1 dst_unused:UNUSED_PRESERVE src0_sel:WORD_1
	v_exp_f16_sdwa v21, v9 dst_sel:WORD_1 dst_unused:UNUSED_PRESERVE src0_sel:WORD_1
	s_nop 0
	v_pk_add_f16 v9, v13, v21
	v_pk_add_f16 v8, v12, v20
	v_pk_add_f16 v7, v11, v19
	v_pk_add_f16 v6, v10, v18
	v_pk_fma_f16 v13, v93, v21, v17
	v_pk_fma_f16 v12, v92, v20, v16
	v_pk_fma_f16 v11, v91, v19, v15
	v_pk_fma_f16 v10, v90, v18, v14
	v_pk_add_f16 v18, v46, v78 neg_lo:[0,1] neg_hi:[0,1]
	v_pk_add_f16 v19, v47, v79 neg_lo:[0,1] neg_hi:[0,1]
	v_pk_add_f16 v20, v48, v80 neg_lo:[0,1] neg_hi:[0,1]
	v_pk_add_f16 v21, v49, v81 neg_lo:[0,1] neg_hi:[0,1]
	v_exp_f16_sdwa v14, v18 dst_sel:WORD_0 dst_unused:UNUSED_PAD src0_sel:WORD_0
	v_exp_f16_sdwa v17, v19 dst_sel:WORD_0 dst_unused:UNUSED_PAD src0_sel:WORD_0
	v_exp_f16_sdwa v15, v20 dst_sel:WORD_0 dst_unused:UNUSED_PAD src0_sel:WORD_0
	v_exp_f16_sdwa v16, v21 dst_sel:WORD_0 dst_unused:UNUSED_PAD src0_sel:WORD_0
	v_exp_f16_sdwa v14, v18 dst_sel:WORD_1 dst_unused:UNUSED_PRESERVE src0_sel:WORD_1
	v_exp_f16_sdwa v17, v19 dst_sel:WORD_1 dst_unused:UNUSED_PRESERVE src0_sel:WORD_1
	v_exp_f16_sdwa v15, v20 dst_sel:WORD_1 dst_unused:UNUSED_PRESERVE src0_sel:WORD_1
	v_exp_f16_sdwa v16, v21 dst_sel:WORD_1 dst_unused:UNUSED_PRESERVE src0_sel:WORD_1
	s_nop 0

.LBB3_7:
	v_add_u32_e32 v182, s33, v161
	v_add_u32_e32 v181, -1, v182
	v_or_b32_e32 v2, v181, v164
	v_add_u32_e32 v180, 0x18400, v171
	v_cmp_gt_u32_e64 s[0:1], 64, v2
	s_mov_b64 s[4:5], -1
	s_and_b64 vcc, exec, s[24:25]
	s_cbranch_vccz .LBB3_45
	s_load_dwordx2 s[4:5], s[22:23], 0x20
	s_waitcnt lgkmcnt(0)
	s_load_dwordx2 s[26:27], s[4:5], 0x0
	s_load_dword s34, s[4:5], 0x8
	v_cmp_lt_u32_e64 s[64:65], 0, v182
	v_cmp_gt_u32_e64 s[66:67], 63, v182
	v_cmp_lt_u32_e64 s[68:69], 0, v162
	v_cmp_gt_u32_e64 s[70:71], 60, v162
	buffer_load_dwordx4 v[186:189], v180, s[16:19], 0 offen
	s_and_b64 s[72:73], s[68:69], s[64:65]
	s_and_b64 s[74:75], s[68:69], s[66:67]
	s_and_b64 s[76:77], s[70:71], s[64:65]
	s_and_b64 s[78:79], s[70:71], s[66:67]
	v_mov_b32_e32 v110, v172
	v_mov_b32_e32 v111, v174
	v_mov_b32_e32 v112, v176
	v_mov_b32_e32 v113, v178
	v_mov_b32_e32 v70, v173
	v_mov_b32_e32 v71, v175
	v_mov_b32_e32 v72, v177
	v_mov_b32_e32 v73, v179
	v_mov_b32_e32 v126, v172
	v_mov_b32_e32 v127, v174
	v_mov_b32_e32 v128, v176
	v_mov_b32_e32 v129, v178
	v_mov_b32_e32 v98, v173
	v_mov_b32_e32 v99, v175
	v_mov_b32_e32 v100, v177
	v_mov_b32_e32 v101, v179
	v_mov_b32_e32 v134, v172
	v_mov_b32_e32 v135, v174
	v_mov_b32_e32 v136, v176
	v_mov_b32_e32 v137, v178
	v_mov_b32_e32 v114, v173
	v_mov_b32_e32 v115, v175
	v_mov_b32_e32 v116, v177
	v_mov_b32_e32 v117, v179
	v_mov_b32_e32 v82, v172
	v_mov_b32_e32 v83, v174
	v_mov_b32_e32 v84, v176
	v_mov_b32_e32 v85, v178
	v_mov_b32_e32 v42, v173
	v_mov_b32_e32 v43, v175
	v_mov_b32_e32 v44, v177
	v_mov_b32_e32 v45, v179
	v_mov_b32_e32 v122, v172
	v_mov_b32_e32 v123, v174
	v_mov_b32_e32 v124, v176
	v_mov_b32_e32 v125, v178
	v_mov_b32_e32 v86, v173
	v_mov_b32_e32 v87, v175
	v_mov_b32_e32 v88, v177
	v_mov_b32_e32 v89, v179
	v_mov_b32_e32 v50, v172
	v_mov_b32_e32 v51, v174
	v_mov_b32_e32 v52, v176
	v_mov_b32_e32 v53, v178
	v_mov_b32_e32 v22, v173
	v_mov_b32_e32 v23, v175
	v_mov_b32_e32 v24, v177
	v_mov_b32_e32 v25, v179
	v_mov_b32_e32 v94, v172
	v_mov_b32_e32 v95, v174
	v_mov_b32_e32 v96, v176
	v_mov_b32_e32 v97, v178
	v_mov_b32_e32 v46, v173
	v_mov_b32_e32 v47, v175
	v_mov_b32_e32 v48, v177
	v_mov_b32_e32 v49, v179
	v_mov_b32_e32 v18, v172
	v_mov_b32_e32 v19, v174
	v_mov_b32_e32 v20, v176
	v_mov_b32_e32 v21, v178
	v_mov_b32_e32 v6, v173
	v_mov_b32_e32 v7, v175
	v_mov_b32_e32 v8, v177
	v_mov_b32_e32 v9, v179
	v_mov_b32_e32 v54, v172
	v_mov_b32_e32 v55, v174
	v_mov_b32_e32 v56, v176
	v_mov_b32_e32 v57, v178
	v_mov_b32_e32 v14, v173
	v_mov_b32_e32 v15, v175
	v_mov_b32_e32 v16, v177
	v_mov_b32_e32 v17, v179
	v_mov_b32_e32 v74, v172
	v_mov_b32_e32 v75, v174
	v_mov_b32_e32 v76, v176
	v_mov_b32_e32 v77, v178
	v_mov_b32_e32 v26, v173
	v_mov_b32_e32 v27, v175
	v_mov_b32_e32 v28, v177
	v_mov_b32_e32 v29, v179
	v_mov_b32_e32 v118, v172
	v_mov_b32_e32 v119, v174
	v_mov_b32_e32 v120, v176
	v_mov_b32_e32 v121, v178
	v_mov_b32_e32 v58, v173
	v_mov_b32_e32 v59, v175
	v_mov_b32_e32 v60, v177
	v_mov_b32_e32 v61, v179
	v_mov_b32_e32 v130, v172
	v_mov_b32_e32 v131, v174
	v_mov_b32_e32 v132, v176
	v_mov_b32_e32 v133, v178
	v_mov_b32_e32 v78, v173
	v_mov_b32_e32 v79, v175
	v_mov_b32_e32 v80, v177
	v_mov_b32_e32 v81, v179
	v_mov_b32_e32 v138, v172
	v_mov_b32_e32 v139, v174
	v_mov_b32_e32 v140, v176
	v_mov_b32_e32 v141, v178
	v_mov_b32_e32 v90, v173
	v_mov_b32_e32 v91, v175
	v_mov_b32_e32 v92, v177
	v_mov_b32_e32 v93, v179
	v_mov_b32_e32 v142, v172
	v_mov_b32_e32 v143, v174
	v_mov_b32_e32 v144, v176
	v_mov_b32_e32 v145, v178
	v_mov_b32_e32 v2, v173
	v_mov_b32_e32 v3, v175
	v_mov_b32_e32 v4, v177
	v_mov_b32_e32 v5, v179
	v_add_u32_e32 v249, 0xfffe7c00, v180
	v_add_u32_e32 v250, 0xfffe8000, v180
	s_mov_b64 exec, s[72:73]
	buffer_load_dwordx4 v[110:113], v249, s[16:19], 0 offen
	buffer_load_dwordx4 v[70:73], v249, s[16:19], 0 offen offset:512
	s_mov_b64 exec, -1
	s_mov_b64 exec, s[68:69]
	buffer_load_dwordx4 v[126:129], v250, s[16:19], 0 offen offset:512
	buffer_load_dwordx4 v[98:101], v250, s[16:19], 0 offen offset:1024
	s_mov_b64 exec, -1
	s_mov_b64 exec, s[74:75]
	buffer_load_dwordx4 v[134:137], v250, s[16:19], 0 offen offset:2048
	buffer_load_dwordx4 v[114:117], v250, s[16:19], 0 offen offset:2560
	s_mov_b64 exec, -1
	v_add_u32_e32 v249, 0xfffffc00, v180
	s_mov_b64 exec, s[64:65]
	buffer_load_dwordx4 v[82:85], v249, s[16:19], 0 offen
	buffer_load_dwordx4 v[42:45], v249, s[16:19], 0 offen offset:512
	s_mov_b64 exec, -1
	buffer_load_dwordx4 v[106:109], v180, s[16:19], 0 offen offset:512
	buffer_load_dwordx4 v[62:65], v180, s[16:19], 0 offen offset:1024
	s_mov_b64 exec, s[66:67]
	buffer_load_dwordx4 v[122:125], v180, s[16:19], 0 offen offset:2048
	buffer_load_dwordx4 v[86:89], v180, s[16:19], 0 offen offset:2560
	s_mov_b64 exec, -1
	v_add_u32_e32 v249, 0x17c00, v180
	v_add_u32_e32 v250, 0x18000, v180
	s_mov_b64 exec, s[64:65]
	buffer_load_dwordx4 v[50:53], v249, s[16:19], 0 offen
	buffer_load_dwordx4 v[22:25], v249, s[16:19], 0 offen offset:512
	s_mov_b64 exec, -1
	buffer_load_dwordx4 v[66:69], v250, s[16:19], 0 offen offset:512
	buffer_load_dwordx4 v[30:33], v250, s[16:19], 0 offen offset:1024
	s_mov_b64 exec, s[66:67]
	buffer_load_dwordx4 v[94:97], v250, s[16:19], 0 offen offset:2048
	buffer_load_dwordx4 v[46:49], v250, s[16:19], 0 offen offset:2560
	s_mov_b64 exec, -1
	v_add_u32_e32 v249, 0x18000, v180
	buffer_load_dwordx4 v[154:157], v249, s[16:19], 0 offen
	v_add_u32_e32 v250, 0x30000, v180
	buffer_load_dwordx4 v[150:153], v250, s[16:19], 0 offen
	v_add_u32_e32 v249, 0x48000, v180
	buffer_load_dwordx4 v[146:149], v249, s[16:19], 0 offen
	v_add_u32_e32 v249, 0x2fc00, v180
	v_add_u32_e32 v250, 0x30000, v180
	v_add_u32_e32 v251, 0x47c00, v180
	v_add_u32_e32 v252, 0x48000, v180
	v_add_u32_e32 v253, 0x5fc00, v180
	v_add_u32_e32 v254, 0x60000, v180
	s_waitcnt lgkmcnt(0)
	v_cvt_f16_f32_e32 v183, s27
	v_cvt_f16_f32_e32 v185, s26
	v_cvt_f16_f32_e32 v184, s34
	s_mov_b64 s[4:5], 0
	s_waitcnt vmcnt(3)
	v_pk_mul_f16 v193, v185, v189 op_sel_hi:[0,1]
	v_pk_mul_f16 v197, v183, v189 op_sel_hi:[0,1]
	v_pk_mul_f16 v201, v184, v189 op_sel_hi:[0,1]
	v_pk_mul_f16 v190, v185, v186 op_sel_hi:[0,1]
	v_pk_mul_f16 v191, v185, v187 op_sel_hi:[0,1]
	v_pk_mul_f16 v192, v185, v188 op_sel_hi:[0,1]
	v_pk_mul_f16 v194, v183, v186 op_sel_hi:[0,1]
	s_mov_b64 exec, s[64:65]
	buffer_load_dwordx4 v[18:21], v249, s[16:19], 0 offen
	buffer_load_dwordx4 v[6:9], v249, s[16:19], 0 offen offset:512
	s_mov_b64 exec, -1
	v_pk_mul_f16 v195, v183, v187 op_sel_hi:[0,1]
	v_pk_mul_f16 v196, v183, v188 op_sel_hi:[0,1]
	v_pk_mul_f16 v198, v184, v186 op_sel_hi:[0,1]
	v_pk_mul_f16 v199, v184, v187 op_sel_hi:[0,1]
	v_pk_mul_f16 v200, v184, v188 op_sel_hi:[0,1]
	v_pk_fma_f16 v113, v113, v189, v193
	v_pk_fma_f16 v129, v129, v189, v197
	v_pk_fma_f16 v137, v137, v189, v201
	v_pk_fma_f16 v202, v85, v189, v193
	v_pk_fma_f16 v206, v109, v189, v197
	v_pk_fma_f16 v210, v125, v189, v201
	v_pk_fma_f16 v193, v53, v189, v193
	v_pk_fma_f16 v197, v69, v189, v197
	buffer_load_dwordx4 v[34:37], v250, s[16:19], 0 offen offset:512
	buffer_load_dwordx4 v[10:13], v250, s[16:19], 0 offen offset:1024
	v_pk_fma_f16 v189, v97, v189, v201
	v_pk_maximum3_f16 v201, v113, v129, v137
	v_pk_fma_f16 v112, v112, v188, v192
	v_pk_fma_f16 v111, v111, v187, v191
	v_pk_fma_f16 v110, v110, v186, v190
	v_pk_fma_f16 v128, v128, v188, v196
	v_pk_fma_f16 v127, v127, v187, v195
	v_pk_fma_f16 v126, v126, v186, v194
	v_pk_fma_f16 v136, v136, v188, v200
	v_pk_fma_f16 v135, v135, v187, v199
	v_pk_fma_f16 v134, v134, v186, v198
	v_pk_fma_f16 v203, v84, v188, v192
	v_pk_fma_f16 v204, v83, v187, v191
	v_pk_fma_f16 v205, v82, v186, v190
	v_pk_fma_f16 v207, v108, v188, v196
	v_pk_fma_f16 v208, v107, v187, v195
	s_mov_b64 exec, s[66:67]
	buffer_load_dwordx4 v[54:57], v250, s[16:19], 0 offen offset:2048
	buffer_load_dwordx4 v[14:17], v250, s[16:19], 0 offen offset:2560
	s_mov_b64 exec, -1
	v_pk_fma_f16 v209, v106, v186, v194
	v_pk_fma_f16 v211, v124, v188, v200
	v_pk_fma_f16 v212, v123, v187, v199
	v_pk_fma_f16 v213, v122, v186, v198
	v_pk_fma_f16 v192, v52, v188, v192
	v_pk_fma_f16 v191, v51, v187, v191
	v_pk_fma_f16 v190, v50, v186, v190
	v_pk_fma_f16 v196, v68, v188, v196
	v_pk_fma_f16 v195, v67, v187, v195
	v_pk_fma_f16 v194, v66, v186, v194
	v_pk_fma_f16 v188, v96, v188, v200
	v_pk_fma_f16 v187, v95, v187, v199
	v_pk_fma_f16 v186, v94, v186, v198
	v_pk_maximum3_f16 v198, v110, v126, v134
	v_pk_maximum3_f16 v199, v111, v127, v135
	v_pk_maximum3_f16 v200, v112, v128, v136
	v_pk_maximum3_f16 v217, v202, v206, v210
	v_pk_maximum3_f16 v221, v193, v197, v189
	v_pk_maximum3_f16 v214, v205, v209, v213
	v_pk_maximum3_f16 v215, v204, v208, v212
	v_pk_maximum3_f16 v216, v203, v207, v211
	v_pk_maximum3_f16 v218, v190, v194, v186
	v_pk_maximum3_f16 v219, v191, v195, v187
	v_pk_maximum3_f16 v201, v201, v217, v221
	v_pk_maximum3_f16 v220, v192, v196, v188
	v_pk_maximum3_f16 v198, v198, v214, v218
	v_pk_maximum3_f16 v199, v199, v215, v219
	v_pk_maximum3_f16 v200, v200, v216, v220
	v_pk_add_f16 v113, v113, v201 neg_lo:[0,1] neg_hi:[0,1]
	s_mov_b64 exec, s[64:65]
	buffer_load_dwordx4 v[74:77], v251, s[16:19], 0 offen
	buffer_load_dwordx4 v[26:29], v251, s[16:19], 0 offen offset:512
	s_mov_b64 exec, -1
	v_pk_add_f16 v110, v110, v198 neg_lo:[0,1] neg_hi:[0,1]
	v_pk_add_f16 v111, v111, v199 neg_lo:[0,1] neg_hi:[0,1]
	v_pk_add_f16 v112, v112, v200 neg_lo:[0,1] neg_hi:[0,1]
	v_pk_add_f16 v126, v126, v198 neg_lo:[0,1] neg_hi:[0,1]
	v_exp_f16_sdwa v214, v110 dst_sel:WORD_0 dst_unused:UNUSED_PAD src0_sel:WORD_0
	v_exp_f16_sdwa v215, v111 dst_sel:WORD_0 dst_unused:UNUSED_PAD src0_sel:WORD_0
	v_exp_f16_sdwa v216, v112 dst_sel:WORD_0 dst_unused:UNUSED_PAD src0_sel:WORD_0
	v_exp_f16_sdwa v217, v113 dst_sel:WORD_0 dst_unused:UNUSED_PAD src0_sel:WORD_0
	v_exp_f16_sdwa v214, v110 dst_sel:WORD_1 dst_unused:UNUSED_PRESERVE src0_sel:WORD_1
	v_exp_f16_sdwa v215, v111 dst_sel:WORD_1 dst_unused:UNUSED_PRESERVE src0_sel:WORD_1
	v_exp_f16_sdwa v216, v112 dst_sel:WORD_1 dst_unused:UNUSED_PRESERVE src0_sel:WORD_1
	v_exp_f16_sdwa v217, v113 dst_sel:WORD_1 dst_unused:UNUSED_PRESERVE src0_sel:WORD_1
	v_pk_add_f16 v127, v127, v199 neg_lo:[0,1] neg_hi:[0,1]
	v_pk_add_f16 v113, v214, 0
	v_pk_fma_f16 v73, v73, v217, 0
	v_pk_add_f16 v110, v217, 0
	v_pk_add_f16 v111, v216, 0
	v_pk_add_f16 v112, v215, 0
	v_pk_fma_f16 v72, v72, v216, 0
	v_pk_fma_f16 v71, v71, v215, 0
	v_pk_fma_f16 v70, v70, v214, 0
	v_pk_add_f16 v128, v128, v200 neg_lo:[0,1] neg_hi:[0,1]
	buffer_load_dwordx4 v[102:105], v252, s[16:19], 0 offen offset:512
	buffer_load_dwordx4 v[38:41], v252, s[16:19], 0 offen offset:1024
	v_pk_add_f16 v129, v129, v201 neg_lo:[0,1] neg_hi:[0,1]
	v_exp_f16_sdwa v214, v126 dst_sel:WORD_0 dst_unused:UNUSED_PAD src0_sel:WORD_0
	v_exp_f16_sdwa v215, v127 dst_sel:WORD_0 dst_unused:UNUSED_PAD src0_sel:WORD_0
	v_exp_f16_sdwa v216, v128 dst_sel:WORD_0 dst_unused:UNUSED_PAD src0_sel:WORD_0
	v_exp_f16_sdwa v217, v129 dst_sel:WORD_0 dst_unused:UNUSED_PAD src0_sel:WORD_0
	v_exp_f16_sdwa v214, v126 dst_sel:WORD_1 dst_unused:UNUSED_PRESERVE src0_sel:WORD_1
	v_exp_f16_sdwa v215, v127 dst_sel:WORD_1 dst_unused:UNUSED_PRESERVE src0_sel:WORD_1
	v_exp_f16_sdwa v216, v128 dst_sel:WORD_1 dst_unused:UNUSED_PRESERVE src0_sel:WORD_1
	v_exp_f16_sdwa v217, v129 dst_sel:WORD_1 dst_unused:UNUSED_PRESERVE src0_sel:WORD_1
	v_pk_add_f16 v113, v113, v214
	v_pk_fma_f16 v73, v101, v217, v73
	v_pk_add_f16 v101, v137, v201 neg_lo:[0,1] neg_hi:[0,1]
	v_pk_add_f16 v112, v112, v215
	v_pk_add_f16 v111, v111, v216
	v_pk_add_f16 v110, v110, v217
	v_pk_fma_f16 v70, v98, v214, v70
	v_pk_fma_f16 v71, v99, v215, v71
	v_pk_fma_f16 v72, v100, v216, v72
	v_pk_add_f16 v98, v134, v198 neg_lo:[0,1] neg_hi:[0,1]
	v_pk_add_f16 v99, v135, v199 neg_lo:[0,1] neg_hi:[0,1]
	v_pk_add_f16 v100, v136, v200 neg_lo:[0,1] neg_hi:[0,1]
	v_exp_f16_sdwa v126, v98 dst_sel:WORD_0 dst_unused:UNUSED_PAD src0_sel:WORD_0
	v_exp_f16_sdwa v127, v99 dst_sel:WORD_0 dst_unused:UNUSED_PAD src0_sel:WORD_0
	v_exp_f16_sdwa v128, v100 dst_sel:WORD_0 dst_unused:UNUSED_PAD src0_sel:WORD_0
	v_exp_f16_sdwa v129, v101 dst_sel:WORD_0 dst_unused:UNUSED_PAD src0_sel:WORD_0
	v_exp_f16_sdwa v126, v98 dst_sel:WORD_1 dst_unused:UNUSED_PRESERVE src0_sel:WORD_1
	v_exp_f16_sdwa v127, v99 dst_sel:WORD_1 dst_unused:UNUSED_PRESERVE src0_sel:WORD_1
	v_exp_f16_sdwa v128, v100 dst_sel:WORD_1 dst_unused:UNUSED_PRESERVE src0_sel:WORD_1
	v_exp_f16_sdwa v129, v101 dst_sel:WORD_1 dst_unused:UNUSED_PRESERVE src0_sel:WORD_1
	v_pk_add_f16 v101, v113, v126
	v_pk_add_f16 v98, v110, v129
	s_mov_b64 exec, s[66:67]
	buffer_load_dwordx4 v[118:121], v252, s[16:19], 0 offen offset:2048
	buffer_load_dwordx4 v[58:61], v252, s[16:19], 0 offen offset:2560
	s_mov_b64 exec, -1
	v_pk_add_f16 v99, v111, v128
	v_pk_add_f16 v100, v112, v127
	v_pk_fma_f16 v73, v117, v129, v73
	v_pk_fma_f16 v72, v116, v128, v72
	v_pk_fma_f16 v71, v115, v127, v71
	v_pk_fma_f16 v70, v114, v126, v70
	v_pk_add_f16 v110, v205, v198 neg_lo:[0,1] neg_hi:[0,1]
	v_pk_add_f16 v111, v204, v199 neg_lo:[0,1] neg_hi:[0,1]
	v_pk_add_f16 v112, v203, v200 neg_lo:[0,1] neg_hi:[0,1]
	v_pk_add_f16 v113, v202, v201 neg_lo:[0,1] neg_hi:[0,1]
	v_exp_f16_sdwa v114, v110 dst_sel:WORD_0 dst_unused:UNUSED_PAD src0_sel:WORD_0
	v_exp_f16_sdwa v115, v111 dst_sel:WORD_0 dst_unused:UNUSED_PAD src0_sel:WORD_0
	v_exp_f16_sdwa v116, v112 dst_sel:WORD_0 dst_unused:UNUSED_PAD src0_sel:WORD_0
	v_exp_f16_sdwa v117, v113 dst_sel:WORD_0 dst_unused:UNUSED_PAD src0_sel:WORD_0
	v_exp_f16_sdwa v114, v110 dst_sel:WORD_1 dst_unused:UNUSED_PRESERVE src0_sel:WORD_1
	v_exp_f16_sdwa v115, v111 dst_sel:WORD_1 dst_unused:UNUSED_PRESERVE src0_sel:WORD_1
	v_exp_f16_sdwa v116, v112 dst_sel:WORD_1 dst_unused:UNUSED_PRESERVE src0_sel:WORD_1
	v_exp_f16_sdwa v117, v113 dst_sel:WORD_1 dst_unused:UNUSED_PRESERVE src0_sel:WORD_1
	v_pk_add_f16 v110, v209, v198 neg_lo:[0,1] neg_hi:[0,1]
	v_pk_add_f16 v101, v101, v114
	v_pk_add_f16 v100, v100, v115
	v_pk_add_f16 v99, v99, v116
	s_mov_b64 exec, s[76:77]
	buffer_load_dwordx4 v[130:133], v253, s[16:19], 0 offen
	buffer_load_dwordx4 v[78:81], v253, s[16:19], 0 offen offset:512
	s_mov_b64 exec, -1
	v_pk_add_f16 v98, v98, v117
	v_pk_fma_f16 v70, v42, v114, v70
	v_pk_fma_f16 v71, v43, v115, v71
	v_pk_fma_f16 v72, v44, v116, v72
	v_pk_fma_f16 v73, v45, v117, v73
	v_pk_add_f16 v111, v208, v199 neg_lo:[0,1] neg_hi:[0,1]
	v_pk_add_f16 v112, v207, v200 neg_lo:[0,1] neg_hi:[0,1]
	v_pk_add_f16 v113, v206, v201 neg_lo:[0,1] neg_hi:[0,1]
	v_exp_f16_sdwa v114, v110 dst_sel:WORD_0 dst_unused:UNUSED_PAD src0_sel:WORD_0
	v_exp_f16_sdwa v115, v111 dst_sel:WORD_0 dst_unused:UNUSED_PAD src0_sel:WORD_0
	v_exp_f16_sdwa v116, v112 dst_sel:WORD_0 dst_unused:UNUSED_PAD src0_sel:WORD_0
	v_exp_f16_sdwa v117, v113 dst_sel:WORD_0 dst_unused:UNUSED_PAD src0_sel:WORD_0
	v_exp_f16_sdwa v114, v110 dst_sel:WORD_1 dst_unused:UNUSED_PRESERVE src0_sel:WORD_1
	v_exp_f16_sdwa v115, v111 dst_sel:WORD_1 dst_unused:UNUSED_PRESERVE src0_sel:WORD_1
	v_exp_f16_sdwa v116, v112 dst_sel:WORD_1 dst_unused:UNUSED_PRESERVE src0_sel:WORD_1
	v_exp_f16_sdwa v117, v113 dst_sel:WORD_1 dst_unused:UNUSED_PRESERVE src0_sel:WORD_1
	v_pk_add_f16 v110, v213, v198 neg_lo:[0,1] neg_hi:[0,1]
	v_pk_add_f16 v101, v101, v114
	v_pk_add_f16 v98, v98, v117
	v_pk_add_f16 v99, v99, v116
	v_pk_add_f16 v100, v100, v115
	v_pk_fma_f16 v73, v65, v117, v73
	v_pk_fma_f16 v72, v64, v116, v72
	s_mov_b64 exec, s[70:71]
	buffer_load_dwordx4 v[138:141], v254, s[16:19], 0 offen offset:512
	buffer_load_dwordx4 v[90:93], v254, s[16:19], 0 offen offset:1024
	s_mov_b64 exec, -1
	v_pk_fma_f16 v71, v63, v115, v71
	v_pk_fma_f16 v70, v62, v114, v70
	v_pk_add_f16 v111, v212, v199 neg_lo:[0,1] neg_hi:[0,1]
	v_pk_add_f16 v112, v211, v200 neg_lo:[0,1] neg_hi:[0,1]
	v_pk_add_f16 v113, v210, v201 neg_lo:[0,1] neg_hi:[0,1]
	v_exp_f16_sdwa v114, v110 dst_sel:WORD_0 dst_unused:UNUSED_PAD src0_sel:WORD_0
	v_exp_f16_sdwa v115, v111 dst_sel:WORD_0 dst_unused:UNUSED_PAD src0_sel:WORD_0
	v_exp_f16_sdwa v116, v112 dst_sel:WORD_0 dst_unused:UNUSED_PAD src0_sel:WORD_0
	v_exp_f16_sdwa v117, v113 dst_sel:WORD_0 dst_unused:UNUSED_PAD src0_sel:WORD_0
	v_exp_f16_sdwa v114, v110 dst_sel:WORD_1 dst_unused:UNUSED_PRESERVE src0_sel:WORD_1
	v_exp_f16_sdwa v115, v111 dst_sel:WORD_1 dst_unused:UNUSED_PRESERVE src0_sel:WORD_1
	v_exp_f16_sdwa v116, v112 dst_sel:WORD_1 dst_unused:UNUSED_PRESERVE src0_sel:WORD_1
	v_exp_f16_sdwa v117, v113 dst_sel:WORD_1 dst_unused:UNUSED_PRESERVE src0_sel:WORD_1
	v_pk_add_f16 v110, v190, v198 neg_lo:[0,1] neg_hi:[0,1]
	v_pk_add_f16 v101, v101, v114
	v_pk_add_f16 v100, v100, v115
	v_pk_add_f16 v99, v99, v116
	v_pk_add_f16 v98, v98, v117
	v_pk_fma_f16 v70, v86, v114, v70
	v_pk_fma_f16 v71, v87, v115, v71
	v_pk_fma_f16 v72, v88, v116, v72
	v_pk_fma_f16 v73, v89, v117, v73
	s_mov_b64 exec, s[78:79]
	buffer_load_dwordx4 v[142:145], v254, s[16:19], 0 offen offset:2048
	buffer_load_dwordx4 v[2:5], v254, s[16:19], 0 offen offset:2560
	s_mov_b64 exec, -1
	v_pk_add_f16 v111, v191, v199 neg_lo:[0,1] neg_hi:[0,1]
	v_pk_add_f16 v112, v192, v200 neg_lo:[0,1] neg_hi:[0,1]
	v_pk_add_f16 v113, v193, v201 neg_lo:[0,1] neg_hi:[0,1]
	v_exp_f16_sdwa v114, v110 dst_sel:WORD_0 dst_unused:UNUSED_PAD src0_sel:WORD_0
	v_exp_f16_sdwa v115, v111 dst_sel:WORD_0 dst_unused:UNUSED_PAD src0_sel:WORD_0
	v_exp_f16_sdwa v116, v112 dst_sel:WORD_0 dst_unused:UNUSED_PAD src0_sel:WORD_0
	v_exp_f16_sdwa v117, v113 dst_sel:WORD_0 dst_unused:UNUSED_PAD src0_sel:WORD_0
	v_exp_f16_sdwa v114, v110 dst_sel:WORD_1 dst_unused:UNUSED_PRESERVE src0_sel:WORD_1
	v_exp_f16_sdwa v115, v111 dst_sel:WORD_1 dst_unused:UNUSED_PRESERVE src0_sel:WORD_1
	v_exp_f16_sdwa v116, v112 dst_sel:WORD_1 dst_unused:UNUSED_PRESERVE src0_sel:WORD_1
	v_exp_f16_sdwa v117, v113 dst_sel:WORD_1 dst_unused:UNUSED_PRESERVE src0_sel:WORD_1
	v_pk_add_f16 v110, v194, v198 neg_lo:[0,1] neg_hi:[0,1]
	v_pk_add_f16 v101, v101, v114
	v_pk_add_f16 v98, v98, v117
	v_pk_add_f16 v99, v99, v116
	v_pk_add_f16 v100, v100, v115
	v_pk_fma_f16 v73, v25, v117, v73
	v_pk_fma_f16 v72, v24, v116, v72
	v_pk_fma_f16 v71, v23, v115, v71
	v_pk_fma_f16 v70, v22, v114, v70
	v_pk_add_f16 v111, v195, v199 neg_lo:[0,1] neg_hi:[0,1]
	v_pk_add_f16 v112, v196, v200 neg_lo:[0,1] neg_hi:[0,1]
	v_pk_add_f16 v113, v197, v201 neg_lo:[0,1] neg_hi:[0,1]
	v_exp_f16_sdwa v114, v110 dst_sel:WORD_0 dst_unused:UNUSED_PAD src0_sel:WORD_0
	v_exp_f16_sdwa v115, v111 dst_sel:WORD_0 dst_unused:UNUSED_PAD src0_sel:WORD_0
	v_exp_f16_sdwa v116, v112 dst_sel:WORD_0 dst_unused:UNUSED_PAD src0_sel:WORD_0
	v_exp_f16_sdwa v117, v113 dst_sel:WORD_0 dst_unused:UNUSED_PAD src0_sel:WORD_0
	v_exp_f16_sdwa v114, v110 dst_sel:WORD_1 dst_unused:UNUSED_PRESERVE src0_sel:WORD_1
	v_exp_f16_sdwa v115, v111 dst_sel:WORD_1 dst_unused:UNUSED_PRESERVE src0_sel:WORD_1
	v_exp_f16_sdwa v116, v112 dst_sel:WORD_1 dst_unused:UNUSED_PRESERVE src0_sel:WORD_1
	v_exp_f16_sdwa v117, v113 dst_sel:WORD_1 dst_unused:UNUSED_PRESERVE src0_sel:WORD_1
	v_pk_add_f16 v110, v186, v198 neg_lo:[0,1] neg_hi:[0,1]
	v_pk_add_f16 v101, v101, v114
	v_pk_add_f16 v100, v100, v115
	v_pk_add_f16 v99, v99, v116
	v_pk_add_f16 v98, v98, v117
	v_pk_fma_f16 v70, v30, v114, v70
	v_pk_fma_f16 v71, v31, v115, v71
	v_pk_fma_f16 v72, v32, v116, v72
	v_pk_fma_f16 v73, v33, v117, v73
	v_pk_add_f16 v111, v187, v199 neg_lo:[0,1] neg_hi:[0,1]
	v_pk_add_f16 v112, v188, v200 neg_lo:[0,1] neg_hi:[0,1]
	v_pk_add_f16 v113, v189, v201 neg_lo:[0,1] neg_hi:[0,1]
	v_exp_f16_sdwa v114, v110 dst_sel:WORD_0 dst_unused:UNUSED_PAD src0_sel:WORD_0
	v_exp_f16_sdwa v115, v111 dst_sel:WORD_0 dst_unused:UNUSED_PAD src0_sel:WORD_0
	v_exp_f16_sdwa v116, v112 dst_sel:WORD_0 dst_unused:UNUSED_PAD src0_sel:WORD_0
	v_exp_f16_sdwa v117, v113 dst_sel:WORD_0 dst_unused:UNUSED_PAD src0_sel:WORD_0
	v_exp_f16_sdwa v114, v110 dst_sel:WORD_1 dst_unused:UNUSED_PRESERVE src0_sel:WORD_1
	v_exp_f16_sdwa v115, v111 dst_sel:WORD_1 dst_unused:UNUSED_PRESERVE src0_sel:WORD_1
	v_exp_f16_sdwa v116, v112 dst_sel:WORD_1 dst_unused:UNUSED_PRESERVE src0_sel:WORD_1
	v_exp_f16_sdwa v117, v113 dst_sel:WORD_1 dst_unused:UNUSED_PRESERVE src0_sel:WORD_1
	v_pk_add_f16 v101, v101, v114
	v_pk_add_f16 v100, v100, v115
	v_rcp_f16_e32 v110, v101
	v_rcp_f16_sdwa v101, v101 dst_sel:DWORD dst_unused:UNUSED_PAD src0_sel:WORD_1
	v_pk_add_f16 v99, v99, v116
	v_rcp_f16_e32 v111, v100
	v_rcp_f16_sdwa v100, v100 dst_sel:DWORD dst_unused:UNUSED_PAD src0_sel:WORD_1
	v_pk_add_f16 v98, v98, v117
	v_rcp_f16_e32 v112, v99
	v_rcp_f16_sdwa v99, v99 dst_sel:DWORD dst_unused:UNUSED_PAD src0_sel:WORD_1
	v_rcp_f16_e32 v113, v98
	v_rcp_f16_sdwa v98, v98 dst_sel:DWORD dst_unused:UNUSED_PAD src0_sel:WORD_1
	v_pk_fma_f16 v70, v46, v114, v70
	v_pack_b32_f16 v101, v110, v101
	v_pk_fma_f16 v71, v47, v115, v71
	v_pk_mul_f16 v110, v70, v101
	v_pack_b32_f16 v70, v111, v100
	v_pk_fma_f16 v72, v48, v116, v72
	v_pk_mul_f16 v111, v71, v70
	v_pack_b32_f16 v70, v112, v99
	v_pk_fma_f16 v73, v49, v117, v73
	v_pk_mul_f16 v112, v72, v70
	v_pack_b32_f16 v70, v113, v98
	v_pk_mul_f16 v113, v73, v70
	s_waitcnt vmcnt(12)
	v_pk_mul_f16 v73, v185, v157 op_sel_hi:[0,1]
	v_pk_mul_f16 v101, v183, v157 op_sel_hi:[0,1]
	v_pk_mul_f16 v117, v184, v157 op_sel_hi:[0,1]
	v_pk_mul_f16 v70, v185, v154 op_sel_hi:[0,1]
	v_pk_mul_f16 v71, v185, v155 op_sel_hi:[0,1]
	v_pk_mul_f16 v72, v185, v156 op_sel_hi:[0,1]
	v_pk_mul_f16 v98, v183, v154 op_sel_hi:[0,1]
	v_pk_mul_f16 v99, v183, v155 op_sel_hi:[0,1]
	v_pk_mul_f16 v100, v183, v156 op_sel_hi:[0,1]
	v_pk_mul_f16 v114, v184, v154 op_sel_hi:[0,1]
	v_pk_mul_f16 v115, v184, v155 op_sel_hi:[0,1]
	v_pk_mul_f16 v116, v184, v156 op_sel_hi:[0,1]
	v_pk_fma_f16 v85, v85, v157, v73
	v_pk_fma_f16 v109, v109, v157, v101
	v_pk_fma_f16 v125, v125, v157, v117
	v_pk_fma_f16 v126, v53, v157, v73
	v_pk_fma_f16 v134, v69, v157, v101
	v_pk_fma_f16 v186, v97, v157, v117
	v_pk_fma_f16 v73, v21, v157, v73
	v_pk_fma_f16 v101, v37, v157, v101
	v_pk_fma_f16 v117, v57, v157, v117
	v_pk_maximum3_f16 v157, v85, v109, v125
	v_pk_fma_f16 v84, v84, v156, v72
	v_pk_fma_f16 v83, v83, v155, v71
	v_pk_fma_f16 v82, v82, v154, v70
	v_pk_fma_f16 v108, v108, v156, v100
	v_pk_fma_f16 v107, v107, v155, v99
	v_pk_fma_f16 v106, v106, v154, v98
	v_pk_fma_f16 v124, v124, v156, v116
	v_pk_fma_f16 v123, v123, v155, v115
	v_pk_fma_f16 v122, v122, v154, v114
	v_pk_fma_f16 v127, v52, v156, v72
	v_pk_fma_f16 v128, v51, v155, v71
	v_pk_fma_f16 v129, v50, v154, v70
	v_pk_fma_f16 v135, v68, v156, v100
	v_pk_fma_f16 v136, v67, v155, v99
	v_pk_fma_f16 v137, v66, v154, v98
	v_pk_fma_f16 v187, v96, v156, v116
	v_pk_fma_f16 v188, v95, v155, v115
	v_pk_fma_f16 v189, v94, v154, v114
	v_pk_fma_f16 v72, v20, v156, v72
	v_pk_fma_f16 v71, v19, v155, v71
	v_pk_fma_f16 v70, v18, v154, v70
	v_pk_fma_f16 v100, v36, v156, v100
	v_pk_fma_f16 v99, v35, v155, v99
	v_pk_fma_f16 v98, v34, v154, v98
	v_pk_fma_f16 v116, v56, v156, v116
	v_pk_fma_f16 v115, v55, v155, v115
	v_pk_fma_f16 v114, v54, v154, v114
	v_pk_maximum3_f16 v154, v82, v106, v122
	v_pk_maximum3_f16 v155, v83, v107, v123
	v_pk_maximum3_f16 v156, v84, v108, v124
	v_pk_maximum3_f16 v193, v126, v134, v186
	v_pk_maximum3_f16 v197, v73, v101, v117
	v_pk_maximum3_f16 v190, v129, v137, v189
	v_pk_maximum3_f16 v191, v128, v136, v188
	v_pk_maximum3_f16 v192, v127, v135, v187
	v_pk_maximum3_f16 v194, v70, v98, v114
	v_pk_maximum3_f16 v195, v71, v99, v115
	v_pk_maximum3_f16 v157, v157, v193, v197
	v_pk_maximum3_f16 v196, v72, v100, v116
	v_pk_maximum3_f16 v154, v154, v190, v194
	v_pk_maximum3_f16 v155, v155, v191, v195
	v_pk_maximum3_f16 v156, v156, v192, v196
	v_pk_add_f16 v85, v85, v157 neg_lo:[0,1] neg_hi:[0,1]
	v_pk_add_f16 v82, v82, v154 neg_lo:[0,1] neg_hi:[0,1]
	v_pk_add_f16 v83, v83, v155 neg_lo:[0,1] neg_hi:[0,1]
	v_pk_add_f16 v84, v84, v156 neg_lo:[0,1] neg_hi:[0,1]
	v_pk_add_f16 v106, v106, v154 neg_lo:[0,1] neg_hi:[0,1]
	v_exp_f16_sdwa v190, v82 dst_sel:WORD_0 dst_unused:UNUSED_PAD src0_sel:WORD_0
	v_exp_f16_sdwa v191, v83 dst_sel:WORD_0 dst_unused:UNUSED_PAD src0_sel:WORD_0
	v_exp_f16_sdwa v192, v84 dst_sel:WORD_0 dst_unused:UNUSED_PAD src0_sel:WORD_0
	v_exp_f16_sdwa v193, v85 dst_sel:WORD_0 dst_unused:UNUSED_PAD src0_sel:WORD_0
	v_exp_f16_sdwa v190, v82 dst_sel:WORD_1 dst_unused:UNUSED_PRESERVE src0_sel:WORD_1
	v_exp_f16_sdwa v191, v83 dst_sel:WORD_1 dst_unused:UNUSED_PRESERVE src0_sel:WORD_1
	v_exp_f16_sdwa v192, v84 dst_sel:WORD_1 dst_unused:UNUSED_PRESERVE src0_sel:WORD_1
	v_exp_f16_sdwa v193, v85 dst_sel:WORD_1 dst_unused:UNUSED_PRESERVE src0_sel:WORD_1
	v_pk_add_f16 v107, v107, v155 neg_lo:[0,1] neg_hi:[0,1]
	v_pk_add_f16 v85, v190, 0
	v_pk_fma_f16 v45, v45, v193, 0
	v_pk_add_f16 v82, v193, 0
	v_pk_add_f16 v83, v192, 0
	v_pk_add_f16 v84, v191, 0
	v_pk_fma_f16 v44, v44, v192, 0
	v_pk_fma_f16 v43, v43, v191, 0
	v_pk_fma_f16 v42, v42, v190, 0
	v_pk_add_f16 v108, v108, v156 neg_lo:[0,1] neg_hi:[0,1]
	v_pk_add_f16 v109, v109, v157 neg_lo:[0,1] neg_hi:[0,1]
	v_pk_add_f16 v70, v70, v154 neg_lo:[0,1] neg_hi:[0,1]
	v_exp_f16_sdwa v190, v106 dst_sel:WORD_0 dst_unused:UNUSED_PAD src0_sel:WORD_0
	v_exp_f16_sdwa v191, v107 dst_sel:WORD_0 dst_unused:UNUSED_PAD src0_sel:WORD_0
	v_exp_f16_sdwa v192, v108 dst_sel:WORD_0 dst_unused:UNUSED_PAD src0_sel:WORD_0
	v_exp_f16_sdwa v193, v109 dst_sel:WORD_0 dst_unused:UNUSED_PAD src0_sel:WORD_0
	v_exp_f16_sdwa v190, v106 dst_sel:WORD_1 dst_unused:UNUSED_PRESERVE src0_sel:WORD_1
	v_exp_f16_sdwa v191, v107 dst_sel:WORD_1 dst_unused:UNUSED_PRESERVE src0_sel:WORD_1
	v_exp_f16_sdwa v192, v108 dst_sel:WORD_1 dst_unused:UNUSED_PRESERVE src0_sel:WORD_1
	v_exp_f16_sdwa v193, v109 dst_sel:WORD_1 dst_unused:UNUSED_PRESERVE src0_sel:WORD_1
	v_pk_add_f16 v71, v71, v155 neg_lo:[0,1] neg_hi:[0,1]
	v_pk_add_f16 v85, v85, v190
	v_pk_fma_f16 v45, v65, v193, v45
	v_pk_add_f16 v65, v125, v157 neg_lo:[0,1] neg_hi:[0,1]
	v_pk_add_f16 v84, v84, v191
	v_pk_add_f16 v83, v83, v192
	v_pk_add_f16 v82, v82, v193
	v_pk_fma_f16 v42, v62, v190, v42
	v_pk_fma_f16 v43, v63, v191, v43
	v_pk_fma_f16 v44, v64, v192, v44
	v_pk_add_f16 v62, v122, v154 neg_lo:[0,1] neg_hi:[0,1]
	v_pk_add_f16 v63, v123, v155 neg_lo:[0,1] neg_hi:[0,1]
	v_pk_add_f16 v64, v124, v156 neg_lo:[0,1] neg_hi:[0,1]
	v_pk_add_f16 v72, v72, v156 neg_lo:[0,1] neg_hi:[0,1]
	v_exp_f16_sdwa v106, v62 dst_sel:WORD_0 dst_unused:UNUSED_PAD src0_sel:WORD_0
	v_exp_f16_sdwa v107, v63 dst_sel:WORD_0 dst_unused:UNUSED_PAD src0_sel:WORD_0
	v_exp_f16_sdwa v108, v64 dst_sel:WORD_0 dst_unused:UNUSED_PAD src0_sel:WORD_0
	v_exp_f16_sdwa v109, v65 dst_sel:WORD_0 dst_unused:UNUSED_PAD src0_sel:WORD_0
	v_exp_f16_sdwa v106, v62 dst_sel:WORD_1 dst_unused:UNUSED_PRESERVE src0_sel:WORD_1
	v_exp_f16_sdwa v107, v63 dst_sel:WORD_1 dst_unused:UNUSED_PRESERVE src0_sel:WORD_1
	v_exp_f16_sdwa v108, v64 dst_sel:WORD_1 dst_unused:UNUSED_PRESERVE src0_sel:WORD_1
	v_exp_f16_sdwa v109, v65 dst_sel:WORD_1 dst_unused:UNUSED_PRESERVE src0_sel:WORD_1
	v_pk_add_f16 v73, v73, v157 neg_lo:[0,1] neg_hi:[0,1]
	v_pk_add_f16 v65, v85, v106
	v_pk_add_f16 v62, v82, v109
	v_pk_add_f16 v63, v83, v108
	v_pk_add_f16 v64, v84, v107
	v_pk_fma_f16 v45, v89, v109, v45
	v_pk_fma_f16 v44, v88, v108, v44
	v_pk_fma_f16 v43, v87, v107, v43
	v_pk_fma_f16 v42, v86, v106, v42
	v_pk_add_f16 v82, v129, v154 neg_lo:[0,1] neg_hi:[0,1]
	v_pk_add_f16 v83, v128, v155 neg_lo:[0,1] neg_hi:[0,1]
	v_pk_add_f16 v84, v127, v156 neg_lo:[0,1] neg_hi:[0,1]
	v_pk_add_f16 v85, v126, v157 neg_lo:[0,1] neg_hi:[0,1]
	v_exp_f16_sdwa v86, v82 dst_sel:WORD_0 dst_unused:UNUSED_PAD src0_sel:WORD_0
	v_exp_f16_sdwa v87, v83 dst_sel:WORD_0 dst_unused:UNUSED_PAD src0_sel:WORD_0
	v_exp_f16_sdwa v88, v84 dst_sel:WORD_0 dst_unused:UNUSED_PAD src0_sel:WORD_0
	v_exp_f16_sdwa v89, v85 dst_sel:WORD_0 dst_unused:UNUSED_PAD src0_sel:WORD_0
	v_exp_f16_sdwa v86, v82 dst_sel:WORD_1 dst_unused:UNUSED_PRESERVE src0_sel:WORD_1
	v_exp_f16_sdwa v87, v83 dst_sel:WORD_1 dst_unused:UNUSED_PRESERVE src0_sel:WORD_1
	v_exp_f16_sdwa v88, v84 dst_sel:WORD_1 dst_unused:UNUSED_PRESERVE src0_sel:WORD_1
	v_exp_f16_sdwa v89, v85 dst_sel:WORD_1 dst_unused:UNUSED_PRESERVE src0_sel:WORD_1
	v_pk_add_f16 v82, v137, v154 neg_lo:[0,1] neg_hi:[0,1]
	v_pk_add_f16 v65, v65, v86
	v_pk_add_f16 v64, v64, v87
	v_pk_add_f16 v63, v63, v88
	v_pk_add_f16 v62, v62, v89
	v_pk_fma_f16 v42, v22, v86, v42
	v_pk_fma_f16 v43, v23, v87, v43
	v_pk_fma_f16 v44, v24, v88, v44
	v_pk_fma_f16 v45, v25, v89, v45
	v_pk_add_f16 v83, v136, v155 neg_lo:[0,1] neg_hi:[0,1]
	v_pk_add_f16 v84, v135, v156 neg_lo:[0,1] neg_hi:[0,1]
	v_pk_add_f16 v85, v134, v157 neg_lo:[0,1] neg_hi:[0,1]
	v_exp_f16_sdwa v86, v82 dst_sel:WORD_0 dst_unused:UNUSED_PAD src0_sel:WORD_0
	v_exp_f16_sdwa v87, v83 dst_sel:WORD_0 dst_unused:UNUSED_PAD src0_sel:WORD_0
	v_exp_f16_sdwa v88, v84 dst_sel:WORD_0 dst_unused:UNUSED_PAD src0_sel:WORD_0
	v_exp_f16_sdwa v89, v85 dst_sel:WORD_0 dst_unused:UNUSED_PAD src0_sel:WORD_0
	v_exp_f16_sdwa v86, v82 dst_sel:WORD_1 dst_unused:UNUSED_PRESERVE src0_sel:WORD_1
	v_exp_f16_sdwa v87, v83 dst_sel:WORD_1 dst_unused:UNUSED_PRESERVE src0_sel:WORD_1
	v_exp_f16_sdwa v88, v84 dst_sel:WORD_1 dst_unused:UNUSED_PRESERVE src0_sel:WORD_1
	v_exp_f16_sdwa v89, v85 dst_sel:WORD_1 dst_unused:UNUSED_PRESERVE src0_sel:WORD_1
	v_pk_add_f16 v82, v189, v154 neg_lo:[0,1] neg_hi:[0,1]
	v_pk_add_f16 v65, v65, v86
	v_pk_add_f16 v62, v62, v89
	v_pk_add_f16 v63, v63, v88
	v_pk_add_f16 v64, v64, v87
	v_pk_fma_f16 v45, v33, v89, v45
	v_pk_fma_f16 v44, v32, v88, v44
	v_pk_fma_f16 v43, v31, v87, v43
	v_pk_fma_f16 v42, v30, v86, v42
	v_pk_add_f16 v83, v188, v155 neg_lo:[0,1] neg_hi:[0,1]
	v_pk_add_f16 v84, v187, v156 neg_lo:[0,1] neg_hi:[0,1]
	v_pk_add_f16 v85, v186, v157 neg_lo:[0,1] neg_hi:[0,1]
	v_exp_f16_sdwa v86, v82 dst_sel:WORD_0 dst_unused:UNUSED_PAD src0_sel:WORD_0
	v_exp_f16_sdwa v87, v83 dst_sel:WORD_0 dst_unused:UNUSED_PAD src0_sel:WORD_0
	v_exp_f16_sdwa v88, v84 dst_sel:WORD_0 dst_unused:UNUSED_PAD src0_sel:WORD_0
	v_exp_f16_sdwa v89, v85 dst_sel:WORD_0 dst_unused:UNUSED_PAD src0_sel:WORD_0
	v_exp_f16_sdwa v86, v82 dst_sel:WORD_1 dst_unused:UNUSED_PRESERVE src0_sel:WORD_1
	v_exp_f16_sdwa v87, v83 dst_sel:WORD_1 dst_unused:UNUSED_PRESERVE src0_sel:WORD_1
	v_exp_f16_sdwa v88, v84 dst_sel:WORD_1 dst_unused:UNUSED_PRESERVE src0_sel:WORD_1
	v_exp_f16_sdwa v89, v85 dst_sel:WORD_1 dst_unused:UNUSED_PRESERVE src0_sel:WORD_1
	v_exp_f16_sdwa v82, v70 dst_sel:WORD_0 dst_unused:UNUSED_PAD src0_sel:WORD_0
	v_exp_f16_sdwa v83, v71 dst_sel:WORD_0 dst_unused:UNUSED_PAD src0_sel:WORD_0
	v_exp_f16_sdwa v84, v72 dst_sel:WORD_0 dst_unused:UNUSED_PAD src0_sel:WORD_0
	v_exp_f16_sdwa v85, v73 dst_sel:WORD_0 dst_unused:UNUSED_PAD src0_sel:WORD_0
	v_exp_f16_sdwa v82, v70 dst_sel:WORD_1 dst_unused:UNUSED_PRESERVE src0_sel:WORD_1
	v_exp_f16_sdwa v83, v71 dst_sel:WORD_1 dst_unused:UNUSED_PRESERVE src0_sel:WORD_1
	v_exp_f16_sdwa v84, v72 dst_sel:WORD_1 dst_unused:UNUSED_PRESERVE src0_sel:WORD_1
	v_exp_f16_sdwa v85, v73 dst_sel:WORD_1 dst_unused:UNUSED_PRESERVE src0_sel:WORD_1
	v_pk_add_f16 v70, v98, v154 neg_lo:[0,1] neg_hi:[0,1]
	v_pk_add_f16 v65, v65, v86
	v_pk_add_f16 v64, v64, v87
	v_pk_add_f16 v63, v63, v88
	v_pk_add_f16 v62, v62, v89
	v_pk_fma_f16 v42, v46, v86, v42
	v_pk_fma_f16 v43, v47, v87, v43
	v_pk_fma_f16 v44, v48, v88, v44
	v_pk_fma_f16 v45, v49, v89, v45
	v_pk_add_f16 v65, v65, v82
	v_pk_add_f16 v62, v62, v85
	v_pk_add_f16 v63, v63, v84
	v_pk_add_f16 v64, v64, v83
	v_pk_fma_f16 v45, v9, v85, v45
	v_pk_fma_f16 v44, v8, v84, v44
	v_pk_fma_f16 v43, v7, v83, v43
	v_pk_fma_f16 v42, v6, v82, v42
	v_pk_add_f16 v71, v99, v155 neg_lo:[0,1] neg_hi:[0,1]
	v_pk_add_f16 v72, v100, v156 neg_lo:[0,1] neg_hi:[0,1]
	v_pk_add_f16 v73, v101, v157 neg_lo:[0,1] neg_hi:[0,1]
	v_exp_f16_sdwa v82, v70 dst_sel:WORD_0 dst_unused:UNUSED_PAD src0_sel:WORD_0
	v_exp_f16_sdwa v83, v71 dst_sel:WORD_0 dst_unused:UNUSED_PAD src0_sel:WORD_0
	v_exp_f16_sdwa v84, v72 dst_sel:WORD_0 dst_unused:UNUSED_PAD src0_sel:WORD_0
	v_exp_f16_sdwa v85, v73 dst_sel:WORD_0 dst_unused:UNUSED_PAD src0_sel:WORD_0
	v_exp_f16_sdwa v82, v70 dst_sel:WORD_1 dst_unused:UNUSED_PRESERVE src0_sel:WORD_1
	v_exp_f16_sdwa v83, v71 dst_sel:WORD_1 dst_unused:UNUSED_PRESERVE src0_sel:WORD_1
	v_exp_f16_sdwa v84, v72 dst_sel:WORD_1 dst_unused:UNUSED_PRESERVE src0_sel:WORD_1
	v_exp_f16_sdwa v85, v73 dst_sel:WORD_1 dst_unused:UNUSED_PRESERVE src0_sel:WORD_1
	v_pk_add_f16 v70, v114, v154 neg_lo:[0,1] neg_hi:[0,1]
	v_pk_add_f16 v65, v65, v82
	v_pk_add_f16 v64, v64, v83
	v_pk_add_f16 v63, v63, v84
	v_pk_add_f16 v62, v62, v85
	v_pk_fma_f16 v42, v10, v82, v42
	v_pk_fma_f16 v43, v11, v83, v43
	v_pk_fma_f16 v44, v12, v84, v44
	v_pk_fma_f16 v45, v13, v85, v45
	v_pk_add_f16 v71, v115, v155 neg_lo:[0,1] neg_hi:[0,1]
	v_pk_add_f16 v72, v116, v156 neg_lo:[0,1] neg_hi:[0,1]
	v_pk_add_f16 v73, v117, v157 neg_lo:[0,1] neg_hi:[0,1]
	v_exp_f16_sdwa v82, v70 dst_sel:WORD_0 dst_unused:UNUSED_PAD src0_sel:WORD_0
	v_exp_f16_sdwa v83, v71 dst_sel:WORD_0 dst_unused:UNUSED_PAD src0_sel:WORD_0
	v_exp_f16_sdwa v84, v72 dst_sel:WORD_0 dst_unused:UNUSED_PAD src0_sel:WORD_0
	v_exp_f16_sdwa v85, v73 dst_sel:WORD_0 dst_unused:UNUSED_PAD src0_sel:WORD_0
	v_exp_f16_sdwa v82, v70 dst_sel:WORD_1 dst_unused:UNUSED_PRESERVE src0_sel:WORD_1
	v_exp_f16_sdwa v83, v71 dst_sel:WORD_1 dst_unused:UNUSED_PRESERVE src0_sel:WORD_1
	v_exp_f16_sdwa v84, v72 dst_sel:WORD_1 dst_unused:UNUSED_PRESERVE src0_sel:WORD_1
	v_exp_f16_sdwa v85, v73 dst_sel:WORD_1 dst_unused:UNUSED_PRESERVE src0_sel:WORD_1
	v_pk_add_f16 v65, v65, v82
	v_pk_add_f16 v64, v64, v83
	v_rcp_f16_e32 v70, v65
	v_rcp_f16_sdwa v65, v65 dst_sel:DWORD dst_unused:UNUSED_PAD src0_sel:WORD_1
	v_pk_add_f16 v63, v63, v84
	v_rcp_f16_e32 v71, v64
	v_rcp_f16_sdwa v64, v64 dst_sel:DWORD dst_unused:UNUSED_PAD src0_sel:WORD_1
	v_pk_add_f16 v62, v62, v85
	v_rcp_f16_e32 v72, v63
	v_rcp_f16_sdwa v73, v63 dst_sel:DWORD dst_unused:UNUSED_PAD src0_sel:WORD_1
	v_pk_fma_f16 v43, v15, v83, v43
	v_pk_fma_f16 v42, v14, v82, v42
	v_rcp_f16_e32 v82, v62
	v_rcp_f16_sdwa v83, v62 dst_sel:DWORD dst_unused:UNUSED_PAD src0_sel:WORD_1
	v_pack_b32_f16 v62, v70, v65
	v_pk_mul_f16 v62, v42, v62
	v_pack_b32_f16 v42, v71, v64
	v_pk_fma_f16 v44, v16, v84, v44
	v_pk_mul_f16 v63, v43, v42
	v_pack_b32_f16 v42, v72, v73
	v_pk_fma_f16 v45, v17, v85, v45
	v_pk_mul_f16 v64, v44, v42
	v_pack_b32_f16 v42, v82, v83
	v_pk_mul_f16 v65, v45, v42
	s_waitcnt vmcnt(6)
	v_pk_mul_f16 v42, v185, v150 op_sel_hi:[0,1]
	v_pk_mul_f16 v70, v183, v150 op_sel_hi:[0,1]
	v_pk_mul_f16 v82, v184, v150 op_sel_hi:[0,1]
	v_pk_mul_f16 v43, v185, v151 op_sel_hi:[0,1]
	v_pk_mul_f16 v44, v185, v152 op_sel_hi:[0,1]
	v_pk_mul_f16 v45, v185, v153 op_sel_hi:[0,1]
	v_pk_mul_f16 v71, v183, v151 op_sel_hi:[0,1]
	v_pk_mul_f16 v72, v183, v152 op_sel_hi:[0,1]
	v_pk_mul_f16 v73, v183, v153 op_sel_hi:[0,1]
	v_pk_mul_f16 v83, v184, v151 op_sel_hi:[0,1]
	v_pk_mul_f16 v84, v184, v152 op_sel_hi:[0,1]
	v_pk_mul_f16 v85, v184, v153 op_sel_hi:[0,1]
	v_pk_fma_f16 v50, v50, v150, v42
	v_pk_fma_f16 v66, v66, v150, v70
	v_pk_fma_f16 v89, v94, v150, v82
	v_pk_fma_f16 v53, v53, v153, v45
	v_pk_maximum3_f16 v114, v50, v66, v89
	v_pk_fma_f16 v52, v52, v152, v44
	v_pk_fma_f16 v51, v51, v151, v43
	v_pk_fma_f16 v69, v69, v153, v73
	v_pk_fma_f16 v68, v68, v152, v72
	v_pk_fma_f16 v67, v67, v151, v71
	v_pk_fma_f16 v86, v97, v153, v85
	v_pk_fma_f16 v87, v96, v152, v84
	v_pk_fma_f16 v88, v95, v151, v83
	v_pk_fma_f16 v97, v18, v150, v42
	v_pk_fma_f16 v101, v34, v150, v70
	v_pk_fma_f16 v109, v54, v150, v82
	v_pk_fma_f16 v42, v74, v150, v42
	v_pk_fma_f16 v70, v102, v150, v70
	v_pk_fma_f16 v82, v118, v150, v82
	v_pk_maximum3_f16 v115, v51, v67, v88
	v_pk_maximum3_f16 v116, v52, v68, v87
	v_pk_maximum3_f16 v117, v53, v69, v86
	v_pk_maximum3_f16 v122, v97, v101, v109
	v_pk_fma_f16 v94, v21, v153, v45
	v_pk_maximum3_f16 v126, v42, v70, v82
	v_pk_fma_f16 v95, v20, v152, v44
	v_pk_maximum3_f16 v114, v114, v122, v126
	v_pk_fma_f16 v96, v19, v151, v43
	v_pk_fma_f16 v98, v37, v153, v73
	v_pk_fma_f16 v99, v36, v152, v72
	v_pk_fma_f16 v100, v35, v151, v71
	v_pk_fma_f16 v106, v57, v153, v85
	v_pk_fma_f16 v107, v56, v152, v84
	v_pk_fma_f16 v108, v55, v151, v83
	v_pk_fma_f16 v45, v77, v153, v45
	v_pk_fma_f16 v44, v76, v152, v44
	v_pk_fma_f16 v43, v75, v151, v43
	v_pk_fma_f16 v73, v105, v153, v73
	v_pk_fma_f16 v72, v104, v152, v72
	v_pk_fma_f16 v71, v103, v151, v71
	v_pk_fma_f16 v85, v121, v153, v85
	v_pk_fma_f16 v84, v120, v152, v84
	v_pk_fma_f16 v83, v119, v151, v83
	v_pk_maximum3_f16 v123, v96, v100, v108
	v_pk_maximum3_f16 v124, v95, v99, v107
	v_pk_maximum3_f16 v125, v94, v98, v106
	v_pk_maximum3_f16 v128, v44, v72, v84
	v_pk_maximum3_f16 v129, v45, v73, v85
	v_pk_maximum3_f16 v127, v43, v71, v83
	v_pk_maximum3_f16 v115, v115, v123, v127
	v_pk_maximum3_f16 v116, v116, v124, v128
	v_pk_maximum3_f16 v117, v117, v125, v129
	v_pk_add_f16 v50, v50, v114 neg_lo:[0,1] neg_hi:[0,1]
	v_pk_add_f16 v51, v51, v115 neg_lo:[0,1] neg_hi:[0,1]
	v_pk_add_f16 v52, v52, v116 neg_lo:[0,1] neg_hi:[0,1]
	v_pk_add_f16 v53, v53, v117 neg_lo:[0,1] neg_hi:[0,1]
	v_pk_add_f16 v66, v66, v114 neg_lo:[0,1] neg_hi:[0,1]
	v_exp_f16_sdwa v122, v50 dst_sel:WORD_0 dst_unused:UNUSED_PAD src0_sel:WORD_0
	v_exp_f16_sdwa v123, v51 dst_sel:WORD_0 dst_unused:UNUSED_PAD src0_sel:WORD_0
	v_exp_f16_sdwa v124, v52 dst_sel:WORD_0 dst_unused:UNUSED_PAD src0_sel:WORD_0
	v_exp_f16_sdwa v125, v53 dst_sel:WORD_0 dst_unused:UNUSED_PAD src0_sel:WORD_0
	v_exp_f16_sdwa v122, v50 dst_sel:WORD_1 dst_unused:UNUSED_PRESERVE src0_sel:WORD_1
	v_exp_f16_sdwa v123, v51 dst_sel:WORD_1 dst_unused:UNUSED_PRESERVE src0_sel:WORD_1
	v_exp_f16_sdwa v124, v52 dst_sel:WORD_1 dst_unused:UNUSED_PRESERVE src0_sel:WORD_1
	v_exp_f16_sdwa v125, v53 dst_sel:WORD_1 dst_unused:UNUSED_PRESERVE src0_sel:WORD_1
	v_pk_add_f16 v67, v67, v115 neg_lo:[0,1] neg_hi:[0,1]
	v_pk_add_f16 v50, v125, 0
	v_pk_fma_f16 v22, v22, v122, 0
	v_pk_add_f16 v51, v124, 0
	v_pk_add_f16 v52, v123, 0
	v_pk_add_f16 v53, v122, 0
	v_pk_fma_f16 v23, v23, v123, 0
	v_pk_fma_f16 v24, v24, v124, 0
	v_pk_fma_f16 v25, v25, v125, 0
	v_pk_add_f16 v68, v68, v116 neg_lo:[0,1] neg_hi:[0,1]
	v_pk_add_f16 v69, v69, v117 neg_lo:[0,1] neg_hi:[0,1]
	v_pk_add_f16 v42, v42, v114 neg_lo:[0,1] neg_hi:[0,1]
	v_exp_f16_sdwa v122, v66 dst_sel:WORD_0 dst_unused:UNUSED_PAD src0_sel:WORD_0
	v_exp_f16_sdwa v123, v67 dst_sel:WORD_0 dst_unused:UNUSED_PAD src0_sel:WORD_0
	v_exp_f16_sdwa v124, v68 dst_sel:WORD_0 dst_unused:UNUSED_PAD src0_sel:WORD_0
	v_exp_f16_sdwa v125, v69 dst_sel:WORD_0 dst_unused:UNUSED_PAD src0_sel:WORD_0
	v_exp_f16_sdwa v122, v66 dst_sel:WORD_1 dst_unused:UNUSED_PRESERVE src0_sel:WORD_1
	v_exp_f16_sdwa v123, v67 dst_sel:WORD_1 dst_unused:UNUSED_PRESERVE src0_sel:WORD_1
	v_exp_f16_sdwa v124, v68 dst_sel:WORD_1 dst_unused:UNUSED_PRESERVE src0_sel:WORD_1
	v_exp_f16_sdwa v125, v69 dst_sel:WORD_1 dst_unused:UNUSED_PRESERVE src0_sel:WORD_1
	v_pk_add_f16 v43, v43, v115 neg_lo:[0,1] neg_hi:[0,1]
	v_pk_add_f16 v50, v50, v125
	v_pk_fma_f16 v22, v30, v122, v22
	v_pk_add_f16 v30, v89, v114 neg_lo:[0,1] neg_hi:[0,1]
	v_pk_add_f16 v53, v53, v122
	v_pk_add_f16 v52, v52, v123
	v_pk_add_f16 v51, v51, v124
	v_pk_fma_f16 v25, v33, v125, v25
	v_pk_fma_f16 v24, v32, v124, v24
	v_pk_fma_f16 v23, v31, v123, v23
	v_pk_add_f16 v31, v88, v115 neg_lo:[0,1] neg_hi:[0,1]
	v_pk_add_f16 v32, v87, v116 neg_lo:[0,1] neg_hi:[0,1]
	v_pk_add_f16 v33, v86, v117 neg_lo:[0,1] neg_hi:[0,1]
	v_pk_add_f16 v44, v44, v116 neg_lo:[0,1] neg_hi:[0,1]
	v_exp_f16_sdwa v66, v30 dst_sel:WORD_0 dst_unused:UNUSED_PAD src0_sel:WORD_0
	v_exp_f16_sdwa v67, v31 dst_sel:WORD_0 dst_unused:UNUSED_PAD src0_sel:WORD_0
	v_exp_f16_sdwa v68, v32 dst_sel:WORD_0 dst_unused:UNUSED_PAD src0_sel:WORD_0
	v_exp_f16_sdwa v69, v33 dst_sel:WORD_0 dst_unused:UNUSED_PAD src0_sel:WORD_0
	v_exp_f16_sdwa v66, v30 dst_sel:WORD_1 dst_unused:UNUSED_PRESERVE src0_sel:WORD_1
	v_exp_f16_sdwa v67, v31 dst_sel:WORD_1 dst_unused:UNUSED_PRESERVE src0_sel:WORD_1
	v_exp_f16_sdwa v68, v32 dst_sel:WORD_1 dst_unused:UNUSED_PRESERVE src0_sel:WORD_1
	v_exp_f16_sdwa v69, v33 dst_sel:WORD_1 dst_unused:UNUSED_PRESERVE src0_sel:WORD_1
	v_pk_add_f16 v45, v45, v117 neg_lo:[0,1] neg_hi:[0,1]
	v_pk_add_f16 v30, v50, v69
	v_pk_add_f16 v31, v51, v68
	v_pk_add_f16 v32, v52, v67
	v_pk_add_f16 v33, v53, v66
	v_pk_fma_f16 v22, v46, v66, v22
	v_pk_fma_f16 v23, v47, v67, v23
	v_pk_fma_f16 v24, v48, v68, v24
	v_pk_fma_f16 v25, v49, v69, v25
	v_pk_add_f16 v46, v97, v114 neg_lo:[0,1] neg_hi:[0,1]
	v_pk_add_f16 v47, v96, v115 neg_lo:[0,1] neg_hi:[0,1]
	v_pk_add_f16 v48, v95, v116 neg_lo:[0,1] neg_hi:[0,1]
	v_pk_add_f16 v49, v94, v117 neg_lo:[0,1] neg_hi:[0,1]
	v_exp_f16_sdwa v50, v46 dst_sel:WORD_0 dst_unused:UNUSED_PAD src0_sel:WORD_0
	v_exp_f16_sdwa v51, v47 dst_sel:WORD_0 dst_unused:UNUSED_PAD src0_sel:WORD_0
	v_exp_f16_sdwa v52, v48 dst_sel:WORD_0 dst_unused:UNUSED_PAD src0_sel:WORD_0
	v_exp_f16_sdwa v53, v49 dst_sel:WORD_0 dst_unused:UNUSED_PAD src0_sel:WORD_0
	v_exp_f16_sdwa v50, v46 dst_sel:WORD_1 dst_unused:UNUSED_PRESERVE src0_sel:WORD_1
	v_exp_f16_sdwa v51, v47 dst_sel:WORD_1 dst_unused:UNUSED_PRESERVE src0_sel:WORD_1
	v_exp_f16_sdwa v52, v48 dst_sel:WORD_1 dst_unused:UNUSED_PRESERVE src0_sel:WORD_1
	v_exp_f16_sdwa v53, v49 dst_sel:WORD_1 dst_unused:UNUSED_PRESERVE src0_sel:WORD_1
	v_pk_add_f16 v46, v101, v114 neg_lo:[0,1] neg_hi:[0,1]
	v_pk_add_f16 v30, v30, v53
	v_pk_add_f16 v33, v33, v50
	v_pk_add_f16 v32, v32, v51
	v_pk_add_f16 v31, v31, v52
	v_pk_fma_f16 v25, v9, v53, v25
	v_pk_fma_f16 v24, v8, v52, v24
	v_pk_fma_f16 v23, v7, v51, v23
	v_pk_fma_f16 v22, v6, v50, v22
	v_pk_add_f16 v47, v100, v115 neg_lo:[0,1] neg_hi:[0,1]
	v_pk_add_f16 v48, v99, v116 neg_lo:[0,1] neg_hi:[0,1]
	v_pk_add_f16 v49, v98, v117 neg_lo:[0,1] neg_hi:[0,1]
	v_exp_f16_sdwa v50, v46 dst_sel:WORD_0 dst_unused:UNUSED_PAD src0_sel:WORD_0
	v_exp_f16_sdwa v51, v47 dst_sel:WORD_0 dst_unused:UNUSED_PAD src0_sel:WORD_0
	v_exp_f16_sdwa v52, v48 dst_sel:WORD_0 dst_unused:UNUSED_PAD src0_sel:WORD_0
	v_exp_f16_sdwa v53, v49 dst_sel:WORD_0 dst_unused:UNUSED_PAD src0_sel:WORD_0
	v_exp_f16_sdwa v50, v46 dst_sel:WORD_1 dst_unused:UNUSED_PRESERVE src0_sel:WORD_1
	v_exp_f16_sdwa v51, v47 dst_sel:WORD_1 dst_unused:UNUSED_PRESERVE src0_sel:WORD_1
	v_exp_f16_sdwa v52, v48 dst_sel:WORD_1 dst_unused:UNUSED_PRESERVE src0_sel:WORD_1
	v_exp_f16_sdwa v53, v49 dst_sel:WORD_1 dst_unused:UNUSED_PRESERVE src0_sel:WORD_1
	v_pk_add_f16 v46, v109, v114 neg_lo:[0,1] neg_hi:[0,1]
	v_pk_add_f16 v30, v30, v53
	v_pk_add_f16 v31, v31, v52
	v_pk_add_f16 v32, v32, v51
	v_pk_add_f16 v33, v33, v50
	v_pk_fma_f16 v22, v10, v50, v22
	v_pk_fma_f16 v23, v11, v51, v23
	v_pk_fma_f16 v24, v12, v52, v24
	v_pk_fma_f16 v25, v13, v53, v25
	v_pk_add_f16 v47, v108, v115 neg_lo:[0,1] neg_hi:[0,1]
	v_pk_add_f16 v48, v107, v116 neg_lo:[0,1] neg_hi:[0,1]
	v_pk_add_f16 v49, v106, v117 neg_lo:[0,1] neg_hi:[0,1]
	v_exp_f16_sdwa v50, v46 dst_sel:WORD_0 dst_unused:UNUSED_PAD src0_sel:WORD_0
	v_exp_f16_sdwa v51, v47 dst_sel:WORD_0 dst_unused:UNUSED_PAD src0_sel:WORD_0
	v_exp_f16_sdwa v52, v48 dst_sel:WORD_0 dst_unused:UNUSED_PAD src0_sel:WORD_0
	v_exp_f16_sdwa v53, v49 dst_sel:WORD_0 dst_unused:UNUSED_PAD src0_sel:WORD_0
	v_exp_f16_sdwa v50, v46 dst_sel:WORD_1 dst_unused:UNUSED_PRESERVE src0_sel:WORD_1
	v_exp_f16_sdwa v51, v47 dst_sel:WORD_1 dst_unused:UNUSED_PRESERVE src0_sel:WORD_1
	v_exp_f16_sdwa v52, v48 dst_sel:WORD_1 dst_unused:UNUSED_PRESERVE src0_sel:WORD_1
	v_exp_f16_sdwa v53, v49 dst_sel:WORD_1 dst_unused:UNUSED_PRESERVE src0_sel:WORD_1
	v_exp_f16_sdwa v46, v42 dst_sel:WORD_0 dst_unused:UNUSED_PAD src0_sel:WORD_0
	v_exp_f16_sdwa v47, v43 dst_sel:WORD_0 dst_unused:UNUSED_PAD src0_sel:WORD_0
	v_exp_f16_sdwa v48, v44 dst_sel:WORD_0 dst_unused:UNUSED_PAD src0_sel:WORD_0
	v_exp_f16_sdwa v49, v45 dst_sel:WORD_0 dst_unused:UNUSED_PAD src0_sel:WORD_0
	v_exp_f16_sdwa v46, v42 dst_sel:WORD_1 dst_unused:UNUSED_PRESERVE src0_sel:WORD_1
	v_exp_f16_sdwa v47, v43 dst_sel:WORD_1 dst_unused:UNUSED_PRESERVE src0_sel:WORD_1
	v_exp_f16_sdwa v48, v44 dst_sel:WORD_1 dst_unused:UNUSED_PRESERVE src0_sel:WORD_1
	v_exp_f16_sdwa v49, v45 dst_sel:WORD_1 dst_unused:UNUSED_PRESERVE src0_sel:WORD_1
	v_pk_add_f16 v42, v70, v114 neg_lo:[0,1] neg_hi:[0,1]
	v_pk_add_f16 v30, v30, v53
	v_pk_add_f16 v33, v33, v50
	v_pk_add_f16 v32, v32, v51
	v_pk_add_f16 v31, v31, v52
	v_pk_fma_f16 v25, v17, v53, v25
	v_pk_fma_f16 v24, v16, v52, v24
	v_pk_fma_f16 v23, v15, v51, v23
	v_pk_fma_f16 v22, v14, v50, v22
	v_pk_add_f16 v30, v30, v49
	v_pk_add_f16 v31, v31, v48
	v_pk_add_f16 v32, v32, v47
	v_pk_add_f16 v33, v33, v46
	v_pk_fma_f16 v22, v26, v46, v22
	v_pk_fma_f16 v23, v27, v47, v23
	v_pk_fma_f16 v24, v28, v48, v24
	v_pk_fma_f16 v25, v29, v49, v25
	v_pk_add_f16 v43, v71, v115 neg_lo:[0,1] neg_hi:[0,1]
	v_pk_add_f16 v44, v72, v116 neg_lo:[0,1] neg_hi:[0,1]
	v_pk_add_f16 v45, v73, v117 neg_lo:[0,1] neg_hi:[0,1]
	v_exp_f16_sdwa v46, v42 dst_sel:WORD_0 dst_unused:UNUSED_PAD src0_sel:WORD_0
	v_exp_f16_sdwa v47, v43 dst_sel:WORD_0 dst_unused:UNUSED_PAD src0_sel:WORD_0
	v_exp_f16_sdwa v48, v44 dst_sel:WORD_0 dst_unused:UNUSED_PAD src0_sel:WORD_0
	v_exp_f16_sdwa v49, v45 dst_sel:WORD_0 dst_unused:UNUSED_PAD src0_sel:WORD_0
	v_exp_f16_sdwa v46, v42 dst_sel:WORD_1 dst_unused:UNUSED_PRESERVE src0_sel:WORD_1
	v_exp_f16_sdwa v47, v43 dst_sel:WORD_1 dst_unused:UNUSED_PRESERVE src0_sel:WORD_1
	v_exp_f16_sdwa v48, v44 dst_sel:WORD_1 dst_unused:UNUSED_PRESERVE src0_sel:WORD_1
	v_exp_f16_sdwa v49, v45 dst_sel:WORD_1 dst_unused:UNUSED_PRESERVE src0_sel:WORD_1
	v_pk_add_f16 v42, v82, v114 neg_lo:[0,1] neg_hi:[0,1]
	v_pk_add_f16 v30, v30, v49
	v_pk_add_f16 v33, v33, v46
	v_pk_add_f16 v32, v32, v47
	v_pk_add_f16 v31, v31, v48
	v_pk_fma_f16 v25, v41, v49, v25
	v_pk_fma_f16 v24, v40, v48, v24
	v_pk_fma_f16 v23, v39, v47, v23
	v_pk_fma_f16 v22, v38, v46, v22
	v_pk_add_f16 v43, v83, v115 neg_lo:[0,1] neg_hi:[0,1]
	v_pk_add_f16 v44, v84, v116 neg_lo:[0,1] neg_hi:[0,1]
	v_pk_add_f16 v45, v85, v117 neg_lo:[0,1] neg_hi:[0,1]
	v_exp_f16_sdwa v46, v42 dst_sel:WORD_0 dst_unused:UNUSED_PAD src0_sel:WORD_0
	v_exp_f16_sdwa v47, v43 dst_sel:WORD_0 dst_unused:UNUSED_PAD src0_sel:WORD_0
	v_exp_f16_sdwa v48, v44 dst_sel:WORD_0 dst_unused:UNUSED_PAD src0_sel:WORD_0
	v_exp_f16_sdwa v49, v45 dst_sel:WORD_0 dst_unused:UNUSED_PAD src0_sel:WORD_0
	v_exp_f16_sdwa v46, v42 dst_sel:WORD_1 dst_unused:UNUSED_PRESERVE src0_sel:WORD_1
	v_exp_f16_sdwa v47, v43 dst_sel:WORD_1 dst_unused:UNUSED_PRESERVE src0_sel:WORD_1
	v_exp_f16_sdwa v48, v44 dst_sel:WORD_1 dst_unused:UNUSED_PRESERVE src0_sel:WORD_1
	v_exp_f16_sdwa v49, v45 dst_sel:WORD_1 dst_unused:UNUSED_PRESERVE src0_sel:WORD_1
	s_nop 0
	v_pk_add_f16 v30, v30, v49
	v_pk_add_f16 v31, v31, v48
	v_rcp_f16_e32 v44, v30
	v_rcp_f16_sdwa v30, v30 dst_sel:DWORD dst_unused:UNUSED_PAD src0_sel:WORD_1
	v_pk_add_f16 v32, v32, v47
	v_rcp_f16_e32 v45, v31
	v_rcp_f16_sdwa v31, v31 dst_sel:DWORD dst_unused:UNUSED_PAD src0_sel:WORD_1
	v_pk_add_f16 v33, v33, v46
	v_rcp_f16_e32 v43, v32
	v_rcp_f16_sdwa v32, v32 dst_sel:DWORD dst_unused:UNUSED_PAD src0_sel:WORD_1
	v_rcp_f16_e32 v42, v33
	v_rcp_f16_sdwa v33, v33 dst_sel:DWORD dst_unused:UNUSED_PAD src0_sel:WORD_1
	v_pk_fma_f16 v25, v61, v49, v25
	v_pack_b32_f16 v30, v44, v30
	v_pk_fma_f16 v24, v60, v48, v24
	v_pk_mul_f16 v25, v25, v30
	v_pack_b32_f16 v30, v45, v31
	v_pk_fma_f16 v23, v59, v47, v23
	v_pk_mul_f16 v24, v24, v30
	v_pack_b32_f16 v30, v43, v32
	v_pk_fma_f16 v22, v58, v46, v22
	v_pk_mul_f16 v23, v23, v30
	v_pack_b32_f16 v30, v42, v33
	v_pk_mul_f16 v22, v22, v30
	s_waitcnt vmcnt(0)
	s_cmp_lg_u32 s10, 1
	s_cbranch_scc1 .Lmywp3_1
	s_mov_b64 s[86:87], s[80:81]
	global_load_dword v254, v255, s[86:87]
	s_add_u32 s86, s86, 0x2000
	s_addc_u32 s87, s87, 0
	global_load_dword v254, v255, s[86:87]
	s_add_u32 s86, s86, 0x2000
	s_addc_u32 s87, s87, 0
	global_load_dword v254, v255, s[86:87]
	s_add_u32 s86, s86, 0x2c000
	s_addc_u32 s87, s87, 0
	global_load_dword v254, v255, s[86:87]
	s_add_u32 s86, s86, 0x2000
	s_addc_u32 s87, s87, 0
	global_load_dword v254, v255, s[86:87]
	s_add_u32 s86, s86, 0x2000
	s_addc_u32 s87, s87, 0
	global_load_dword v254, v255, s[86:87]
.Lmywp3_1:
	v_pk_mul_f16 v30, v185, v146 op_sel_hi:[0,1]
	v_pk_mul_f16 v31, v185, v147 op_sel_hi:[0,1]
	v_pk_mul_f16 v32, v185, v148 op_sel_hi:[0,1]
	v_pk_mul_f16 v33, v185, v149 op_sel_hi:[0,1]
	v_pk_mul_f16 v42, v183, v146 op_sel_hi:[0,1]
	v_pk_mul_f16 v43, v183, v147 op_sel_hi:[0,1]
	v_pk_mul_f16 v44, v183, v148 op_sel_hi:[0,1]
	v_pk_mul_f16 v45, v183, v149 op_sel_hi:[0,1]
	v_pk_mul_f16 v46, v184, v146 op_sel_hi:[0,1]
	v_pk_mul_f16 v47, v184, v147 op_sel_hi:[0,1]
	v_pk_mul_f16 v48, v184, v148 op_sel_hi:[0,1]
	v_pk_mul_f16 v49, v184, v149 op_sel_hi:[0,1]
	v_pk_fma_f16 v21, v21, v149, v33
	v_pk_fma_f16 v20, v20, v148, v32
	v_pk_fma_f16 v19, v19, v147, v31
	v_pk_fma_f16 v18, v18, v146, v30
	v_pk_fma_f16 v37, v37, v149, v45
	v_pk_fma_f16 v36, v36, v148, v44
	v_pk_fma_f16 v35, v35, v147, v43
	v_pk_fma_f16 v34, v34, v146, v42
	v_pk_fma_f16 v50, v57, v149, v49
	v_pk_fma_f16 v51, v56, v148, v48
	v_pk_fma_f16 v52, v55, v147, v47
	v_pk_fma_f16 v53, v54, v146, v46
	v_pk_fma_f16 v54, v77, v149, v33
	v_pk_fma_f16 v55, v76, v148, v32
	v_pk_fma_f16 v56, v75, v147, v31
	v_pk_fma_f16 v57, v74, v146, v30
	v_pk_maximum3_f16 v74, v18, v34, v53
	v_pk_maximum3_f16 v75, v19, v35, v52
	v_pk_maximum3_f16 v76, v20, v36, v51
	v_pk_maximum3_f16 v77, v21, v37, v50
	v_pk_fma_f16 v66, v105, v149, v45
	v_pk_fma_f16 v67, v104, v148, v44
	v_pk_fma_f16 v68, v103, v147, v43
	v_pk_fma_f16 v69, v102, v146, v42
	v_pk_fma_f16 v70, v121, v149, v49
	v_pk_fma_f16 v71, v120, v148, v48
	v_pk_fma_f16 v72, v119, v147, v47
	v_pk_fma_f16 v73, v118, v146, v46
	v_pk_fma_f16 v33, v133, v149, v33
	v_pk_fma_f16 v32, v132, v148, v32
	v_pk_fma_f16 v31, v131, v147, v31
	v_pk_fma_f16 v30, v130, v146, v30
	v_pk_fma_f16 v45, v141, v149, v45
	v_pk_fma_f16 v44, v140, v148, v44
	v_pk_fma_f16 v43, v139, v147, v43
	v_pk_fma_f16 v42, v138, v146, v42
	v_pk_fma_f16 v49, v145, v149, v49
	v_pk_fma_f16 v48, v144, v148, v48
	v_pk_fma_f16 v47, v143, v147, v47
	v_pk_fma_f16 v46, v142, v146, v46
	v_pk_maximum3_f16 v82, v57, v69, v73
	v_pk_maximum3_f16 v83, v56, v68, v72
	v_pk_maximum3_f16 v84, v55, v67, v71
	v_pk_maximum3_f16 v85, v54, v66, v70
	v_pk_maximum3_f16 v87, v31, v43, v47
	v_pk_maximum3_f16 v86, v30, v42, v46
	v_pk_maximum3_f16 v88, v32, v44, v48
	v_pk_maximum3_f16 v89, v33, v45, v49
	v_pk_maximum3_f16 v74, v74, v82, v86
	v_pk_maximum3_f16 v75, v75, v83, v87
	v_pk_maximum3_f16 v76, v76, v84, v88
	v_pk_maximum3_f16 v77, v77, v85, v89
	s_nop 0
	v_pk_add_f16 v18, v18, v74 neg_lo:[0,1] neg_hi:[0,1]
	v_pk_add_f16 v19, v19, v75 neg_lo:[0,1] neg_hi:[0,1]
	v_pk_add_f16 v20, v20, v76 neg_lo:[0,1] neg_hi:[0,1]
	v_pk_add_f16 v21, v21, v77 neg_lo:[0,1] neg_hi:[0,1]
	v_pk_add_f16 v34, v34, v74 neg_lo:[0,1] neg_hi:[0,1]
	v_exp_f16_sdwa v82, v18 dst_sel:WORD_0 dst_unused:UNUSED_PAD src0_sel:WORD_0
	v_exp_f16_sdwa v83, v19 dst_sel:WORD_0 dst_unused:UNUSED_PAD src0_sel:WORD_0
	v_exp_f16_sdwa v84, v20 dst_sel:WORD_0 dst_unused:UNUSED_PAD src0_sel:WORD_0
	v_exp_f16_sdwa v85, v21 dst_sel:WORD_0 dst_unused:UNUSED_PAD src0_sel:WORD_0
	v_exp_f16_sdwa v82, v18 dst_sel:WORD_1 dst_unused:UNUSED_PRESERVE src0_sel:WORD_1
	v_exp_f16_sdwa v83, v19 dst_sel:WORD_1 dst_unused:UNUSED_PRESERVE src0_sel:WORD_1
	v_exp_f16_sdwa v84, v20 dst_sel:WORD_1 dst_unused:UNUSED_PRESERVE src0_sel:WORD_1
	v_exp_f16_sdwa v85, v21 dst_sel:WORD_1 dst_unused:UNUSED_PRESERVE src0_sel:WORD_1
	v_pk_add_f16 v35, v35, v75 neg_lo:[0,1] neg_hi:[0,1]
	v_pk_add_f16 v18, v82, 0
	v_pk_add_f16 v19, v83, 0
	v_pk_add_f16 v20, v84, 0
	v_pk_add_f16 v21, v85, 0
	v_pk_fma_f16 v6, v6, v82, 0
	v_pk_fma_f16 v7, v7, v83, 0
	v_pk_fma_f16 v8, v8, v84, 0
	v_pk_fma_f16 v9, v9, v85, 0
	v_pk_add_f16 v36, v36, v76 neg_lo:[0,1] neg_hi:[0,1]
	v_pk_add_f16 v37, v37, v77 neg_lo:[0,1] neg_hi:[0,1]
	v_exp_f16_sdwa v82, v34 dst_sel:WORD_0 dst_unused:UNUSED_PAD src0_sel:WORD_0
	v_exp_f16_sdwa v83, v35 dst_sel:WORD_0 dst_unused:UNUSED_PAD src0_sel:WORD_0
	v_exp_f16_sdwa v84, v36 dst_sel:WORD_0 dst_unused:UNUSED_PAD src0_sel:WORD_0
	v_exp_f16_sdwa v85, v37 dst_sel:WORD_0 dst_unused:UNUSED_PAD src0_sel:WORD_0
	v_exp_f16_sdwa v82, v34 dst_sel:WORD_1 dst_unused:UNUSED_PRESERVE src0_sel:WORD_1
	v_exp_f16_sdwa v83, v35 dst_sel:WORD_1 dst_unused:UNUSED_PRESERVE src0_sel:WORD_1
	v_exp_f16_sdwa v84, v36 dst_sel:WORD_1 dst_unused:UNUSED_PRESERVE src0_sel:WORD_1
	v_exp_f16_sdwa v85, v37 dst_sel:WORD_1 dst_unused:UNUSED_PRESERVE src0_sel:WORD_1
	s_nop 0
	v_pk_add_f16 v21, v21, v85
	v_pk_add_f16 v20, v20, v84
	v_pk_add_f16 v19, v19, v83
	v_pk_add_f16 v18, v18, v82
	v_pk_fma_f16 v9, v13, v85, v9
	v_pk_fma_f16 v8, v12, v84, v8
	v_pk_fma_f16 v7, v11, v83, v7
	v_pk_fma_f16 v6, v10, v82, v6
	v_pk_add_f16 v10, v53, v74 neg_lo:[0,1] neg_hi:[0,1]
	v_pk_add_f16 v11, v52, v75 neg_lo:[0,1] neg_hi:[0,1]
	v_pk_add_f16 v12, v51, v76 neg_lo:[0,1] neg_hi:[0,1]
	v_pk_add_f16 v13, v50, v77 neg_lo:[0,1] neg_hi:[0,1]
	v_exp_f16_sdwa v34, v10 dst_sel:WORD_0 dst_unused:UNUSED_PAD src0_sel:WORD_0
	v_exp_f16_sdwa v35, v11 dst_sel:WORD_0 dst_unused:UNUSED_PAD src0_sel:WORD_0
	v_exp_f16_sdwa v36, v12 dst_sel:WORD_0 dst_unused:UNUSED_PAD src0_sel:WORD_0
	v_exp_f16_sdwa v37, v13 dst_sel:WORD_0 dst_unused:UNUSED_PAD src0_sel:WORD_0
	v_exp_f16_sdwa v34, v10 dst_sel:WORD_1 dst_unused:UNUSED_PRESERVE src0_sel:WORD_1
	v_exp_f16_sdwa v35, v11 dst_sel:WORD_1 dst_unused:UNUSED_PRESERVE src0_sel:WORD_1
	v_exp_f16_sdwa v36, v12 dst_sel:WORD_1 dst_unused:UNUSED_PRESERVE src0_sel:WORD_1
	v_exp_f16_sdwa v37, v13 dst_sel:WORD_1 dst_unused:UNUSED_PRESERVE src0_sel:WORD_1
	v_pk_add_f16 v10, v18, v34
	v_pk_add_f16 v11, v19, v35
	v_pk_add_f16 v12, v20, v36
	v_pk_add_f16 v13, v21, v37
	v_pk_fma_f16 v6, v14, v34, v6
	v_pk_fma_f16 v7, v15, v35, v7
	v_pk_fma_f16 v8, v16, v36, v8
	v_pk_fma_f16 v9, v17, v37, v9
	v_pk_add_f16 v14, v57, v74 neg_lo:[0,1] neg_hi:[0,1]
	v_pk_add_f16 v15, v56, v75 neg_lo:[0,1] neg_hi:[0,1]
	v_pk_add_f16 v16, v55, v76 neg_lo:[0,1] neg_hi:[0,1]
	v_pk_add_f16 v17, v54, v77 neg_lo:[0,1] neg_hi:[0,1]
	v_exp_f16_sdwa v18, v14 dst_sel:WORD_0 dst_unused:UNUSED_PAD src0_sel:WORD_0
	v_exp_f16_sdwa v19, v15 dst_sel:WORD_0 dst_unused:UNUSED_PAD src0_sel:WORD_0
	v_exp_f16_sdwa v20, v16 dst_sel:WORD_0 dst_unused:UNUSED_PAD src0_sel:WORD_0
	v_exp_f16_sdwa v21, v17 dst_sel:WORD_0 dst_unused:UNUSED_PAD src0_sel:WORD_0
	v_exp_f16_sdwa v18, v14 dst_sel:WORD_1 dst_unused:UNUSED_PRESERVE src0_sel:WORD_1
	v_exp_f16_sdwa v19, v15 dst_sel:WORD_1 dst_unused:UNUSED_PRESERVE src0_sel:WORD_1
	v_exp_f16_sdwa v20, v16 dst_sel:WORD_1 dst_unused:UNUSED_PRESERVE src0_sel:WORD_1
	v_exp_f16_sdwa v21, v17 dst_sel:WORD_1 dst_unused:UNUSED_PRESERVE src0_sel:WORD_1
	v_pk_add_f16 v14, v69, v74 neg_lo:[0,1] neg_hi:[0,1]
	v_pk_add_f16 v13, v13, v21
	v_pk_add_f16 v12, v12, v20
	v_pk_add_f16 v11, v11, v19
	v_pk_add_f16 v10, v10, v18
	v_pk_fma_f16 v9, v29, v21, v9
	v_pk_fma_f16 v8, v28, v20, v8
	v_pk_fma_f16 v7, v27, v19, v7
	v_pk_fma_f16 v6, v26, v18, v6
	v_pk_add_f16 v15, v68, v75 neg_lo:[0,1] neg_hi:[0,1]
	v_pk_add_f16 v16, v67, v76 neg_lo:[0,1] neg_hi:[0,1]
	v_pk_add_f16 v17, v66, v77 neg_lo:[0,1] neg_hi:[0,1]
	v_exp_f16_sdwa v18, v14 dst_sel:WORD_0 dst_unused:UNUSED_PAD src0_sel:WORD_0
	v_exp_f16_sdwa v19, v15 dst_sel:WORD_0 dst_unused:UNUSED_PAD src0_sel:WORD_0
	v_exp_f16_sdwa v20, v16 dst_sel:WORD_0 dst_unused:UNUSED_PAD src0_sel:WORD_0
	v_exp_f16_sdwa v21, v17 dst_sel:WORD_0 dst_unused:UNUSED_PAD src0_sel:WORD_0
	v_exp_f16_sdwa v18, v14 dst_sel:WORD_1 dst_unused:UNUSED_PRESERVE src0_sel:WORD_1
	v_exp_f16_sdwa v19, v15 dst_sel:WORD_1 dst_unused:UNUSED_PRESERVE src0_sel:WORD_1
	v_exp_f16_sdwa v20, v16 dst_sel:WORD_1 dst_unused:UNUSED_PRESERVE src0_sel:WORD_1
	v_exp_f16_sdwa v21, v17 dst_sel:WORD_1 dst_unused:UNUSED_PRESERVE src0_sel:WORD_1
	v_pk_add_f16 v14, v73, v74 neg_lo:[0,1] neg_hi:[0,1]
	v_pk_add_f16 v10, v10, v18
	v_pk_add_f16 v11, v11, v19
	v_pk_add_f16 v12, v12, v20
	v_pk_add_f16 v13, v13, v21
	v_pk_fma_f16 v6, v38, v18, v6
	v_pk_fma_f16 v7, v39, v19, v7
	v_pk_fma_f16 v8, v40, v20, v8
	v_pk_fma_f16 v9, v41, v21, v9
	v_pk_add_f16 v15, v72, v75 neg_lo:[0,1] neg_hi:[0,1]
	v_pk_add_f16 v16, v71, v76 neg_lo:[0,1] neg_hi:[0,1]
	v_pk_add_f16 v17, v70, v77 neg_lo:[0,1] neg_hi:[0,1]
	v_exp_f16_sdwa v18, v14 dst_sel:WORD_0 dst_unused:UNUSED_PAD src0_sel:WORD_0
	v_exp_f16_sdwa v19, v15 dst_sel:WORD_0 dst_unused:UNUSED_PAD src0_sel:WORD_0
	v_exp_f16_sdwa v20, v16 dst_sel:WORD_0 dst_unused:UNUSED_PAD src0_sel:WORD_0
	v_exp_f16_sdwa v21, v17 dst_sel:WORD_0 dst_unused:UNUSED_PAD src0_sel:WORD_0
	v_exp_f16_sdwa v18, v14 dst_sel:WORD_1 dst_unused:UNUSED_PRESERVE src0_sel:WORD_1
	v_exp_f16_sdwa v19, v15 dst_sel:WORD_1 dst_unused:UNUSED_PRESERVE src0_sel:WORD_1
	v_exp_f16_sdwa v20, v16 dst_sel:WORD_1 dst_unused:UNUSED_PRESERVE src0_sel:WORD_1
	v_exp_f16_sdwa v21, v17 dst_sel:WORD_1 dst_unused:UNUSED_PRESERVE src0_sel:WORD_1
	v_pk_add_f16 v14, v30, v74 neg_lo:[0,1] neg_hi:[0,1]
	v_pk_add_f16 v13, v13, v21
	v_pk_add_f16 v12, v12, v20
	v_pk_add_f16 v11, v11, v19
	v_pk_add_f16 v10, v10, v18
	v_pk_fma_f16 v9, v61, v21, v9
	v_pk_fma_f16 v8, v60, v20, v8
	v_pk_fma_f16 v7, v59, v19, v7
	v_pk_fma_f16 v6, v58, v18, v6
	v_pk_add_f16 v15, v31, v75 neg_lo:[0,1] neg_hi:[0,1]
	v_pk_add_f16 v16, v32, v76 neg_lo:[0,1] neg_hi:[0,1]
	v_pk_add_f16 v17, v33, v77 neg_lo:[0,1] neg_hi:[0,1]
	v_exp_f16_sdwa v18, v14 dst_sel:WORD_0 dst_unused:UNUSED_PAD src0_sel:WORD_0
	v_exp_f16_sdwa v19, v15 dst_sel:WORD_0 dst_unused:UNUSED_PAD src0_sel:WORD_0
	v_exp_f16_sdwa v20, v16 dst_sel:WORD_0 dst_unused:UNUSED_PAD src0_sel:WORD_0
	v_exp_f16_sdwa v21, v17 dst_sel:WORD_0 dst_unused:UNUSED_PAD src0_sel:WORD_0
	v_exp_f16_sdwa v18, v14 dst_sel:WORD_1 dst_unused:UNUSED_PRESERVE src0_sel:WORD_1
	v_exp_f16_sdwa v19, v15 dst_sel:WORD_1 dst_unused:UNUSED_PRESERVE src0_sel:WORD_1
	v_exp_f16_sdwa v20, v16 dst_sel:WORD_1 dst_unused:UNUSED_PRESERVE src0_sel:WORD_1
	v_exp_f16_sdwa v21, v17 dst_sel:WORD_1 dst_unused:UNUSED_PRESERVE src0_sel:WORD_1
	v_pk_add_f16 v10, v10, v18
	v_pk_add_f16 v11, v11, v19
	v_pk_add_f16 v12, v12, v20
	v_pk_add_f16 v13, v13, v21
	v_pk_fma_f16 v14, v78, v18, v6
	v_pk_fma_f16 v15, v79, v19, v7
	v_pk_fma_f16 v16, v80, v20, v8
	v_pk_fma_f16 v17, v81, v21, v9
	v_pk_add_f16 v6, v42, v74 neg_lo:[0,1] neg_hi:[0,1]
	v_pk_add_f16 v7, v43, v75 neg_lo:[0,1] neg_hi:[0,1]
	v_pk_add_f16 v8, v44, v76 neg_lo:[0,1] neg_hi:[0,1]
	v_pk_add_f16 v9, v45, v77 neg_lo:[0,1] neg_hi:[0,1]
	v_exp_f16_sdwa v18, v6 dst_sel:WORD_0 dst_unused:UNUSED_PAD src0_sel:WORD_0
	v_exp_f16_sdwa v19, v7 dst_sel:WORD_0 dst_unused:UNUSED_PAD src0_sel:WORD_0
	v_exp_f16_sdwa v20, v8 dst_sel:WORD_0 dst_unused:UNUSED_PAD src0_sel:WORD_0
	v_exp_f16_sdwa v21, v9 dst_sel:WORD_0 dst_unused:UNUSED_PAD src0_sel:WORD_0
	v_exp_f16_sdwa v18, v6 dst_sel:WORD_1 dst_unused:UNUSED_PRESERVE src0_sel:WORD_1
	v_exp_f16_sdwa v19, v7 dst_sel:WORD_1 dst_unused:UNUSED_PRESERVE src0_sel:WORD_1
	v_exp_f16_sdwa v20, v8 dst_sel:WORD_1 dst_unused:UNUSED_PRESERVE src0_sel:WORD_1
	v_exp_f16_sdwa v21, v9 dst_sel:WORD_1 dst_unused:UNUSED_PRESERVE src0_sel:WORD_1
	s_nop 0
	v_pk_add_f16 v9, v13, v21
	v_pk_add_f16 v8, v12, v20
	v_pk_add_f16 v7, v11, v19
	v_pk_add_f16 v6, v10, v18
	v_pk_fma_f16 v13, v93, v21, v17
	v_pk_fma_f16 v12, v92, v20, v16
	v_pk_fma_f16 v11, v91, v19, v15
	v_pk_fma_f16 v10, v90, v18, v14
	v_pk_add_f16 v18, v46, v74 neg_lo:[0,1] neg_hi:[0,1]
	v_pk_add_f16 v19, v47, v75 neg_lo:[0,1] neg_hi:[0,1]
	v_pk_add_f16 v20, v48, v76 neg_lo:[0,1] neg_hi:[0,1]
	v_pk_add_f16 v21, v49, v77 neg_lo:[0,1] neg_hi:[0,1]
	v_exp_f16_sdwa v14, v18 dst_sel:WORD_0 dst_unused:UNUSED_PAD src0_sel:WORD_0
	v_exp_f16_sdwa v17, v19 dst_sel:WORD_0 dst_unused:UNUSED_PAD src0_sel:WORD_0
	v_exp_f16_sdwa v15, v20 dst_sel:WORD_0 dst_unused:UNUSED_PAD src0_sel:WORD_0
	v_exp_f16_sdwa v16, v21 dst_sel:WORD_0 dst_unused:UNUSED_PAD src0_sel:WORD_0
	v_exp_f16_sdwa v14, v18 dst_sel:WORD_1 dst_unused:UNUSED_PRESERVE src0_sel:WORD_1
	v_exp_f16_sdwa v17, v19 dst_sel:WORD_1 dst_unused:UNUSED_PRESERVE src0_sel:WORD_1
	v_exp_f16_sdwa v15, v20 dst_sel:WORD_1 dst_unused:UNUSED_PRESERVE src0_sel:WORD_1
	v_exp_f16_sdwa v16, v21 dst_sel:WORD_1 dst_unused:UNUSED_PRESERVE src0_sel:WORD_1
	s_nop 0

.Lmystag3_5:
	global_load_dwordx4 v[50:53], v[122:123], off
	global_load_dwordx4 v[54:57], v[122:123], off offset:1024
	global_load_dwordx4 v[58:61], v[122:123], off offset:2048
	ds_read_b128 v[62:65], v83
	ds_read_b128 v[70:73], v84
	v_add_u32_e32 v0, v68, v111
	ds_read_b128 v[74:77], v99
	s_waitcnt lgkmcnt(2)
	buffer_store_dwordx4 v[62:65], v0, s[0:3], 0 offen sc1
	v_or_b32_e32 v0, s6, v154
	v_mul_lo_u32 v69, v0, s4
	ds_read_b128 v[62:65], v92
	v_add_u32_e32 v0, v69, v113
	s_waitcnt lgkmcnt(2)
	buffer_store_dwordx4 v[70:73], v0, s[0:3], 0 offen sc1
	v_or_b32_e32 v0, s6, v155
	s_nop 0
	v_mul_lo_u32 v72, v0, s4
	v_add_u32_e32 v0, v72, v115
	s_waitcnt lgkmcnt(0)
	buffer_store_dwordx4 v[62:65], v0, s[0:3], 0 offen sc1
	v_add_u32_e32 v0, s6, v156
	v_mul_lo_u32 v70, v0, s4
	ds_read_b128 v[62:65], v100
	v_add_u32_e32 v0, v70, v117
	buffer_store_dwordx4 v[74:77], v0, s[0:3], 0 offen sc1
	v_or_b32_e32 v0, s6, v157
	v_mul_lo_u32 v71, v0, s4
	v_add_u32_e32 v0, v71, v144
	ds_read_b128 v[74:77], v110
	s_waitcnt lgkmcnt(1)
	buffer_store_dwordx4 v[62:65], v0, s[0:3], 0 offen sc1
	ds_read_b128 v[62:65], v135
	ds_read_b128 v[78:81], v135 offset:8192
	ds_read_b128 v[86:89], v135 offset:16384
	ds_read_b128 v[94:97], v135 offset:24576
	ds_read_b128 v[102:105], v135 offset:32768
	ds_read_b128 v[106:109], v135 offset:40960
	ds_read_b128 v[124:127], v135 offset:49152
	ds_read_b128 v[148:151], v135 offset:57344
	v_add_u32_e32 v0, s6, v147
	v_mul_lo_u32 v73, v0, s4
	v_add_u32_e32 v0, v73, v145
	s_waitcnt lgkmcnt(8)
	buffer_store_dwordx4 v[74:77], v0, s[0:3], 0 offen sc1
	s_waitcnt lgkmcnt(7)
	s_nop 0
	v_mfma_f32_16x16x32_f16 v[74:77], v[38:41], v[62:65], 0
	s_waitcnt lgkmcnt(6)
	v_mfma_f32_16x16x32_f16 v[152:155], v[38:41], v[78:81], 0
	s_waitcnt lgkmcnt(5)
	v_mfma_f32_16x16x32_f16 v[156:159], v[38:41], v[86:89], 0
	s_waitcnt lgkmcnt(4)
	v_mfma_f32_16x16x32_f16 v[160:163], v[38:41], v[94:97], 0
	s_waitcnt lgkmcnt(3)
	v_mfma_f32_16x16x32_f16 v[164:167], v[38:41], v[102:105], 0
	s_waitcnt lgkmcnt(2)
	v_mfma_f32_16x16x32_f16 v[168:171], v[38:41], v[106:109], 0
	s_waitcnt lgkmcnt(1)
	v_mfma_f32_16x16x32_f16 v[172:175], v[38:41], v[124:127], 0
	s_waitcnt lgkmcnt(0)
	v_mfma_f32_16x16x32_f16 v[38:41], v[38:41], v[148:151], 0
	v_mfma_f32_16x16x32_f16 v[176:179], v[26:29], v[62:65], 0
	v_mfma_f32_16x16x32_f16 v[180:183], v[26:29], v[78:81], 0
	v_mfma_f32_16x16x32_f16 v[184:187], v[26:29], v[86:89], 0
	v_mfma_f32_16x16x32_f16 v[188:191], v[26:29], v[94:97], 0
	v_mfma_f32_16x16x32_f16 v[192:195], v[26:29], v[102:105], 0
	v_mfma_f32_16x16x32_f16 v[196:199], v[26:29], v[106:109], 0
	v_mfma_f32_16x16x32_f16 v[200:203], v[26:29], v[124:127], 0
	v_mfma_f32_16x16x32_f16 v[26:29], v[26:29], v[148:151], 0
	v_mfma_f32_16x16x32_f16 v[62:65], v[10:13], v[62:65], 0
	v_mfma_f32_16x16x32_f16 v[78:81], v[10:13], v[78:81], 0
	v_mfma_f32_16x16x32_f16 v[86:89], v[10:13], v[86:89], 0
	v_mfma_f32_16x16x32_f16 v[94:97], v[10:13], v[94:97], 0
	v_mfma_f32_16x16x32_f16 v[102:105], v[10:13], v[102:105], 0
	v_mfma_f32_16x16x32_f16 v[106:109], v[10:13], v[106:109], 0
	v_mfma_f32_16x16x32_f16 v[124:127], v[10:13], v[124:127], 0
	v_mfma_f32_16x16x32_f16 v[10:13], v[10:13], v[148:151], 0
	s_mov_b32 s4, 0x34000
	v_add_co_u32_e32 v66, vcc, s4, v118
	s_mov_b32 s4, 0x35000
	s_nop 0
	v_addc_co_u32_e32 v67, vcc, 0, v119, vcc
	v_add_co_u32_e32 v118, vcc, s4, v118
	s_nop 1
	v_addc_co_u32_e32 v119, vcc, 0, v119, vcc
	global_load_dwordx4 v[148:151], v[118:119], off offset:-4096
	global_load_dwordx4 v[204:207], v[122:123], off offset:3072
	global_load_dwordx4 v[208:211], v[66:67], off offset:1024
	ds_read_b128 v[212:215], v133
	ds_read_b128 v[216:219], v133 offset:8192
	ds_read_b128 v[220:223], v133 offset:16384
	ds_read_b128 v[224:227], v133 offset:24576
	ds_read_b128 v[228:231], v133 offset:32768
	ds_read_b128 v[232:235], v133 offset:40960
	ds_read_b128 v[236:239], v133 offset:49152
	ds_read_b128 v[240:243], v133 offset:57344
	s_waitcnt lgkmcnt(7)
	v_mfma_f32_16x16x32_f16 v[74:77], v[22:25], v[212:215], v[74:77]
	s_waitcnt lgkmcnt(6)
	v_mfma_f32_16x16x32_f16 v[152:155], v[22:25], v[216:219], v[152:155]
	s_waitcnt lgkmcnt(5)
	v_mfma_f32_16x16x32_f16 v[156:159], v[22:25], v[220:223], v[156:159]
	s_waitcnt lgkmcnt(4)
	v_mfma_f32_16x16x32_f16 v[160:163], v[22:25], v[224:227], v[160:163]
	s_waitcnt lgkmcnt(3)
	v_mfma_f32_16x16x32_f16 v[164:167], v[22:25], v[228:231], v[164:167]
	s_waitcnt lgkmcnt(2)
	v_mfma_f32_16x16x32_f16 v[168:171], v[22:25], v[232:235], v[168:171]
	s_waitcnt lgkmcnt(1)
	v_mfma_f32_16x16x32_f16 v[172:175], v[22:25], v[236:239], v[172:175]
	s_waitcnt lgkmcnt(0)
	v_mfma_f32_16x16x32_f16 v[22:25], v[22:25], v[240:243], v[38:41]
	v_mfma_f32_16x16x32_f16 v[38:41], v[6:9], v[212:215], v[176:179]
	v_mfma_f32_16x16x32_f16 v[176:179], v[6:9], v[216:219], v[180:183]
	v_mfma_f32_16x16x32_f16 v[180:183], v[6:9], v[220:223], v[184:187]
	v_mfma_f32_16x16x32_f16 v[184:187], v[6:9], v[224:227], v[188:191]
	v_mfma_f32_16x16x32_f16 v[188:191], v[6:9], v[228:231], v[192:195]
	v_mfma_f32_16x16x32_f16 v[192:195], v[6:9], v[232:235], v[196:199]
	v_mfma_f32_16x16x32_f16 v[196:199], v[6:9], v[236:239], v[200:203]
	v_mfma_f32_16x16x32_f16 v[6:9], v[6:9], v[240:243], v[26:29]
	v_mfma_f32_16x16x32_f16 v[26:29], v[2:5], v[212:215], v[62:65]
	v_mfma_f32_16x16x32_f16 v[62:65], v[2:5], v[216:219], v[78:81]
	v_mfma_f32_16x16x32_f16 v[78:81], v[2:5], v[220:223], v[86:89]
	v_mfma_f32_16x16x32_f16 v[86:89], v[2:5], v[224:227], v[94:97]
	v_mfma_f32_16x16x32_f16 v[94:97], v[2:5], v[228:231], v[102:105]
	v_mfma_f32_16x16x32_f16 v[102:105], v[2:5], v[232:235], v[106:109]
	v_mfma_f32_16x16x32_f16 v[106:109], v[2:5], v[236:239], v[124:127]
	v_mfma_f32_16x16x32_f16 v[0:3], v[2:5], v[240:243], v[10:13]
	s_nop 2
	global_load_dwordx4 v[10:13], v[66:67], off offset:2048
	global_load_dwordx4 v[122:125], v[66:67], off offset:3072
	global_load_dwordx4 v[126:129], v[118:119], off
	ds_read_b128 v[200:203], v134
	ds_read_b128 v[212:215], v134 offset:8192
	ds_read_b128 v[216:219], v134 offset:16384
	ds_read_b128 v[220:223], v134 offset:24576
	ds_read_b128 v[224:227], v134 offset:32768
	ds_read_b128 v[228:231], v134 offset:40960
	ds_read_b128 v[232:235], v134 offset:49152
	ds_read_b128 v[236:239], v134 offset:57344
	s_waitcnt lgkmcnt(7)
	v_mfma_f32_16x16x32_f16 v[74:77], v[30:33], v[200:203], v[74:77]
	s_waitcnt lgkmcnt(6)
	v_mfma_f32_16x16x32_f16 v[152:155], v[30:33], v[212:215], v[152:155]
	s_waitcnt lgkmcnt(5)
	v_mfma_f32_16x16x32_f16 v[156:159], v[30:33], v[216:219], v[156:159]
	s_waitcnt lgkmcnt(4)
	v_mfma_f32_16x16x32_f16 v[160:163], v[30:33], v[220:223], v[160:163]
	s_waitcnt lgkmcnt(3)
	v_mfma_f32_16x16x32_f16 v[164:167], v[30:33], v[224:227], v[164:167]
	s_waitcnt lgkmcnt(2)
	v_mfma_f32_16x16x32_f16 v[168:171], v[30:33], v[228:231], v[168:171]
	s_waitcnt lgkmcnt(1)
	v_mfma_f32_16x16x32_f16 v[172:175], v[30:33], v[232:235], v[172:175]
	s_waitcnt lgkmcnt(0)
	v_mfma_f32_16x16x32_f16 v[22:25], v[30:33], v[236:239], v[22:25]
	v_mfma_f32_16x16x32_f16 v[30:33], v[14:17], v[200:203], v[38:41]
	v_mfma_f32_16x16x32_f16 v[38:41], v[14:17], v[212:215], v[176:179]
	v_mfma_f32_16x16x32_f16 v[176:179], v[14:17], v[216:219], v[180:183]
	v_mfma_f32_16x16x32_f16 v[180:183], v[14:17], v[220:223], v[184:187]
	v_mfma_f32_16x16x32_f16 v[184:187], v[14:17], v[224:227], v[188:191]
	v_mfma_f32_16x16x32_f16 v[188:191], v[14:17], v[228:231], v[192:195]
	v_mfma_f32_16x16x32_f16 v[192:195], v[14:17], v[232:235], v[196:199]
	v_mfma_f32_16x16x32_f16 v[4:7], v[14:17], v[236:239], v[6:9]
	v_mfma_f32_16x16x32_f16 v[14:17], v[18:21], v[200:203], v[26:29]
	v_mfma_f32_16x16x32_f16 v[26:29], v[18:21], v[212:215], v[62:65]
	v_mfma_f32_16x16x32_f16 v[62:65], v[18:21], v[216:219], v[78:81]
	v_mfma_f32_16x16x32_f16 v[78:81], v[18:21], v[220:223], v[86:89]
	v_mfma_f32_16x16x32_f16 v[86:89], v[18:21], v[224:227], v[94:97]
	v_mfma_f32_16x16x32_f16 v[94:97], v[18:21], v[228:231], v[102:105]
	v_mfma_f32_16x16x32_f16 v[102:105], v[18:21], v[232:235], v[106:109]
	v_mfma_f32_16x16x32_f16 v[0:3], v[18:21], v[236:239], v[0:3]
	global_load_dwordx4 v[18:21], v[118:119], off offset:1024
	s_nop 0
	global_load_dwordx4 v[106:109], v[118:119], off offset:2048
	global_load_dwordx4 v[196:199], v[118:119], off offset:3072
	ds_read_b128 v[200:203], v136
	ds_read_b128 v[212:215], v136 offset:8192
	ds_read_b128 v[216:219], v136 offset:16384
	ds_read_b128 v[220:223], v136 offset:24576
	ds_read_b128 v[224:227], v136 offset:32768
	ds_read_b128 v[228:231], v136 offset:40960
	ds_read_b128 v[232:235], v136 offset:49152
	ds_read_b128 v[236:239], v136 offset:57344
	s_waitcnt lgkmcnt(7)
	v_mfma_f32_16x16x32_f16 v[74:77], v[46:49], v[200:203], v[74:77]
	s_waitcnt lgkmcnt(6)
	v_mfma_f32_16x16x32_f16 v[152:155], v[46:49], v[212:215], v[152:155]
	s_waitcnt lgkmcnt(5)
	v_mfma_f32_16x16x32_f16 v[156:159], v[46:49], v[216:219], v[156:159]
	s_waitcnt lgkmcnt(4)
	v_mfma_f32_16x16x32_f16 v[160:163], v[46:49], v[220:223], v[160:163]
	s_waitcnt lgkmcnt(3)
	v_mfma_f32_16x16x32_f16 v[164:167], v[46:49], v[224:227], v[164:167]
	s_waitcnt lgkmcnt(2)
	v_mfma_f32_16x16x32_f16 v[168:171], v[46:49], v[228:231], v[168:171]
	s_waitcnt lgkmcnt(1)
	v_mfma_f32_16x16x32_f16 v[172:175], v[46:49], v[232:235], v[172:175]
	s_waitcnt lgkmcnt(0)
	v_mfma_f32_16x16x32_f16 v[22:25], v[46:49], v[236:239], v[22:25]
	v_mfma_f32_16x16x32_f16 v[30:33], v[42:45], v[200:203], v[30:33]
	v_mfma_f32_16x16x32_f16 v[38:41], v[42:45], v[212:215], v[38:41]
	v_mfma_f32_16x16x32_f16 v[46:49], v[42:45], v[216:219], v[176:179]
	v_mfma_f32_16x16x32_f16 v[176:179], v[42:45], v[220:223], v[180:183]
	v_mfma_f32_16x16x32_f16 v[180:183], v[42:45], v[224:227], v[184:187]
	v_mfma_f32_16x16x32_f16 v[184:187], v[42:45], v[228:231], v[188:191]
	v_mfma_f32_16x16x32_f16 v[188:191], v[42:45], v[232:235], v[192:195]
	v_mfma_f32_16x16x32_f16 v[4:7], v[42:45], v[236:239], v[4:7]
	v_mfma_f32_16x16x32_f16 v[14:17], v[34:37], v[200:203], v[14:17]
	v_mfma_f32_16x16x32_f16 v[26:29], v[34:37], v[212:215], v[26:29]
	v_mfma_f32_16x16x32_f16 v[42:45], v[34:37], v[216:219], v[62:65]
	v_mfma_f32_16x16x32_f16 v[62:65], v[34:37], v[220:223], v[78:81]
	v_mfma_f32_16x16x32_f16 v[78:81], v[34:37], v[224:227], v[86:89]
	v_mfma_f32_16x16x32_f16 v[86:89], v[34:37], v[228:231], v[94:97]
	v_mfma_f32_16x16x32_f16 v[94:97], v[34:37], v[232:235], v[102:105]
	v_mfma_f32_16x16x32_f16 v[0:3], v[34:37], v[236:239], v[0:3]
	ds_read_b128 v[34:37], v137
	s_nop 0
	ds_read_b128 v[102:105], v137 offset:8192
	ds_read_b128 v[192:195], v137 offset:16384
	ds_read_b128 v[200:203], v137 offset:24576
	ds_read_b128 v[212:215], v137 offset:32768
	ds_read_b128 v[216:219], v137 offset:40960
	ds_read_b128 v[220:223], v137 offset:49152
	ds_read_b128 v[134:137], v137 offset:57344
	s_waitcnt vmcnt(17) lgkmcnt(7)
	v_mfma_f32_16x16x32_f16 v[74:77], v[50:53], v[34:37], v[74:77]
	s_waitcnt lgkmcnt(6)
	v_mfma_f32_16x16x32_f16 v[152:155], v[50:53], v[102:105], v[152:155]
	s_waitcnt lgkmcnt(5)
	v_mfma_f32_16x16x32_f16 v[156:159], v[50:53], v[192:195], v[156:159]
	s_waitcnt lgkmcnt(4)
	v_mfma_f32_16x16x32_f16 v[160:163], v[50:53], v[200:203], v[160:163]
	s_waitcnt lgkmcnt(3)
	v_mfma_f32_16x16x32_f16 v[164:167], v[50:53], v[212:215], v[164:167]
	s_waitcnt lgkmcnt(2)
	v_mfma_f32_16x16x32_f16 v[168:171], v[50:53], v[216:219], v[168:171]
	s_waitcnt lgkmcnt(1)
	v_mfma_f32_16x16x32_f16 v[172:175], v[50:53], v[220:223], v[172:175]
	s_waitcnt lgkmcnt(0)
	v_mfma_f32_16x16x32_f16 v[22:25], v[50:53], v[134:137], v[22:25]
	s_waitcnt vmcnt(16)
	v_mfma_f32_16x16x32_f16 v[30:33], v[54:57], v[34:37], v[30:33]
	v_mfma_f32_16x16x32_f16 v[38:41], v[54:57], v[102:105], v[38:41]
	v_mfma_f32_16x16x32_f16 v[46:49], v[54:57], v[192:195], v[46:49]
	v_mfma_f32_16x16x32_f16 v[50:53], v[54:57], v[200:203], v[176:179]
	v_mfma_f32_16x16x32_f16 v[176:179], v[54:57], v[212:215], v[180:183]
	v_mfma_f32_16x16x32_f16 v[180:183], v[54:57], v[216:219], v[184:187]
	v_mfma_f32_16x16x32_f16 v[184:187], v[54:57], v[220:223], v[188:191]
	v_mfma_f32_16x16x32_f16 v[4:7], v[54:57], v[134:137], v[4:7]
	s_waitcnt vmcnt(15)
	v_mfma_f32_16x16x32_f16 v[14:17], v[58:61], v[34:37], v[14:17]
	v_mfma_f32_16x16x32_f16 v[26:29], v[58:61], v[102:105], v[26:29]
	v_mfma_f32_16x16x32_f16 v[34:37], v[58:61], v[192:195], v[42:45]
	v_mfma_f32_16x16x32_f16 v[42:45], v[58:61], v[200:203], v[62:65]
	v_mfma_f32_16x16x32_f16 v[54:57], v[58:61], v[212:215], v[78:81]
	v_mfma_f32_16x16x32_f16 v[62:65], v[58:61], v[216:219], v[86:89]
	v_mfma_f32_16x16x32_f16 v[78:81], v[58:61], v[220:223], v[94:97]
	v_mfma_f32_16x16x32_f16 v[0:3], v[58:61], v[134:137], v[0:3]
	ds_read_b128 v[58:61], v138
	ds_read_b128 v[86:89], v138 offset:8192
	ds_read_b128 v[94:97], v138 offset:16384
	ds_read_b128 v[102:105], v138 offset:24576
	ds_read_b128 v[134:137], v138 offset:32768
	ds_read_b128 v[188:191], v138 offset:40960
	ds_read_b128 v[192:195], v138 offset:49152
	ds_read_b128 v[200:203], v138 offset:57344
	s_waitcnt vmcnt(7) lgkmcnt(7)
	v_mfma_f32_16x16x32_f16 v[74:77], v[204:207], v[58:61], v[74:77]
	s_waitcnt lgkmcnt(6)
	v_mfma_f32_16x16x32_f16 v[152:155], v[204:207], v[86:89], v[152:155]
	s_waitcnt lgkmcnt(5)
	v_mfma_f32_16x16x32_f16 v[156:159], v[204:207], v[94:97], v[156:159]
	s_waitcnt lgkmcnt(4)
	v_mfma_f32_16x16x32_f16 v[160:163], v[204:207], v[102:105], v[160:163]
	s_waitcnt lgkmcnt(3)
	v_mfma_f32_16x16x32_f16 v[164:167], v[204:207], v[134:137], v[164:167]
	s_waitcnt lgkmcnt(2)
	v_mfma_f32_16x16x32_f16 v[168:171], v[204:207], v[188:191], v[168:171]
	s_waitcnt lgkmcnt(1)
	v_mfma_f32_16x16x32_f16 v[172:175], v[204:207], v[192:195], v[172:175]
	s_waitcnt lgkmcnt(0)
	v_mfma_f32_16x16x32_f16 v[22:25], v[204:207], v[200:203], v[22:25]
	v_mfma_f32_16x16x32_f16 v[30:33], v[148:151], v[58:61], v[30:33]
	v_mfma_f32_16x16x32_f16 v[38:41], v[148:151], v[86:89], v[38:41]
	v_mfma_f32_16x16x32_f16 v[46:49], v[148:151], v[94:97], v[46:49]
	v_mfma_f32_16x16x32_f16 v[50:53], v[148:151], v[102:105], v[50:53]
	v_mfma_f32_16x16x32_f16 v[176:179], v[148:151], v[134:137], v[176:179]
	v_mfma_f32_16x16x32_f16 v[180:183], v[148:151], v[188:191], v[180:183]
	v_mfma_f32_16x16x32_f16 v[184:187], v[148:151], v[192:195], v[184:187]
	v_mfma_f32_16x16x32_f16 v[4:7], v[148:151], v[200:203], v[4:7]
	s_waitcnt vmcnt(6)
	v_mfma_f32_16x16x32_f16 v[14:17], v[208:211], v[58:61], v[14:17]
	v_mfma_f32_16x16x32_f16 v[26:29], v[208:211], v[86:89], v[26:29]
	v_mfma_f32_16x16x32_f16 v[34:37], v[208:211], v[94:97], v[34:37]
	v_mfma_f32_16x16x32_f16 v[42:45], v[208:211], v[102:105], v[42:45]
	v_mfma_f32_16x16x32_f16 v[54:57], v[208:211], v[134:137], v[54:57]
	v_mfma_f32_16x16x32_f16 v[58:61], v[208:211], v[188:191], v[62:65]
	v_mfma_f32_16x16x32_f16 v[62:65], v[208:211], v[192:195], v[78:81]
	v_mfma_f32_16x16x32_f16 v[0:3], v[208:211], v[200:203], v[0:3]
	s_nop 1
	ds_read_b128 v[78:81], v139
	ds_read_b128 v[86:89], v139 offset:8192
	ds_read_b128 v[94:97], v139 offset:16384
	ds_read_b128 v[102:105], v139 offset:24576
	ds_read_b128 v[134:137], v139 offset:32768
	ds_read_b128 v[148:151], v139 offset:40960
	ds_read_b128 v[188:191], v139 offset:49152
	ds_read_b128 v[192:195], v139 offset:57344
	s_waitcnt vmcnt(5) lgkmcnt(7)
	v_mfma_f32_16x16x32_f16 v[74:77], v[10:13], v[78:81], v[74:77]
	s_waitcnt lgkmcnt(6)
	v_mfma_f32_16x16x32_f16 v[152:155], v[10:13], v[86:89], v[152:155]
	s_waitcnt lgkmcnt(5)
	v_mfma_f32_16x16x32_f16 v[156:159], v[10:13], v[94:97], v[156:159]
	s_waitcnt lgkmcnt(4)
	v_mfma_f32_16x16x32_f16 v[160:163], v[10:13], v[102:105], v[160:163]
	s_waitcnt lgkmcnt(3)
	v_mfma_f32_16x16x32_f16 v[164:167], v[10:13], v[134:137], v[164:167]
	s_waitcnt lgkmcnt(2)
	v_mfma_f32_16x16x32_f16 v[168:171], v[10:13], v[148:151], v[168:171]
	s_waitcnt lgkmcnt(1)
	v_mfma_f32_16x16x32_f16 v[172:175], v[10:13], v[188:191], v[172:175]
	s_waitcnt lgkmcnt(0)
	v_mfma_f32_16x16x32_f16 v[8:11], v[10:13], v[192:195], v[22:25]
	s_waitcnt vmcnt(4)
	v_mfma_f32_16x16x32_f16 v[22:25], v[122:125], v[78:81], v[30:33]
	v_mfma_f32_16x16x32_f16 v[30:33], v[122:125], v[86:89], v[38:41]
	v_mfma_f32_16x16x32_f16 v[200:203], v[122:125], v[94:97], v[46:49]
	v_mfma_f32_16x16x32_f16 v[48:51], v[122:125], v[102:105], v[50:53]
	v_mfma_f32_16x16x32_f16 v[176:179], v[122:125], v[134:137], v[176:179]
	v_mfma_f32_16x16x32_f16 v[180:183], v[122:125], v[148:151], v[180:183]
	v_mfma_f32_16x16x32_f16 v[184:187], v[122:125], v[188:191], v[184:187]
	v_mfma_f32_16x16x32_f16 v[4:7], v[122:125], v[192:195], v[4:7]
	s_waitcnt vmcnt(3)
	v_mfma_f32_16x16x32_f16 v[12:15], v[126:129], v[78:81], v[14:17]
	v_mfma_f32_16x16x32_f16 v[78:81], v[126:129], v[86:89], v[26:29]
	v_mfma_f32_16x16x32_f16 v[86:89], v[126:129], v[94:97], v[34:37]
	v_mfma_f32_16x16x32_f16 v[40:43], v[126:129], v[102:105], v[42:45]
	v_mfma_f32_16x16x32_f16 v[94:97], v[126:129], v[134:137], v[54:57]
	v_mfma_f32_16x16x32_f16 v[102:105], v[126:129], v[148:151], v[58:61]
	v_mfma_f32_16x16x32_f16 v[64:67], v[126:129], v[188:191], v[62:65]
	v_mfma_f32_16x16x32_f16 v[0:3], v[126:129], v[192:195], v[0:3]
	s_nop 1
	ds_read_b128 v[60:63], v141
	ds_read_b128 v[122:125], v141 offset:8192
	ds_read_b128 v[126:129], v141 offset:16384
	ds_read_b128 v[134:137], v141 offset:24576
	ds_read_b128 v[148:151], v141 offset:32768
	ds_read_b128 v[188:191], v141 offset:40960
	ds_read_b128 v[192:195], v141 offset:49152
	ds_read_b128 v[138:141], v141 offset:57344
	s_waitcnt vmcnt(2) lgkmcnt(7)
	v_mfma_f32_16x16x32_f16 v[74:77], v[18:21], v[60:63], v[74:77]
	s_waitcnt lgkmcnt(6)
	v_mfma_f32_16x16x32_f16 v[152:155], v[18:21], v[122:125], v[152:155]
	s_waitcnt lgkmcnt(5)
	v_mfma_f32_16x16x32_f16 v[156:159], v[18:21], v[126:129], v[156:159]
	s_waitcnt lgkmcnt(4)
	v_mfma_f32_16x16x32_f16 v[160:163], v[18:21], v[134:137], v[160:163]
	s_waitcnt lgkmcnt(3)
	v_mfma_f32_16x16x32_f16 v[56:59], v[18:21], v[148:151], v[164:167]
	s_waitcnt lgkmcnt(2)
	v_mfma_f32_16x16x32_f16 v[52:55], v[18:21], v[188:191], v[168:171]
	s_waitcnt lgkmcnt(1)
	v_mfma_f32_16x16x32_f16 v[44:47], v[18:21], v[192:195], v[172:175]
	s_waitcnt lgkmcnt(0)
	v_mfma_f32_16x16x32_f16 v[36:39], v[18:21], v[138:141], v[8:11]
	s_waitcnt vmcnt(1)
	v_mfma_f32_16x16x32_f16 v[164:167], v[106:109], v[60:63], v[22:25]
	v_mfma_f32_16x16x32_f16 v[168:171], v[106:109], v[122:125], v[30:33]
	v_mfma_f32_16x16x32_f16 v[172:175], v[106:109], v[126:129], v[200:203]
	v_mfma_f32_16x16x32_f16 v[200:203], v[106:109], v[134:137], v[48:51]
	v_mfma_f32_16x16x32_f16 v[32:35], v[106:109], v[148:151], v[176:179]
	v_mfma_f32_16x16x32_f16 v[24:27], v[106:109], v[188:191], v[180:183]
	v_mfma_f32_16x16x32_f16 v[20:23], v[106:109], v[192:195], v[184:187]
	v_mfma_f32_16x16x32_f16 v[16:19], v[106:109], v[138:141], v[4:7]
	s_waitcnt vmcnt(0)
	s_cmp_lg_u32 s10, 1
	s_cbranch_scc1 .Lmywp3_0
	s_mov_b64 s[86:87], s[80:81]
	global_load_dword v254, v255, s[86:87]
	s_add_u32 s86, s86, 0x2000
	s_addc_u32 s87, s87, 0
	global_load_dword v254, v255, s[86:87]
	s_add_u32 s86, s86, 0x2000
	s_addc_u32 s87, s87, 0
	global_load_dword v254, v255, s[86:87]
	s_add_u32 s86, s86, 0x2c000
	s_addc_u32 s87, s87, 0
	global_load_dword v254, v255, s[86:87]
	s_add_u32 s86, s86, 0x2000
	s_addc_u32 s87, s87, 0
	global_load_dword v254, v255, s[86:87]
	s_add_u32 s86, s86, 0x2000
	s_addc_u32 s87, s87, 0
	global_load_dword v254, v255, s[86:87]
.Lmywp3_0:
	v_mfma_f32_16x16x32_f16 v[106:109], v[196:199], v[60:63], v[12:15]
	v_mfma_f32_16x16x32_f16 v[78:81], v[196:199], v[122:125], v[78:81]
	v_mfma_f32_16x16x32_f16 v[86:89], v[196:199], v[126:129], v[86:89]
	v_mfma_f32_16x16x32_f16 v[60:63], v[196:199], v[134:137], v[40:43]
	v_mfma_f32_16x16x32_f16 v[12:15], v[196:199], v[148:151], v[94:97]
	v_mfma_f32_16x16x32_f16 v[8:11], v[196:199], v[188:191], v[102:105]
	v_mfma_f32_16x16x32_f16 v[4:7], v[196:199], v[192:195], v[64:67]
	v_mfma_f32_16x16x32_f16 v[0:3], v[196:199], v[138:141], v[0:3]
	global_load_dwordx4 v[48:51], v[120:121], off offset:1536
	global_load_dwordx4 v[40:43], v[120:121], off offset:1600
	global_load_dwordx4 v[28:31], v[120:121], off offset:1664
	v_mov_b32_e32 v94, v157
	v_mov_b32_e32 v95, v158
	v_mov_b32_e32 v96, v161
	v_mov_b32_e32 v97, v162
	v_mov_b32_e32 v64, v153
	v_mov_b32_e32 v65, v154
	v_mov_b32_e32 v102, v169
	v_mov_b32_e32 v103, v170
	v_mov_b32_e32 v104, v173
	v_mov_b32_e32 v105, v174
	v_mov_b32_e32 v118, v201
	v_mov_b32_e32 v119, v202
	s_barrier
	s_waitcnt vmcnt(2)
	v_pk_add_f32 v[74:75], v[74:75], v[48:49]
	v_add_f32_e32 v82, v152, v48
	v_pk_mov_b32 v[120:121], v[48:49], v[50:51] op_sel:[1,0]
	v_add_f32_e32 v49, v155, v51
	s_waitcnt vmcnt(1)
	v_pk_add_f32 v[122:123], v[164:165], v[40:41]
	v_add_f32_e32 v98, v168, v40
	v_pk_mov_b32 v[66:67], v[40:41], v[42:43] op_sel:[1,0]
	v_add_f32_e32 v41, v171, v43
	v_pk_add_f32 v[76:77], v[76:77], v[50:51]
	v_add_f32_e32 v50, v156, v48
	v_add_f32_e32 v85, v159, v51
	v_add_f32_e32 v90, v160, v48
	v_add_f32_e32 v93, v163, v51
	v_pk_add_f32 v[124:125], v[166:167], v[42:43]
	v_add_f32_e32 v42, v172, v40
	v_add_f32_e32 v101, v175, v43
	v_add_f32_e32 v126, v200, v40
	v_add_f32_e32 v127, v203, v43
	v_cvt_f16_f32_e32 v82, v82
	v_cvt_f16_f32_e32 v49, v49
	v_cvt_f16_f32_e32 v98, v98
	v_cvt_f16_f32_e32 v41, v41
	v_cvt_pk_f16_f32 v74, v74, v75
	v_cvt_pk_f16_f32 v75, v76, v77
	v_cvt_f16_f32_e32 v50, v50
	v_pk_add_f32 v[76:77], v[94:95], v[120:121]
	v_cvt_f16_f32_e32 v85, v85
	v_cvt_f16_f32_e32 v90, v90
	v_pk_add_f32 v[94:95], v[96:97], v[120:121]
	v_cvt_f16_f32_e32 v93, v93
	v_cvt_pk_f16_f32 v96, v122, v123
	v_cvt_f16_f32_e32 v42, v42
	v_cvt_f16_f32_e32 v101, v101
	v_cvt_f16_f32_e32 v122, v126
	v_cvt_f16_f32_e32 v123, v127
	v_pk_add_f32 v[64:65], v[64:65], v[120:121]
	v_pk_add_f32 v[102:103], v[102:103], v[66:67]
	v_pk_add_f32 v[104:105], v[104:105], v[66:67]
	v_pk_add_f32 v[118:119], v[118:119], v[66:67]
	v_cvt_pk_f16_f32 v65, v64, v65
	v_cvt_pk_f16_f32 v76, v76, v77
	v_cvt_pk_f16_f32 v77, v94, v95
	v_cvt_pk_f16_f32 v95, v102, v103
	s_waitcnt vmcnt(0)
	v_pk_add_f32 v[106:107], v[106:107], v[28:29]
	v_pk_add_f32 v[108:109], v[108:109], v[30:31]
	v_cvt_pk_f16_f32 v97, v124, v125
	v_cvt_pk_f16_f32 v102, v104, v105
	v_cvt_pk_f16_f32 v103, v118, v119
	v_pack_b32_f16 v64, v82, v65
	v_alignbit_b32 v65, v49, v65, 16
	v_pack_b32_f16 v94, v98, v95
	v_alignbit_b32 v95, v41, v95, 16
	v_add_f32_e32 v78, v78, v28
	v_cvt_pk_f16_f32 v106, v106, v107
	v_cvt_pk_f16_f32 v107, v108, v109
	ds_write2_b64 v130, v[74:75], v[96:97] offset1:4
	ds_write_b64 v130, v[106:107] offset:64
	v_pack_b32_f16 v74, v50, v76
	v_alignbit_b32 v75, v85, v76, 16
	v_pack_b32_f16 v76, v90, v77
	v_alignbit_b32 v77, v93, v77, 16
	v_pack_b32_f16 v96, v42, v102
	v_alignbit_b32 v97, v101, v102, 16
	v_pack_b32_f16 v102, v122, v103
	v_alignbit_b32 v103, v123, v103, 16
	ds_write2_b64 v132, v[64:65], v[94:95] offset0:32 offset1:36
	ds_write2_b64 v131, v[74:75], v[96:97] offset0:64 offset1:68
	ds_write2_b64 v91, v[76:77], v[102:103] offset0:96 offset1:100
	v_pk_mov_b32 v[64:65], v[28:29], v[30:31] op_sel:[1,0]
	v_add_f32_e32 v29, v81, v31
	v_cvt_f16_f32_e32 v78, v78
	v_cvt_f16_f32_e32 v29, v29
	v_mov_b32_e32 v74, v79
	v_mov_b32_e32 v75, v80
	v_pk_add_f32 v[74:75], v[74:75], v[64:65]
	v_add_f32_e32 v56, v56, v48
	v_cvt_pk_f16_f32 v30, v74, v75
	v_pack_b32_f16 v74, v78, v30
	v_alignbit_b32 v75, v29, v30, 16
	v_add_f32_e32 v29, v86, v28
	v_add_f32_e32 v30, v89, v31
	v_cvt_f16_f32_e32 v29, v29
	v_cvt_f16_f32_e32 v30, v30
	ds_write_b64 v130, v[74:75] offset:12608
	v_mov_b32_e32 v74, v87
	v_mov_b32_e32 v75, v88
	v_pk_add_f32 v[74:75], v[74:75], v[64:65]
	v_add_f32_e32 v52, v52, v48
	v_cvt_pk_f16_f32 v41, v74, v75
	v_pack_b32_f16 v74, v29, v41
	v_alignbit_b32 v75, v30, v41, 16
	v_add_f32_e32 v29, v60, v28
	v_add_f32_e32 v30, v63, v31
	v_cvt_f16_f32_e32 v29, v29
	v_cvt_f16_f32_e32 v30, v30
	v_mov_b32_e32 v60, v61
	v_mov_b32_e32 v61, v62
	v_pk_add_f32 v[60:61], v[60:61], v[64:65]
	ds_write_b64 v130, v[74:75] offset:25152
	v_cvt_pk_f16_f32 v41, v60, v61
	v_pack_b32_f16 v60, v29, v41
	v_alignbit_b32 v61, v30, v41, 16
	ds_write_b64 v130, v[60:61] offset:37696
	s_waitcnt lgkmcnt(0)
	s_barrier
	ds_read_b128 v[60:63], v83
	ds_read_b128 v[74:77], v84
	v_add_u32_e32 v29, 0x300, v111
	v_add_u32_e32 v30, v29, v112
	v_add_f32_e32 v44, v44, v48
	s_waitcnt lgkmcnt(1)
	buffer_store_dwordx4 v[60:63], v30, s[0:3], 0 offen sc1
	v_add_u32_e32 v30, 0x300, v113
	ds_read_b128 v[60:63], v92
	v_add_u32_e32 v41, v30, v114
	s_waitcnt lgkmcnt(1)
	buffer_store_dwordx4 v[74:77], v41, s[0:3], 0 offen sc1
	ds_read_b128 v[74:77], v99
	v_add_u32_e32 v41, 0x300, v115
	v_add_u32_e32 v42, v41, v116
	s_waitcnt lgkmcnt(1)
	buffer_store_dwordx4 v[60:63], v42, s[0:3], 0 offen sc1
	v_add_u32_e32 v42, 0x300, v117
	ds_read_b128 v[60:63], v100
	v_add_u32_e32 v49, v42, v142
	s_waitcnt lgkmcnt(1)
	buffer_store_dwordx4 v[74:77], v49, s[0:3], 0 offen sc1
	ds_read_b128 v[74:77], v110
	v_add_u32_e32 v49, 0x300, v144
	v_add_u32_e32 v50, v49, v143
	s_waitcnt lgkmcnt(1)
	buffer_store_dwordx4 v[60:63], v50, s[0:3], 0 offen sc1
	v_add_u32_e32 v50, 0x300, v145
	v_add_f32_e32 v36, v36, v48
	v_add_u32_e32 v60, v50, v146
	s_waitcnt lgkmcnt(0)
	buffer_store_dwordx4 v[74:77], v60, s[0:3], 0 offen sc1
	v_cvt_f16_f32_e32 v60, v56
	v_mov_b32_e32 v56, v57
	v_mov_b32_e32 v57, v58
	v_add_f32_e32 v58, v59, v51
	v_cvt_f16_f32_e32 v58, v58
	v_pk_add_f32 v[56:57], v[56:57], v[120:121]
	v_add_f32_e32 v32, v32, v40
	v_cvt_pk_f16_f32 v57, v56, v57
	v_pack_b32_f16 v56, v60, v57
	v_alignbit_b32 v57, v58, v57, 16
	v_cvt_f16_f32_e32 v58, v52
	v_mov_b32_e32 v52, v53
	v_mov_b32_e32 v53, v54
	v_add_f32_e32 v54, v55, v51
	v_cvt_f16_f32_e32 v54, v54
	v_pk_add_f32 v[52:53], v[52:53], v[120:121]
	v_add_f32_e32 v24, v24, v40
	v_cvt_pk_f16_f32 v53, v52, v53
	v_pack_b32_f16 v52, v58, v53
	v_alignbit_b32 v53, v54, v53, 16
	v_cvt_f16_f32_e32 v54, v44
	v_mov_b32_e32 v44, v45
	v_mov_b32_e32 v45, v46
	v_add_f32_e32 v46, v47, v51
	v_cvt_f16_f32_e32 v46, v46
	v_pk_add_f32 v[44:45], v[44:45], v[120:121]
	s_nop 0
	v_cvt_pk_f16_f32 v45, v44, v45
	v_pack_b32_f16 v44, v54, v45
	v_alignbit_b32 v45, v46, v45, 16
	v_cvt_f16_f32_e32 v46, v36
	v_mov_b32_e32 v36, v37
	v_mov_b32_e32 v37, v38
	v_add_f32_e32 v38, v39, v51
	v_cvt_f16_f32_e32 v38, v38
	v_pk_add_f32 v[36:37], v[36:37], v[120:121]
	s_barrier
	v_cvt_pk_f16_f32 v37, v36, v37
	v_pack_b32_f16 v36, v46, v37
	v_alignbit_b32 v37, v38, v37, 16
	v_cvt_f16_f32_e32 v38, v32
	v_mov_b32_e32 v32, v33
	v_mov_b32_e32 v33, v34
	v_add_f32_e32 v34, v35, v43
	v_cvt_f16_f32_e32 v34, v34
	v_pk_add_f32 v[32:33], v[32:33], v[66:67]
	s_nop 0
	v_cvt_pk_f16_f32 v33, v32, v33
	v_pack_b32_f16 v32, v38, v33
	v_alignbit_b32 v33, v34, v33, 16
	ds_write2_b64 v130, v[56:57], v[32:33] offset1:4
	v_cvt_f16_f32_e32 v32, v24
	v_mov_b32_e32 v24, v25
	v_mov_b32_e32 v25, v26
	v_add_f32_e32 v26, v27, v43
	v_cvt_f16_f32_e32 v26, v26
	v_pk_add_f32 v[24:25], v[24:25], v[66:67]
	v_add_f32_e32 v20, v20, v40
	v_cvt_pk_f16_f32 v25, v24, v25
	v_pack_b32_f16 v24, v32, v25
	v_alignbit_b32 v25, v26, v25, 16
	ds_write2_b64 v132, v[52:53], v[24:25] offset0:32 offset1:36
	v_cvt_f16_f32_e32 v24, v20
	v_mov_b32_e32 v20, v21
	v_mov_b32_e32 v21, v22
	v_add_f32_e32 v22, v23, v43
	v_cvt_f16_f32_e32 v22, v22
	v_pk_add_f32 v[20:21], v[20:21], v[66:67]
	v_add_f32_e32 v16, v16, v40
	v_cvt_pk_f16_f32 v21, v20, v21
	v_pack_b32_f16 v20, v24, v21
	v_alignbit_b32 v21, v22, v21, 16
	ds_write2_b64 v131, v[44:45], v[20:21] offset0:64 offset1:68
	v_cvt_f16_f32_e32 v20, v16
	v_mov_b32_e32 v16, v17
	v_mov_b32_e32 v17, v18
	v_add_f32_e32 v18, v19, v43
	v_cvt_f16_f32_e32 v18, v18
	v_pk_add_f32 v[16:17], v[16:17], v[66:67]
	v_add_f32_e32 v12, v12, v28
	v_cvt_pk_f16_f32 v17, v16, v17
	v_pack_b32_f16 v16, v20, v17
	v_alignbit_b32 v17, v18, v17, 16
	ds_write2_b64 v91, v[36:37], v[16:17] offset0:96 offset1:100
	v_cvt_f16_f32_e32 v16, v12
	v_mov_b32_e32 v12, v13
	v_mov_b32_e32 v13, v14
	v_add_f32_e32 v14, v15, v31
	v_cvt_f16_f32_e32 v14, v14
	v_pk_add_f32 v[12:13], v[12:13], v[64:65]
	v_add_f32_e32 v8, v8, v28
	v_cvt_pk_f16_f32 v13, v12, v13
	v_pack_b32_f16 v12, v16, v13
	v_alignbit_b32 v13, v14, v13, 16
	ds_write_b64 v130, v[12:13] offset:64
	v_cvt_f16_f32_e32 v12, v8
	v_mov_b32_e32 v8, v9
	v_mov_b32_e32 v9, v10
	v_add_f32_e32 v10, v11, v31
	v_cvt_f16_f32_e32 v10, v10
	v_pk_add_f32 v[8:9], v[8:9], v[64:65]
	v_add_f32_e32 v4, v4, v28
	v_cvt_pk_f16_f32 v9, v8, v9
	v_pack_b32_f16 v8, v12, v9
	v_alignbit_b32 v9, v10, v9, 16
	ds_write_b64 v130, v[8:9] offset:12608
	v_cvt_f16_f32_e32 v8, v4
	v_mov_b32_e32 v4, v5
	v_mov_b32_e32 v5, v6
	v_add_f32_e32 v6, v7, v31
	v_cvt_f16_f32_e32 v6, v6
	v_pk_add_f32 v[4:5], v[4:5], v[64:65]
	v_add_f32_e32 v0, v0, v28
	v_cvt_pk_f16_f32 v5, v4, v5
	v_pack_b32_f16 v4, v8, v5
	v_alignbit_b32 v5, v6, v5, 16
	ds_write_b64 v130, v[4:5] offset:25152
	v_cvt_f16_f32_e32 v4, v0
	v_mov_b32_e32 v0, v1
	v_mov_b32_e32 v1, v2
	v_add_f32_e32 v2, v3, v31
	v_cvt_f16_f32_e32 v2, v2
	v_pk_add_f32 v[0:1], v[0:1], v[64:65]
	v_add_u32_e32 v8, v29, v68
	v_cvt_pk_f16_f32 v1, v0, v1
	v_pack_b32_f16 v0, v4, v1
	v_alignbit_b32 v1, v2, v1, 16
	ds_write_b64 v130, v[0:1] offset:37696
	s_waitcnt lgkmcnt(0)
	s_barrier
	ds_read_b128 v[0:3], v83
	ds_read_b128 v[4:7], v84
	v_add_u32_e32 v12, v42, v70
	s_waitcnt lgkmcnt(1)
	buffer_store_dwordx4 v[0:3], v8, s[0:3], 0 offen sc1
	ds_read_b128 v[0:3], v92
	v_add_u32_e32 v8, v30, v69
	s_waitcnt lgkmcnt(1)
	buffer_store_dwordx4 v[4:7], v8, s[0:3], 0 offen sc1
	v_add_u32_e32 v8, v41, v72
	ds_read_b128 v[4:7], v99
	s_waitcnt lgkmcnt(1)
	buffer_store_dwordx4 v[0:3], v8, s[0:3], 0 offen sc1
	ds_read_b128 v[0:3], v100
	ds_read_b128 v[8:11], v110
	s_waitcnt lgkmcnt(2)
	buffer_store_dwordx4 v[4:7], v12, s[0:3], 0 offen sc1
	s_nop 1
	v_add_u32_e32 v4, v49, v71
	s_waitcnt lgkmcnt(1)
	buffer_store_dwordx4 v[0:3], v4, s[0:3], 0 offen sc1
	s_nop 1
	v_add_u32_e32 v0, v50, v73
	s_waitcnt lgkmcnt(0)
	buffer_store_dwordx4 v[8:11], v0, s[0:3], 0 offen sc1
	s_endpgm
	.p2alignl 8, 3212836864

_Z7k_stageILi1ELi4EEv8AttnArgsPKDF16_PKfPDF16_iii:
	v_readfirstlane_b32 s94, v0
	s_nop 0
	s_lshr_b32 s94, s94, 6
	s_load_dwordx2 s[80:81], s[0:1], 0x70
	s_load_dwordx2 s[82:83], s[0:1], 0x88
	v_and_b32_e32 v255, 63, v0
	v_lshlrev_b32_e32 v255, 7, v255
	s_load_dwordx4 s[28:31], s[0:1], 0x70
	s_load_dwordx2 s[24:25], s[0:1], 0x80
	s_load_dword s33, s[0:1], 0x90
	s_lshl_b32 s4, s2, 5
	s_and_b32 s45, s4, 0xe0
	s_lshr_b32 s4, s2, 3
	s_add_i32 s45, s45, s4
	s_and_b32 s44, s2, 56
	v_readfirstlane_b32 s3, v0
	v_and_b32_e32 v1, 15, v0
	s_waitcnt lgkmcnt(0)
	s_mul_i32 s84, s3, s83
	s_add_i32 s84, s84, s82
	s_mul_i32 s84, s84, 0x60000
	s_mul_i32 s85, s94, 0x6000
	s_add_u32 s84, s84, s85
	s_add_u32 s80, s80, s84
	s_addc_u32 s81, s81, 0
	s_cmp_lt_i32 s33, 1
	v_bfe_u32 v167, v0, 4, 2
	s_cbranch_scc1 .LBB4_155
	s_lshr_b32 s2, s3, 2
	v_lshrrev_b32_e32 v7, 7, v0
	v_lshrrev_b32_e32 v2, 5, v0
	v_lshrrev_b32_e32 v3, 4, v0
	s_and_b32 s2, s2, 16
	v_lshrrev_b32_e32 v4, 6, v0
	v_and_b32_e32 v7, 1, v7
	v_and_b32_e32 v2, 4, v2
	v_or_b32_e32 v179, s2, v1
	v_and_b32_e32 v5, 4, v4
	s_load_dwordx2 s[40:41], s[0:1], 0x60
	s_bitcmp1_b32 s3, 6
	v_lshlrev_b16_e32 v7, 2, v7
	v_and_b32_e32 v8, 3, v3
	s_load_dwordx4 s[36:39], s[0:1], 0x0
	s_load_dwordx2 s[4:5], s[0:1], 0x10
	s_load_dwordx8 s[8:15], s[0:1], 0x18
	s_load_dwordx2 s[6:7], s[0:1], 0x38
	s_load_dwordx8 s[16:23], s[0:1], 0x40
	v_or_b32_e32 v178, v2, v167
	v_and_or_b32 v180, s45, 56, v5
	s_cselect_b64 s[26:27], -1, 0
	s_and_b32 s3, s45, 0x3ffffc0
	v_bitop3_b16 v3, v7, v3, 3 bitop3:0xf8
	v_bitop3_b16 v7, v7, 8, v8 bitop3:0xfe
	v_lshlrev_b32_e32 v8, 12, v5
	v_bitop3_b32 v2, v2, v179, v167 bitop3:0x36
	v_or_b32_e32 v6, s3, v180
	s_and_b32 s3, s45, 0x1ffc0
	v_and_b32_e32 v3, 0xffff, v3
	v_lshl_or_b32 v184, v2, 4, v8
	v_lshlrev_b32_e32 v2, 3, v5
	v_mov_b32_e32 v169, 0
	v_lshlrev_b32_e32 v168, 5, v179
	v_lshlrev_b32_e32 v181, 6, v6
	v_or_b32_e32 v6, s3, v180
	v_and_b32_e32 v7, 0xffff, v7
	v_or_b32_e32 v186, 8, v2
	v_or_b32_e32 v188, 16, v2
	v_bitop3_b32 v2, s2, v3, v1 bitop3:0x36
	v_lshlrev_b32_e32 v166, 3, v179
	s_waitcnt lgkmcnt(0)
	v_lshl_add_u64 v[170:171], s[38:39], 0, v[168:169]
	s_mov_b32 s39, 0x20000
	v_lshlrev_b32_e32 v189, 4, v2
	v_bitop3_b32 v2, s2, v7, v1 bitop3:0x36
	v_lshlrev_b32_e32 v193, 15, v6
	v_lshl_add_u64 v[172:173], s[4:5], 0, v[168:169]
	s_and_b32 s37, s37, 0xffff
	s_mov_b32 s38, 0x1800000
	v_add_u32_e32 v182, -1, v180
	v_add_u32_e32 v183, 4, v180
	v_lshl_add_u64 v[174:175], s[14:15], 0, v[168:169]
	v_lshl_add_u64 v[176:177], s[6:7], 0, v[168:169]
	s_and_b32 s13, s13, 0xffff
	s_mov_b32 s42, 0x800000
	s_mov_b32 s43, s39
	s_and_b32 s41, s41, 0xffff
	v_or_b32_e32 v185, 64, v181
	v_or_b32_e32 v187, 0x80, v181
	v_or_b32_e32 v190, 0xc0, v181
	v_lshl_or_b32 v191, v4, 3, 24
	v_lshlrev_b32_e32 v192, 4, v2
	v_lshlrev_b32_e32 v194, 4, v179
	v_or_b32_e32 v195, 0x8000, v193
	v_or_b32_e32 v196, 0x10000, v193
	v_or_b32_e32 v197, 0x18000, v193
	s_mov_b32 s46, 0
	s_movk_i32 s47, 0x300
	v_lshlrev_b32_e32 v198, 1, v166
	s_branch .LBB4_4
.LBB4_2:
	s_waitcnt vmcnt(3)
	v_pk_mul_f16 v161, v160, v162 op_sel_hi:[0,1]
	v_pk_mul_f16 v206, v160, v165 op_sel_hi:[0,1]
	v_pk_mul_f16 v210, v158, v165 op_sel_hi:[0,1]
	v_pk_mul_f16 v214, v159, v165 op_sel_hi:[0,1]
	v_pk_mul_f16 v200, v160, v163 op_sel_hi:[0,1]
	v_pk_mul_f16 v201, v160, v164 op_sel_hi:[0,1]
	v_pk_mul_f16 v207, v158, v162 op_sel_hi:[0,1]
	s_mov_b64 exec, s[64:65]
	buffer_load_dwordx4 v[26:29], v245, s[12:15], 0 offen
	buffer_load_dwordx4 v[10:13], v245, s[12:15], 0 offen offset:512
	s_mov_b64 exec, -1
	v_pk_mul_f16 v208, v158, v163 op_sel_hi:[0,1]
	v_pk_mul_f16 v209, v158, v164 op_sel_hi:[0,1]
	v_pk_mul_f16 v211, v159, v162 op_sel_hi:[0,1]
	v_pk_mul_f16 v212, v159, v163 op_sel_hi:[0,1]
	v_pk_mul_f16 v213, v159, v164 op_sel_hi:[0,1]
	v_pk_fma_f16 v117, v117, v165, v206
	v_pk_fma_f16 v114, v114, v162, v161
	v_pk_fma_f16 v133, v133, v165, v206
	v_pk_fma_f16 v130, v130, v162, v161
	v_pk_fma_f16 v141, v141, v165, v206
	v_pk_fma_f16 v138, v138, v162, v161
	v_pk_fma_f16 v161, v89, v165, v210
	v_pk_fma_f16 v215, v113, v165, v210
	buffer_load_dwordx4 v[38:41], v246, s[12:15], 0 offen offset:512
	buffer_load_dwordx4 v[14:17], v246, s[12:15], 0 offen offset:1024
	v_pk_fma_f16 v210, v129, v165, v210
	v_pk_fma_f16 v219, v57, v165, v214
	v_pk_fma_f16 v223, v77, v165, v214
	v_pk_fma_f16 v165, v101, v165, v214
	v_pk_maximum3_f16 v214, v117, v133, v141
	v_pk_fma_f16 v116, v116, v164, v201
	v_pk_fma_f16 v115, v115, v163, v200
	v_pk_fma_f16 v132, v132, v164, v201
	v_pk_fma_f16 v131, v131, v163, v200
	v_pk_fma_f16 v140, v140, v164, v201
	v_pk_fma_f16 v139, v139, v163, v200
	v_pk_fma_f16 v200, v88, v164, v209
	v_pk_fma_f16 v201, v87, v163, v208
	v_pk_fma_f16 v206, v86, v162, v207
	v_pk_fma_f16 v216, v112, v164, v209
	v_pk_fma_f16 v217, v111, v163, v208
	s_mov_b64 exec, s[66:67]
	buffer_load_dwordx4 v[58:61], v246, s[12:15], 0 offen offset:2048
	buffer_load_dwordx4 v[18:21], v246, s[12:15], 0 offen offset:2560
	s_mov_b64 exec, -1
	v_pk_fma_f16 v218, v110, v162, v207
	v_pk_fma_f16 v209, v128, v164, v209
	v_pk_fma_f16 v208, v127, v163, v208
	v_pk_fma_f16 v207, v126, v162, v207
	v_pk_fma_f16 v220, v56, v164, v213
	v_pk_fma_f16 v221, v55, v163, v212
	v_pk_fma_f16 v222, v54, v162, v211
	v_pk_fma_f16 v224, v76, v164, v213
	v_pk_fma_f16 v225, v75, v163, v212
	v_pk_fma_f16 v226, v74, v162, v211
	v_pk_fma_f16 v164, v100, v164, v213
	v_pk_fma_f16 v163, v99, v163, v212
	v_pk_fma_f16 v162, v98, v162, v211
	v_pk_maximum3_f16 v211, v114, v130, v138
	v_pk_maximum3_f16 v212, v115, v131, v139
	v_pk_maximum3_f16 v213, v116, v132, v140
	v_pk_maximum3_f16 v230, v161, v215, v210
	v_pk_maximum3_f16 v234, v219, v223, v165
	v_pk_maximum3_f16 v227, v206, v218, v207
	v_pk_maximum3_f16 v228, v201, v217, v208
	v_pk_maximum3_f16 v229, v200, v216, v209
	v_pk_maximum3_f16 v231, v222, v226, v162
	v_pk_maximum3_f16 v232, v221, v225, v163
	v_pk_maximum3_f16 v214, v214, v230, v234
	v_pk_maximum3_f16 v233, v220, v224, v164
	v_pk_maximum3_f16 v211, v211, v227, v231
	v_pk_maximum3_f16 v212, v212, v228, v232
	v_pk_maximum3_f16 v213, v213, v229, v233
	v_pk_add_f16 v117, v117, v214 neg_lo:[0,1] neg_hi:[0,1]
	s_mov_b64 exec, s[64:65]
	buffer_load_dwordx4 v[78:81], v247, s[12:15], 0 offen
	buffer_load_dwordx4 v[30:33], v247, s[12:15], 0 offen offset:512
	s_mov_b64 exec, -1
	v_pk_add_f16 v114, v114, v211 neg_lo:[0,1] neg_hi:[0,1]
	v_pk_add_f16 v115, v115, v212 neg_lo:[0,1] neg_hi:[0,1]
	v_pk_add_f16 v116, v116, v213 neg_lo:[0,1] neg_hi:[0,1]
	v_pk_add_f16 v130, v130, v211 neg_lo:[0,1] neg_hi:[0,1]
	v_exp_f16_sdwa v227, v114 dst_sel:WORD_0 dst_unused:UNUSED_PAD src0_sel:WORD_0
	v_exp_f16_sdwa v228, v115 dst_sel:WORD_0 dst_unused:UNUSED_PAD src0_sel:WORD_0
	v_exp_f16_sdwa v229, v116 dst_sel:WORD_0 dst_unused:UNUSED_PAD src0_sel:WORD_0
	v_exp_f16_sdwa v230, v117 dst_sel:WORD_0 dst_unused:UNUSED_PAD src0_sel:WORD_0
	v_exp_f16_sdwa v227, v114 dst_sel:WORD_1 dst_unused:UNUSED_PRESERVE src0_sel:WORD_1
	v_exp_f16_sdwa v228, v115 dst_sel:WORD_1 dst_unused:UNUSED_PRESERVE src0_sel:WORD_1
	v_exp_f16_sdwa v229, v116 dst_sel:WORD_1 dst_unused:UNUSED_PRESERVE src0_sel:WORD_1
	v_exp_f16_sdwa v230, v117 dst_sel:WORD_1 dst_unused:UNUSED_PRESERVE src0_sel:WORD_1
	v_pk_add_f16 v131, v131, v212 neg_lo:[0,1] neg_hi:[0,1]
	v_pk_add_f16 v117, v227, 0
	v_pk_fma_f16 v73, v73, v230, 0
	v_pk_add_f16 v114, v230, 0
	v_pk_add_f16 v115, v229, 0
	v_pk_add_f16 v116, v228, 0
	v_pk_fma_f16 v72, v72, v229, 0
	v_pk_fma_f16 v71, v71, v228, 0
	v_pk_fma_f16 v70, v70, v227, 0
	v_pk_add_f16 v132, v132, v213 neg_lo:[0,1] neg_hi:[0,1]
	buffer_load_dwordx4 v[106:109], v248, s[12:15], 0 offen offset:512
	buffer_load_dwordx4 v[46:49], v248, s[12:15], 0 offen offset:1024
	v_pk_add_f16 v133, v133, v214 neg_lo:[0,1] neg_hi:[0,1]
	v_exp_f16_sdwa v227, v130 dst_sel:WORD_0 dst_unused:UNUSED_PAD src0_sel:WORD_0
	v_exp_f16_sdwa v228, v131 dst_sel:WORD_0 dst_unused:UNUSED_PAD src0_sel:WORD_0
	v_exp_f16_sdwa v229, v132 dst_sel:WORD_0 dst_unused:UNUSED_PAD src0_sel:WORD_0
	v_exp_f16_sdwa v230, v133 dst_sel:WORD_0 dst_unused:UNUSED_PAD src0_sel:WORD_0
	v_exp_f16_sdwa v227, v130 dst_sel:WORD_1 dst_unused:UNUSED_PRESERVE src0_sel:WORD_1
	v_exp_f16_sdwa v228, v131 dst_sel:WORD_1 dst_unused:UNUSED_PRESERVE src0_sel:WORD_1
	v_exp_f16_sdwa v229, v132 dst_sel:WORD_1 dst_unused:UNUSED_PRESERVE src0_sel:WORD_1
	v_exp_f16_sdwa v230, v133 dst_sel:WORD_1 dst_unused:UNUSED_PRESERVE src0_sel:WORD_1
	v_pk_add_f16 v117, v117, v227
	v_pk_fma_f16 v73, v97, v230, v73
	v_pk_add_f16 v97, v141, v214 neg_lo:[0,1] neg_hi:[0,1]
	v_pk_add_f16 v116, v116, v228
	v_pk_add_f16 v115, v115, v229
	v_pk_add_f16 v114, v114, v230
	v_pk_fma_f16 v70, v94, v227, v70
	v_pk_fma_f16 v71, v95, v228, v71
	v_pk_fma_f16 v72, v96, v229, v72
	v_pk_add_f16 v94, v138, v211 neg_lo:[0,1] neg_hi:[0,1]
	v_pk_add_f16 v95, v139, v212 neg_lo:[0,1] neg_hi:[0,1]
	v_pk_add_f16 v96, v140, v213 neg_lo:[0,1] neg_hi:[0,1]
	v_exp_f16_sdwa v130, v94 dst_sel:WORD_0 dst_unused:UNUSED_PAD src0_sel:WORD_0
	v_exp_f16_sdwa v131, v95 dst_sel:WORD_0 dst_unused:UNUSED_PAD src0_sel:WORD_0
	v_exp_f16_sdwa v132, v96 dst_sel:WORD_0 dst_unused:UNUSED_PAD src0_sel:WORD_0
	v_exp_f16_sdwa v133, v97 dst_sel:WORD_0 dst_unused:UNUSED_PAD src0_sel:WORD_0
	v_exp_f16_sdwa v130, v94 dst_sel:WORD_1 dst_unused:UNUSED_PRESERVE src0_sel:WORD_1
	v_exp_f16_sdwa v131, v95 dst_sel:WORD_1 dst_unused:UNUSED_PRESERVE src0_sel:WORD_1
	v_exp_f16_sdwa v132, v96 dst_sel:WORD_1 dst_unused:UNUSED_PRESERVE src0_sel:WORD_1
	v_exp_f16_sdwa v133, v97 dst_sel:WORD_1 dst_unused:UNUSED_PRESERVE src0_sel:WORD_1
	v_pk_add_f16 v97, v117, v130
	v_pk_add_f16 v94, v114, v133
	s_mov_b64 exec, s[66:67]
	buffer_load_dwordx4 v[122:125], v248, s[12:15], 0 offen offset:2048
	buffer_load_dwordx4 v[62:65], v248, s[12:15], 0 offen offset:2560
	s_mov_b64 exec, -1
	v_pk_add_f16 v95, v115, v132
	v_pk_add_f16 v96, v116, v131
	v_pk_fma_f16 v73, v121, v133, v73
	v_pk_fma_f16 v72, v120, v132, v72
	v_pk_fma_f16 v71, v119, v131, v71
	v_pk_fma_f16 v70, v118, v130, v70
	v_pk_add_f16 v114, v206, v211 neg_lo:[0,1] neg_hi:[0,1]
	v_pk_add_f16 v115, v201, v212 neg_lo:[0,1] neg_hi:[0,1]
	v_pk_add_f16 v116, v200, v213 neg_lo:[0,1] neg_hi:[0,1]
	v_pk_add_f16 v117, v161, v214 neg_lo:[0,1] neg_hi:[0,1]
	v_exp_f16_sdwa v118, v114 dst_sel:WORD_0 dst_unused:UNUSED_PAD src0_sel:WORD_0
	v_exp_f16_sdwa v119, v115 dst_sel:WORD_0 dst_unused:UNUSED_PAD src0_sel:WORD_0
	v_exp_f16_sdwa v120, v116 dst_sel:WORD_0 dst_unused:UNUSED_PAD src0_sel:WORD_0
	v_exp_f16_sdwa v121, v117 dst_sel:WORD_0 dst_unused:UNUSED_PAD src0_sel:WORD_0
	v_exp_f16_sdwa v118, v114 dst_sel:WORD_1 dst_unused:UNUSED_PRESERVE src0_sel:WORD_1
	v_exp_f16_sdwa v119, v115 dst_sel:WORD_1 dst_unused:UNUSED_PRESERVE src0_sel:WORD_1
	v_exp_f16_sdwa v120, v116 dst_sel:WORD_1 dst_unused:UNUSED_PRESERVE src0_sel:WORD_1
	v_exp_f16_sdwa v121, v117 dst_sel:WORD_1 dst_unused:UNUSED_PRESERVE src0_sel:WORD_1
	v_pk_add_f16 v114, v218, v211 neg_lo:[0,1] neg_hi:[0,1]
	v_pk_add_f16 v97, v97, v118
	v_pk_add_f16 v96, v96, v119
	v_pk_add_f16 v95, v95, v120
	s_mov_b64 exec, s[76:77]
	buffer_load_dwordx4 v[134:137], v249, s[12:15], 0 offen
	buffer_load_dwordx4 v[82:85], v249, s[12:15], 0 offen offset:512
	s_mov_b64 exec, -1
	v_pk_add_f16 v94, v94, v121
	v_pk_fma_f16 v70, v42, v118, v70
	v_pk_fma_f16 v71, v43, v119, v71
	v_pk_fma_f16 v72, v44, v120, v72
	v_pk_fma_f16 v73, v45, v121, v73
	v_pk_add_f16 v115, v217, v212 neg_lo:[0,1] neg_hi:[0,1]
	v_pk_add_f16 v116, v216, v213 neg_lo:[0,1] neg_hi:[0,1]
	v_pk_add_f16 v117, v215, v214 neg_lo:[0,1] neg_hi:[0,1]
	v_exp_f16_sdwa v118, v114 dst_sel:WORD_0 dst_unused:UNUSED_PAD src0_sel:WORD_0
	v_exp_f16_sdwa v119, v115 dst_sel:WORD_0 dst_unused:UNUSED_PAD src0_sel:WORD_0
	v_exp_f16_sdwa v120, v116 dst_sel:WORD_0 dst_unused:UNUSED_PAD src0_sel:WORD_0
	v_exp_f16_sdwa v121, v117 dst_sel:WORD_0 dst_unused:UNUSED_PAD src0_sel:WORD_0
	v_exp_f16_sdwa v118, v114 dst_sel:WORD_1 dst_unused:UNUSED_PRESERVE src0_sel:WORD_1
	v_exp_f16_sdwa v119, v115 dst_sel:WORD_1 dst_unused:UNUSED_PRESERVE src0_sel:WORD_1
	v_exp_f16_sdwa v120, v116 dst_sel:WORD_1 dst_unused:UNUSED_PRESERVE src0_sel:WORD_1
	v_exp_f16_sdwa v121, v117 dst_sel:WORD_1 dst_unused:UNUSED_PRESERVE src0_sel:WORD_1
	v_pk_add_f16 v114, v207, v211 neg_lo:[0,1] neg_hi:[0,1]
	v_pk_add_f16 v97, v97, v118
	v_pk_add_f16 v94, v94, v121
	v_pk_add_f16 v95, v95, v120
	v_pk_add_f16 v96, v96, v119
	v_pk_fma_f16 v73, v69, v121, v73
	v_pk_fma_f16 v72, v68, v120, v72
	s_mov_b64 exec, s[70:71]
	buffer_load_dwordx4 v[142:145], v250, s[12:15], 0 offen offset:512
	buffer_load_dwordx4 v[102:105], v250, s[12:15], 0 offen offset:1024
	s_mov_b64 exec, -1
	v_pk_fma_f16 v71, v67, v119, v71
	v_pk_fma_f16 v70, v66, v118, v70
	v_pk_add_f16 v115, v208, v212 neg_lo:[0,1] neg_hi:[0,1]
	v_pk_add_f16 v116, v209, v213 neg_lo:[0,1] neg_hi:[0,1]
	v_pk_add_f16 v117, v210, v214 neg_lo:[0,1] neg_hi:[0,1]
	v_exp_f16_sdwa v118, v114 dst_sel:WORD_0 dst_unused:UNUSED_PAD src0_sel:WORD_0
	v_exp_f16_sdwa v119, v115 dst_sel:WORD_0 dst_unused:UNUSED_PAD src0_sel:WORD_0
	v_exp_f16_sdwa v120, v116 dst_sel:WORD_0 dst_unused:UNUSED_PAD src0_sel:WORD_0
	v_exp_f16_sdwa v121, v117 dst_sel:WORD_0 dst_unused:UNUSED_PAD src0_sel:WORD_0
	v_exp_f16_sdwa v118, v114 dst_sel:WORD_1 dst_unused:UNUSED_PRESERVE src0_sel:WORD_1
	v_exp_f16_sdwa v119, v115 dst_sel:WORD_1 dst_unused:UNUSED_PRESERVE src0_sel:WORD_1
	v_exp_f16_sdwa v120, v116 dst_sel:WORD_1 dst_unused:UNUSED_PRESERVE src0_sel:WORD_1
	v_exp_f16_sdwa v121, v117 dst_sel:WORD_1 dst_unused:UNUSED_PRESERVE src0_sel:WORD_1
	v_pk_add_f16 v114, v222, v211 neg_lo:[0,1] neg_hi:[0,1]
	v_pk_add_f16 v97, v97, v118
	v_pk_add_f16 v96, v96, v119
	v_pk_add_f16 v95, v95, v120
	v_pk_add_f16 v94, v94, v121
	v_pk_fma_f16 v70, v90, v118, v70
	v_pk_fma_f16 v71, v91, v119, v71
	v_pk_fma_f16 v72, v92, v120, v72
	v_pk_fma_f16 v73, v93, v121, v73
	s_mov_b64 exec, s[78:79]
	buffer_load_dwordx4 v[6:9], v250, s[12:15], 0 offen offset:2048
	buffer_load_dwordx4 v[2:5], v250, s[12:15], 0 offen offset:2560
	s_mov_b64 exec, -1
	v_pk_add_f16 v115, v221, v212 neg_lo:[0,1] neg_hi:[0,1]
	v_pk_add_f16 v116, v220, v213 neg_lo:[0,1] neg_hi:[0,1]
	v_pk_add_f16 v117, v219, v214 neg_lo:[0,1] neg_hi:[0,1]
	v_exp_f16_sdwa v118, v114 dst_sel:WORD_0 dst_unused:UNUSED_PAD src0_sel:WORD_0
	v_exp_f16_sdwa v119, v115 dst_sel:WORD_0 dst_unused:UNUSED_PAD src0_sel:WORD_0
	v_exp_f16_sdwa v120, v116 dst_sel:WORD_0 dst_unused:UNUSED_PAD src0_sel:WORD_0
	v_exp_f16_sdwa v121, v117 dst_sel:WORD_0 dst_unused:UNUSED_PAD src0_sel:WORD_0
	v_exp_f16_sdwa v118, v114 dst_sel:WORD_1 dst_unused:UNUSED_PRESERVE src0_sel:WORD_1
	v_exp_f16_sdwa v119, v115 dst_sel:WORD_1 dst_unused:UNUSED_PRESERVE src0_sel:WORD_1
	v_exp_f16_sdwa v120, v116 dst_sel:WORD_1 dst_unused:UNUSED_PRESERVE src0_sel:WORD_1
	v_exp_f16_sdwa v121, v117 dst_sel:WORD_1 dst_unused:UNUSED_PRESERVE src0_sel:WORD_1
	v_pk_add_f16 v114, v226, v211 neg_lo:[0,1] neg_hi:[0,1]
	v_pk_add_f16 v97, v97, v118
	v_pk_add_f16 v94, v94, v121
	v_pk_add_f16 v95, v95, v120
	v_pk_add_f16 v96, v96, v119
	v_pk_fma_f16 v73, v25, v121, v73
	v_pk_fma_f16 v72, v24, v120, v72
	v_pk_fma_f16 v71, v23, v119, v71
	v_pk_fma_f16 v70, v22, v118, v70
	v_pk_add_f16 v115, v225, v212 neg_lo:[0,1] neg_hi:[0,1]
	v_pk_add_f16 v116, v224, v213 neg_lo:[0,1] neg_hi:[0,1]
	v_pk_add_f16 v117, v223, v214 neg_lo:[0,1] neg_hi:[0,1]
	v_exp_f16_sdwa v118, v114 dst_sel:WORD_0 dst_unused:UNUSED_PAD src0_sel:WORD_0
	v_exp_f16_sdwa v119, v115 dst_sel:WORD_0 dst_unused:UNUSED_PAD src0_sel:WORD_0
	v_exp_f16_sdwa v120, v116 dst_sel:WORD_0 dst_unused:UNUSED_PAD src0_sel:WORD_0
	v_exp_f16_sdwa v121, v117 dst_sel:WORD_0 dst_unused:UNUSED_PAD src0_sel:WORD_0
	v_exp_f16_sdwa v118, v114 dst_sel:WORD_1 dst_unused:UNUSED_PRESERVE src0_sel:WORD_1
	v_exp_f16_sdwa v119, v115 dst_sel:WORD_1 dst_unused:UNUSED_PRESERVE src0_sel:WORD_1
	v_exp_f16_sdwa v120, v116 dst_sel:WORD_1 dst_unused:UNUSED_PRESERVE src0_sel:WORD_1
	v_exp_f16_sdwa v121, v117 dst_sel:WORD_1 dst_unused:UNUSED_PRESERVE src0_sel:WORD_1
	v_pk_add_f16 v114, v162, v211 neg_lo:[0,1] neg_hi:[0,1]
	v_pk_add_f16 v97, v97, v118
	v_pk_add_f16 v96, v96, v119
	v_pk_add_f16 v95, v95, v120
	v_pk_add_f16 v94, v94, v121
	v_pk_fma_f16 v70, v34, v118, v70
	v_pk_fma_f16 v71, v35, v119, v71
	v_pk_fma_f16 v72, v36, v120, v72
	v_pk_fma_f16 v73, v37, v121, v73
	v_pk_add_f16 v115, v163, v212 neg_lo:[0,1] neg_hi:[0,1]
	v_pk_add_f16 v116, v164, v213 neg_lo:[0,1] neg_hi:[0,1]
	v_pk_add_f16 v117, v165, v214 neg_lo:[0,1] neg_hi:[0,1]
	v_exp_f16_sdwa v118, v114 dst_sel:WORD_0 dst_unused:UNUSED_PAD src0_sel:WORD_0
	v_exp_f16_sdwa v119, v115 dst_sel:WORD_0 dst_unused:UNUSED_PAD src0_sel:WORD_0
	v_exp_f16_sdwa v120, v116 dst_sel:WORD_0 dst_unused:UNUSED_PAD src0_sel:WORD_0
	v_exp_f16_sdwa v121, v117 dst_sel:WORD_0 dst_unused:UNUSED_PAD src0_sel:WORD_0
	v_exp_f16_sdwa v118, v114 dst_sel:WORD_1 dst_unused:UNUSED_PRESERVE src0_sel:WORD_1
	v_exp_f16_sdwa v119, v115 dst_sel:WORD_1 dst_unused:UNUSED_PRESERVE src0_sel:WORD_1
	v_exp_f16_sdwa v120, v116 dst_sel:WORD_1 dst_unused:UNUSED_PRESERVE src0_sel:WORD_1
	v_exp_f16_sdwa v121, v117 dst_sel:WORD_1 dst_unused:UNUSED_PRESERVE src0_sel:WORD_1
	v_pk_add_f16 v97, v97, v118
	v_pk_add_f16 v96, v96, v119
	v_rcp_f16_e32 v114, v97
	v_rcp_f16_sdwa v97, v97 dst_sel:DWORD dst_unused:UNUSED_PAD src0_sel:WORD_1
	v_pk_add_f16 v95, v95, v120
	v_rcp_f16_e32 v115, v96
	v_rcp_f16_sdwa v96, v96 dst_sel:DWORD dst_unused:UNUSED_PAD src0_sel:WORD_1
	v_pk_add_f16 v94, v94, v121
	v_rcp_f16_e32 v116, v95
	v_rcp_f16_sdwa v95, v95 dst_sel:DWORD dst_unused:UNUSED_PAD src0_sel:WORD_1
	v_rcp_f16_e32 v117, v94
	v_rcp_f16_sdwa v94, v94 dst_sel:DWORD dst_unused:UNUSED_PAD src0_sel:WORD_1
	v_pk_fma_f16 v70, v50, v118, v70
	v_pack_b32_f16 v97, v114, v97
	v_pk_fma_f16 v71, v51, v119, v71
	v_pk_mul_f16 v141, v70, v97
	v_pack_b32_f16 v70, v115, v96
	v_pk_fma_f16 v72, v52, v120, v72
	v_pk_mul_f16 v140, v71, v70
	v_pack_b32_f16 v70, v116, v95
	v_pk_fma_f16 v73, v53, v121, v73
	v_pk_mul_f16 v139, v72, v70
	v_pack_b32_f16 v70, v117, v94
	v_pk_mul_f16 v138, v73, v70
	s_waitcnt vmcnt(12)
	v_pk_mul_f16 v70, v160, v154 op_sel_hi:[0,1]
	v_pk_mul_f16 v73, v160, v157 op_sel_hi:[0,1]
	v_pk_mul_f16 v97, v158, v157 op_sel_hi:[0,1]
	v_pk_mul_f16 v117, v159, v157 op_sel_hi:[0,1]
	v_pk_mul_f16 v71, v160, v155 op_sel_hi:[0,1]
	v_pk_mul_f16 v72, v160, v156 op_sel_hi:[0,1]
	v_pk_mul_f16 v94, v158, v154 op_sel_hi:[0,1]
	v_pk_mul_f16 v95, v158, v155 op_sel_hi:[0,1]
	v_pk_mul_f16 v96, v158, v156 op_sel_hi:[0,1]
	v_pk_mul_f16 v114, v159, v154 op_sel_hi:[0,1]
	v_pk_mul_f16 v115, v159, v155 op_sel_hi:[0,1]
	v_pk_mul_f16 v116, v159, v156 op_sel_hi:[0,1]
	v_pk_fma_f16 v89, v89, v157, v73
	v_pk_fma_f16 v86, v86, v154, v70
	v_pk_fma_f16 v113, v113, v157, v73
	v_pk_fma_f16 v110, v110, v154, v70
	v_pk_fma_f16 v73, v129, v157, v73
	v_pk_fma_f16 v70, v126, v154, v70
	v_pk_fma_f16 v118, v57, v157, v97
	v_pk_fma_f16 v126, v77, v157, v97
	v_pk_fma_f16 v97, v101, v157, v97
	v_pk_fma_f16 v130, v29, v157, v117
	v_pk_fma_f16 v161, v41, v157, v117
	v_pk_fma_f16 v117, v61, v157, v117
	v_pk_maximum3_f16 v157, v89, v113, v73
	v_pk_fma_f16 v88, v88, v156, v72
	v_pk_fma_f16 v87, v87, v155, v71
	v_pk_fma_f16 v112, v112, v156, v72
	v_pk_fma_f16 v111, v111, v155, v71
	v_pk_fma_f16 v72, v128, v156, v72
	v_pk_fma_f16 v71, v127, v155, v71
	v_pk_fma_f16 v119, v56, v156, v96
	v_pk_fma_f16 v120, v55, v155, v95
	v_pk_fma_f16 v121, v54, v154, v94
	v_pk_fma_f16 v127, v76, v156, v96
	v_pk_fma_f16 v128, v75, v155, v95
	v_pk_fma_f16 v129, v74, v154, v94
	v_pk_fma_f16 v96, v100, v156, v96
	v_pk_fma_f16 v95, v99, v155, v95
	v_pk_fma_f16 v94, v98, v154, v94
	v_pk_fma_f16 v131, v28, v156, v116
	v_pk_fma_f16 v132, v27, v155, v115
	v_pk_fma_f16 v133, v26, v154, v114
	v_pk_fma_f16 v162, v40, v156, v116
	v_pk_fma_f16 v163, v39, v155, v115
	v_pk_fma_f16 v164, v38, v154, v114
	v_pk_fma_f16 v116, v60, v156, v116
	v_pk_fma_f16 v115, v59, v155, v115
	v_pk_fma_f16 v114, v58, v154, v114
	v_pk_maximum3_f16 v154, v86, v110, v70
	v_pk_maximum3_f16 v155, v87, v111, v71
	v_pk_maximum3_f16 v156, v88, v112, v72
	v_pk_maximum3_f16 v206, v118, v126, v97
	v_pk_maximum3_f16 v210, v130, v161, v117
	v_pk_maximum3_f16 v165, v121, v129, v94
	v_pk_maximum3_f16 v200, v120, v128, v95
	v_pk_maximum3_f16 v201, v119, v127, v96
	v_pk_maximum3_f16 v207, v133, v164, v114
	v_pk_maximum3_f16 v208, v132, v163, v115
	v_pk_maximum3_f16 v157, v157, v206, v210
	v_pk_maximum3_f16 v209, v131, v162, v116
	v_pk_maximum3_f16 v154, v154, v165, v207
	v_pk_maximum3_f16 v155, v155, v200, v208
	v_pk_maximum3_f16 v156, v156, v201, v209
	v_pk_add_f16 v89, v89, v157 neg_lo:[0,1] neg_hi:[0,1]
	v_pk_add_f16 v86, v86, v154 neg_lo:[0,1] neg_hi:[0,1]
	v_pk_add_f16 v87, v87, v155 neg_lo:[0,1] neg_hi:[0,1]
	v_pk_add_f16 v88, v88, v156 neg_lo:[0,1] neg_hi:[0,1]
	v_pk_add_f16 v110, v110, v154 neg_lo:[0,1] neg_hi:[0,1]
	v_exp_f16_sdwa v165, v86 dst_sel:WORD_0 dst_unused:UNUSED_PAD src0_sel:WORD_0
	v_exp_f16_sdwa v200, v87 dst_sel:WORD_0 dst_unused:UNUSED_PAD src0_sel:WORD_0
	v_exp_f16_sdwa v201, v88 dst_sel:WORD_0 dst_unused:UNUSED_PAD src0_sel:WORD_0
	v_exp_f16_sdwa v206, v89 dst_sel:WORD_0 dst_unused:UNUSED_PAD src0_sel:WORD_0
	v_exp_f16_sdwa v165, v86 dst_sel:WORD_1 dst_unused:UNUSED_PRESERVE src0_sel:WORD_1
	v_exp_f16_sdwa v200, v87 dst_sel:WORD_1 dst_unused:UNUSED_PRESERVE src0_sel:WORD_1
	v_exp_f16_sdwa v201, v88 dst_sel:WORD_1 dst_unused:UNUSED_PRESERVE src0_sel:WORD_1
	v_exp_f16_sdwa v206, v89 dst_sel:WORD_1 dst_unused:UNUSED_PRESERVE src0_sel:WORD_1
	v_pk_add_f16 v111, v111, v155 neg_lo:[0,1] neg_hi:[0,1]
	v_pk_add_f16 v89, v165, 0
	v_pk_fma_f16 v45, v45, v206, 0
	v_pk_add_f16 v86, v206, 0
	v_pk_add_f16 v87, v201, 0
	v_pk_add_f16 v88, v200, 0
	v_pk_fma_f16 v44, v44, v201, 0
	v_pk_fma_f16 v43, v43, v200, 0
	v_pk_fma_f16 v42, v42, v165, 0
	v_pk_add_f16 v112, v112, v156 neg_lo:[0,1] neg_hi:[0,1]
	v_pk_add_f16 v113, v113, v157 neg_lo:[0,1] neg_hi:[0,1]
	v_exp_f16_sdwa v165, v110 dst_sel:WORD_0 dst_unused:UNUSED_PAD src0_sel:WORD_0
	v_exp_f16_sdwa v200, v111 dst_sel:WORD_0 dst_unused:UNUSED_PAD src0_sel:WORD_0
	v_exp_f16_sdwa v201, v112 dst_sel:WORD_0 dst_unused:UNUSED_PAD src0_sel:WORD_0
	v_exp_f16_sdwa v206, v113 dst_sel:WORD_0 dst_unused:UNUSED_PAD src0_sel:WORD_0
	v_exp_f16_sdwa v165, v110 dst_sel:WORD_1 dst_unused:UNUSED_PRESERVE src0_sel:WORD_1
	v_exp_f16_sdwa v200, v111 dst_sel:WORD_1 dst_unused:UNUSED_PRESERVE src0_sel:WORD_1
	v_exp_f16_sdwa v201, v112 dst_sel:WORD_1 dst_unused:UNUSED_PRESERVE src0_sel:WORD_1
	v_exp_f16_sdwa v206, v113 dst_sel:WORD_1 dst_unused:UNUSED_PRESERVE src0_sel:WORD_1
	v_pk_add_f16 v89, v89, v165
	v_pk_fma_f16 v45, v69, v206, v45
	v_pk_add_f16 v69, v73, v157 neg_lo:[0,1] neg_hi:[0,1]
	v_pk_add_f16 v88, v88, v200
	v_pk_add_f16 v87, v87, v201
	v_pk_add_f16 v86, v86, v206
	v_pk_fma_f16 v42, v66, v165, v42
	v_pk_fma_f16 v43, v67, v200, v43
	v_pk_fma_f16 v44, v68, v201, v44
	v_pk_add_f16 v66, v70, v154 neg_lo:[0,1] neg_hi:[0,1]
	v_pk_add_f16 v67, v71, v155 neg_lo:[0,1] neg_hi:[0,1]
	v_pk_add_f16 v68, v72, v156 neg_lo:[0,1] neg_hi:[0,1]
	v_exp_f16_sdwa v70, v66 dst_sel:WORD_0 dst_unused:UNUSED_PAD src0_sel:WORD_0
	v_exp_f16_sdwa v71, v67 dst_sel:WORD_0 dst_unused:UNUSED_PAD src0_sel:WORD_0
	v_exp_f16_sdwa v72, v68 dst_sel:WORD_0 dst_unused:UNUSED_PAD src0_sel:WORD_0
	v_exp_f16_sdwa v73, v69 dst_sel:WORD_0 dst_unused:UNUSED_PAD src0_sel:WORD_0
	v_exp_f16_sdwa v70, v66 dst_sel:WORD_1 dst_unused:UNUSED_PRESERVE src0_sel:WORD_1
	v_exp_f16_sdwa v71, v67 dst_sel:WORD_1 dst_unused:UNUSED_PRESERVE src0_sel:WORD_1
	v_exp_f16_sdwa v72, v68 dst_sel:WORD_1 dst_unused:UNUSED_PRESERVE src0_sel:WORD_1
	v_exp_f16_sdwa v73, v69 dst_sel:WORD_1 dst_unused:UNUSED_PRESERVE src0_sel:WORD_1
	v_pk_add_f16 v69, v89, v70
	v_pk_add_f16 v66, v86, v73
	v_pk_add_f16 v67, v87, v72
	v_pk_add_f16 v68, v88, v71
	v_pk_fma_f16 v45, v93, v73, v45
	v_pk_fma_f16 v44, v92, v72, v44
	v_pk_fma_f16 v43, v91, v71, v43
	v_pk_fma_f16 v42, v90, v70, v42
	v_pk_add_f16 v70, v121, v154 neg_lo:[0,1] neg_hi:[0,1]
	v_pk_add_f16 v71, v120, v155 neg_lo:[0,1] neg_hi:[0,1]
	v_pk_add_f16 v72, v119, v156 neg_lo:[0,1] neg_hi:[0,1]
	v_pk_add_f16 v73, v118, v157 neg_lo:[0,1] neg_hi:[0,1]
	v_exp_f16_sdwa v86, v70 dst_sel:WORD_0 dst_unused:UNUSED_PAD src0_sel:WORD_0
	v_exp_f16_sdwa v87, v71 dst_sel:WORD_0 dst_unused:UNUSED_PAD src0_sel:WORD_0
	v_exp_f16_sdwa v88, v72 dst_sel:WORD_0 dst_unused:UNUSED_PAD src0_sel:WORD_0
	v_exp_f16_sdwa v89, v73 dst_sel:WORD_0 dst_unused:UNUSED_PAD src0_sel:WORD_0
	v_exp_f16_sdwa v86, v70 dst_sel:WORD_1 dst_unused:UNUSED_PRESERVE src0_sel:WORD_1
	v_exp_f16_sdwa v87, v71 dst_sel:WORD_1 dst_unused:UNUSED_PRESERVE src0_sel:WORD_1
	v_exp_f16_sdwa v88, v72 dst_sel:WORD_1 dst_unused:UNUSED_PRESERVE src0_sel:WORD_1
	v_exp_f16_sdwa v89, v73 dst_sel:WORD_1 dst_unused:UNUSED_PRESERVE src0_sel:WORD_1
	v_pk_add_f16 v70, v129, v154 neg_lo:[0,1] neg_hi:[0,1]
	v_pk_add_f16 v69, v69, v86
	v_pk_add_f16 v68, v68, v87
	v_pk_add_f16 v67, v67, v88
	v_pk_add_f16 v66, v66, v89
	v_pk_fma_f16 v42, v22, v86, v42
	v_pk_fma_f16 v43, v23, v87, v43
	v_pk_fma_f16 v44, v24, v88, v44
	v_pk_fma_f16 v45, v25, v89, v45
	v_pk_add_f16 v71, v128, v155 neg_lo:[0,1] neg_hi:[0,1]
	v_pk_add_f16 v72, v127, v156 neg_lo:[0,1] neg_hi:[0,1]
	v_pk_add_f16 v73, v126, v157 neg_lo:[0,1] neg_hi:[0,1]
	v_exp_f16_sdwa v86, v70 dst_sel:WORD_0 dst_unused:UNUSED_PAD src0_sel:WORD_0
	v_exp_f16_sdwa v87, v71 dst_sel:WORD_0 dst_unused:UNUSED_PAD src0_sel:WORD_0
	v_exp_f16_sdwa v88, v72 dst_sel:WORD_0 dst_unused:UNUSED_PAD src0_sel:WORD_0
	v_exp_f16_sdwa v89, v73 dst_sel:WORD_0 dst_unused:UNUSED_PAD src0_sel:WORD_0
	v_exp_f16_sdwa v86, v70 dst_sel:WORD_1 dst_unused:UNUSED_PRESERVE src0_sel:WORD_1
	v_exp_f16_sdwa v87, v71 dst_sel:WORD_1 dst_unused:UNUSED_PRESERVE src0_sel:WORD_1
	v_exp_f16_sdwa v88, v72 dst_sel:WORD_1 dst_unused:UNUSED_PRESERVE src0_sel:WORD_1
	v_exp_f16_sdwa v89, v73 dst_sel:WORD_1 dst_unused:UNUSED_PRESERVE src0_sel:WORD_1
	v_pk_add_f16 v70, v94, v154 neg_lo:[0,1] neg_hi:[0,1]
	v_pk_add_f16 v69, v69, v86
	v_pk_add_f16 v66, v66, v89
	v_pk_add_f16 v67, v67, v88
	v_pk_add_f16 v68, v68, v87
	v_pk_fma_f16 v45, v37, v89, v45
	v_pk_fma_f16 v44, v36, v88, v44
	v_pk_fma_f16 v43, v35, v87, v43
	v_pk_fma_f16 v42, v34, v86, v42
	v_pk_add_f16 v71, v95, v155 neg_lo:[0,1] neg_hi:[0,1]
	v_pk_add_f16 v72, v96, v156 neg_lo:[0,1] neg_hi:[0,1]
	v_pk_add_f16 v73, v97, v157 neg_lo:[0,1] neg_hi:[0,1]
	v_exp_f16_sdwa v86, v70 dst_sel:WORD_0 dst_unused:UNUSED_PAD src0_sel:WORD_0
	v_exp_f16_sdwa v87, v71 dst_sel:WORD_0 dst_unused:UNUSED_PAD src0_sel:WORD_0
	v_exp_f16_sdwa v88, v72 dst_sel:WORD_0 dst_unused:UNUSED_PAD src0_sel:WORD_0
	v_exp_f16_sdwa v89, v73 dst_sel:WORD_0 dst_unused:UNUSED_PAD src0_sel:WORD_0
	v_exp_f16_sdwa v86, v70 dst_sel:WORD_1 dst_unused:UNUSED_PRESERVE src0_sel:WORD_1
	v_exp_f16_sdwa v87, v71 dst_sel:WORD_1 dst_unused:UNUSED_PRESERVE src0_sel:WORD_1
	v_exp_f16_sdwa v88, v72 dst_sel:WORD_1 dst_unused:UNUSED_PRESERVE src0_sel:WORD_1
	v_exp_f16_sdwa v89, v73 dst_sel:WORD_1 dst_unused:UNUSED_PRESERVE src0_sel:WORD_1
	v_pk_add_f16 v70, v133, v154 neg_lo:[0,1] neg_hi:[0,1]
	v_pk_add_f16 v69, v69, v86
	v_pk_add_f16 v68, v68, v87
	v_pk_add_f16 v67, v67, v88
	v_pk_add_f16 v66, v66, v89
	v_pk_fma_f16 v42, v50, v86, v42
	v_pk_fma_f16 v43, v51, v87, v43
	v_pk_fma_f16 v44, v52, v88, v44
	v_pk_fma_f16 v45, v53, v89, v45
	v_pk_add_f16 v71, v132, v155 neg_lo:[0,1] neg_hi:[0,1]
	v_pk_add_f16 v72, v131, v156 neg_lo:[0,1] neg_hi:[0,1]
	v_pk_add_f16 v73, v130, v157 neg_lo:[0,1] neg_hi:[0,1]
	v_exp_f16_sdwa v86, v70 dst_sel:WORD_0 dst_unused:UNUSED_PAD src0_sel:WORD_0
	v_exp_f16_sdwa v87, v71 dst_sel:WORD_0 dst_unused:UNUSED_PAD src0_sel:WORD_0
	v_exp_f16_sdwa v88, v72 dst_sel:WORD_0 dst_unused:UNUSED_PAD src0_sel:WORD_0
	v_exp_f16_sdwa v89, v73 dst_sel:WORD_0 dst_unused:UNUSED_PAD src0_sel:WORD_0
	v_exp_f16_sdwa v86, v70 dst_sel:WORD_1 dst_unused:UNUSED_PRESERVE src0_sel:WORD_1
	v_exp_f16_sdwa v87, v71 dst_sel:WORD_1 dst_unused:UNUSED_PRESERVE src0_sel:WORD_1
	v_exp_f16_sdwa v88, v72 dst_sel:WORD_1 dst_unused:UNUSED_PRESERVE src0_sel:WORD_1
	v_exp_f16_sdwa v89, v73 dst_sel:WORD_1 dst_unused:UNUSED_PRESERVE src0_sel:WORD_1
	v_pk_add_f16 v70, v164, v154 neg_lo:[0,1] neg_hi:[0,1]
	v_pk_add_f16 v69, v69, v86
	v_pk_add_f16 v66, v66, v89
	v_pk_add_f16 v67, v67, v88
	v_pk_add_f16 v68, v68, v87
	v_pk_fma_f16 v45, v13, v89, v45
	v_pk_fma_f16 v44, v12, v88, v44
	v_pk_fma_f16 v43, v11, v87, v43
	v_pk_fma_f16 v42, v10, v86, v42
	v_pk_add_f16 v71, v163, v155 neg_lo:[0,1] neg_hi:[0,1]
	v_pk_add_f16 v72, v162, v156 neg_lo:[0,1] neg_hi:[0,1]
	v_pk_add_f16 v73, v161, v157 neg_lo:[0,1] neg_hi:[0,1]
	v_exp_f16_sdwa v86, v70 dst_sel:WORD_0 dst_unused:UNUSED_PAD src0_sel:WORD_0
	v_exp_f16_sdwa v87, v71 dst_sel:WORD_0 dst_unused:UNUSED_PAD src0_sel:WORD_0
	v_exp_f16_sdwa v88, v72 dst_sel:WORD_0 dst_unused:UNUSED_PAD src0_sel:WORD_0
	v_exp_f16_sdwa v89, v73 dst_sel:WORD_0 dst_unused:UNUSED_PAD src0_sel:WORD_0
	v_exp_f16_sdwa v86, v70 dst_sel:WORD_1 dst_unused:UNUSED_PRESERVE src0_sel:WORD_1
	v_exp_f16_sdwa v87, v71 dst_sel:WORD_1 dst_unused:UNUSED_PRESERVE src0_sel:WORD_1
	v_exp_f16_sdwa v88, v72 dst_sel:WORD_1 dst_unused:UNUSED_PRESERVE src0_sel:WORD_1
	v_exp_f16_sdwa v89, v73 dst_sel:WORD_1 dst_unused:UNUSED_PRESERVE src0_sel:WORD_1
	v_pk_add_f16 v70, v114, v154 neg_lo:[0,1] neg_hi:[0,1]
	v_pk_add_f16 v69, v69, v86
	v_pk_add_f16 v68, v68, v87
	v_pk_add_f16 v67, v67, v88
	v_pk_add_f16 v66, v66, v89
	v_pk_fma_f16 v42, v14, v86, v42
	v_pk_fma_f16 v43, v15, v87, v43
	v_pk_fma_f16 v44, v16, v88, v44
	v_pk_fma_f16 v45, v17, v89, v45
	v_pk_add_f16 v71, v115, v155 neg_lo:[0,1] neg_hi:[0,1]
	v_pk_add_f16 v72, v116, v156 neg_lo:[0,1] neg_hi:[0,1]
	v_pk_add_f16 v73, v117, v157 neg_lo:[0,1] neg_hi:[0,1]
	v_exp_f16_sdwa v86, v70 dst_sel:WORD_0 dst_unused:UNUSED_PAD src0_sel:WORD_0
	v_exp_f16_sdwa v87, v71 dst_sel:WORD_0 dst_unused:UNUSED_PAD src0_sel:WORD_0
	v_exp_f16_sdwa v88, v72 dst_sel:WORD_0 dst_unused:UNUSED_PAD src0_sel:WORD_0
	v_exp_f16_sdwa v89, v73 dst_sel:WORD_0 dst_unused:UNUSED_PAD src0_sel:WORD_0
	v_exp_f16_sdwa v86, v70 dst_sel:WORD_1 dst_unused:UNUSED_PRESERVE src0_sel:WORD_1
	v_exp_f16_sdwa v87, v71 dst_sel:WORD_1 dst_unused:UNUSED_PRESERVE src0_sel:WORD_1
	v_exp_f16_sdwa v88, v72 dst_sel:WORD_1 dst_unused:UNUSED_PRESERVE src0_sel:WORD_1
	v_exp_f16_sdwa v89, v73 dst_sel:WORD_1 dst_unused:UNUSED_PRESERVE src0_sel:WORD_1
	v_pk_add_f16 v69, v69, v86
	v_pk_add_f16 v68, v68, v87
	v_rcp_f16_e32 v70, v69
	v_rcp_f16_sdwa v69, v69 dst_sel:DWORD dst_unused:UNUSED_PAD src0_sel:WORD_1
	v_pk_add_f16 v67, v67, v88
	v_rcp_f16_e32 v71, v68
	v_rcp_f16_sdwa v68, v68 dst_sel:DWORD dst_unused:UNUSED_PAD src0_sel:WORD_1
	v_pk_add_f16 v66, v66, v89
	v_rcp_f16_e32 v72, v67
	v_rcp_f16_sdwa v67, v67 dst_sel:DWORD dst_unused:UNUSED_PAD src0_sel:WORD_1
	v_rcp_f16_e32 v73, v66
	v_rcp_f16_sdwa v66, v66 dst_sel:DWORD dst_unused:UNUSED_PAD src0_sel:WORD_1
	v_pk_fma_f16 v42, v18, v86, v42
	v_pack_b32_f16 v69, v70, v69
	v_pk_fma_f16 v43, v19, v87, v43
	v_pk_mul_f16 v97, v42, v69
	v_pack_b32_f16 v42, v71, v68
	v_pk_fma_f16 v44, v20, v88, v44
	v_pk_mul_f16 v96, v43, v42
	v_pack_b32_f16 v42, v72, v67
	v_pk_fma_f16 v45, v21, v89, v45
	v_pk_mul_f16 v95, v44, v42
	v_pack_b32_f16 v42, v73, v66
	v_pk_mul_f16 v94, v45, v42
	s_waitcnt vmcnt(6)
	v_pk_mul_f16 v45, v160, v153 op_sel_hi:[0,1]
	v_pk_mul_f16 v42, v160, v150 op_sel_hi:[0,1]
	v_pk_mul_f16 v43, v160, v151 op_sel_hi:[0,1]
	v_pk_mul_f16 v44, v160, v152 op_sel_hi:[0,1]
	v_pk_mul_f16 v69, v158, v153 op_sel_hi:[0,1]
	v_pk_mul_f16 v73, v159, v153 op_sel_hi:[0,1]
	v_pk_fma_f16 v57, v57, v153, v45
	v_pk_fma_f16 v77, v77, v153, v45
	v_pk_fma_f16 v45, v101, v153, v45
	v_pk_mul_f16 v66, v158, v150 op_sel_hi:[0,1]
	v_pk_maximum3_f16 v117, v57, v77, v45
	v_pk_mul_f16 v67, v158, v151 op_sel_hi:[0,1]
	v_pk_mul_f16 v68, v158, v152 op_sel_hi:[0,1]
	v_pk_mul_f16 v70, v159, v150 op_sel_hi:[0,1]
	v_pk_mul_f16 v71, v159, v151 op_sel_hi:[0,1]
	v_pk_mul_f16 v72, v159, v152 op_sel_hi:[0,1]
	v_pk_fma_f16 v56, v56, v152, v44
	v_pk_fma_f16 v55, v55, v151, v43
	v_pk_fma_f16 v54, v54, v150, v42
	v_pk_fma_f16 v76, v76, v152, v44
	v_pk_fma_f16 v75, v75, v151, v43
	v_pk_fma_f16 v74, v74, v150, v42
	v_pk_fma_f16 v44, v100, v152, v44
	v_pk_fma_f16 v43, v99, v151, v43
	v_pk_fma_f16 v42, v98, v150, v42
	v_pk_fma_f16 v86, v29, v153, v69
	v_pk_fma_f16 v90, v41, v153, v69
	v_pk_fma_f16 v69, v61, v153, v69
	v_pk_fma_f16 v98, v81, v153, v73
	v_pk_fma_f16 v110, v109, v153, v73
	v_pk_fma_f16 v73, v125, v153, v73
	v_pk_maximum3_f16 v114, v54, v74, v42
	v_pk_maximum3_f16 v115, v55, v75, v43
	v_pk_maximum3_f16 v116, v56, v76, v44
	v_pk_maximum3_f16 v121, v86, v90, v69
	v_pk_fma_f16 v87, v28, v152, v68
	v_pk_maximum3_f16 v129, v98, v110, v73
	v_pk_fma_f16 v88, v27, v151, v67
	v_pk_maximum3_f16 v117, v117, v121, v129
	v_pk_fma_f16 v89, v26, v150, v66
	v_pk_fma_f16 v91, v40, v152, v68
	v_pk_fma_f16 v92, v39, v151, v67
	v_pk_fma_f16 v93, v38, v150, v66
	v_pk_fma_f16 v68, v60, v152, v68
	v_pk_fma_f16 v67, v59, v151, v67
	v_pk_fma_f16 v66, v58, v150, v66
	v_pk_fma_f16 v99, v80, v152, v72
	v_pk_fma_f16 v100, v79, v151, v71
	v_pk_fma_f16 v101, v78, v150, v70
	v_pk_fma_f16 v111, v108, v152, v72
	v_pk_fma_f16 v112, v107, v151, v71
	v_pk_fma_f16 v113, v106, v150, v70
	v_pk_fma_f16 v72, v124, v152, v72
	v_pk_fma_f16 v71, v123, v151, v71
	v_pk_fma_f16 v70, v122, v150, v70
	v_pk_maximum3_f16 v118, v89, v93, v66
	v_pk_maximum3_f16 v119, v88, v92, v67
	v_pk_maximum3_f16 v120, v87, v91, v68
	v_pk_maximum3_f16 v127, v100, v112, v71
	v_pk_maximum3_f16 v128, v99, v111, v72
	v_pk_maximum3_f16 v126, v101, v113, v70
	v_pk_maximum3_f16 v114, v114, v118, v126
	v_pk_maximum3_f16 v115, v115, v119, v127
	v_pk_maximum3_f16 v116, v116, v120, v128
	v_pk_add_f16 v57, v57, v117 neg_lo:[0,1] neg_hi:[0,1]
	v_pk_add_f16 v54, v54, v114 neg_lo:[0,1] neg_hi:[0,1]
	v_pk_add_f16 v55, v55, v115 neg_lo:[0,1] neg_hi:[0,1]
	v_pk_add_f16 v56, v56, v116 neg_lo:[0,1] neg_hi:[0,1]
	v_pk_add_f16 v74, v74, v114 neg_lo:[0,1] neg_hi:[0,1]
	v_exp_f16_sdwa v118, v54 dst_sel:WORD_0 dst_unused:UNUSED_PAD src0_sel:WORD_0
	v_exp_f16_sdwa v119, v55 dst_sel:WORD_0 dst_unused:UNUSED_PAD src0_sel:WORD_0
	v_exp_f16_sdwa v120, v56 dst_sel:WORD_0 dst_unused:UNUSED_PAD src0_sel:WORD_0
	v_exp_f16_sdwa v121, v57 dst_sel:WORD_0 dst_unused:UNUSED_PAD src0_sel:WORD_0
	v_exp_f16_sdwa v118, v54 dst_sel:WORD_1 dst_unused:UNUSED_PRESERVE src0_sel:WORD_1
	v_exp_f16_sdwa v119, v55 dst_sel:WORD_1 dst_unused:UNUSED_PRESERVE src0_sel:WORD_1
	v_exp_f16_sdwa v120, v56 dst_sel:WORD_1 dst_unused:UNUSED_PRESERVE src0_sel:WORD_1
	v_exp_f16_sdwa v121, v57 dst_sel:WORD_1 dst_unused:UNUSED_PRESERVE src0_sel:WORD_1
	v_pk_add_f16 v75, v75, v115 neg_lo:[0,1] neg_hi:[0,1]
	v_pk_add_f16 v57, v118, 0
	v_pk_fma_f16 v25, v25, v121, 0
	v_pk_add_f16 v54, v121, 0
	v_pk_add_f16 v55, v120, 0
	v_pk_add_f16 v56, v119, 0
	v_pk_fma_f16 v24, v24, v120, 0
	v_pk_fma_f16 v23, v23, v119, 0
	v_pk_fma_f16 v22, v22, v118, 0
	v_pk_add_f16 v76, v76, v116 neg_lo:[0,1] neg_hi:[0,1]
	v_pk_add_f16 v77, v77, v117 neg_lo:[0,1] neg_hi:[0,1]
	v_exp_f16_sdwa v118, v74 dst_sel:WORD_0 dst_unused:UNUSED_PAD src0_sel:WORD_0
	v_exp_f16_sdwa v119, v75 dst_sel:WORD_0 dst_unused:UNUSED_PAD src0_sel:WORD_0
	v_exp_f16_sdwa v120, v76 dst_sel:WORD_0 dst_unused:UNUSED_PAD src0_sel:WORD_0
	v_exp_f16_sdwa v121, v77 dst_sel:WORD_0 dst_unused:UNUSED_PAD src0_sel:WORD_0
	v_exp_f16_sdwa v118, v74 dst_sel:WORD_1 dst_unused:UNUSED_PRESERVE src0_sel:WORD_1
	v_exp_f16_sdwa v119, v75 dst_sel:WORD_1 dst_unused:UNUSED_PRESERVE src0_sel:WORD_1
	v_exp_f16_sdwa v120, v76 dst_sel:WORD_1 dst_unused:UNUSED_PRESERVE src0_sel:WORD_1
	v_exp_f16_sdwa v121, v77 dst_sel:WORD_1 dst_unused:UNUSED_PRESERVE src0_sel:WORD_1
	v_pk_add_f16 v57, v57, v118
	v_pk_fma_f16 v25, v37, v121, v25
	v_pk_add_f16 v37, v45, v117 neg_lo:[0,1] neg_hi:[0,1]
	v_pk_add_f16 v56, v56, v119
	v_pk_add_f16 v55, v55, v120
	v_pk_add_f16 v54, v54, v121
	v_pk_fma_f16 v22, v34, v118, v22
	v_pk_fma_f16 v23, v35, v119, v23
	v_pk_fma_f16 v24, v36, v120, v24
	v_pk_add_f16 v34, v42, v114 neg_lo:[0,1] neg_hi:[0,1]
	v_pk_add_f16 v35, v43, v115 neg_lo:[0,1] neg_hi:[0,1]
	v_pk_add_f16 v36, v44, v116 neg_lo:[0,1] neg_hi:[0,1]
	v_exp_f16_sdwa v42, v34 dst_sel:WORD_0 dst_unused:UNUSED_PAD src0_sel:WORD_0
	v_exp_f16_sdwa v43, v35 dst_sel:WORD_0 dst_unused:UNUSED_PAD src0_sel:WORD_0
	v_exp_f16_sdwa v44, v36 dst_sel:WORD_0 dst_unused:UNUSED_PAD src0_sel:WORD_0
	v_exp_f16_sdwa v45, v37 dst_sel:WORD_0 dst_unused:UNUSED_PAD src0_sel:WORD_0
	v_exp_f16_sdwa v42, v34 dst_sel:WORD_1 dst_unused:UNUSED_PRESERVE src0_sel:WORD_1
	v_exp_f16_sdwa v43, v35 dst_sel:WORD_1 dst_unused:UNUSED_PRESERVE src0_sel:WORD_1
	v_exp_f16_sdwa v44, v36 dst_sel:WORD_1 dst_unused:UNUSED_PRESERVE src0_sel:WORD_1
	v_exp_f16_sdwa v45, v37 dst_sel:WORD_1 dst_unused:UNUSED_PRESERVE src0_sel:WORD_1
	v_pk_add_f16 v37, v57, v42
	v_pk_add_f16 v34, v54, v45
	v_pk_add_f16 v35, v55, v44
	v_pk_add_f16 v36, v56, v43
	v_pk_fma_f16 v25, v53, v45, v25
	v_pk_fma_f16 v24, v52, v44, v24
	v_pk_fma_f16 v23, v51, v43, v23
	v_pk_fma_f16 v22, v50, v42, v22
	v_pk_add_f16 v42, v89, v114 neg_lo:[0,1] neg_hi:[0,1]
	v_pk_add_f16 v43, v88, v115 neg_lo:[0,1] neg_hi:[0,1]
	v_pk_add_f16 v44, v87, v116 neg_lo:[0,1] neg_hi:[0,1]
	v_pk_add_f16 v45, v86, v117 neg_lo:[0,1] neg_hi:[0,1]
	v_exp_f16_sdwa v50, v42 dst_sel:WORD_0 dst_unused:UNUSED_PAD src0_sel:WORD_0
	v_exp_f16_sdwa v51, v43 dst_sel:WORD_0 dst_unused:UNUSED_PAD src0_sel:WORD_0
	v_exp_f16_sdwa v52, v44 dst_sel:WORD_0 dst_unused:UNUSED_PAD src0_sel:WORD_0
	v_exp_f16_sdwa v53, v45 dst_sel:WORD_0 dst_unused:UNUSED_PAD src0_sel:WORD_0
	v_exp_f16_sdwa v50, v42 dst_sel:WORD_1 dst_unused:UNUSED_PRESERVE src0_sel:WORD_1
	v_exp_f16_sdwa v51, v43 dst_sel:WORD_1 dst_unused:UNUSED_PRESERVE src0_sel:WORD_1
	v_exp_f16_sdwa v52, v44 dst_sel:WORD_1 dst_unused:UNUSED_PRESERVE src0_sel:WORD_1
	v_exp_f16_sdwa v53, v45 dst_sel:WORD_1 dst_unused:UNUSED_PRESERVE src0_sel:WORD_1
	v_pk_add_f16 v42, v93, v114 neg_lo:[0,1] neg_hi:[0,1]
	v_pk_add_f16 v37, v37, v50
	v_pk_add_f16 v36, v36, v51
	v_pk_add_f16 v35, v35, v52
	v_pk_add_f16 v34, v34, v53
	v_pk_fma_f16 v22, v10, v50, v22
	v_pk_fma_f16 v23, v11, v51, v23
	v_pk_fma_f16 v24, v12, v52, v24
	v_pk_fma_f16 v25, v13, v53, v25
	v_pk_add_f16 v43, v92, v115 neg_lo:[0,1] neg_hi:[0,1]
	v_pk_add_f16 v44, v91, v116 neg_lo:[0,1] neg_hi:[0,1]
	v_pk_add_f16 v45, v90, v117 neg_lo:[0,1] neg_hi:[0,1]
	v_exp_f16_sdwa v50, v42 dst_sel:WORD_0 dst_unused:UNUSED_PAD src0_sel:WORD_0
	v_exp_f16_sdwa v51, v43 dst_sel:WORD_0 dst_unused:UNUSED_PAD src0_sel:WORD_0
	v_exp_f16_sdwa v52, v44 dst_sel:WORD_0 dst_unused:UNUSED_PAD src0_sel:WORD_0
	v_exp_f16_sdwa v53, v45 dst_sel:WORD_0 dst_unused:UNUSED_PAD src0_sel:WORD_0
	v_exp_f16_sdwa v50, v42 dst_sel:WORD_1 dst_unused:UNUSED_PRESERVE src0_sel:WORD_1
	v_exp_f16_sdwa v51, v43 dst_sel:WORD_1 dst_unused:UNUSED_PRESERVE src0_sel:WORD_1
	v_exp_f16_sdwa v52, v44 dst_sel:WORD_1 dst_unused:UNUSED_PRESERVE src0_sel:WORD_1
	v_exp_f16_sdwa v53, v45 dst_sel:WORD_1 dst_unused:UNUSED_PRESERVE src0_sel:WORD_1
	v_pk_add_f16 v42, v66, v114 neg_lo:[0,1] neg_hi:[0,1]
	v_pk_add_f16 v37, v37, v50
	v_pk_add_f16 v34, v34, v53
	v_pk_add_f16 v35, v35, v52
	v_pk_add_f16 v36, v36, v51
	v_pk_fma_f16 v25, v17, v53, v25
	v_pk_fma_f16 v24, v16, v52, v24
	v_pk_fma_f16 v23, v15, v51, v23
	v_pk_fma_f16 v22, v14, v50, v22
	v_pk_add_f16 v43, v67, v115 neg_lo:[0,1] neg_hi:[0,1]
	v_pk_add_f16 v44, v68, v116 neg_lo:[0,1] neg_hi:[0,1]
	v_pk_add_f16 v45, v69, v117 neg_lo:[0,1] neg_hi:[0,1]
	v_exp_f16_sdwa v50, v42 dst_sel:WORD_0 dst_unused:UNUSED_PAD src0_sel:WORD_0
	v_exp_f16_sdwa v51, v43 dst_sel:WORD_0 dst_unused:UNUSED_PAD src0_sel:WORD_0
	v_exp_f16_sdwa v52, v44 dst_sel:WORD_0 dst_unused:UNUSED_PAD src0_sel:WORD_0
	v_exp_f16_sdwa v53, v45 dst_sel:WORD_0 dst_unused:UNUSED_PAD src0_sel:WORD_0
	v_exp_f16_sdwa v50, v42 dst_sel:WORD_1 dst_unused:UNUSED_PRESERVE src0_sel:WORD_1
	v_exp_f16_sdwa v51, v43 dst_sel:WORD_1 dst_unused:UNUSED_PRESERVE src0_sel:WORD_1
	v_exp_f16_sdwa v52, v44 dst_sel:WORD_1 dst_unused:UNUSED_PRESERVE src0_sel:WORD_1
	v_exp_f16_sdwa v53, v45 dst_sel:WORD_1 dst_unused:UNUSED_PRESERVE src0_sel:WORD_1
	v_pk_add_f16 v42, v101, v114 neg_lo:[0,1] neg_hi:[0,1]
	v_pk_add_f16 v37, v37, v50
	v_pk_add_f16 v36, v36, v51
	v_pk_add_f16 v35, v35, v52
	v_pk_add_f16 v34, v34, v53
	v_pk_fma_f16 v22, v18, v50, v22
	v_pk_fma_f16 v23, v19, v51, v23
	v_pk_fma_f16 v24, v20, v52, v24
	v_pk_fma_f16 v25, v21, v53, v25
	v_pk_add_f16 v43, v100, v115 neg_lo:[0,1] neg_hi:[0,1]
	v_pk_add_f16 v44, v99, v116 neg_lo:[0,1] neg_hi:[0,1]
	v_pk_add_f16 v45, v98, v117 neg_lo:[0,1] neg_hi:[0,1]
	v_exp_f16_sdwa v50, v42 dst_sel:WORD_0 dst_unused:UNUSED_PAD src0_sel:WORD_0
	v_exp_f16_sdwa v51, v43 dst_sel:WORD_0 dst_unused:UNUSED_PAD src0_sel:WORD_0
	v_exp_f16_sdwa v52, v44 dst_sel:WORD_0 dst_unused:UNUSED_PAD src0_sel:WORD_0
	v_exp_f16_sdwa v53, v45 dst_sel:WORD_0 dst_unused:UNUSED_PAD src0_sel:WORD_0
	v_exp_f16_sdwa v50, v42 dst_sel:WORD_1 dst_unused:UNUSED_PRESERVE src0_sel:WORD_1
	v_exp_f16_sdwa v51, v43 dst_sel:WORD_1 dst_unused:UNUSED_PRESERVE src0_sel:WORD_1
	v_exp_f16_sdwa v52, v44 dst_sel:WORD_1 dst_unused:UNUSED_PRESERVE src0_sel:WORD_1
	v_exp_f16_sdwa v53, v45 dst_sel:WORD_1 dst_unused:UNUSED_PRESERVE src0_sel:WORD_1
	v_pk_add_f16 v42, v113, v114 neg_lo:[0,1] neg_hi:[0,1]
	v_pk_add_f16 v37, v37, v50
	v_pk_add_f16 v34, v34, v53
	v_pk_add_f16 v35, v35, v52
	v_pk_add_f16 v36, v36, v51
	v_pk_fma_f16 v25, v33, v53, v25
	v_pk_fma_f16 v24, v32, v52, v24
	v_pk_fma_f16 v23, v31, v51, v23
	v_pk_fma_f16 v22, v30, v50, v22
	v_pk_add_f16 v43, v112, v115 neg_lo:[0,1] neg_hi:[0,1]
	v_pk_add_f16 v44, v111, v116 neg_lo:[0,1] neg_hi:[0,1]
	v_pk_add_f16 v45, v110, v117 neg_lo:[0,1] neg_hi:[0,1]
	v_exp_f16_sdwa v50, v42 dst_sel:WORD_0 dst_unused:UNUSED_PAD src0_sel:WORD_0
	v_exp_f16_sdwa v51, v43 dst_sel:WORD_0 dst_unused:UNUSED_PAD src0_sel:WORD_0
	v_exp_f16_sdwa v52, v44 dst_sel:WORD_0 dst_unused:UNUSED_PAD src0_sel:WORD_0
	v_exp_f16_sdwa v53, v45 dst_sel:WORD_0 dst_unused:UNUSED_PAD src0_sel:WORD_0
	v_exp_f16_sdwa v50, v42 dst_sel:WORD_1 dst_unused:UNUSED_PRESERVE src0_sel:WORD_1
	v_exp_f16_sdwa v51, v43 dst_sel:WORD_1 dst_unused:UNUSED_PRESERVE src0_sel:WORD_1
	v_exp_f16_sdwa v52, v44 dst_sel:WORD_1 dst_unused:UNUSED_PRESERVE src0_sel:WORD_1
	v_exp_f16_sdwa v53, v45 dst_sel:WORD_1 dst_unused:UNUSED_PRESERVE src0_sel:WORD_1
	v_pk_add_f16 v42, v70, v114 neg_lo:[0,1] neg_hi:[0,1]
	v_pk_add_f16 v37, v37, v50
	v_pk_add_f16 v36, v36, v51
	v_pk_add_f16 v35, v35, v52
	v_pk_add_f16 v34, v34, v53
	v_pk_fma_f16 v22, v46, v50, v22
	v_pk_fma_f16 v23, v47, v51, v23
	v_pk_fma_f16 v24, v48, v52, v24
	v_pk_fma_f16 v25, v49, v53, v25
	v_pk_add_f16 v43, v71, v115 neg_lo:[0,1] neg_hi:[0,1]
	v_pk_add_f16 v44, v72, v116 neg_lo:[0,1] neg_hi:[0,1]
	v_pk_add_f16 v45, v73, v117 neg_lo:[0,1] neg_hi:[0,1]
	v_exp_f16_sdwa v50, v42 dst_sel:WORD_0 dst_unused:UNUSED_PAD src0_sel:WORD_0
	v_exp_f16_sdwa v51, v43 dst_sel:WORD_0 dst_unused:UNUSED_PAD src0_sel:WORD_0
	v_exp_f16_sdwa v52, v44 dst_sel:WORD_0 dst_unused:UNUSED_PAD src0_sel:WORD_0
	v_exp_f16_sdwa v53, v45 dst_sel:WORD_0 dst_unused:UNUSED_PAD src0_sel:WORD_0
	v_exp_f16_sdwa v50, v42 dst_sel:WORD_1 dst_unused:UNUSED_PRESERVE src0_sel:WORD_1
	v_exp_f16_sdwa v51, v43 dst_sel:WORD_1 dst_unused:UNUSED_PRESERVE src0_sel:WORD_1
	v_exp_f16_sdwa v52, v44 dst_sel:WORD_1 dst_unused:UNUSED_PRESERVE src0_sel:WORD_1
	v_exp_f16_sdwa v53, v45 dst_sel:WORD_1 dst_unused:UNUSED_PRESERVE src0_sel:WORD_1
	v_pk_add_f16 v37, v37, v50
	v_pk_add_f16 v36, v36, v51
	v_rcp_f16_e32 v42, v37
	v_rcp_f16_sdwa v37, v37 dst_sel:DWORD dst_unused:UNUSED_PAD src0_sel:WORD_1
	v_pk_add_f16 v35, v35, v52
	v_rcp_f16_e32 v43, v36
	v_rcp_f16_sdwa v36, v36 dst_sel:DWORD dst_unused:UNUSED_PAD src0_sel:WORD_1
	v_pk_add_f16 v34, v34, v53
	v_pk_fma_f16 v22, v62, v50, v22
	v_rcp_f16_e32 v50, v35
	v_rcp_f16_sdwa v35, v35 dst_sel:DWORD dst_unused:UNUSED_PAD src0_sel:WORD_1
	v_pk_fma_f16 v23, v63, v51, v23
	v_rcp_f16_e32 v51, v34
	v_rcp_f16_sdwa v34, v34 dst_sel:DWORD dst_unused:UNUSED_PAD src0_sel:WORD_1
	v_pack_b32_f16 v37, v42, v37
	v_pk_mul_f16 v45, v22, v37
	v_pack_b32_f16 v22, v43, v36
	v_pk_fma_f16 v24, v64, v52, v24
	v_pk_mul_f16 v44, v23, v22
	v_pack_b32_f16 v22, v50, v35
	v_pk_fma_f16 v25, v65, v53, v25
	v_pk_mul_f16 v43, v24, v22
	v_pack_b32_f16 v22, v51, v34
	v_pk_mul_f16 v42, v25, v22
	s_waitcnt vmcnt(0)
	s_mov_b64 s[86:87], s[80:81]
	global_load_dword v254, v255, s[86:87]
	s_add_u32 s86, s86, 0x2000
	s_addc_u32 s87, s87, 0
	global_load_dword v254, v255, s[86:87]
	s_add_u32 s86, s86, 0x2000
	s_addc_u32 s87, s87, 0
	global_load_dword v254, v255, s[86:87]
	s_add_u32 s86, s86, 0x2c000
	s_addc_u32 s87, s87, 0
	global_load_dword v254, v255, s[86:87]
	s_add_u32 s86, s86, 0x2000
	s_addc_u32 s87, s87, 0
	global_load_dword v254, v255, s[86:87]
	s_add_u32 s86, s86, 0x2000
	s_addc_u32 s87, s87, 0
	global_load_dword v254, v255, s[86:87]
	v_pk_mul_f16 v22, v160, v146 op_sel_hi:[0,1]
	v_pk_mul_f16 v23, v160, v147 op_sel_hi:[0,1]
	v_pk_mul_f16 v24, v160, v148 op_sel_hi:[0,1]
	v_pk_mul_f16 v25, v160, v149 op_sel_hi:[0,1]
	v_pk_mul_f16 v50, v159, v146 op_sel_hi:[0,1]
	v_pk_mul_f16 v51, v159, v147 op_sel_hi:[0,1]
	v_pk_mul_f16 v52, v159, v148 op_sel_hi:[0,1]
	v_pk_mul_f16 v53, v159, v149 op_sel_hi:[0,1]
	v_pk_mul_f16 v34, v158, v146 op_sel_hi:[0,1]
	v_pk_mul_f16 v35, v158, v147 op_sel_hi:[0,1]
	v_pk_mul_f16 v36, v158, v148 op_sel_hi:[0,1]
	v_pk_mul_f16 v37, v158, v149 op_sel_hi:[0,1]
	v_pk_fma_f16 v29, v29, v149, v25
	v_pk_fma_f16 v28, v28, v148, v24
	v_pk_fma_f16 v27, v27, v147, v23
	v_pk_fma_f16 v26, v26, v146, v22
	v_pk_fma_f16 v41, v41, v149, v25
	v_pk_fma_f16 v40, v40, v148, v24
	v_pk_fma_f16 v39, v39, v147, v23
	v_pk_fma_f16 v38, v38, v146, v22
	v_pk_fma_f16 v25, v61, v149, v25
	v_pk_fma_f16 v24, v60, v148, v24
	v_pk_fma_f16 v23, v59, v147, v23
	v_pk_fma_f16 v22, v58, v146, v22
	v_pk_fma_f16 v66, v137, v149, v53
	v_pk_fma_f16 v67, v136, v148, v52
	v_pk_fma_f16 v68, v135, v147, v51
	v_pk_fma_f16 v69, v134, v146, v50
	v_pk_fma_f16 v70, v145, v149, v53
	v_pk_fma_f16 v71, v144, v148, v52
	v_pk_fma_f16 v72, v143, v147, v51
	v_pk_fma_f16 v73, v142, v146, v50
	v_pk_fma_f16 v9, v9, v149, v53
	v_pk_fma_f16 v8, v8, v148, v52
	v_pk_fma_f16 v7, v7, v147, v51
	v_pk_fma_f16 v6, v6, v146, v50
	v_pk_maximum3_f16 v50, v26, v38, v22
	v_pk_maximum3_f16 v51, v27, v39, v23
	v_pk_maximum3_f16 v52, v28, v40, v24
	v_pk_maximum3_f16 v53, v29, v41, v25
	v_pk_fma_f16 v54, v81, v149, v37
	v_pk_fma_f16 v55, v80, v148, v36
	v_pk_fma_f16 v56, v79, v147, v35
	v_pk_fma_f16 v57, v78, v146, v34
	v_pk_fma_f16 v58, v109, v149, v37
	v_pk_fma_f16 v59, v108, v148, v36
	v_pk_fma_f16 v60, v107, v147, v35
	v_pk_fma_f16 v61, v106, v146, v34
	v_pk_fma_f16 v37, v125, v149, v37
	v_pk_fma_f16 v36, v124, v148, v36
	v_pk_fma_f16 v35, v123, v147, v35
	v_pk_fma_f16 v34, v122, v146, v34
	v_pk_maximum3_f16 v75, v56, v60, v35
	v_pk_maximum3_f16 v76, v55, v59, v36
	v_pk_maximum3_f16 v77, v54, v58, v37
	v_pk_maximum3_f16 v78, v69, v73, v6
	v_pk_maximum3_f16 v79, v68, v72, v7
	v_pk_maximum3_f16 v74, v57, v61, v34
	v_pk_maximum3_f16 v80, v67, v71, v8
	v_pk_maximum3_f16 v81, v66, v70, v9
	v_pk_maximum3_f16 v50, v50, v74, v78
	v_pk_maximum3_f16 v51, v51, v75, v79
	v_pk_maximum3_f16 v52, v52, v76, v80
	v_pk_maximum3_f16 v53, v53, v77, v81
	s_nop 0
	v_pk_add_f16 v26, v26, v50 neg_lo:[0,1] neg_hi:[0,1]
	v_pk_add_f16 v27, v27, v51 neg_lo:[0,1] neg_hi:[0,1]
	v_pk_add_f16 v28, v28, v52 neg_lo:[0,1] neg_hi:[0,1]
	v_pk_add_f16 v29, v29, v53 neg_lo:[0,1] neg_hi:[0,1]
	v_pk_add_f16 v38, v38, v50 neg_lo:[0,1] neg_hi:[0,1]
	v_exp_f16_sdwa v74, v26 dst_sel:WORD_0 dst_unused:UNUSED_PAD src0_sel:WORD_0
	v_exp_f16_sdwa v75, v27 dst_sel:WORD_0 dst_unused:UNUSED_PAD src0_sel:WORD_0
	v_exp_f16_sdwa v76, v28 dst_sel:WORD_0 dst_unused:UNUSED_PAD src0_sel:WORD_0
	v_exp_f16_sdwa v77, v29 dst_sel:WORD_0 dst_unused:UNUSED_PAD src0_sel:WORD_0
	v_exp_f16_sdwa v74, v26 dst_sel:WORD_1 dst_unused:UNUSED_PRESERVE src0_sel:WORD_1
	v_exp_f16_sdwa v75, v27 dst_sel:WORD_1 dst_unused:UNUSED_PRESERVE src0_sel:WORD_1
	v_exp_f16_sdwa v76, v28 dst_sel:WORD_1 dst_unused:UNUSED_PRESERVE src0_sel:WORD_1
	v_exp_f16_sdwa v77, v29 dst_sel:WORD_1 dst_unused:UNUSED_PRESERVE src0_sel:WORD_1
	v_pk_add_f16 v39, v39, v51 neg_lo:[0,1] neg_hi:[0,1]
	v_pk_add_f16 v26, v74, 0
	v_pk_add_f16 v27, v75, 0
	v_pk_add_f16 v28, v76, 0
	v_pk_add_f16 v29, v77, 0
	v_pk_fma_f16 v10, v10, v74, 0
	v_pk_fma_f16 v11, v11, v75, 0
	v_pk_fma_f16 v12, v12, v76, 0
	v_pk_fma_f16 v13, v13, v77, 0
	v_pk_add_f16 v40, v40, v52 neg_lo:[0,1] neg_hi:[0,1]
	v_pk_add_f16 v41, v41, v53 neg_lo:[0,1] neg_hi:[0,1]
	v_pk_add_f16 v6, v6, v50 neg_lo:[0,1] neg_hi:[0,1]
	v_exp_f16_sdwa v74, v38 dst_sel:WORD_0 dst_unused:UNUSED_PAD src0_sel:WORD_0
	v_exp_f16_sdwa v75, v39 dst_sel:WORD_0 dst_unused:UNUSED_PAD src0_sel:WORD_0
	v_exp_f16_sdwa v76, v40 dst_sel:WORD_0 dst_unused:UNUSED_PAD src0_sel:WORD_0
	v_exp_f16_sdwa v77, v41 dst_sel:WORD_0 dst_unused:UNUSED_PAD src0_sel:WORD_0
	v_exp_f16_sdwa v74, v38 dst_sel:WORD_1 dst_unused:UNUSED_PRESERVE src0_sel:WORD_1
	v_exp_f16_sdwa v75, v39 dst_sel:WORD_1 dst_unused:UNUSED_PRESERVE src0_sel:WORD_1
	v_exp_f16_sdwa v76, v40 dst_sel:WORD_1 dst_unused:UNUSED_PRESERVE src0_sel:WORD_1
	v_exp_f16_sdwa v77, v41 dst_sel:WORD_1 dst_unused:UNUSED_PRESERVE src0_sel:WORD_1
	v_pk_add_f16 v7, v7, v51 neg_lo:[0,1] neg_hi:[0,1]
	v_pk_add_f16 v29, v29, v77
	v_pk_add_f16 v28, v28, v76
	v_pk_add_f16 v27, v27, v75
	v_pk_add_f16 v26, v26, v74
	v_pk_fma_f16 v13, v17, v77, v13
	v_pk_fma_f16 v12, v16, v76, v12
	v_pk_fma_f16 v11, v15, v75, v11
	v_pk_fma_f16 v10, v14, v74, v10
	v_pk_add_f16 v14, v22, v50 neg_lo:[0,1] neg_hi:[0,1]
	v_pk_add_f16 v15, v23, v51 neg_lo:[0,1] neg_hi:[0,1]
	v_pk_add_f16 v16, v24, v52 neg_lo:[0,1] neg_hi:[0,1]
	v_pk_add_f16 v17, v25, v53 neg_lo:[0,1] neg_hi:[0,1]
	v_pk_add_f16 v8, v8, v52 neg_lo:[0,1] neg_hi:[0,1]
	v_exp_f16_sdwa v22, v14 dst_sel:WORD_0 dst_unused:UNUSED_PAD src0_sel:WORD_0
	v_exp_f16_sdwa v23, v15 dst_sel:WORD_0 dst_unused:UNUSED_PAD src0_sel:WORD_0
	v_exp_f16_sdwa v24, v16 dst_sel:WORD_0 dst_unused:UNUSED_PAD src0_sel:WORD_0
	v_exp_f16_sdwa v25, v17 dst_sel:WORD_0 dst_unused:UNUSED_PAD src0_sel:WORD_0
	v_exp_f16_sdwa v22, v14 dst_sel:WORD_1 dst_unused:UNUSED_PRESERVE src0_sel:WORD_1
	v_exp_f16_sdwa v23, v15 dst_sel:WORD_1 dst_unused:UNUSED_PRESERVE src0_sel:WORD_1
	v_exp_f16_sdwa v24, v16 dst_sel:WORD_1 dst_unused:UNUSED_PRESERVE src0_sel:WORD_1
	v_exp_f16_sdwa v25, v17 dst_sel:WORD_1 dst_unused:UNUSED_PRESERVE src0_sel:WORD_1
	v_pk_add_f16 v9, v9, v53 neg_lo:[0,1] neg_hi:[0,1]
	v_pk_add_f16 v14, v26, v22
	v_pk_add_f16 v15, v27, v23
	v_pk_add_f16 v16, v28, v24
	v_pk_add_f16 v17, v29, v25
	v_pk_fma_f16 v10, v18, v22, v10
	v_pk_fma_f16 v11, v19, v23, v11
	v_pk_fma_f16 v12, v20, v24, v12
	v_pk_fma_f16 v13, v21, v25, v13
	v_pk_add_f16 v18, v57, v50 neg_lo:[0,1] neg_hi:[0,1]
	v_pk_add_f16 v19, v56, v51 neg_lo:[0,1] neg_hi:[0,1]
	v_pk_add_f16 v20, v55, v52 neg_lo:[0,1] neg_hi:[0,1]
	v_pk_add_f16 v21, v54, v53 neg_lo:[0,1] neg_hi:[0,1]
	v_exp_f16_sdwa v22, v18 dst_sel:WORD_0 dst_unused:UNUSED_PAD src0_sel:WORD_0
	v_exp_f16_sdwa v23, v19 dst_sel:WORD_0 dst_unused:UNUSED_PAD src0_sel:WORD_0
	v_exp_f16_sdwa v24, v20 dst_sel:WORD_0 dst_unused:UNUSED_PAD src0_sel:WORD_0
	v_exp_f16_sdwa v25, v21 dst_sel:WORD_0 dst_unused:UNUSED_PAD src0_sel:WORD_0
	v_exp_f16_sdwa v22, v18 dst_sel:WORD_1 dst_unused:UNUSED_PRESERVE src0_sel:WORD_1
	v_exp_f16_sdwa v23, v19 dst_sel:WORD_1 dst_unused:UNUSED_PRESERVE src0_sel:WORD_1
	v_exp_f16_sdwa v24, v20 dst_sel:WORD_1 dst_unused:UNUSED_PRESERVE src0_sel:WORD_1
	v_exp_f16_sdwa v25, v21 dst_sel:WORD_1 dst_unused:UNUSED_PRESERVE src0_sel:WORD_1
	v_pk_add_f16 v18, v61, v50 neg_lo:[0,1] neg_hi:[0,1]
	v_pk_add_f16 v17, v17, v25
	v_pk_add_f16 v16, v16, v24
	v_pk_add_f16 v15, v15, v23
	v_pk_add_f16 v14, v14, v22
	v_pk_fma_f16 v13, v33, v25, v13
	v_pk_fma_f16 v12, v32, v24, v12
	v_pk_fma_f16 v11, v31, v23, v11
	v_pk_fma_f16 v10, v30, v22, v10
	v_pk_add_f16 v19, v60, v51 neg_lo:[0,1] neg_hi:[0,1]
	v_pk_add_f16 v20, v59, v52 neg_lo:[0,1] neg_hi:[0,1]
	v_pk_add_f16 v21, v58, v53 neg_lo:[0,1] neg_hi:[0,1]
	v_exp_f16_sdwa v22, v18 dst_sel:WORD_0 dst_unused:UNUSED_PAD src0_sel:WORD_0
	v_exp_f16_sdwa v23, v19 dst_sel:WORD_0 dst_unused:UNUSED_PAD src0_sel:WORD_0
	v_exp_f16_sdwa v24, v20 dst_sel:WORD_0 dst_unused:UNUSED_PAD src0_sel:WORD_0
	v_exp_f16_sdwa v25, v21 dst_sel:WORD_0 dst_unused:UNUSED_PAD src0_sel:WORD_0
	v_exp_f16_sdwa v22, v18 dst_sel:WORD_1 dst_unused:UNUSED_PRESERVE src0_sel:WORD_1
	v_exp_f16_sdwa v23, v19 dst_sel:WORD_1 dst_unused:UNUSED_PRESERVE src0_sel:WORD_1
	v_exp_f16_sdwa v24, v20 dst_sel:WORD_1 dst_unused:UNUSED_PRESERVE src0_sel:WORD_1
	v_exp_f16_sdwa v25, v21 dst_sel:WORD_1 dst_unused:UNUSED_PRESERVE src0_sel:WORD_1
	v_pk_add_f16 v18, v34, v50 neg_lo:[0,1] neg_hi:[0,1]
	v_pk_add_f16 v14, v14, v22
	v_pk_add_f16 v15, v15, v23
	v_pk_add_f16 v16, v16, v24
	v_pk_add_f16 v17, v17, v25
	v_pk_fma_f16 v10, v46, v22, v10
	v_pk_fma_f16 v11, v47, v23, v11
	v_pk_fma_f16 v12, v48, v24, v12
	v_pk_fma_f16 v13, v49, v25, v13
	v_pk_add_f16 v19, v35, v51 neg_lo:[0,1] neg_hi:[0,1]
	v_pk_add_f16 v20, v36, v52 neg_lo:[0,1] neg_hi:[0,1]
	v_pk_add_f16 v21, v37, v53 neg_lo:[0,1] neg_hi:[0,1]
	v_exp_f16_sdwa v22, v18 dst_sel:WORD_0 dst_unused:UNUSED_PAD src0_sel:WORD_0
	v_exp_f16_sdwa v23, v19 dst_sel:WORD_0 dst_unused:UNUSED_PAD src0_sel:WORD_0
	v_exp_f16_sdwa v24, v20 dst_sel:WORD_0 dst_unused:UNUSED_PAD src0_sel:WORD_0
	v_exp_f16_sdwa v25, v21 dst_sel:WORD_0 dst_unused:UNUSED_PAD src0_sel:WORD_0
	v_exp_f16_sdwa v22, v18 dst_sel:WORD_1 dst_unused:UNUSED_PRESERVE src0_sel:WORD_1
	v_exp_f16_sdwa v23, v19 dst_sel:WORD_1 dst_unused:UNUSED_PRESERVE src0_sel:WORD_1
	v_exp_f16_sdwa v24, v20 dst_sel:WORD_1 dst_unused:UNUSED_PRESERVE src0_sel:WORD_1
	v_exp_f16_sdwa v25, v21 dst_sel:WORD_1 dst_unused:UNUSED_PRESERVE src0_sel:WORD_1
	v_pk_add_f16 v18, v69, v50 neg_lo:[0,1] neg_hi:[0,1]
	v_pk_add_f16 v17, v17, v25
	v_pk_add_f16 v16, v16, v24
	v_pk_add_f16 v15, v15, v23
	v_pk_add_f16 v14, v14, v22
	v_pk_fma_f16 v13, v65, v25, v13
	v_pk_fma_f16 v12, v64, v24, v12
	v_pk_fma_f16 v11, v63, v23, v11
	v_pk_fma_f16 v10, v62, v22, v10
	v_pk_add_f16 v19, v68, v51 neg_lo:[0,1] neg_hi:[0,1]
	v_pk_add_f16 v20, v67, v52 neg_lo:[0,1] neg_hi:[0,1]
	v_pk_add_f16 v21, v66, v53 neg_lo:[0,1] neg_hi:[0,1]
	v_exp_f16_sdwa v22, v18 dst_sel:WORD_0 dst_unused:UNUSED_PAD src0_sel:WORD_0
	v_exp_f16_sdwa v23, v19 dst_sel:WORD_0 dst_unused:UNUSED_PAD src0_sel:WORD_0
	v_exp_f16_sdwa v24, v20 dst_sel:WORD_0 dst_unused:UNUSED_PAD src0_sel:WORD_0
	v_exp_f16_sdwa v25, v21 dst_sel:WORD_0 dst_unused:UNUSED_PAD src0_sel:WORD_0
	v_exp_f16_sdwa v22, v18 dst_sel:WORD_1 dst_unused:UNUSED_PRESERVE src0_sel:WORD_1
	v_exp_f16_sdwa v23, v19 dst_sel:WORD_1 dst_unused:UNUSED_PRESERVE src0_sel:WORD_1
	v_exp_f16_sdwa v24, v20 dst_sel:WORD_1 dst_unused:UNUSED_PRESERVE src0_sel:WORD_1
	v_exp_f16_sdwa v25, v21 dst_sel:WORD_1 dst_unused:UNUSED_PRESERVE src0_sel:WORD_1
	v_pk_add_f16 v18, v73, v50 neg_lo:[0,1] neg_hi:[0,1]
	v_pk_add_f16 v14, v14, v22
	v_pk_add_f16 v15, v15, v23
	v_pk_add_f16 v16, v16, v24
	v_pk_add_f16 v17, v17, v25
	v_pk_fma_f16 v10, v82, v22, v10
	v_pk_fma_f16 v11, v83, v23, v11
	v_pk_fma_f16 v12, v84, v24, v12
	v_pk_fma_f16 v13, v85, v25, v13
	v_pk_add_f16 v19, v72, v51 neg_lo:[0,1] neg_hi:[0,1]
	v_pk_add_f16 v20, v71, v52 neg_lo:[0,1] neg_hi:[0,1]
	v_pk_add_f16 v21, v70, v53 neg_lo:[0,1] neg_hi:[0,1]
	v_exp_f16_sdwa v22, v18 dst_sel:WORD_0 dst_unused:UNUSED_PAD src0_sel:WORD_0
	v_exp_f16_sdwa v23, v19 dst_sel:WORD_0 dst_unused:UNUSED_PAD src0_sel:WORD_0
	v_exp_f16_sdwa v24, v20 dst_sel:WORD_0 dst_unused:UNUSED_PAD src0_sel:WORD_0
	v_exp_f16_sdwa v25, v21 dst_sel:WORD_0 dst_unused:UNUSED_PAD src0_sel:WORD_0
	v_exp_f16_sdwa v22, v18 dst_sel:WORD_1 dst_unused:UNUSED_PRESERVE src0_sel:WORD_1
	v_exp_f16_sdwa v23, v19 dst_sel:WORD_1 dst_unused:UNUSED_PRESERVE src0_sel:WORD_1
	v_exp_f16_sdwa v24, v20 dst_sel:WORD_1 dst_unused:UNUSED_PRESERVE src0_sel:WORD_1
	v_exp_f16_sdwa v25, v21 dst_sel:WORD_1 dst_unused:UNUSED_PRESERVE src0_sel:WORD_1
	s_nop 0
	v_pk_add_f16 v17, v17, v25
	v_pk_add_f16 v16, v16, v24
	v_pk_add_f16 v15, v15, v23
	v_pk_add_f16 v14, v14, v22
	v_pk_fma_f16 v21, v105, v25, v13
	v_pk_fma_f16 v20, v104, v24, v12
	v_pk_fma_f16 v19, v103, v23, v11
	v_pk_fma_f16 v18, v102, v22, v10
	v_mov_b32_e32 v13, v5
	v_mov_b32_e32 v12, v4
	v_mov_b32_e32 v11, v3
	v_mov_b32_e32 v10, v2
	v_exp_f16_sdwa v22, v6 dst_sel:WORD_0 dst_unused:UNUSED_PAD src0_sel:WORD_0
	v_exp_f16_sdwa v23, v7 dst_sel:WORD_0 dst_unused:UNUSED_PAD src0_sel:WORD_0
	v_exp_f16_sdwa v24, v8 dst_sel:WORD_0 dst_unused:UNUSED_PAD src0_sel:WORD_0
	v_exp_f16_sdwa v25, v9 dst_sel:WORD_0 dst_unused:UNUSED_PAD src0_sel:WORD_0
	v_exp_f16_sdwa v22, v6 dst_sel:WORD_1 dst_unused:UNUSED_PRESERVE src0_sel:WORD_1
	v_exp_f16_sdwa v23, v7 dst_sel:WORD_1 dst_unused:UNUSED_PRESERVE src0_sel:WORD_1
	v_exp_f16_sdwa v24, v8 dst_sel:WORD_1 dst_unused:UNUSED_PRESERVE src0_sel:WORD_1
	v_exp_f16_sdwa v25, v9 dst_sel:WORD_1 dst_unused:UNUSED_PRESERVE src0_sel:WORD_1
	s_nop 0

.LBB4_80:
	v_lshlrev_b64 v[6:7], 9, v[168:169]
	v_or_b32_e32 v6, v6, v198
	v_lshl_add_u64 v[2:3], s[20:21], 0, v[6:7]
	global_load_dwordx4 v[2:5], v[2:3], off nt
	v_lshl_add_u64 v[6:7], s[22:23], 0, v[6:7]
	global_load_dwordx4 v[6:9], v[6:7], off nt
	v_add_u32_e32 v168, v185, v199
	v_lshlrev_b64 v[26:27], 9, v[168:169]
	v_or_b32_e32 v26, v26, v198
	v_lshl_add_u64 v[22:23], s[20:21], 0, v[26:27]
	global_load_dwordx4 v[22:25], v[22:23], off nt
	v_lshl_add_u64 v[26:27], s[22:23], 0, v[26:27]
	global_load_dwordx4 v[26:29], v[26:27], off nt
	v_pk_add_f16 v17, v17, v33
	v_pk_add_f16 v16, v16, v32
	v_pk_add_f16 v15, v15, v31
	v_pk_add_f16 v14, v14, v30
	v_pk_fma_f16 v42, v13, v33, v21
	v_pk_fma_f16 v43, v12, v32, v20
	v_rcp_f16_e32 v12, v14
	v_rcp_f16_sdwa v13, v14 dst_sel:DWORD dst_unused:UNUSED_PAD src0_sel:WORD_1
	v_rcp_f16_e32 v14, v15
	v_rcp_f16_sdwa v15, v15 dst_sel:DWORD dst_unused:UNUSED_PAD src0_sel:WORD_1
	v_rcp_f16_e32 v46, v16
	v_rcp_f16_sdwa v16, v16 dst_sel:DWORD dst_unused:UNUSED_PAD src0_sel:WORD_1
	v_rcp_f16_e32 v47, v17
	v_rcp_f16_sdwa v17, v17 dst_sel:DWORD dst_unused:UNUSED_PAD src0_sel:WORD_1
	v_add_u32_e32 v168, v187, v199
	v_pk_fma_f16 v44, v10, v30, v18
	v_pk_fma_f16 v45, v11, v31, v19
	v_lshlrev_b64 v[10:11], 9, v[168:169]
	v_or_b32_e32 v10, v10, v198
	v_lshl_add_u64 v[38:39], s[20:21], 0, v[10:11]
	v_lshl_add_u64 v[40:41], s[22:23], 0, v[10:11]
	v_pack_b32_f16 v48, v14, v15
	v_pack_b32_f16 v49, v12, v13
	v_pack_b32_f16 v46, v46, v16
	v_pack_b32_f16 v47, v47, v17
	global_load_dwordx4 v[10:13], v[38:39], off nt
	global_load_dwordx4 v[14:17], v[40:41], off nt
	v_cvt_f32_f16_sdwa v21, v139 dst_sel:DWORD dst_unused:UNUSED_PAD src0_sel:WORD_1
	v_cvt_f32_f16_e32 v20, v139
	v_cvt_f32_f16_sdwa v19, v138 dst_sel:DWORD dst_unused:UNUSED_PAD src0_sel:WORD_1
	v_cvt_f32_f16_e32 v18, v138
	v_cvt_f32_f16_sdwa v33, v141 dst_sel:DWORD dst_unused:UNUSED_PAD src0_sel:WORD_1
	v_cvt_f32_f16_e32 v32, v141
	v_pk_mul_f16 v58, v43, v46
	v_pk_mul_f16 v59, v42, v47
	v_cvt_f32_f16_sdwa v31, v140 dst_sel:DWORD dst_unused:UNUSED_PAD src0_sel:WORD_1
	v_cvt_f32_f16_e32 v30, v140
	v_pk_mul_f16 v52, v45, v48
	v_pk_mul_f16 v53, v44, v49
	v_add_u32_e32 v168, v190, v199
	v_lshlrev_b64 v[36:37], 9, v[168:169]
	v_or_b32_e32 v36, v36, v198
	v_lshl_or_b32 v50, s46, 6, v178
	v_lshlrev_b32_e32 v51, 9, v50
	v_add_u32_e32 v203, v184, v51
	v_cvt_f32_f16_sdwa v35, v77 dst_sel:DWORD dst_unused:UNUSED_PAD src0_sel:WORD_1
	v_cvt_f32_f16_e32 v34, v77
	v_add_lshl_u32 v202, v188, v50, 9
	s_mov_b64 s[4:5], -1
	s_and_b64 vcc, exec, s[26:27]
	s_waitcnt vmcnt(5)
	v_cvt_f32_f16_e32 v38, v2
	v_cvt_f32_f16_sdwa v39, v2 dst_sel:DWORD dst_unused:UNUSED_PAD src0_sel:WORD_1
	v_cvt_f32_f16_e32 v2, v3
	v_cvt_f32_f16_sdwa v3, v3 dst_sel:DWORD dst_unused:UNUSED_PAD src0_sel:WORD_1
	s_waitcnt vmcnt(4)
	v_cvt_f32_f16_e32 v40, v6
	v_cvt_f32_f16_sdwa v41, v6 dst_sel:DWORD dst_unused:UNUSED_PAD src0_sel:WORD_1
	v_cvt_f32_f16_e32 v6, v7
	v_cvt_f32_f16_sdwa v7, v7 dst_sel:DWORD dst_unused:UNUSED_PAD src0_sel:WORD_1
	v_cvt_f32_f16_e32 v42, v4
	v_cvt_f32_f16_sdwa v43, v4 dst_sel:DWORD dst_unused:UNUSED_PAD src0_sel:WORD_1
	v_cvt_f32_f16_e32 v4, v5
	v_cvt_f32_f16_sdwa v5, v5 dst_sel:DWORD dst_unused:UNUSED_PAD src0_sel:WORD_1
	v_cvt_f32_f16_e32 v44, v8
	v_cvt_f32_f16_sdwa v45, v8 dst_sel:DWORD dst_unused:UNUSED_PAD src0_sel:WORD_1
	v_cvt_f32_f16_e32 v8, v9
	v_cvt_f32_f16_sdwa v9, v9 dst_sel:DWORD dst_unused:UNUSED_PAD src0_sel:WORD_1
	v_pk_add_f32 v[2:3], v[20:21], v[2:3]
	v_pk_add_f32 v[18:19], v[18:19], v[38:39]
	v_pk_add_f32 v[4:5], v[32:33], v[4:5]
	v_pk_add_f32 v[6:7], v[2:3], v[6:7]
	v_pk_add_f32 v[20:21], v[30:31], v[42:43]
	v_pk_add_f32 v[18:19], v[18:19], v[40:41]
	v_pk_add_f32 v[8:9], v[4:5], v[8:9]
	v_cvt_pk_f16_f32 v3, v6, v7
	v_lshl_add_u64 v[6:7], s[20:21], 0, v[36:37]
	v_pk_add_f32 v[20:21], v[20:21], v[44:45]
	v_cvt_pk_f16_f32 v2, v18, v19
	v_cvt_pk_f16_f32 v5, v8, v9
	global_load_dwordx4 v[6:9], v[6:7], off nt
	v_lshl_add_u64 v[18:19], s[22:23], 0, v[36:37]
	v_cvt_pk_f16_f32 v4, v20, v21
	global_load_dwordx4 v[18:21], v[18:19], off nt
	s_waitcnt vmcnt(5)
	v_cvt_f32_f16_e32 v46, v22
	v_cvt_f32_f16_sdwa v47, v22 dst_sel:DWORD dst_unused:UNUSED_PAD src0_sel:WORD_1
	ds_write_b128 v203, v[2:5]
	v_cvt_f32_f16_sdwa v5, v76 dst_sel:DWORD dst_unused:UNUSED_PAD src0_sel:WORD_1
	v_cvt_f32_f16_e32 v4, v76
	v_cvt_f32_f16_e32 v22, v23
	v_cvt_f32_f16_sdwa v23, v23 dst_sel:DWORD dst_unused:UNUSED_PAD src0_sel:WORD_1
	s_waitcnt vmcnt(4)
	v_cvt_f32_f16_e32 v48, v26
	v_cvt_f32_f16_sdwa v49, v26 dst_sel:DWORD dst_unused:UNUSED_PAD src0_sel:WORD_1
	v_cvt_f32_f16_e32 v26, v27
	v_cvt_f32_f16_sdwa v27, v27 dst_sel:DWORD dst_unused:UNUSED_PAD src0_sel:WORD_1
	v_cvt_f32_f16_sdwa v31, v75 dst_sel:DWORD dst_unused:UNUSED_PAD src0_sel:WORD_1
	v_cvt_f32_f16_e32 v30, v75
	v_cvt_f32_f16_e32 v32, v24
	v_cvt_f32_f16_sdwa v33, v24 dst_sel:DWORD dst_unused:UNUSED_PAD src0_sel:WORD_1
	v_pk_add_f32 v[4:5], v[4:5], v[22:23]
	v_cvt_f32_f16_e32 v22, v28
	v_pk_add_f32 v[4:5], v[4:5], v[26:27]
	v_cvt_f32_f16_sdwa v23, v28 dst_sel:DWORD dst_unused:UNUSED_PAD src0_sel:WORD_1
	v_cvt_f32_f16_sdwa v27, v74 dst_sel:DWORD dst_unused:UNUSED_PAD src0_sel:WORD_1
	v_cvt_f32_f16_e32 v26, v74
	v_cvt_f32_f16_e32 v24, v25
	v_cvt_f32_f16_sdwa v25, v25 dst_sel:DWORD dst_unused:UNUSED_PAD src0_sel:WORD_1
	v_pk_add_f32 v[2:3], v[34:35], v[46:47]
	v_cvt_f32_f16_e32 v28, v29
	v_cvt_f32_f16_sdwa v29, v29 dst_sel:DWORD dst_unused:UNUSED_PAD src0_sel:WORD_1
	v_pk_add_f32 v[2:3], v[2:3], v[48:49]
	s_nop 0
	v_cvt_pk_f16_f32 v2, v2, v3
	v_cvt_pk_f16_f32 v3, v4, v5
	v_pk_add_f32 v[4:5], v[30:31], v[32:33]
	s_nop 0
	v_pk_add_f32 v[4:5], v[4:5], v[22:23]
	v_pk_add_f32 v[22:23], v[26:27], v[24:25]
	v_cvt_pk_f16_f32 v4, v4, v5
	v_pk_add_f32 v[22:23], v[22:23], v[28:29]
	s_waitcnt vmcnt(3)
	v_cvt_f32_f16_e32 v24, v10
	v_cvt_pk_f16_f32 v5, v22, v23
	v_add_u32_e32 v22, v186, v50
	v_lshlrev_b32_e32 v204, 9, v22
	v_bitop3_b32 v22, v22, v179, 15 bitop3:0x6c
	v_lshlrev_b32_e32 v205, 4, v22
	v_cvt_f32_f16_sdwa v25, v10 dst_sel:DWORD dst_unused:UNUSED_PAD src0_sel:WORD_1
	v_or_b32_e32 v10, v205, v204
	v_cvt_f32_f16_sdwa v23, v57 dst_sel:DWORD dst_unused:UNUSED_PAD src0_sel:WORD_1
	v_cvt_f32_f16_e32 v22, v57
	ds_write_b128 v10, v[2:5]
	v_cvt_f32_f16_sdwa v5, v56 dst_sel:DWORD dst_unused:UNUSED_PAD src0_sel:WORD_1
	v_cvt_f32_f16_e32 v4, v56
	v_cvt_f32_f16_e32 v10, v11
	v_cvt_f32_f16_sdwa v11, v11 dst_sel:DWORD dst_unused:UNUSED_PAD src0_sel:WORD_1
	s_waitcnt vmcnt(2)
	v_cvt_f32_f16_e32 v26, v14
	v_cvt_f32_f16_sdwa v27, v14 dst_sel:DWORD dst_unused:UNUSED_PAD src0_sel:WORD_1
	v_cvt_f32_f16_e32 v14, v15
	v_cvt_f32_f16_sdwa v15, v15 dst_sel:DWORD dst_unused:UNUSED_PAD src0_sel:WORD_1
	v_pk_add_f32 v[2:3], v[22:23], v[24:25]
	v_cvt_f32_f16_sdwa v23, v55 dst_sel:DWORD dst_unused:UNUSED_PAD src0_sel:WORD_1
	v_cvt_f32_f16_e32 v22, v55
	v_cvt_f32_f16_e32 v24, v12
	v_cvt_f32_f16_sdwa v25, v12 dst_sel:DWORD dst_unused:UNUSED_PAD src0_sel:WORD_1
	v_pk_add_f32 v[4:5], v[4:5], v[10:11]
	v_cvt_f32_f16_e32 v10, v16
	v_pk_add_f32 v[4:5], v[4:5], v[14:15]
	v_cvt_f32_f16_sdwa v11, v16 dst_sel:DWORD dst_unused:UNUSED_PAD src0_sel:WORD_1
	v_cvt_f32_f16_sdwa v15, v54 dst_sel:DWORD dst_unused:UNUSED_PAD src0_sel:WORD_1
	v_cvt_f32_f16_e32 v14, v54
	v_cvt_f32_f16_e32 v12, v13
	v_cvt_f32_f16_sdwa v13, v13 dst_sel:DWORD dst_unused:UNUSED_PAD src0_sel:WORD_1
	v_cvt_f32_f16_e32 v16, v17
	v_cvt_f32_f16_sdwa v17, v17 dst_sel:DWORD dst_unused:UNUSED_PAD src0_sel:WORD_1
	v_pk_add_f32 v[2:3], v[2:3], v[26:27]
	s_nop 0
	v_cvt_pk_f16_f32 v2, v2, v3
	v_cvt_pk_f16_f32 v3, v4, v5
	v_pk_add_f32 v[4:5], v[22:23], v[24:25]
	s_nop 0
	v_pk_add_f32 v[4:5], v[4:5], v[10:11]
	v_pk_add_f32 v[10:11], v[14:15], v[12:13]
	v_cvt_pk_f16_f32 v4, v4, v5
	v_pk_add_f32 v[10:11], v[10:11], v[16:17]
	s_waitcnt vmcnt(1)
	v_cvt_f32_f16_e32 v12, v6
	v_cvt_pk_f16_f32 v5, v10, v11
	v_cvt_f32_f16_e32 v10, v53
	v_cvt_f32_f16_sdwa v11, v53 dst_sel:DWORD dst_unused:UNUSED_PAD src0_sel:WORD_1
	v_cvt_f32_f16_sdwa v13, v6 dst_sel:DWORD dst_unused:UNUSED_PAD src0_sel:WORD_1
	s_waitcnt vmcnt(0)
	v_cvt_f32_f16_e32 v14, v18
	v_cvt_f32_f16_sdwa v15, v18 dst_sel:DWORD dst_unused:UNUSED_PAD src0_sel:WORD_1
	v_or_b32_e32 v6, v189, v202
	ds_write_b128 v6, v[2:5]
	v_cvt_f32_f16_e32 v4, v52
	v_cvt_f32_f16_sdwa v5, v52 dst_sel:DWORD dst_unused:UNUSED_PAD src0_sel:WORD_1
	v_cvt_f32_f16_e32 v6, v7
	v_cvt_f32_f16_sdwa v7, v7 dst_sel:DWORD dst_unused:UNUSED_PAD src0_sel:WORD_1
	v_pk_add_f32 v[2:3], v[10:11], v[12:13]
	v_cvt_f32_f16_e32 v10, v19
	v_cvt_f32_f16_sdwa v11, v19 dst_sel:DWORD dst_unused:UNUSED_PAD src0_sel:WORD_1
	v_pk_add_f32 v[2:3], v[2:3], v[14:15]
	v_cvt_f32_f16_e32 v12, v58
	v_cvt_f32_f16_sdwa v13, v58 dst_sel:DWORD dst_unused:UNUSED_PAD src0_sel:WORD_1
	v_cvt_f32_f16_e32 v14, v8
	v_cvt_f32_f16_sdwa v15, v8 dst_sel:DWORD dst_unused:UNUSED_PAD src0_sel:WORD_1
	v_pk_add_f32 v[4:5], v[4:5], v[6:7]
	v_cvt_f32_f16_e32 v6, v20
	v_pk_add_f32 v[4:5], v[4:5], v[10:11]
	v_cvt_f32_f16_sdwa v7, v20 dst_sel:DWORD dst_unused:UNUSED_PAD src0_sel:WORD_1
	v_cvt_f32_f16_e32 v10, v59
	v_cvt_f32_f16_sdwa v11, v59 dst_sel:DWORD dst_unused:UNUSED_PAD src0_sel:WORD_1
	v_cvt_f32_f16_e32 v8, v9
	v_cvt_f32_f16_sdwa v9, v9 dst_sel:DWORD dst_unused:UNUSED_PAD src0_sel:WORD_1
	v_cvt_pk_f16_f32 v2, v2, v3
	v_cvt_pk_f16_f32 v3, v4, v5
	v_pk_add_f32 v[4:5], v[12:13], v[14:15]
	v_cvt_f32_f16_e32 v12, v21
	v_cvt_f32_f16_sdwa v13, v21 dst_sel:DWORD dst_unused:UNUSED_PAD src0_sel:WORD_1
	v_pk_add_f32 v[4:5], v[4:5], v[6:7]
	v_pk_add_f32 v[6:7], v[10:11], v[8:9]
	v_cvt_pk_f16_f32 v4, v4, v5
	v_pk_add_f32 v[6:7], v[6:7], v[12:13]
	s_nop 0
	v_cvt_pk_f16_f32 v5, v6, v7
	v_add_lshl_u32 v6, v191, v50, 9
	v_add_u32_e32 v168, v192, v6
	ds_write_b128 v168, v[2:5]
	global_load_dwordx4 v[2:5], v[174:175], off
	global_load_dwordx4 v[8:11], v[176:177], off
	global_load_dwordx4 v[12:15], v[174:175], off offset:16
	global_load_dwordx4 v[16:19], v[176:177], off offset:16
	s_waitcnt vmcnt(3)
	v_cvt_pk_f16_f32 v6, v2, v3
	s_waitcnt vmcnt(2)
	v_cvt_pk_f16_f32 v2, v8, v9
	v_cvt_pk_f16_f32 v7, v4, v5
	v_cvt_pk_f16_f32 v3, v10, v11
	s_waitcnt vmcnt(1)
	v_cvt_pk_f16_f32 v8, v12, v13
	s_waitcnt vmcnt(0)
	v_cvt_pk_f16_f32 v4, v16, v17
	v_cvt_pk_f16_f32 v9, v14, v15
	v_cvt_pk_f16_f32 v5, v18, v19
	s_cbranch_vccz .LBB4_118
	global_load_dwordx3 v[154:156], v169, s[18:19]
	s_mov_b32 s14, s38
	s_mov_b32 s15, s39
	v_cmp_lt_u32_e64 s[64:65], 0, v199
	v_cmp_gt_u32_e64 s[66:67], 63, v199
	v_cmp_lt_u32_e64 s[68:69], 0, v180
	v_cmp_gt_u32_e64 s[70:71], 60, v180
	buffer_load_dwordx4 v[210:213], v200, s[12:15], 0 offen
	s_and_b64 s[72:73], s[68:69], s[64:65]
	s_and_b64 s[74:75], s[68:69], s[66:67]
	s_and_b64 s[76:77], s[70:71], s[64:65]
	s_and_b64 s[78:79], s[70:71], s[66:67]
	v_mov_b32_e32 v122, v6
	v_mov_b32_e32 v123, v7
	v_mov_b32_e32 v124, v8
	v_mov_b32_e32 v125, v9
	v_mov_b32_e32 v82, v2
	v_mov_b32_e32 v83, v3
	v_mov_b32_e32 v84, v4
	v_mov_b32_e32 v85, v5
	v_mov_b32_e32 v138, v6
	v_mov_b32_e32 v139, v7
	v_mov_b32_e32 v140, v8
	v_mov_b32_e32 v141, v9
	v_mov_b32_e32 v106, v2
	v_mov_b32_e32 v107, v3
	v_mov_b32_e32 v108, v4
	v_mov_b32_e32 v109, v5
	v_mov_b32_e32 v146, v6
	v_mov_b32_e32 v147, v7
	v_mov_b32_e32 v148, v8
	v_mov_b32_e32 v149, v9
	v_mov_b32_e32 v126, v2
	v_mov_b32_e32 v127, v3
	v_mov_b32_e32 v128, v4
	v_mov_b32_e32 v129, v5
	v_mov_b32_e32 v94, v6
	v_mov_b32_e32 v95, v7
	v_mov_b32_e32 v96, v8
	v_mov_b32_e32 v97, v9
	v_mov_b32_e32 v54, v2
	v_mov_b32_e32 v55, v3
	v_mov_b32_e32 v56, v4
	v_mov_b32_e32 v57, v5
	v_mov_b32_e32 v134, v6
	v_mov_b32_e32 v135, v7
	v_mov_b32_e32 v136, v8
	v_mov_b32_e32 v137, v9
	v_mov_b32_e32 v98, v2
	v_mov_b32_e32 v99, v3
	v_mov_b32_e32 v100, v4
	v_mov_b32_e32 v101, v5
	v_mov_b32_e32 v62, v6
	v_mov_b32_e32 v63, v7
	v_mov_b32_e32 v64, v8
	v_mov_b32_e32 v65, v9
	v_mov_b32_e32 v30, v2
	v_mov_b32_e32 v31, v3
	v_mov_b32_e32 v32, v4
	v_mov_b32_e32 v33, v5
	v_mov_b32_e32 v102, v6
	v_mov_b32_e32 v103, v7
	v_mov_b32_e32 v104, v8
	v_mov_b32_e32 v105, v9
	v_mov_b32_e32 v58, v2
	v_mov_b32_e32 v59, v3
	v_mov_b32_e32 v60, v4
	v_mov_b32_e32 v61, v5
	v_mov_b32_e32 v34, v6
	v_mov_b32_e32 v35, v7
	v_mov_b32_e32 v36, v8
	v_mov_b32_e32 v37, v9
	v_mov_b32_e32 v18, v2
	v_mov_b32_e32 v19, v3
	v_mov_b32_e32 v20, v4
	v_mov_b32_e32 v21, v5
	v_mov_b32_e32 v66, v6
	v_mov_b32_e32 v67, v7
	v_mov_b32_e32 v68, v8
	v_mov_b32_e32 v69, v9
	v_mov_b32_e32 v26, v2
	v_mov_b32_e32 v27, v3
	v_mov_b32_e32 v28, v4
	v_mov_b32_e32 v29, v5
	v_mov_b32_e32 v86, v6
	v_mov_b32_e32 v87, v7
	v_mov_b32_e32 v88, v8
	v_mov_b32_e32 v89, v9
	v_mov_b32_e32 v38, v2
	v_mov_b32_e32 v39, v3
	v_mov_b32_e32 v40, v4
	v_mov_b32_e32 v41, v5
	v_mov_b32_e32 v130, v6
	v_mov_b32_e32 v131, v7
	v_mov_b32_e32 v132, v8
	v_mov_b32_e32 v133, v9
	v_mov_b32_e32 v70, v2
	v_mov_b32_e32 v71, v3
	v_mov_b32_e32 v72, v4
	v_mov_b32_e32 v73, v5
	v_mov_b32_e32 v142, v6
	v_mov_b32_e32 v143, v7
	v_mov_b32_e32 v144, v8
	v_mov_b32_e32 v145, v9
	v_mov_b32_e32 v90, v2
	v_mov_b32_e32 v91, v3
	v_mov_b32_e32 v92, v4
	v_mov_b32_e32 v93, v5
	v_mov_b32_e32 v150, v6
	v_mov_b32_e32 v151, v7
	v_mov_b32_e32 v152, v8
	v_mov_b32_e32 v153, v9
	v_mov_b32_e32 v110, v2
	v_mov_b32_e32 v111, v3
	v_mov_b32_e32 v112, v4
	v_mov_b32_e32 v113, v5
	v_mov_b32_e32 v14, v6
	v_mov_b32_e32 v15, v7
	v_mov_b32_e32 v16, v8
	v_mov_b32_e32 v17, v9
	v_mov_b32_e32 v10, v2
	v_mov_b32_e32 v11, v3
	v_mov_b32_e32 v12, v4
	v_mov_b32_e32 v13, v5
	v_add_u32_e32 v245, 0xfffe7c00, v200
	v_add_u32_e32 v246, 0xfffe8000, v200
	s_mov_b64 exec, s[72:73]
	buffer_load_dwordx4 v[122:125], v245, s[12:15], 0 offen
	buffer_load_dwordx4 v[82:85], v245, s[12:15], 0 offen offset:512
	s_mov_b64 exec, -1
	s_mov_b64 exec, s[68:69]
	buffer_load_dwordx4 v[138:141], v246, s[12:15], 0 offen offset:512
	buffer_load_dwordx4 v[106:109], v246, s[12:15], 0 offen offset:1024
	s_mov_b64 exec, -1
	s_mov_b64 exec, s[74:75]
	buffer_load_dwordx4 v[146:149], v246, s[12:15], 0 offen offset:2048
	buffer_load_dwordx4 v[126:129], v246, s[12:15], 0 offen offset:2560
	s_mov_b64 exec, -1
	v_add_u32_e32 v245, 0xfffffc00, v200
	s_mov_b64 exec, s[64:65]
	buffer_load_dwordx4 v[94:97], v245, s[12:15], 0 offen
	buffer_load_dwordx4 v[54:57], v245, s[12:15], 0 offen offset:512
	s_mov_b64 exec, -1
	buffer_load_dwordx4 v[118:121], v200, s[12:15], 0 offen offset:512
	buffer_load_dwordx4 v[74:77], v200, s[12:15], 0 offen offset:1024
	s_mov_b64 exec, s[66:67]
	buffer_load_dwordx4 v[134:137], v200, s[12:15], 0 offen offset:2048
	buffer_load_dwordx4 v[98:101], v200, s[12:15], 0 offen offset:2560
	s_mov_b64 exec, -1
	v_add_u32_e32 v245, 0x17c00, v200
	v_add_u32_e32 v246, 0x18000, v200
	s_mov_b64 exec, s[64:65]
	buffer_load_dwordx4 v[62:65], v245, s[12:15], 0 offen
	buffer_load_dwordx4 v[30:33], v245, s[12:15], 0 offen offset:512
	s_mov_b64 exec, -1
	buffer_load_dwordx4 v[78:81], v246, s[12:15], 0 offen offset:512
	buffer_load_dwordx4 v[42:45], v246, s[12:15], 0 offen offset:1024
	s_mov_b64 exec, s[66:67]
	buffer_load_dwordx4 v[102:105], v246, s[12:15], 0 offen offset:2048
	buffer_load_dwordx4 v[58:61], v246, s[12:15], 0 offen offset:2560
	s_mov_b64 exec, -1
	v_add_u32_e32 v245, 0x18000, v200
	buffer_load_dwordx4 v[162:165], v245, s[12:15], 0 offen
	v_add_u32_e32 v246, 0x30000, v200
	buffer_load_dwordx4 v[158:161], v246, s[12:15], 0 offen
	v_add_u32_e32 v245, 0x2fc00, v200
	v_add_u32_e32 v246, 0x30000, v200
	v_add_u32_e32 v247, 0x47c00, v200
	v_add_u32_e32 v248, 0x48000, v200
	v_add_u32_e32 v249, 0x5fc00, v200
	v_add_u32_e32 v250, 0x60000, v200
	s_waitcnt vmcnt(21)
	v_cvt_f16_f32_e32 v206, v155
	v_cvt_f16_f32_e32 v208, v154
	v_cvt_f16_f32_e32 v207, v156
	v_add_u32_e32 v251, 0x48000, v200
	buffer_load_dwordx4 v[154:157], v251, s[12:15], 0 offen
	s_mov_b64 s[4:5], 0
	s_waitcnt vmcnt(3)
	v_pk_mul_f16 v216, v208, v213 op_sel_hi:[0,1]
	v_pk_mul_f16 v220, v206, v213 op_sel_hi:[0,1]
	v_pk_mul_f16 v224, v207, v213 op_sel_hi:[0,1]
	v_pk_mul_f16 v209, v208, v210 op_sel_hi:[0,1]
	v_pk_mul_f16 v214, v208, v211 op_sel_hi:[0,1]
	v_pk_mul_f16 v215, v208, v212 op_sel_hi:[0,1]
	v_pk_mul_f16 v217, v206, v210 op_sel_hi:[0,1]
	s_mov_b64 exec, s[64:65]
	buffer_load_dwordx4 v[34:37], v245, s[12:15], 0 offen
	buffer_load_dwordx4 v[18:21], v245, s[12:15], 0 offen offset:512
	s_mov_b64 exec, -1
	v_pk_mul_f16 v218, v206, v211 op_sel_hi:[0,1]
	v_pk_mul_f16 v219, v206, v212 op_sel_hi:[0,1]
	v_pk_mul_f16 v221, v207, v210 op_sel_hi:[0,1]
	v_pk_mul_f16 v222, v207, v211 op_sel_hi:[0,1]
	v_pk_mul_f16 v223, v207, v212 op_sel_hi:[0,1]
	v_pk_fma_f16 v125, v125, v213, v216
	v_pk_fma_f16 v141, v141, v213, v220
	v_pk_fma_f16 v149, v149, v213, v224
	v_pk_fma_f16 v225, v97, v213, v216
	v_pk_fma_f16 v229, v121, v213, v220
	v_pk_fma_f16 v233, v137, v213, v224
	v_pk_fma_f16 v216, v65, v213, v216
	v_pk_fma_f16 v220, v81, v213, v220
	buffer_load_dwordx4 v[46:49], v246, s[12:15], 0 offen offset:512
	buffer_load_dwordx4 v[22:25], v246, s[12:15], 0 offen offset:1024
	v_pk_fma_f16 v213, v105, v213, v224
	v_pk_maximum3_f16 v224, v125, v141, v149
	v_pk_fma_f16 v124, v124, v212, v215
	v_pk_fma_f16 v123, v123, v211, v214
	v_pk_fma_f16 v122, v122, v210, v209
	v_pk_fma_f16 v140, v140, v212, v219
	v_pk_fma_f16 v139, v139, v211, v218
	v_pk_fma_f16 v138, v138, v210, v217
	v_pk_fma_f16 v148, v148, v212, v223
	v_pk_fma_f16 v147, v147, v211, v222
	v_pk_fma_f16 v146, v146, v210, v221
	v_pk_fma_f16 v226, v96, v212, v215
	v_pk_fma_f16 v227, v95, v211, v214
	v_pk_fma_f16 v228, v94, v210, v209
	v_pk_fma_f16 v230, v120, v212, v219
	v_pk_fma_f16 v231, v119, v211, v218
	s_mov_b64 exec, s[66:67]
	buffer_load_dwordx4 v[66:69], v246, s[12:15], 0 offen offset:2048
	buffer_load_dwordx4 v[26:29], v246, s[12:15], 0 offen offset:2560
	s_mov_b64 exec, -1
	v_pk_fma_f16 v232, v118, v210, v217
	v_pk_fma_f16 v234, v136, v212, v223
	v_pk_fma_f16 v235, v135, v211, v222
	v_pk_fma_f16 v236, v134, v210, v221
	v_pk_fma_f16 v215, v64, v212, v215
	v_pk_fma_f16 v214, v63, v211, v214
	v_pk_fma_f16 v209, v62, v210, v209
	v_pk_fma_f16 v219, v80, v212, v219
	v_pk_fma_f16 v218, v79, v211, v218
	v_pk_fma_f16 v217, v78, v210, v217
	v_pk_fma_f16 v212, v104, v212, v223
	v_pk_fma_f16 v211, v103, v211, v222
	v_pk_fma_f16 v210, v102, v210, v221
	v_pk_maximum3_f16 v221, v122, v138, v146
	v_pk_maximum3_f16 v222, v123, v139, v147
	v_pk_maximum3_f16 v223, v124, v140, v148
	v_pk_maximum3_f16 v240, v225, v229, v233
	v_pk_maximum3_f16 v244, v216, v220, v213
	v_pk_maximum3_f16 v237, v228, v232, v236
	v_pk_maximum3_f16 v238, v227, v231, v235
	v_pk_maximum3_f16 v239, v226, v230, v234
	v_pk_maximum3_f16 v241, v209, v217, v210
	v_pk_maximum3_f16 v242, v214, v218, v211
	v_pk_maximum3_f16 v224, v224, v240, v244
	v_pk_maximum3_f16 v243, v215, v219, v212
	v_pk_maximum3_f16 v221, v221, v237, v241
	v_pk_maximum3_f16 v222, v222, v238, v242
	v_pk_maximum3_f16 v223, v223, v239, v243
	v_pk_add_f16 v125, v125, v224 neg_lo:[0,1] neg_hi:[0,1]
	s_mov_b64 exec, s[64:65]
	buffer_load_dwordx4 v[86:89], v247, s[12:15], 0 offen
	buffer_load_dwordx4 v[38:41], v247, s[12:15], 0 offen offset:512
	s_mov_b64 exec, -1
	v_pk_add_f16 v122, v122, v221 neg_lo:[0,1] neg_hi:[0,1]
	v_pk_add_f16 v123, v123, v222 neg_lo:[0,1] neg_hi:[0,1]
	v_pk_add_f16 v124, v124, v223 neg_lo:[0,1] neg_hi:[0,1]
	v_pk_add_f16 v138, v138, v221 neg_lo:[0,1] neg_hi:[0,1]
	v_exp_f16_sdwa v237, v122 dst_sel:WORD_0 dst_unused:UNUSED_PAD src0_sel:WORD_0
	v_exp_f16_sdwa v238, v123 dst_sel:WORD_0 dst_unused:UNUSED_PAD src0_sel:WORD_0
	v_exp_f16_sdwa v239, v124 dst_sel:WORD_0 dst_unused:UNUSED_PAD src0_sel:WORD_0
	v_exp_f16_sdwa v240, v125 dst_sel:WORD_0 dst_unused:UNUSED_PAD src0_sel:WORD_0
	v_exp_f16_sdwa v237, v122 dst_sel:WORD_1 dst_unused:UNUSED_PRESERVE src0_sel:WORD_1
	v_exp_f16_sdwa v238, v123 dst_sel:WORD_1 dst_unused:UNUSED_PRESERVE src0_sel:WORD_1
	v_exp_f16_sdwa v239, v124 dst_sel:WORD_1 dst_unused:UNUSED_PRESERVE src0_sel:WORD_1
	v_exp_f16_sdwa v240, v125 dst_sel:WORD_1 dst_unused:UNUSED_PRESERVE src0_sel:WORD_1
	v_pk_add_f16 v139, v139, v222 neg_lo:[0,1] neg_hi:[0,1]
	v_pk_add_f16 v125, v237, 0
	v_pk_fma_f16 v85, v85, v240, 0
	v_pk_add_f16 v122, v240, 0
	v_pk_add_f16 v123, v239, 0
	v_pk_add_f16 v124, v238, 0
	v_pk_fma_f16 v84, v84, v239, 0
	v_pk_fma_f16 v83, v83, v238, 0
	v_pk_fma_f16 v82, v82, v237, 0
	v_pk_add_f16 v140, v140, v223 neg_lo:[0,1] neg_hi:[0,1]
	buffer_load_dwordx4 v[114:117], v248, s[12:15], 0 offen offset:512
	buffer_load_dwordx4 v[50:53], v248, s[12:15], 0 offen offset:1024
	v_pk_add_f16 v141, v141, v224 neg_lo:[0,1] neg_hi:[0,1]
	v_exp_f16_sdwa v237, v138 dst_sel:WORD_0 dst_unused:UNUSED_PAD src0_sel:WORD_0
	v_exp_f16_sdwa v238, v139 dst_sel:WORD_0 dst_unused:UNUSED_PAD src0_sel:WORD_0
	v_exp_f16_sdwa v239, v140 dst_sel:WORD_0 dst_unused:UNUSED_PAD src0_sel:WORD_0
	v_exp_f16_sdwa v240, v141 dst_sel:WORD_0 dst_unused:UNUSED_PAD src0_sel:WORD_0
	v_exp_f16_sdwa v237, v138 dst_sel:WORD_1 dst_unused:UNUSED_PRESERVE src0_sel:WORD_1
	v_exp_f16_sdwa v238, v139 dst_sel:WORD_1 dst_unused:UNUSED_PRESERVE src0_sel:WORD_1
	v_exp_f16_sdwa v239, v140 dst_sel:WORD_1 dst_unused:UNUSED_PRESERVE src0_sel:WORD_1
	v_exp_f16_sdwa v240, v141 dst_sel:WORD_1 dst_unused:UNUSED_PRESERVE src0_sel:WORD_1
	v_pk_add_f16 v125, v125, v237
	v_pk_fma_f16 v85, v109, v240, v85
	v_pk_add_f16 v109, v149, v224 neg_lo:[0,1] neg_hi:[0,1]
	v_pk_add_f16 v124, v124, v238
	v_pk_add_f16 v123, v123, v239
	v_pk_add_f16 v122, v122, v240
	v_pk_fma_f16 v82, v106, v237, v82
	v_pk_fma_f16 v83, v107, v238, v83
	v_pk_fma_f16 v84, v108, v239, v84
	v_pk_add_f16 v106, v146, v221 neg_lo:[0,1] neg_hi:[0,1]
	v_pk_add_f16 v107, v147, v222 neg_lo:[0,1] neg_hi:[0,1]
	v_pk_add_f16 v108, v148, v223 neg_lo:[0,1] neg_hi:[0,1]
	v_exp_f16_sdwa v138, v106 dst_sel:WORD_0 dst_unused:UNUSED_PAD src0_sel:WORD_0
	v_exp_f16_sdwa v139, v107 dst_sel:WORD_0 dst_unused:UNUSED_PAD src0_sel:WORD_0
	v_exp_f16_sdwa v140, v108 dst_sel:WORD_0 dst_unused:UNUSED_PAD src0_sel:WORD_0
	v_exp_f16_sdwa v141, v109 dst_sel:WORD_0 dst_unused:UNUSED_PAD src0_sel:WORD_0
	v_exp_f16_sdwa v138, v106 dst_sel:WORD_1 dst_unused:UNUSED_PRESERVE src0_sel:WORD_1
	v_exp_f16_sdwa v139, v107 dst_sel:WORD_1 dst_unused:UNUSED_PRESERVE src0_sel:WORD_1
	v_exp_f16_sdwa v140, v108 dst_sel:WORD_1 dst_unused:UNUSED_PRESERVE src0_sel:WORD_1
	v_exp_f16_sdwa v141, v109 dst_sel:WORD_1 dst_unused:UNUSED_PRESERVE src0_sel:WORD_1
	v_pk_add_f16 v109, v125, v138
	v_pk_add_f16 v106, v122, v141
	s_mov_b64 exec, s[66:67]
	buffer_load_dwordx4 v[130:133], v248, s[12:15], 0 offen offset:2048
	buffer_load_dwordx4 v[70:73], v248, s[12:15], 0 offen offset:2560
	s_mov_b64 exec, -1
	v_pk_add_f16 v107, v123, v140
	v_pk_add_f16 v108, v124, v139
	v_pk_fma_f16 v85, v129, v141, v85
	v_pk_fma_f16 v84, v128, v140, v84
	v_pk_fma_f16 v83, v127, v139, v83
	v_pk_fma_f16 v82, v126, v138, v82
	v_pk_add_f16 v122, v228, v221 neg_lo:[0,1] neg_hi:[0,1]
	v_pk_add_f16 v123, v227, v222 neg_lo:[0,1] neg_hi:[0,1]
	v_pk_add_f16 v124, v226, v223 neg_lo:[0,1] neg_hi:[0,1]
	v_pk_add_f16 v125, v225, v224 neg_lo:[0,1] neg_hi:[0,1]
	v_exp_f16_sdwa v126, v122 dst_sel:WORD_0 dst_unused:UNUSED_PAD src0_sel:WORD_0
	v_exp_f16_sdwa v127, v123 dst_sel:WORD_0 dst_unused:UNUSED_PAD src0_sel:WORD_0
	v_exp_f16_sdwa v128, v124 dst_sel:WORD_0 dst_unused:UNUSED_PAD src0_sel:WORD_0
	v_exp_f16_sdwa v129, v125 dst_sel:WORD_0 dst_unused:UNUSED_PAD src0_sel:WORD_0
	v_exp_f16_sdwa v126, v122 dst_sel:WORD_1 dst_unused:UNUSED_PRESERVE src0_sel:WORD_1
	v_exp_f16_sdwa v127, v123 dst_sel:WORD_1 dst_unused:UNUSED_PRESERVE src0_sel:WORD_1
	v_exp_f16_sdwa v128, v124 dst_sel:WORD_1 dst_unused:UNUSED_PRESERVE src0_sel:WORD_1
	v_exp_f16_sdwa v129, v125 dst_sel:WORD_1 dst_unused:UNUSED_PRESERVE src0_sel:WORD_1
	v_pk_add_f16 v122, v232, v221 neg_lo:[0,1] neg_hi:[0,1]
	v_pk_add_f16 v109, v109, v126
	v_pk_add_f16 v108, v108, v127
	v_pk_add_f16 v107, v107, v128
	s_mov_b64 exec, s[76:77]
	buffer_load_dwordx4 v[142:145], v249, s[12:15], 0 offen
	buffer_load_dwordx4 v[90:93], v249, s[12:15], 0 offen offset:512
	s_mov_b64 exec, -1
	v_pk_add_f16 v106, v106, v129
	v_pk_fma_f16 v82, v54, v126, v82
	v_pk_fma_f16 v83, v55, v127, v83
	v_pk_fma_f16 v84, v56, v128, v84
	v_pk_fma_f16 v85, v57, v129, v85
	v_pk_add_f16 v123, v231, v222 neg_lo:[0,1] neg_hi:[0,1]
	v_pk_add_f16 v124, v230, v223 neg_lo:[0,1] neg_hi:[0,1]
	v_pk_add_f16 v125, v229, v224 neg_lo:[0,1] neg_hi:[0,1]
	v_exp_f16_sdwa v126, v122 dst_sel:WORD_0 dst_unused:UNUSED_PAD src0_sel:WORD_0
	v_exp_f16_sdwa v127, v123 dst_sel:WORD_0 dst_unused:UNUSED_PAD src0_sel:WORD_0
	v_exp_f16_sdwa v128, v124 dst_sel:WORD_0 dst_unused:UNUSED_PAD src0_sel:WORD_0
	v_exp_f16_sdwa v129, v125 dst_sel:WORD_0 dst_unused:UNUSED_PAD src0_sel:WORD_0
	v_exp_f16_sdwa v126, v122 dst_sel:WORD_1 dst_unused:UNUSED_PRESERVE src0_sel:WORD_1
	v_exp_f16_sdwa v127, v123 dst_sel:WORD_1 dst_unused:UNUSED_PRESERVE src0_sel:WORD_1
	v_exp_f16_sdwa v128, v124 dst_sel:WORD_1 dst_unused:UNUSED_PRESERVE src0_sel:WORD_1
	v_exp_f16_sdwa v129, v125 dst_sel:WORD_1 dst_unused:UNUSED_PRESERVE src0_sel:WORD_1
	v_pk_add_f16 v122, v236, v221 neg_lo:[0,1] neg_hi:[0,1]
	v_pk_add_f16 v109, v109, v126
	v_pk_add_f16 v106, v106, v129
	v_pk_add_f16 v107, v107, v128
	v_pk_add_f16 v108, v108, v127
	v_pk_fma_f16 v85, v77, v129, v85
	v_pk_fma_f16 v84, v76, v128, v84
	s_mov_b64 exec, s[70:71]
	buffer_load_dwordx4 v[150:153], v250, s[12:15], 0 offen offset:512
	buffer_load_dwordx4 v[110:113], v250, s[12:15], 0 offen offset:1024
	s_mov_b64 exec, -1
	v_pk_fma_f16 v83, v75, v127, v83
	v_pk_fma_f16 v82, v74, v126, v82
	v_pk_add_f16 v123, v235, v222 neg_lo:[0,1] neg_hi:[0,1]
	v_pk_add_f16 v124, v234, v223 neg_lo:[0,1] neg_hi:[0,1]
	v_pk_add_f16 v125, v233, v224 neg_lo:[0,1] neg_hi:[0,1]
	v_exp_f16_sdwa v126, v122 dst_sel:WORD_0 dst_unused:UNUSED_PAD src0_sel:WORD_0
	v_exp_f16_sdwa v127, v123 dst_sel:WORD_0 dst_unused:UNUSED_PAD src0_sel:WORD_0
	v_exp_f16_sdwa v128, v124 dst_sel:WORD_0 dst_unused:UNUSED_PAD src0_sel:WORD_0
	v_exp_f16_sdwa v129, v125 dst_sel:WORD_0 dst_unused:UNUSED_PAD src0_sel:WORD_0
	v_exp_f16_sdwa v126, v122 dst_sel:WORD_1 dst_unused:UNUSED_PRESERVE src0_sel:WORD_1
	v_exp_f16_sdwa v127, v123 dst_sel:WORD_1 dst_unused:UNUSED_PRESERVE src0_sel:WORD_1
	v_exp_f16_sdwa v128, v124 dst_sel:WORD_1 dst_unused:UNUSED_PRESERVE src0_sel:WORD_1
	v_exp_f16_sdwa v129, v125 dst_sel:WORD_1 dst_unused:UNUSED_PRESERVE src0_sel:WORD_1
	v_pk_add_f16 v122, v209, v221 neg_lo:[0,1] neg_hi:[0,1]
	v_pk_add_f16 v109, v109, v126
	v_pk_add_f16 v108, v108, v127
	v_pk_add_f16 v107, v107, v128
	v_pk_add_f16 v106, v106, v129
	v_pk_fma_f16 v82, v98, v126, v82
	v_pk_fma_f16 v83, v99, v127, v83
	v_pk_fma_f16 v84, v100, v128, v84
	v_pk_fma_f16 v85, v101, v129, v85
	s_mov_b64 exec, s[78:79]
	buffer_load_dwordx4 v[14:17], v250, s[12:15], 0 offen offset:2048
	buffer_load_dwordx4 v[10:13], v250, s[12:15], 0 offen offset:2560
	s_mov_b64 exec, -1
	v_pk_add_f16 v123, v214, v222 neg_lo:[0,1] neg_hi:[0,1]
	v_pk_add_f16 v124, v215, v223 neg_lo:[0,1] neg_hi:[0,1]
	v_pk_add_f16 v125, v216, v224 neg_lo:[0,1] neg_hi:[0,1]
	v_exp_f16_sdwa v126, v122 dst_sel:WORD_0 dst_unused:UNUSED_PAD src0_sel:WORD_0
	v_exp_f16_sdwa v127, v123 dst_sel:WORD_0 dst_unused:UNUSED_PAD src0_sel:WORD_0
	v_exp_f16_sdwa v128, v124 dst_sel:WORD_0 dst_unused:UNUSED_PAD src0_sel:WORD_0
	v_exp_f16_sdwa v129, v125 dst_sel:WORD_0 dst_unused:UNUSED_PAD src0_sel:WORD_0
	v_exp_f16_sdwa v126, v122 dst_sel:WORD_1 dst_unused:UNUSED_PRESERVE src0_sel:WORD_1
	v_exp_f16_sdwa v127, v123 dst_sel:WORD_1 dst_unused:UNUSED_PRESERVE src0_sel:WORD_1
	v_exp_f16_sdwa v128, v124 dst_sel:WORD_1 dst_unused:UNUSED_PRESERVE src0_sel:WORD_1
	v_exp_f16_sdwa v129, v125 dst_sel:WORD_1 dst_unused:UNUSED_PRESERVE src0_sel:WORD_1
	v_pk_add_f16 v122, v217, v221 neg_lo:[0,1] neg_hi:[0,1]
	v_pk_add_f16 v109, v109, v126
	v_pk_add_f16 v106, v106, v129
	v_pk_add_f16 v107, v107, v128
	v_pk_add_f16 v108, v108, v127
	v_pk_fma_f16 v85, v33, v129, v85
	v_pk_fma_f16 v84, v32, v128, v84
	v_pk_fma_f16 v83, v31, v127, v83
	v_pk_fma_f16 v82, v30, v126, v82
	v_pk_add_f16 v123, v218, v222 neg_lo:[0,1] neg_hi:[0,1]
	v_pk_add_f16 v124, v219, v223 neg_lo:[0,1] neg_hi:[0,1]
	v_pk_add_f16 v125, v220, v224 neg_lo:[0,1] neg_hi:[0,1]
	v_exp_f16_sdwa v126, v122 dst_sel:WORD_0 dst_unused:UNUSED_PAD src0_sel:WORD_0
	v_exp_f16_sdwa v127, v123 dst_sel:WORD_0 dst_unused:UNUSED_PAD src0_sel:WORD_0
	v_exp_f16_sdwa v128, v124 dst_sel:WORD_0 dst_unused:UNUSED_PAD src0_sel:WORD_0
	v_exp_f16_sdwa v129, v125 dst_sel:WORD_0 dst_unused:UNUSED_PAD src0_sel:WORD_0
	v_exp_f16_sdwa v126, v122 dst_sel:WORD_1 dst_unused:UNUSED_PRESERVE src0_sel:WORD_1
	v_exp_f16_sdwa v127, v123 dst_sel:WORD_1 dst_unused:UNUSED_PRESERVE src0_sel:WORD_1
	v_exp_f16_sdwa v128, v124 dst_sel:WORD_1 dst_unused:UNUSED_PRESERVE src0_sel:WORD_1
	v_exp_f16_sdwa v129, v125 dst_sel:WORD_1 dst_unused:UNUSED_PRESERVE src0_sel:WORD_1
	v_pk_add_f16 v122, v210, v221 neg_lo:[0,1] neg_hi:[0,1]
	v_pk_add_f16 v109, v109, v126
	v_pk_add_f16 v108, v108, v127
	v_pk_add_f16 v107, v107, v128
	v_pk_add_f16 v106, v106, v129
	v_pk_fma_f16 v82, v42, v126, v82
	v_pk_fma_f16 v83, v43, v127, v83
	v_pk_fma_f16 v84, v44, v128, v84
	v_pk_fma_f16 v85, v45, v129, v85
	v_pk_add_f16 v123, v211, v222 neg_lo:[0,1] neg_hi:[0,1]
	v_pk_add_f16 v124, v212, v223 neg_lo:[0,1] neg_hi:[0,1]
	v_pk_add_f16 v125, v213, v224 neg_lo:[0,1] neg_hi:[0,1]
	v_exp_f16_sdwa v126, v122 dst_sel:WORD_0 dst_unused:UNUSED_PAD src0_sel:WORD_0
	v_exp_f16_sdwa v127, v123 dst_sel:WORD_0 dst_unused:UNUSED_PAD src0_sel:WORD_0
	v_exp_f16_sdwa v128, v124 dst_sel:WORD_0 dst_unused:UNUSED_PAD src0_sel:WORD_0
	v_exp_f16_sdwa v129, v125 dst_sel:WORD_0 dst_unused:UNUSED_PAD src0_sel:WORD_0
	v_exp_f16_sdwa v126, v122 dst_sel:WORD_1 dst_unused:UNUSED_PRESERVE src0_sel:WORD_1
	v_exp_f16_sdwa v127, v123 dst_sel:WORD_1 dst_unused:UNUSED_PRESERVE src0_sel:WORD_1
	v_exp_f16_sdwa v128, v124 dst_sel:WORD_1 dst_unused:UNUSED_PRESERVE src0_sel:WORD_1
	v_exp_f16_sdwa v129, v125 dst_sel:WORD_1 dst_unused:UNUSED_PRESERVE src0_sel:WORD_1
	v_pk_add_f16 v109, v109, v126
	v_pk_add_f16 v108, v108, v127
	v_rcp_f16_e32 v122, v109
	v_rcp_f16_sdwa v109, v109 dst_sel:DWORD dst_unused:UNUSED_PAD src0_sel:WORD_1
	v_pk_add_f16 v107, v107, v128
	v_rcp_f16_e32 v123, v108
	v_rcp_f16_sdwa v108, v108 dst_sel:DWORD dst_unused:UNUSED_PAD src0_sel:WORD_1
	v_pk_add_f16 v106, v106, v129
	v_rcp_f16_e32 v124, v107
	v_rcp_f16_sdwa v107, v107 dst_sel:DWORD dst_unused:UNUSED_PAD src0_sel:WORD_1
	v_rcp_f16_e32 v125, v106
	v_rcp_f16_sdwa v106, v106 dst_sel:DWORD dst_unused:UNUSED_PAD src0_sel:WORD_1
	v_pk_fma_f16 v82, v58, v126, v82
	v_pack_b32_f16 v109, v122, v109
	v_pk_fma_f16 v83, v59, v127, v83
	v_pk_mul_f16 v141, v82, v109
	v_pack_b32_f16 v82, v123, v108
	v_pk_fma_f16 v84, v60, v128, v84
	v_pk_mul_f16 v140, v83, v82
	v_pack_b32_f16 v82, v124, v107
	v_pk_fma_f16 v85, v61, v129, v85
	v_pk_mul_f16 v139, v84, v82
	v_pack_b32_f16 v82, v125, v106
	v_pk_mul_f16 v138, v85, v82
	s_waitcnt vmcnt(12)
	v_pk_mul_f16 v85, v208, v165 op_sel_hi:[0,1]
	v_pk_mul_f16 v109, v206, v165 op_sel_hi:[0,1]
	v_pk_mul_f16 v122, v207, v162 op_sel_hi:[0,1]
	v_pk_mul_f16 v125, v207, v165 op_sel_hi:[0,1]
	v_pk_mul_f16 v82, v208, v162 op_sel_hi:[0,1]
	v_pk_mul_f16 v83, v208, v163 op_sel_hi:[0,1]
	v_pk_mul_f16 v84, v208, v164 op_sel_hi:[0,1]
	v_pk_mul_f16 v106, v206, v162 op_sel_hi:[0,1]
	v_pk_mul_f16 v107, v206, v163 op_sel_hi:[0,1]
	v_pk_mul_f16 v108, v206, v164 op_sel_hi:[0,1]
	v_pk_mul_f16 v123, v207, v163 op_sel_hi:[0,1]
	v_pk_mul_f16 v124, v207, v164 op_sel_hi:[0,1]
	v_pk_fma_f16 v97, v97, v165, v85
	v_pk_fma_f16 v121, v121, v165, v109
	v_pk_fma_f16 v126, v137, v165, v125
	v_pk_fma_f16 v129, v134, v162, v122
	v_pk_fma_f16 v134, v65, v165, v85
	v_pk_fma_f16 v146, v81, v165, v109
	v_pk_fma_f16 v209, v105, v165, v125
	v_pk_fma_f16 v85, v37, v165, v85
	v_pk_fma_f16 v109, v49, v165, v109
	v_pk_fma_f16 v125, v69, v165, v125
	v_pk_maximum3_f16 v165, v97, v121, v126
	v_pk_fma_f16 v96, v96, v164, v84
	v_pk_fma_f16 v95, v95, v163, v83
	v_pk_fma_f16 v94, v94, v162, v82
	v_pk_fma_f16 v120, v120, v164, v108
	v_pk_fma_f16 v119, v119, v163, v107
	v_pk_fma_f16 v118, v118, v162, v106
	v_pk_fma_f16 v127, v136, v164, v124
	v_pk_fma_f16 v128, v135, v163, v123
	v_pk_fma_f16 v135, v64, v164, v84
	v_pk_fma_f16 v136, v63, v163, v83
	v_pk_fma_f16 v137, v62, v162, v82
	v_pk_fma_f16 v147, v80, v164, v108
	v_pk_fma_f16 v148, v79, v163, v107
	v_pk_fma_f16 v149, v78, v162, v106
	v_pk_fma_f16 v210, v104, v164, v124
	v_pk_fma_f16 v211, v103, v163, v123
	v_pk_fma_f16 v212, v102, v162, v122
	v_pk_fma_f16 v84, v36, v164, v84
	v_pk_fma_f16 v83, v35, v163, v83
	v_pk_fma_f16 v82, v34, v162, v82
	v_pk_fma_f16 v108, v48, v164, v108
	v_pk_fma_f16 v107, v47, v163, v107
	v_pk_fma_f16 v106, v46, v162, v106
	v_pk_fma_f16 v124, v68, v164, v124
	v_pk_fma_f16 v123, v67, v163, v123
	v_pk_fma_f16 v122, v66, v162, v122
	v_pk_maximum3_f16 v162, v94, v118, v129
	v_pk_maximum3_f16 v163, v95, v119, v128
	v_pk_maximum3_f16 v164, v96, v120, v127
	v_pk_maximum3_f16 v216, v134, v146, v209
	v_pk_maximum3_f16 v220, v85, v109, v125
	v_pk_maximum3_f16 v213, v137, v149, v212
	v_pk_maximum3_f16 v214, v136, v148, v211
	v_pk_maximum3_f16 v215, v135, v147, v210
	v_pk_maximum3_f16 v217, v82, v106, v122
	v_pk_maximum3_f16 v218, v83, v107, v123
	v_pk_maximum3_f16 v165, v165, v216, v220
	v_pk_maximum3_f16 v219, v84, v108, v124
	v_pk_maximum3_f16 v162, v162, v213, v217
	v_pk_maximum3_f16 v163, v163, v214, v218
	v_pk_maximum3_f16 v164, v164, v215, v219
	v_pk_add_f16 v97, v97, v165 neg_lo:[0,1] neg_hi:[0,1]
	v_pk_add_f16 v94, v94, v162 neg_lo:[0,1] neg_hi:[0,1]
	v_pk_add_f16 v95, v95, v163 neg_lo:[0,1] neg_hi:[0,1]
	v_pk_add_f16 v96, v96, v164 neg_lo:[0,1] neg_hi:[0,1]
	v_pk_add_f16 v118, v118, v162 neg_lo:[0,1] neg_hi:[0,1]
	v_exp_f16_sdwa v213, v94 dst_sel:WORD_0 dst_unused:UNUSED_PAD src0_sel:WORD_0
	v_exp_f16_sdwa v214, v95 dst_sel:WORD_0 dst_unused:UNUSED_PAD src0_sel:WORD_0
	v_exp_f16_sdwa v215, v96 dst_sel:WORD_0 dst_unused:UNUSED_PAD src0_sel:WORD_0
	v_exp_f16_sdwa v216, v97 dst_sel:WORD_0 dst_unused:UNUSED_PAD src0_sel:WORD_0
	v_exp_f16_sdwa v213, v94 dst_sel:WORD_1 dst_unused:UNUSED_PRESERVE src0_sel:WORD_1
	v_exp_f16_sdwa v214, v95 dst_sel:WORD_1 dst_unused:UNUSED_PRESERVE src0_sel:WORD_1
	v_exp_f16_sdwa v215, v96 dst_sel:WORD_1 dst_unused:UNUSED_PRESERVE src0_sel:WORD_1
	v_exp_f16_sdwa v216, v97 dst_sel:WORD_1 dst_unused:UNUSED_PRESERVE src0_sel:WORD_1
	v_pk_add_f16 v119, v119, v163 neg_lo:[0,1] neg_hi:[0,1]
	v_pk_add_f16 v97, v213, 0
	v_pk_fma_f16 v57, v57, v216, 0
	v_pk_add_f16 v94, v216, 0
	v_pk_add_f16 v95, v215, 0
	v_pk_add_f16 v96, v214, 0
	v_pk_fma_f16 v56, v56, v215, 0
	v_pk_fma_f16 v55, v55, v214, 0
	v_pk_fma_f16 v54, v54, v213, 0
	v_pk_add_f16 v120, v120, v164 neg_lo:[0,1] neg_hi:[0,1]
	v_pk_add_f16 v121, v121, v165 neg_lo:[0,1] neg_hi:[0,1]
	v_pk_add_f16 v82, v82, v162 neg_lo:[0,1] neg_hi:[0,1]
	v_exp_f16_sdwa v213, v118 dst_sel:WORD_0 dst_unused:UNUSED_PAD src0_sel:WORD_0
	v_exp_f16_sdwa v214, v119 dst_sel:WORD_0 dst_unused:UNUSED_PAD src0_sel:WORD_0
	v_exp_f16_sdwa v215, v120 dst_sel:WORD_0 dst_unused:UNUSED_PAD src0_sel:WORD_0
	v_exp_f16_sdwa v216, v121 dst_sel:WORD_0 dst_unused:UNUSED_PAD src0_sel:WORD_0
	v_exp_f16_sdwa v213, v118 dst_sel:WORD_1 dst_unused:UNUSED_PRESERVE src0_sel:WORD_1
	v_exp_f16_sdwa v214, v119 dst_sel:WORD_1 dst_unused:UNUSED_PRESERVE src0_sel:WORD_1
	v_exp_f16_sdwa v215, v120 dst_sel:WORD_1 dst_unused:UNUSED_PRESERVE src0_sel:WORD_1
	v_exp_f16_sdwa v216, v121 dst_sel:WORD_1 dst_unused:UNUSED_PRESERVE src0_sel:WORD_1
	v_pk_add_f16 v83, v83, v163 neg_lo:[0,1] neg_hi:[0,1]
	v_pk_add_f16 v97, v97, v213
	v_pk_fma_f16 v57, v77, v216, v57
	v_pk_add_f16 v77, v126, v165 neg_lo:[0,1] neg_hi:[0,1]
	v_pk_add_f16 v96, v96, v214
	v_pk_add_f16 v95, v95, v215
	v_pk_add_f16 v94, v94, v216
	v_pk_fma_f16 v54, v74, v213, v54
	v_pk_fma_f16 v55, v75, v214, v55
	v_pk_fma_f16 v56, v76, v215, v56
	v_pk_add_f16 v74, v129, v162 neg_lo:[0,1] neg_hi:[0,1]
	v_pk_add_f16 v75, v128, v163 neg_lo:[0,1] neg_hi:[0,1]
	v_pk_add_f16 v76, v127, v164 neg_lo:[0,1] neg_hi:[0,1]
	v_pk_add_f16 v84, v84, v164 neg_lo:[0,1] neg_hi:[0,1]
	v_exp_f16_sdwa v118, v74 dst_sel:WORD_0 dst_unused:UNUSED_PAD src0_sel:WORD_0
	v_exp_f16_sdwa v119, v75 dst_sel:WORD_0 dst_unused:UNUSED_PAD src0_sel:WORD_0
	v_exp_f16_sdwa v120, v76 dst_sel:WORD_0 dst_unused:UNUSED_PAD src0_sel:WORD_0
	v_exp_f16_sdwa v121, v77 dst_sel:WORD_0 dst_unused:UNUSED_PAD src0_sel:WORD_0
	v_exp_f16_sdwa v118, v74 dst_sel:WORD_1 dst_unused:UNUSED_PRESERVE src0_sel:WORD_1
	v_exp_f16_sdwa v119, v75 dst_sel:WORD_1 dst_unused:UNUSED_PRESERVE src0_sel:WORD_1
	v_exp_f16_sdwa v120, v76 dst_sel:WORD_1 dst_unused:UNUSED_PRESERVE src0_sel:WORD_1
	v_exp_f16_sdwa v121, v77 dst_sel:WORD_1 dst_unused:UNUSED_PRESERVE src0_sel:WORD_1
	v_pk_add_f16 v85, v85, v165 neg_lo:[0,1] neg_hi:[0,1]
	v_pk_add_f16 v77, v97, v118
	v_pk_add_f16 v74, v94, v121
	v_pk_add_f16 v75, v95, v120
	v_pk_add_f16 v76, v96, v119
	v_pk_fma_f16 v57, v101, v121, v57
	v_pk_fma_f16 v56, v100, v120, v56
	v_pk_fma_f16 v55, v99, v119, v55
	v_pk_fma_f16 v54, v98, v118, v54
	v_pk_add_f16 v94, v137, v162 neg_lo:[0,1] neg_hi:[0,1]
	v_pk_add_f16 v95, v136, v163 neg_lo:[0,1] neg_hi:[0,1]
	v_pk_add_f16 v96, v135, v164 neg_lo:[0,1] neg_hi:[0,1]
	v_pk_add_f16 v97, v134, v165 neg_lo:[0,1] neg_hi:[0,1]
	v_exp_f16_sdwa v98, v94 dst_sel:WORD_0 dst_unused:UNUSED_PAD src0_sel:WORD_0
	v_exp_f16_sdwa v99, v95 dst_sel:WORD_0 dst_unused:UNUSED_PAD src0_sel:WORD_0
	v_exp_f16_sdwa v100, v96 dst_sel:WORD_0 dst_unused:UNUSED_PAD src0_sel:WORD_0
	v_exp_f16_sdwa v101, v97 dst_sel:WORD_0 dst_unused:UNUSED_PAD src0_sel:WORD_0
	v_exp_f16_sdwa v98, v94 dst_sel:WORD_1 dst_unused:UNUSED_PRESERVE src0_sel:WORD_1
	v_exp_f16_sdwa v99, v95 dst_sel:WORD_1 dst_unused:UNUSED_PRESERVE src0_sel:WORD_1
	v_exp_f16_sdwa v100, v96 dst_sel:WORD_1 dst_unused:UNUSED_PRESERVE src0_sel:WORD_1
	v_exp_f16_sdwa v101, v97 dst_sel:WORD_1 dst_unused:UNUSED_PRESERVE src0_sel:WORD_1
	v_pk_add_f16 v94, v149, v162 neg_lo:[0,1] neg_hi:[0,1]
	v_pk_add_f16 v77, v77, v98
	v_pk_add_f16 v76, v76, v99
	v_pk_add_f16 v75, v75, v100
	v_pk_add_f16 v74, v74, v101
	v_pk_fma_f16 v54, v30, v98, v54
	v_pk_fma_f16 v55, v31, v99, v55
	v_pk_fma_f16 v56, v32, v100, v56
	v_pk_fma_f16 v57, v33, v101, v57
	v_pk_add_f16 v95, v148, v163 neg_lo:[0,1] neg_hi:[0,1]
	v_pk_add_f16 v96, v147, v164 neg_lo:[0,1] neg_hi:[0,1]
	v_pk_add_f16 v97, v146, v165 neg_lo:[0,1] neg_hi:[0,1]
	v_exp_f16_sdwa v98, v94 dst_sel:WORD_0 dst_unused:UNUSED_PAD src0_sel:WORD_0
	v_exp_f16_sdwa v99, v95 dst_sel:WORD_0 dst_unused:UNUSED_PAD src0_sel:WORD_0
	v_exp_f16_sdwa v100, v96 dst_sel:WORD_0 dst_unused:UNUSED_PAD src0_sel:WORD_0
	v_exp_f16_sdwa v101, v97 dst_sel:WORD_0 dst_unused:UNUSED_PAD src0_sel:WORD_0
	v_exp_f16_sdwa v98, v94 dst_sel:WORD_1 dst_unused:UNUSED_PRESERVE src0_sel:WORD_1
	v_exp_f16_sdwa v99, v95 dst_sel:WORD_1 dst_unused:UNUSED_PRESERVE src0_sel:WORD_1
	v_exp_f16_sdwa v100, v96 dst_sel:WORD_1 dst_unused:UNUSED_PRESERVE src0_sel:WORD_1
	v_exp_f16_sdwa v101, v97 dst_sel:WORD_1 dst_unused:UNUSED_PRESERVE src0_sel:WORD_1
	v_pk_add_f16 v94, v212, v162 neg_lo:[0,1] neg_hi:[0,1]
	v_pk_add_f16 v77, v77, v98
	v_pk_add_f16 v74, v74, v101
	v_pk_add_f16 v75, v75, v100
	v_pk_add_f16 v76, v76, v99
	v_pk_fma_f16 v57, v45, v101, v57
	v_pk_fma_f16 v56, v44, v100, v56
	v_pk_fma_f16 v55, v43, v99, v55
	v_pk_fma_f16 v54, v42, v98, v54
	v_pk_add_f16 v95, v211, v163 neg_lo:[0,1] neg_hi:[0,1]
	v_pk_add_f16 v96, v210, v164 neg_lo:[0,1] neg_hi:[0,1]
	v_pk_add_f16 v97, v209, v165 neg_lo:[0,1] neg_hi:[0,1]
	v_exp_f16_sdwa v98, v94 dst_sel:WORD_0 dst_unused:UNUSED_PAD src0_sel:WORD_0
	v_exp_f16_sdwa v99, v95 dst_sel:WORD_0 dst_unused:UNUSED_PAD src0_sel:WORD_0
	v_exp_f16_sdwa v100, v96 dst_sel:WORD_0 dst_unused:UNUSED_PAD src0_sel:WORD_0
	v_exp_f16_sdwa v101, v97 dst_sel:WORD_0 dst_unused:UNUSED_PAD src0_sel:WORD_0
	v_exp_f16_sdwa v98, v94 dst_sel:WORD_1 dst_unused:UNUSED_PRESERVE src0_sel:WORD_1
	v_exp_f16_sdwa v99, v95 dst_sel:WORD_1 dst_unused:UNUSED_PRESERVE src0_sel:WORD_1
	v_exp_f16_sdwa v100, v96 dst_sel:WORD_1 dst_unused:UNUSED_PRESERVE src0_sel:WORD_1
	v_exp_f16_sdwa v101, v97 dst_sel:WORD_1 dst_unused:UNUSED_PRESERVE src0_sel:WORD_1
	v_exp_f16_sdwa v94, v82 dst_sel:WORD_0 dst_unused:UNUSED_PAD src0_sel:WORD_0
	v_exp_f16_sdwa v95, v83 dst_sel:WORD_0 dst_unused:UNUSED_PAD src0_sel:WORD_0
	v_exp_f16_sdwa v96, v84 dst_sel:WORD_0 dst_unused:UNUSED_PAD src0_sel:WORD_0
	v_exp_f16_sdwa v97, v85 dst_sel:WORD_0 dst_unused:UNUSED_PAD src0_sel:WORD_0
	v_exp_f16_sdwa v94, v82 dst_sel:WORD_1 dst_unused:UNUSED_PRESERVE src0_sel:WORD_1
	v_exp_f16_sdwa v95, v83 dst_sel:WORD_1 dst_unused:UNUSED_PRESERVE src0_sel:WORD_1
	v_exp_f16_sdwa v96, v84 dst_sel:WORD_1 dst_unused:UNUSED_PRESERVE src0_sel:WORD_1
	v_exp_f16_sdwa v97, v85 dst_sel:WORD_1 dst_unused:UNUSED_PRESERVE src0_sel:WORD_1
	v_pk_add_f16 v82, v106, v162 neg_lo:[0,1] neg_hi:[0,1]
	v_pk_add_f16 v77, v77, v98
	v_pk_add_f16 v76, v76, v99
	v_pk_add_f16 v75, v75, v100
	v_pk_add_f16 v74, v74, v101
	v_pk_fma_f16 v54, v58, v98, v54
	v_pk_fma_f16 v55, v59, v99, v55
	v_pk_fma_f16 v56, v60, v100, v56
	v_pk_fma_f16 v57, v61, v101, v57
	v_pk_add_f16 v77, v77, v94
	v_pk_add_f16 v74, v74, v97
	v_pk_add_f16 v75, v75, v96
	v_pk_add_f16 v76, v76, v95
	v_pk_fma_f16 v57, v21, v97, v57
	v_pk_fma_f16 v56, v20, v96, v56
	v_pk_fma_f16 v55, v19, v95, v55
	v_pk_fma_f16 v54, v18, v94, v54
	v_pk_add_f16 v83, v107, v163 neg_lo:[0,1] neg_hi:[0,1]
	v_pk_add_f16 v84, v108, v164 neg_lo:[0,1] neg_hi:[0,1]
	v_pk_add_f16 v85, v109, v165 neg_lo:[0,1] neg_hi:[0,1]
	v_exp_f16_sdwa v94, v82 dst_sel:WORD_0 dst_unused:UNUSED_PAD src0_sel:WORD_0
	v_exp_f16_sdwa v95, v83 dst_sel:WORD_0 dst_unused:UNUSED_PAD src0_sel:WORD_0
	v_exp_f16_sdwa v96, v84 dst_sel:WORD_0 dst_unused:UNUSED_PAD src0_sel:WORD_0
	v_exp_f16_sdwa v97, v85 dst_sel:WORD_0 dst_unused:UNUSED_PAD src0_sel:WORD_0
	v_exp_f16_sdwa v94, v82 dst_sel:WORD_1 dst_unused:UNUSED_PRESERVE src0_sel:WORD_1
	v_exp_f16_sdwa v95, v83 dst_sel:WORD_1 dst_unused:UNUSED_PRESERVE src0_sel:WORD_1
	v_exp_f16_sdwa v96, v84 dst_sel:WORD_1 dst_unused:UNUSED_PRESERVE src0_sel:WORD_1
	v_exp_f16_sdwa v97, v85 dst_sel:WORD_1 dst_unused:UNUSED_PRESERVE src0_sel:WORD_1
	v_pk_add_f16 v82, v122, v162 neg_lo:[0,1] neg_hi:[0,1]
	v_pk_add_f16 v77, v77, v94
	v_pk_add_f16 v76, v76, v95
	v_pk_add_f16 v75, v75, v96
	v_pk_add_f16 v74, v74, v97
	v_pk_fma_f16 v54, v22, v94, v54
	v_pk_fma_f16 v55, v23, v95, v55
	v_pk_fma_f16 v56, v24, v96, v56
	v_pk_fma_f16 v57, v25, v97, v57
	v_pk_add_f16 v83, v123, v163 neg_lo:[0,1] neg_hi:[0,1]
	v_pk_add_f16 v84, v124, v164 neg_lo:[0,1] neg_hi:[0,1]
	v_pk_add_f16 v85, v125, v165 neg_lo:[0,1] neg_hi:[0,1]
	v_exp_f16_sdwa v94, v82 dst_sel:WORD_0 dst_unused:UNUSED_PAD src0_sel:WORD_0
	v_exp_f16_sdwa v95, v83 dst_sel:WORD_0 dst_unused:UNUSED_PAD src0_sel:WORD_0
	v_exp_f16_sdwa v96, v84 dst_sel:WORD_0 dst_unused:UNUSED_PAD src0_sel:WORD_0
	v_exp_f16_sdwa v97, v85 dst_sel:WORD_0 dst_unused:UNUSED_PAD src0_sel:WORD_0
	v_exp_f16_sdwa v94, v82 dst_sel:WORD_1 dst_unused:UNUSED_PRESERVE src0_sel:WORD_1
	v_exp_f16_sdwa v95, v83 dst_sel:WORD_1 dst_unused:UNUSED_PRESERVE src0_sel:WORD_1
	v_exp_f16_sdwa v96, v84 dst_sel:WORD_1 dst_unused:UNUSED_PRESERVE src0_sel:WORD_1
	v_exp_f16_sdwa v97, v85 dst_sel:WORD_1 dst_unused:UNUSED_PRESERVE src0_sel:WORD_1
	v_pk_add_f16 v77, v77, v94
	v_pk_add_f16 v76, v76, v95
	v_rcp_f16_e32 v82, v77
	v_rcp_f16_sdwa v77, v77 dst_sel:DWORD dst_unused:UNUSED_PAD src0_sel:WORD_1
	v_pk_add_f16 v75, v75, v96
	v_rcp_f16_e32 v83, v76
	v_rcp_f16_sdwa v76, v76 dst_sel:DWORD dst_unused:UNUSED_PAD src0_sel:WORD_1
	v_pk_add_f16 v74, v74, v97
	v_rcp_f16_e32 v84, v75
	v_rcp_f16_sdwa v75, v75 dst_sel:DWORD dst_unused:UNUSED_PAD src0_sel:WORD_1
	v_rcp_f16_e32 v85, v74
	v_rcp_f16_sdwa v74, v74 dst_sel:DWORD dst_unused:UNUSED_PAD src0_sel:WORD_1
	v_pk_fma_f16 v54, v26, v94, v54
	v_pack_b32_f16 v77, v82, v77
	v_pk_fma_f16 v57, v29, v97, v57
	v_pk_fma_f16 v55, v27, v95, v55
	v_pk_mul_f16 v97, v54, v77
	v_pack_b32_f16 v54, v83, v76
	v_pk_fma_f16 v56, v28, v96, v56
	v_pk_mul_f16 v96, v55, v54
	v_pack_b32_f16 v54, v84, v75
	v_pk_mul_f16 v95, v56, v54
	v_pack_b32_f16 v54, v85, v74
	v_pk_mul_f16 v94, v57, v54
	s_waitcnt vmcnt(6)
	v_pk_mul_f16 v57, v208, v161 op_sel_hi:[0,1]
	v_pk_mul_f16 v77, v206, v161 op_sel_hi:[0,1]
	v_pk_mul_f16 v85, v207, v161 op_sel_hi:[0,1]
	v_pk_mul_f16 v54, v208, v158 op_sel_hi:[0,1]
	v_pk_mul_f16 v55, v208, v159 op_sel_hi:[0,1]
	v_pk_mul_f16 v56, v208, v160 op_sel_hi:[0,1]
	v_pk_mul_f16 v74, v206, v158 op_sel_hi:[0,1]
	v_pk_mul_f16 v75, v206, v159 op_sel_hi:[0,1]
	v_pk_mul_f16 v76, v206, v160 op_sel_hi:[0,1]
	v_pk_mul_f16 v82, v207, v158 op_sel_hi:[0,1]
	v_pk_mul_f16 v83, v207, v159 op_sel_hi:[0,1]
	v_pk_mul_f16 v84, v207, v160 op_sel_hi:[0,1]
	v_pk_fma_f16 v65, v65, v161, v57
	v_pk_fma_f16 v81, v81, v161, v77
	v_pk_fma_f16 v98, v105, v161, v85
	v_pk_fma_f16 v64, v64, v160, v56
	v_pk_maximum3_f16 v125, v65, v81, v98
	v_pk_fma_f16 v63, v63, v159, v55
	v_pk_fma_f16 v62, v62, v158, v54
	v_pk_fma_f16 v80, v80, v160, v76
	v_pk_fma_f16 v79, v79, v159, v75
	v_pk_fma_f16 v78, v78, v158, v74
	v_pk_fma_f16 v99, v104, v160, v84
	v_pk_fma_f16 v100, v103, v159, v83
	v_pk_fma_f16 v101, v102, v158, v82
	v_pk_fma_f16 v102, v37, v161, v57
	v_pk_fma_f16 v106, v49, v161, v77
	v_pk_fma_f16 v118, v69, v161, v85
	v_pk_fma_f16 v57, v89, v161, v57
	v_pk_fma_f16 v77, v117, v161, v77
	v_pk_fma_f16 v85, v133, v161, v85
	v_pk_maximum3_f16 v122, v62, v78, v101
	v_pk_maximum3_f16 v123, v63, v79, v100
	v_pk_maximum3_f16 v124, v64, v80, v99
	v_pk_maximum3_f16 v129, v102, v106, v118
	v_pk_fma_f16 v103, v36, v160, v56
	v_pk_maximum3_f16 v137, v57, v77, v85
	v_pk_fma_f16 v104, v35, v159, v55
	v_pk_maximum3_f16 v125, v125, v129, v137
	v_pk_fma_f16 v105, v34, v158, v54
	v_pk_fma_f16 v107, v48, v160, v76
	v_pk_fma_f16 v108, v47, v159, v75
	v_pk_fma_f16 v109, v46, v158, v74
	v_pk_fma_f16 v119, v68, v160, v84
	v_pk_fma_f16 v120, v67, v159, v83
	v_pk_fma_f16 v121, v66, v158, v82
	v_pk_fma_f16 v56, v88, v160, v56
	v_pk_fma_f16 v55, v87, v159, v55
	v_pk_fma_f16 v54, v86, v158, v54
	v_pk_fma_f16 v76, v116, v160, v76
	v_pk_fma_f16 v75, v115, v159, v75
	v_pk_fma_f16 v74, v114, v158, v74
	v_pk_fma_f16 v84, v132, v160, v84
	v_pk_fma_f16 v83, v131, v159, v83
	v_pk_fma_f16 v82, v130, v158, v82
	v_pk_maximum3_f16 v126, v105, v109, v121
	v_pk_maximum3_f16 v127, v104, v108, v120
	v_pk_maximum3_f16 v128, v103, v107, v119
	v_pk_maximum3_f16 v135, v55, v75, v83
	v_pk_maximum3_f16 v136, v56, v76, v84
	v_pk_maximum3_f16 v134, v54, v74, v82
	v_pk_maximum3_f16 v122, v122, v126, v134
	v_pk_maximum3_f16 v123, v123, v127, v135
	v_pk_maximum3_f16 v124, v124, v128, v136
	v_pk_add_f16 v65, v65, v125 neg_lo:[0,1] neg_hi:[0,1]
	v_pk_add_f16 v62, v62, v122 neg_lo:[0,1] neg_hi:[0,1]
	v_pk_add_f16 v63, v63, v123 neg_lo:[0,1] neg_hi:[0,1]
	v_pk_add_f16 v64, v64, v124 neg_lo:[0,1] neg_hi:[0,1]
	v_pk_add_f16 v78, v78, v122 neg_lo:[0,1] neg_hi:[0,1]
	v_exp_f16_sdwa v126, v62 dst_sel:WORD_0 dst_unused:UNUSED_PAD src0_sel:WORD_0
	v_exp_f16_sdwa v127, v63 dst_sel:WORD_0 dst_unused:UNUSED_PAD src0_sel:WORD_0
	v_exp_f16_sdwa v128, v64 dst_sel:WORD_0 dst_unused:UNUSED_PAD src0_sel:WORD_0
	v_exp_f16_sdwa v129, v65 dst_sel:WORD_0 dst_unused:UNUSED_PAD src0_sel:WORD_0
	v_exp_f16_sdwa v126, v62 dst_sel:WORD_1 dst_unused:UNUSED_PRESERVE src0_sel:WORD_1
	v_exp_f16_sdwa v127, v63 dst_sel:WORD_1 dst_unused:UNUSED_PRESERVE src0_sel:WORD_1
	v_exp_f16_sdwa v128, v64 dst_sel:WORD_1 dst_unused:UNUSED_PRESERVE src0_sel:WORD_1
	v_exp_f16_sdwa v129, v65 dst_sel:WORD_1 dst_unused:UNUSED_PRESERVE src0_sel:WORD_1
	v_pk_add_f16 v79, v79, v123 neg_lo:[0,1] neg_hi:[0,1]
	v_pk_add_f16 v65, v126, 0
	v_pk_fma_f16 v33, v33, v129, 0
	v_pk_add_f16 v62, v129, 0
	v_pk_add_f16 v63, v128, 0
	v_pk_add_f16 v64, v127, 0
	v_pk_fma_f16 v32, v32, v128, 0
	v_pk_fma_f16 v31, v31, v127, 0
	v_pk_fma_f16 v30, v30, v126, 0
	v_pk_add_f16 v80, v80, v124 neg_lo:[0,1] neg_hi:[0,1]
	v_pk_add_f16 v81, v81, v125 neg_lo:[0,1] neg_hi:[0,1]
	v_pk_add_f16 v54, v54, v122 neg_lo:[0,1] neg_hi:[0,1]
	v_exp_f16_sdwa v126, v78 dst_sel:WORD_0 dst_unused:UNUSED_PAD src0_sel:WORD_0
	v_exp_f16_sdwa v127, v79 dst_sel:WORD_0 dst_unused:UNUSED_PAD src0_sel:WORD_0
	v_exp_f16_sdwa v128, v80 dst_sel:WORD_0 dst_unused:UNUSED_PAD src0_sel:WORD_0
	v_exp_f16_sdwa v129, v81 dst_sel:WORD_0 dst_unused:UNUSED_PAD src0_sel:WORD_0
	v_exp_f16_sdwa v126, v78 dst_sel:WORD_1 dst_unused:UNUSED_PRESERVE src0_sel:WORD_1
	v_exp_f16_sdwa v127, v79 dst_sel:WORD_1 dst_unused:UNUSED_PRESERVE src0_sel:WORD_1
	v_exp_f16_sdwa v128, v80 dst_sel:WORD_1 dst_unused:UNUSED_PRESERVE src0_sel:WORD_1
	v_exp_f16_sdwa v129, v81 dst_sel:WORD_1 dst_unused:UNUSED_PRESERVE src0_sel:WORD_1
	v_pk_add_f16 v55, v55, v123 neg_lo:[0,1] neg_hi:[0,1]
	v_pk_add_f16 v65, v65, v126
	v_pk_fma_f16 v33, v45, v129, v33
	v_pk_add_f16 v45, v98, v125 neg_lo:[0,1] neg_hi:[0,1]
	v_pk_add_f16 v64, v64, v127
	v_pk_add_f16 v63, v63, v128
	v_pk_add_f16 v62, v62, v129
	v_pk_fma_f16 v30, v42, v126, v30
	v_pk_fma_f16 v31, v43, v127, v31
	v_pk_fma_f16 v32, v44, v128, v32
	v_pk_add_f16 v42, v101, v122 neg_lo:[0,1] neg_hi:[0,1]
	v_pk_add_f16 v43, v100, v123 neg_lo:[0,1] neg_hi:[0,1]
	v_pk_add_f16 v44, v99, v124 neg_lo:[0,1] neg_hi:[0,1]
	v_pk_add_f16 v56, v56, v124 neg_lo:[0,1] neg_hi:[0,1]
	v_exp_f16_sdwa v78, v42 dst_sel:WORD_0 dst_unused:UNUSED_PAD src0_sel:WORD_0
	v_exp_f16_sdwa v79, v43 dst_sel:WORD_0 dst_unused:UNUSED_PAD src0_sel:WORD_0
	v_exp_f16_sdwa v80, v44 dst_sel:WORD_0 dst_unused:UNUSED_PAD src0_sel:WORD_0
	v_exp_f16_sdwa v81, v45 dst_sel:WORD_0 dst_unused:UNUSED_PAD src0_sel:WORD_0
	v_exp_f16_sdwa v78, v42 dst_sel:WORD_1 dst_unused:UNUSED_PRESERVE src0_sel:WORD_1
	v_exp_f16_sdwa v79, v43 dst_sel:WORD_1 dst_unused:UNUSED_PRESERVE src0_sel:WORD_1
	v_exp_f16_sdwa v80, v44 dst_sel:WORD_1 dst_unused:UNUSED_PRESERVE src0_sel:WORD_1
	v_exp_f16_sdwa v81, v45 dst_sel:WORD_1 dst_unused:UNUSED_PRESERVE src0_sel:WORD_1
	v_pk_add_f16 v57, v57, v125 neg_lo:[0,1] neg_hi:[0,1]
	v_pk_add_f16 v45, v65, v78
	v_pk_add_f16 v42, v62, v81
	v_pk_add_f16 v43, v63, v80
	v_pk_add_f16 v44, v64, v79
	v_pk_fma_f16 v33, v61, v81, v33
	v_pk_fma_f16 v32, v60, v80, v32
	v_pk_fma_f16 v31, v59, v79, v31
	v_pk_fma_f16 v30, v58, v78, v30
	v_pk_add_f16 v58, v105, v122 neg_lo:[0,1] neg_hi:[0,1]
	v_pk_add_f16 v59, v104, v123 neg_lo:[0,1] neg_hi:[0,1]
	v_pk_add_f16 v60, v103, v124 neg_lo:[0,1] neg_hi:[0,1]
	v_pk_add_f16 v61, v102, v125 neg_lo:[0,1] neg_hi:[0,1]
	v_exp_f16_sdwa v62, v58 dst_sel:WORD_0 dst_unused:UNUSED_PAD src0_sel:WORD_0
	v_exp_f16_sdwa v63, v59 dst_sel:WORD_0 dst_unused:UNUSED_PAD src0_sel:WORD_0
	v_exp_f16_sdwa v64, v60 dst_sel:WORD_0 dst_unused:UNUSED_PAD src0_sel:WORD_0
	v_exp_f16_sdwa v65, v61 dst_sel:WORD_0 dst_unused:UNUSED_PAD src0_sel:WORD_0
	v_exp_f16_sdwa v62, v58 dst_sel:WORD_1 dst_unused:UNUSED_PRESERVE src0_sel:WORD_1
	v_exp_f16_sdwa v63, v59 dst_sel:WORD_1 dst_unused:UNUSED_PRESERVE src0_sel:WORD_1
	v_exp_f16_sdwa v64, v60 dst_sel:WORD_1 dst_unused:UNUSED_PRESERVE src0_sel:WORD_1
	v_exp_f16_sdwa v65, v61 dst_sel:WORD_1 dst_unused:UNUSED_PRESERVE src0_sel:WORD_1
	v_pk_add_f16 v58, v109, v122 neg_lo:[0,1] neg_hi:[0,1]
	v_pk_add_f16 v45, v45, v62
	v_pk_add_f16 v44, v44, v63
	v_pk_add_f16 v43, v43, v64
	v_pk_add_f16 v42, v42, v65
	v_pk_fma_f16 v30, v18, v62, v30
	v_pk_fma_f16 v31, v19, v63, v31
	v_pk_fma_f16 v32, v20, v64, v32
	v_pk_fma_f16 v33, v21, v65, v33
	v_pk_add_f16 v59, v108, v123 neg_lo:[0,1] neg_hi:[0,1]
	v_pk_add_f16 v60, v107, v124 neg_lo:[0,1] neg_hi:[0,1]
	v_pk_add_f16 v61, v106, v125 neg_lo:[0,1] neg_hi:[0,1]
	v_exp_f16_sdwa v62, v58 dst_sel:WORD_0 dst_unused:UNUSED_PAD src0_sel:WORD_0
	v_exp_f16_sdwa v63, v59 dst_sel:WORD_0 dst_unused:UNUSED_PAD src0_sel:WORD_0
	v_exp_f16_sdwa v64, v60 dst_sel:WORD_0 dst_unused:UNUSED_PAD src0_sel:WORD_0
	v_exp_f16_sdwa v65, v61 dst_sel:WORD_0 dst_unused:UNUSED_PAD src0_sel:WORD_0
	v_exp_f16_sdwa v62, v58 dst_sel:WORD_1 dst_unused:UNUSED_PRESERVE src0_sel:WORD_1
	v_exp_f16_sdwa v63, v59 dst_sel:WORD_1 dst_unused:UNUSED_PRESERVE src0_sel:WORD_1
	v_exp_f16_sdwa v64, v60 dst_sel:WORD_1 dst_unused:UNUSED_PRESERVE src0_sel:WORD_1
	v_exp_f16_sdwa v65, v61 dst_sel:WORD_1 dst_unused:UNUSED_PRESERVE src0_sel:WORD_1
	v_pk_add_f16 v58, v121, v122 neg_lo:[0,1] neg_hi:[0,1]
	v_pk_add_f16 v45, v45, v62
	v_pk_add_f16 v42, v42, v65
	v_pk_add_f16 v43, v43, v64
	v_pk_add_f16 v44, v44, v63
	v_pk_fma_f16 v33, v25, v65, v33
	v_pk_fma_f16 v32, v24, v64, v32
	v_pk_fma_f16 v31, v23, v63, v31
	v_pk_fma_f16 v30, v22, v62, v30
	v_pk_add_f16 v59, v120, v123 neg_lo:[0,1] neg_hi:[0,1]
	v_pk_add_f16 v60, v119, v124 neg_lo:[0,1] neg_hi:[0,1]
	v_pk_add_f16 v61, v118, v125 neg_lo:[0,1] neg_hi:[0,1]
	v_exp_f16_sdwa v62, v58 dst_sel:WORD_0 dst_unused:UNUSED_PAD src0_sel:WORD_0
	v_exp_f16_sdwa v63, v59 dst_sel:WORD_0 dst_unused:UNUSED_PAD src0_sel:WORD_0
	v_exp_f16_sdwa v64, v60 dst_sel:WORD_0 dst_unused:UNUSED_PAD src0_sel:WORD_0
	v_exp_f16_sdwa v65, v61 dst_sel:WORD_0 dst_unused:UNUSED_PAD src0_sel:WORD_0
	v_exp_f16_sdwa v62, v58 dst_sel:WORD_1 dst_unused:UNUSED_PRESERVE src0_sel:WORD_1
	v_exp_f16_sdwa v63, v59 dst_sel:WORD_1 dst_unused:UNUSED_PRESERVE src0_sel:WORD_1
	v_exp_f16_sdwa v64, v60 dst_sel:WORD_1 dst_unused:UNUSED_PRESERVE src0_sel:WORD_1
	v_exp_f16_sdwa v65, v61 dst_sel:WORD_1 dst_unused:UNUSED_PRESERVE src0_sel:WORD_1
	v_exp_f16_sdwa v58, v54 dst_sel:WORD_0 dst_unused:UNUSED_PAD src0_sel:WORD_0
	v_exp_f16_sdwa v59, v55 dst_sel:WORD_0 dst_unused:UNUSED_PAD src0_sel:WORD_0
	v_exp_f16_sdwa v60, v56 dst_sel:WORD_0 dst_unused:UNUSED_PAD src0_sel:WORD_0
	v_exp_f16_sdwa v61, v57 dst_sel:WORD_0 dst_unused:UNUSED_PAD src0_sel:WORD_0
	v_exp_f16_sdwa v58, v54 dst_sel:WORD_1 dst_unused:UNUSED_PRESERVE src0_sel:WORD_1
	v_exp_f16_sdwa v59, v55 dst_sel:WORD_1 dst_unused:UNUSED_PRESERVE src0_sel:WORD_1
	v_exp_f16_sdwa v60, v56 dst_sel:WORD_1 dst_unused:UNUSED_PRESERVE src0_sel:WORD_1
	v_exp_f16_sdwa v61, v57 dst_sel:WORD_1 dst_unused:UNUSED_PRESERVE src0_sel:WORD_1
	v_pk_add_f16 v54, v74, v122 neg_lo:[0,1] neg_hi:[0,1]
	v_pk_add_f16 v45, v45, v62
	v_pk_add_f16 v44, v44, v63
	v_pk_add_f16 v43, v43, v64
	v_pk_add_f16 v42, v42, v65
	v_pk_fma_f16 v30, v26, v62, v30
	v_pk_fma_f16 v31, v27, v63, v31
	v_pk_fma_f16 v32, v28, v64, v32
	v_pk_fma_f16 v33, v29, v65, v33
	v_pk_add_f16 v45, v45, v58
	v_pk_add_f16 v42, v42, v61
	v_pk_add_f16 v43, v43, v60
	v_pk_add_f16 v44, v44, v59
	v_pk_fma_f16 v33, v41, v61, v33
	v_pk_fma_f16 v32, v40, v60, v32
	v_pk_fma_f16 v31, v39, v59, v31
	v_pk_fma_f16 v30, v38, v58, v30
	v_pk_add_f16 v55, v75, v123 neg_lo:[0,1] neg_hi:[0,1]
	v_pk_add_f16 v56, v76, v124 neg_lo:[0,1] neg_hi:[0,1]
	v_pk_add_f16 v57, v77, v125 neg_lo:[0,1] neg_hi:[0,1]
	v_exp_f16_sdwa v58, v54 dst_sel:WORD_0 dst_unused:UNUSED_PAD src0_sel:WORD_0
	v_exp_f16_sdwa v59, v55 dst_sel:WORD_0 dst_unused:UNUSED_PAD src0_sel:WORD_0
	v_exp_f16_sdwa v60, v56 dst_sel:WORD_0 dst_unused:UNUSED_PAD src0_sel:WORD_0
	v_exp_f16_sdwa v61, v57 dst_sel:WORD_0 dst_unused:UNUSED_PAD src0_sel:WORD_0
	v_exp_f16_sdwa v58, v54 dst_sel:WORD_1 dst_unused:UNUSED_PRESERVE src0_sel:WORD_1
	v_exp_f16_sdwa v59, v55 dst_sel:WORD_1 dst_unused:UNUSED_PRESERVE src0_sel:WORD_1
	v_exp_f16_sdwa v60, v56 dst_sel:WORD_1 dst_unused:UNUSED_PRESERVE src0_sel:WORD_1
	v_exp_f16_sdwa v61, v57 dst_sel:WORD_1 dst_unused:UNUSED_PRESERVE src0_sel:WORD_1
	v_pk_add_f16 v54, v82, v122 neg_lo:[0,1] neg_hi:[0,1]
	v_pk_add_f16 v45, v45, v58
	v_pk_add_f16 v44, v44, v59
	v_pk_add_f16 v43, v43, v60
	v_pk_add_f16 v42, v42, v61
	v_pk_fma_f16 v30, v50, v58, v30
	v_pk_fma_f16 v31, v51, v59, v31
	v_pk_fma_f16 v32, v52, v60, v32
	v_pk_fma_f16 v33, v53, v61, v33
	v_pk_add_f16 v55, v83, v123 neg_lo:[0,1] neg_hi:[0,1]
	v_pk_add_f16 v56, v84, v124 neg_lo:[0,1] neg_hi:[0,1]
	v_pk_add_f16 v57, v85, v125 neg_lo:[0,1] neg_hi:[0,1]
	v_exp_f16_sdwa v58, v54 dst_sel:WORD_0 dst_unused:UNUSED_PAD src0_sel:WORD_0
	v_exp_f16_sdwa v59, v55 dst_sel:WORD_0 dst_unused:UNUSED_PAD src0_sel:WORD_0
	v_exp_f16_sdwa v60, v56 dst_sel:WORD_0 dst_unused:UNUSED_PAD src0_sel:WORD_0
	v_exp_f16_sdwa v61, v57 dst_sel:WORD_0 dst_unused:UNUSED_PAD src0_sel:WORD_0
	v_exp_f16_sdwa v58, v54 dst_sel:WORD_1 dst_unused:UNUSED_PRESERVE src0_sel:WORD_1
	v_exp_f16_sdwa v59, v55 dst_sel:WORD_1 dst_unused:UNUSED_PRESERVE src0_sel:WORD_1
	v_exp_f16_sdwa v60, v56 dst_sel:WORD_1 dst_unused:UNUSED_PRESERVE src0_sel:WORD_1
	v_exp_f16_sdwa v61, v57 dst_sel:WORD_1 dst_unused:UNUSED_PRESERVE src0_sel:WORD_1
	v_pk_add_f16 v45, v45, v58
	v_pk_add_f16 v44, v44, v59
	v_rcp_f16_e32 v54, v45
	v_rcp_f16_sdwa v45, v45 dst_sel:DWORD dst_unused:UNUSED_PAD src0_sel:WORD_1
	v_pk_add_f16 v43, v43, v60
	v_rcp_f16_e32 v55, v44
	v_rcp_f16_sdwa v44, v44 dst_sel:DWORD dst_unused:UNUSED_PAD src0_sel:WORD_1
	v_pk_add_f16 v42, v42, v61
	v_rcp_f16_e32 v56, v43
	v_rcp_f16_sdwa v43, v43 dst_sel:DWORD dst_unused:UNUSED_PAD src0_sel:WORD_1
	v_rcp_f16_e32 v57, v42
	v_rcp_f16_sdwa v42, v42 dst_sel:DWORD dst_unused:UNUSED_PAD src0_sel:WORD_1
	v_pk_fma_f16 v30, v70, v58, v30
	v_pack_b32_f16 v45, v54, v45
	v_pk_fma_f16 v31, v71, v59, v31
	v_pk_mul_f16 v45, v30, v45
	v_pack_b32_f16 v30, v55, v44
	v_pk_fma_f16 v32, v72, v60, v32
	v_pk_mul_f16 v44, v31, v30
	v_pack_b32_f16 v30, v56, v43
	v_pk_fma_f16 v33, v73, v61, v33
	v_pk_mul_f16 v43, v32, v30
	v_pack_b32_f16 v30, v57, v42
	v_pk_mul_f16 v42, v33, v30
	s_waitcnt vmcnt(0)
	s_mov_b64 s[86:87], s[80:81]
	global_load_dword v254, v255, s[86:87]
	s_add_u32 s86, s86, 0x2000
	s_addc_u32 s87, s87, 0
	global_load_dword v254, v255, s[86:87]
	s_add_u32 s86, s86, 0x2000
	s_addc_u32 s87, s87, 0
	global_load_dword v254, v255, s[86:87]
	s_add_u32 s86, s86, 0x2c000
	s_addc_u32 s87, s87, 0
	global_load_dword v254, v255, s[86:87]
	s_add_u32 s86, s86, 0x2000
	s_addc_u32 s87, s87, 0
	global_load_dword v254, v255, s[86:87]
	s_add_u32 s86, s86, 0x2000
	s_addc_u32 s87, s87, 0
	global_load_dword v254, v255, s[86:87]
	v_pk_mul_f16 v30, v208, v154 op_sel_hi:[0,1]
	v_pk_mul_f16 v31, v208, v155 op_sel_hi:[0,1]
	v_pk_mul_f16 v32, v208, v156 op_sel_hi:[0,1]
	v_pk_mul_f16 v33, v208, v157 op_sel_hi:[0,1]
	v_pk_mul_f16 v54, v206, v154 op_sel_hi:[0,1]
	v_pk_mul_f16 v55, v206, v155 op_sel_hi:[0,1]
	v_pk_mul_f16 v56, v206, v156 op_sel_hi:[0,1]
	v_pk_mul_f16 v57, v206, v157 op_sel_hi:[0,1]
	v_pk_mul_f16 v58, v207, v154 op_sel_hi:[0,1]
	v_pk_mul_f16 v59, v207, v155 op_sel_hi:[0,1]
	v_pk_mul_f16 v60, v207, v156 op_sel_hi:[0,1]
	v_pk_mul_f16 v61, v207, v157 op_sel_hi:[0,1]
	v_pk_fma_f16 v37, v37, v157, v33
	v_pk_fma_f16 v36, v36, v156, v32
	v_pk_fma_f16 v35, v35, v155, v31
	v_pk_fma_f16 v34, v34, v154, v30
	v_pk_fma_f16 v49, v49, v157, v57
	v_pk_fma_f16 v48, v48, v156, v56
	v_pk_fma_f16 v47, v47, v155, v55
	v_pk_fma_f16 v46, v46, v154, v54
	v_pk_fma_f16 v62, v69, v157, v61
	v_pk_fma_f16 v63, v68, v156, v60
	v_pk_fma_f16 v64, v67, v155, v59
	v_pk_fma_f16 v65, v66, v154, v58
	v_pk_fma_f16 v66, v89, v157, v33
	v_pk_fma_f16 v67, v88, v156, v32
	v_pk_fma_f16 v68, v87, v155, v31
	v_pk_fma_f16 v69, v86, v154, v30
	v_pk_fma_f16 v74, v117, v157, v57
	v_pk_fma_f16 v75, v116, v156, v56
	v_pk_fma_f16 v76, v115, v155, v55
	v_pk_fma_f16 v77, v114, v154, v54
	v_pk_fma_f16 v78, v133, v157, v61
	v_pk_fma_f16 v79, v132, v156, v60
	v_pk_fma_f16 v80, v131, v155, v59
	v_pk_fma_f16 v81, v130, v154, v58
	v_pk_fma_f16 v61, v17, v157, v61
	v_pk_fma_f16 v60, v16, v156, v60
	v_pk_fma_f16 v59, v15, v155, v59
	v_pk_fma_f16 v58, v14, v154, v58
	v_pk_maximum3_f16 v14, v34, v46, v65
	v_pk_maximum3_f16 v15, v35, v47, v64
	v_pk_maximum3_f16 v16, v36, v48, v63
	v_pk_maximum3_f16 v17, v37, v49, v62
	v_pk_maximum3_f16 v82, v69, v77, v81
	v_pk_maximum3_f16 v83, v68, v76, v80
	v_pk_maximum3_f16 v84, v67, v75, v79
	v_pk_maximum3_f16 v85, v66, v74, v78
	v_pk_fma_f16 v33, v145, v157, v33
	v_pk_fma_f16 v32, v144, v156, v32
	v_pk_fma_f16 v31, v143, v155, v31
	v_pk_fma_f16 v30, v142, v154, v30
	v_pk_fma_f16 v57, v153, v157, v57
	v_pk_fma_f16 v56, v152, v156, v56
	v_pk_fma_f16 v55, v151, v155, v55
	v_pk_fma_f16 v54, v150, v154, v54
	v_pk_maximum3_f16 v87, v31, v55, v59
	v_pk_maximum3_f16 v88, v32, v56, v60
	v_pk_maximum3_f16 v89, v33, v57, v61
	v_pk_maximum3_f16 v86, v30, v54, v58
	v_pk_maximum3_f16 v15, v15, v83, v87
	v_pk_maximum3_f16 v16, v16, v84, v88
	v_pk_maximum3_f16 v17, v17, v85, v89
	v_pk_maximum3_f16 v14, v14, v82, v86
	v_xor_b32_e32 v82, 0x80008000, v17
	v_xor_b32_e32 v83, 0x80008000, v16
	v_xor_b32_e32 v84, 0x80008000, v15
	v_xor_b32_e32 v85, 0x80008000, v14
	v_pk_add_f16 v14, v34, v85
	v_pk_add_f16 v15, v35, v84
	v_pk_add_f16 v16, v36, v83
	v_pk_add_f16 v17, v37, v82
	v_exp_f16_sdwa v34, v14 dst_sel:WORD_0 dst_unused:UNUSED_PAD src0_sel:WORD_0
	v_exp_f16_sdwa v35, v15 dst_sel:WORD_0 dst_unused:UNUSED_PAD src0_sel:WORD_0
	v_exp_f16_sdwa v36, v16 dst_sel:WORD_0 dst_unused:UNUSED_PAD src0_sel:WORD_0
	v_exp_f16_sdwa v37, v17 dst_sel:WORD_0 dst_unused:UNUSED_PAD src0_sel:WORD_0
	v_exp_f16_sdwa v34, v14 dst_sel:WORD_1 dst_unused:UNUSED_PRESERVE src0_sel:WORD_1
	v_exp_f16_sdwa v35, v15 dst_sel:WORD_1 dst_unused:UNUSED_PRESERVE src0_sel:WORD_1
	v_exp_f16_sdwa v36, v16 dst_sel:WORD_1 dst_unused:UNUSED_PRESERVE src0_sel:WORD_1
	v_exp_f16_sdwa v37, v17 dst_sel:WORD_1 dst_unused:UNUSED_PRESERVE src0_sel:WORD_1
	v_pk_add_f16 v14, v34, 0
	v_pk_add_f16 v15, v35, 0
	v_pk_add_f16 v16, v36, 0
	v_pk_add_f16 v17, v37, 0
	v_pk_fma_f16 v18, v18, v34, 0
	v_pk_fma_f16 v19, v19, v35, 0
	v_pk_fma_f16 v20, v20, v36, 0
	v_pk_fma_f16 v21, v21, v37, 0
	v_pk_add_f16 v34, v46, v85
	v_pk_add_f16 v35, v47, v84
	v_pk_add_f16 v36, v48, v83
	v_pk_add_f16 v37, v49, v82
	v_exp_f16_sdwa v46, v34 dst_sel:WORD_0 dst_unused:UNUSED_PAD src0_sel:WORD_0
	v_exp_f16_sdwa v47, v35 dst_sel:WORD_0 dst_unused:UNUSED_PAD src0_sel:WORD_0
	v_exp_f16_sdwa v48, v36 dst_sel:WORD_0 dst_unused:UNUSED_PAD src0_sel:WORD_0
	v_exp_f16_sdwa v49, v37 dst_sel:WORD_0 dst_unused:UNUSED_PAD src0_sel:WORD_0
	v_exp_f16_sdwa v46, v34 dst_sel:WORD_1 dst_unused:UNUSED_PRESERVE src0_sel:WORD_1
	v_exp_f16_sdwa v47, v35 dst_sel:WORD_1 dst_unused:UNUSED_PRESERVE src0_sel:WORD_1
	v_exp_f16_sdwa v48, v36 dst_sel:WORD_1 dst_unused:UNUSED_PRESERVE src0_sel:WORD_1
	v_exp_f16_sdwa v49, v37 dst_sel:WORD_1 dst_unused:UNUSED_PRESERVE src0_sel:WORD_1
	s_nop 0
	v_pk_add_f16 v17, v17, v49
	v_pk_add_f16 v16, v16, v48
	v_pk_add_f16 v15, v15, v47
	v_pk_add_f16 v14, v14, v46
	v_pk_fma_f16 v21, v25, v49, v21
	v_pk_fma_f16 v20, v24, v48, v20
	v_pk_fma_f16 v19, v23, v47, v19
	v_pk_fma_f16 v18, v22, v46, v18
	v_pk_add_f16 v22, v65, v85
	v_pk_add_f16 v23, v64, v84
	v_pk_add_f16 v24, v63, v83
	v_pk_add_f16 v25, v62, v82
	v_exp_f16_sdwa v34, v22 dst_sel:WORD_0 dst_unused:UNUSED_PAD src0_sel:WORD_0
	v_exp_f16_sdwa v35, v23 dst_sel:WORD_0 dst_unused:UNUSED_PAD src0_sel:WORD_0
	v_exp_f16_sdwa v36, v24 dst_sel:WORD_0 dst_unused:UNUSED_PAD src0_sel:WORD_0
	v_exp_f16_sdwa v37, v25 dst_sel:WORD_0 dst_unused:UNUSED_PAD src0_sel:WORD_0
	v_exp_f16_sdwa v34, v22 dst_sel:WORD_1 dst_unused:UNUSED_PRESERVE src0_sel:WORD_1
	v_exp_f16_sdwa v35, v23 dst_sel:WORD_1 dst_unused:UNUSED_PRESERVE src0_sel:WORD_1
	v_exp_f16_sdwa v36, v24 dst_sel:WORD_1 dst_unused:UNUSED_PRESERVE src0_sel:WORD_1
	v_exp_f16_sdwa v37, v25 dst_sel:WORD_1 dst_unused:UNUSED_PRESERVE src0_sel:WORD_1
	v_pk_add_f16 v22, v69, v85
	v_pk_add_f16 v14, v14, v34
	v_pk_add_f16 v15, v15, v35
	v_pk_add_f16 v16, v16, v36
	v_pk_add_f16 v17, v17, v37
	v_pk_fma_f16 v18, v26, v34, v18
	v_pk_fma_f16 v19, v27, v35, v19
	v_pk_fma_f16 v20, v28, v36, v20
	v_pk_fma_f16 v21, v29, v37, v21
	v_pk_add_f16 v23, v68, v84
	v_pk_add_f16 v24, v67, v83
	v_pk_add_f16 v25, v66, v82
	v_exp_f16_sdwa v26, v22 dst_sel:WORD_0 dst_unused:UNUSED_PAD src0_sel:WORD_0
	v_exp_f16_sdwa v27, v23 dst_sel:WORD_0 dst_unused:UNUSED_PAD src0_sel:WORD_0
	v_exp_f16_sdwa v28, v24 dst_sel:WORD_0 dst_unused:UNUSED_PAD src0_sel:WORD_0
	v_exp_f16_sdwa v29, v25 dst_sel:WORD_0 dst_unused:UNUSED_PAD src0_sel:WORD_0
	v_exp_f16_sdwa v26, v22 dst_sel:WORD_1 dst_unused:UNUSED_PRESERVE src0_sel:WORD_1
	v_exp_f16_sdwa v27, v23 dst_sel:WORD_1 dst_unused:UNUSED_PRESERVE src0_sel:WORD_1
	v_exp_f16_sdwa v28, v24 dst_sel:WORD_1 dst_unused:UNUSED_PRESERVE src0_sel:WORD_1
	v_exp_f16_sdwa v29, v25 dst_sel:WORD_1 dst_unused:UNUSED_PRESERVE src0_sel:WORD_1
	v_pk_add_f16 v22, v77, v85
	v_pk_add_f16 v17, v17, v29
	v_pk_add_f16 v16, v16, v28
	v_pk_add_f16 v15, v15, v27
	v_pk_add_f16 v14, v14, v26
	v_pk_fma_f16 v21, v41, v29, v21
	v_pk_fma_f16 v20, v40, v28, v20
	v_pk_fma_f16 v19, v39, v27, v19
	v_pk_fma_f16 v18, v38, v26, v18
	v_pk_add_f16 v23, v76, v84
	v_pk_add_f16 v24, v75, v83
	v_pk_add_f16 v25, v74, v82
	v_exp_f16_sdwa v26, v22 dst_sel:WORD_0 dst_unused:UNUSED_PAD src0_sel:WORD_0
	v_exp_f16_sdwa v27, v23 dst_sel:WORD_0 dst_unused:UNUSED_PAD src0_sel:WORD_0
	v_exp_f16_sdwa v28, v24 dst_sel:WORD_0 dst_unused:UNUSED_PAD src0_sel:WORD_0
	v_exp_f16_sdwa v29, v25 dst_sel:WORD_0 dst_unused:UNUSED_PAD src0_sel:WORD_0
	v_exp_f16_sdwa v26, v22 dst_sel:WORD_1 dst_unused:UNUSED_PRESERVE src0_sel:WORD_1
	v_exp_f16_sdwa v27, v23 dst_sel:WORD_1 dst_unused:UNUSED_PRESERVE src0_sel:WORD_1
	v_exp_f16_sdwa v28, v24 dst_sel:WORD_1 dst_unused:UNUSED_PRESERVE src0_sel:WORD_1
	v_exp_f16_sdwa v29, v25 dst_sel:WORD_1 dst_unused:UNUSED_PRESERVE src0_sel:WORD_1
	v_pk_add_f16 v22, v81, v85
	v_pk_add_f16 v14, v14, v26
	v_pk_add_f16 v15, v15, v27
	v_pk_add_f16 v16, v16, v28
	v_pk_add_f16 v17, v17, v29
	v_pk_fma_f16 v18, v50, v26, v18
	v_pk_fma_f16 v19, v51, v27, v19
	v_pk_fma_f16 v20, v52, v28, v20
	v_pk_fma_f16 v21, v53, v29, v21
	v_pk_add_f16 v23, v80, v84
	v_pk_add_f16 v24, v79, v83
	v_pk_add_f16 v25, v78, v82
	v_exp_f16_sdwa v26, v22 dst_sel:WORD_0 dst_unused:UNUSED_PAD src0_sel:WORD_0
	v_exp_f16_sdwa v27, v23 dst_sel:WORD_0 dst_unused:UNUSED_PAD src0_sel:WORD_0
	v_exp_f16_sdwa v28, v24 dst_sel:WORD_0 dst_unused:UNUSED_PAD src0_sel:WORD_0
	v_exp_f16_sdwa v29, v25 dst_sel:WORD_0 dst_unused:UNUSED_PAD src0_sel:WORD_0
	v_exp_f16_sdwa v26, v22 dst_sel:WORD_1 dst_unused:UNUSED_PRESERVE src0_sel:WORD_1
	v_exp_f16_sdwa v27, v23 dst_sel:WORD_1 dst_unused:UNUSED_PRESERVE src0_sel:WORD_1
	v_exp_f16_sdwa v28, v24 dst_sel:WORD_1 dst_unused:UNUSED_PRESERVE src0_sel:WORD_1
	v_exp_f16_sdwa v29, v25 dst_sel:WORD_1 dst_unused:UNUSED_PRESERVE src0_sel:WORD_1
	v_pk_add_f16 v22, v30, v85
	v_pk_add_f16 v17, v17, v29
	v_pk_add_f16 v16, v16, v28
	v_pk_add_f16 v15, v15, v27
	v_pk_add_f16 v14, v14, v26
	v_pk_fma_f16 v21, v73, v29, v21
	v_pk_fma_f16 v20, v72, v28, v20
	v_pk_fma_f16 v19, v71, v27, v19
	v_pk_fma_f16 v18, v70, v26, v18
	v_pk_add_f16 v23, v31, v84
	v_pk_add_f16 v24, v32, v83
	v_pk_add_f16 v25, v33, v82
	v_exp_f16_sdwa v26, v22 dst_sel:WORD_0 dst_unused:UNUSED_PAD src0_sel:WORD_0
	v_exp_f16_sdwa v27, v23 dst_sel:WORD_0 dst_unused:UNUSED_PAD src0_sel:WORD_0
	v_exp_f16_sdwa v28, v24 dst_sel:WORD_0 dst_unused:UNUSED_PAD src0_sel:WORD_0
	v_exp_f16_sdwa v29, v25 dst_sel:WORD_0 dst_unused:UNUSED_PAD src0_sel:WORD_0
	v_exp_f16_sdwa v26, v22 dst_sel:WORD_1 dst_unused:UNUSED_PRESERVE src0_sel:WORD_1
	v_exp_f16_sdwa v27, v23 dst_sel:WORD_1 dst_unused:UNUSED_PRESERVE src0_sel:WORD_1
	v_exp_f16_sdwa v28, v24 dst_sel:WORD_1 dst_unused:UNUSED_PRESERVE src0_sel:WORD_1
	v_exp_f16_sdwa v29, v25 dst_sel:WORD_1 dst_unused:UNUSED_PRESERVE src0_sel:WORD_1
	v_pk_add_f16 v22, v54, v85
	v_pk_add_f16 v14, v14, v26
	v_pk_add_f16 v15, v15, v27
	v_pk_add_f16 v16, v16, v28
	v_pk_add_f16 v17, v17, v29
	v_pk_fma_f16 v18, v90, v26, v18
	v_pk_fma_f16 v19, v91, v27, v19
	v_pk_fma_f16 v20, v92, v28, v20
	v_pk_fma_f16 v21, v93, v29, v21
	v_pk_add_f16 v23, v55, v84
	v_pk_add_f16 v24, v56, v83
	v_pk_add_f16 v25, v57, v82
	v_exp_f16_sdwa v26, v22 dst_sel:WORD_0 dst_unused:UNUSED_PAD src0_sel:WORD_0
	v_exp_f16_sdwa v27, v23 dst_sel:WORD_0 dst_unused:UNUSED_PAD src0_sel:WORD_0
	v_exp_f16_sdwa v28, v24 dst_sel:WORD_0 dst_unused:UNUSED_PAD src0_sel:WORD_0
	v_exp_f16_sdwa v29, v25 dst_sel:WORD_0 dst_unused:UNUSED_PAD src0_sel:WORD_0
	v_exp_f16_sdwa v26, v22 dst_sel:WORD_1 dst_unused:UNUSED_PRESERVE src0_sel:WORD_1
	v_exp_f16_sdwa v27, v23 dst_sel:WORD_1 dst_unused:UNUSED_PRESERVE src0_sel:WORD_1
	v_exp_f16_sdwa v28, v24 dst_sel:WORD_1 dst_unused:UNUSED_PRESERVE src0_sel:WORD_1
	v_exp_f16_sdwa v29, v25 dst_sel:WORD_1 dst_unused:UNUSED_PRESERVE src0_sel:WORD_1
	s_nop 0
	v_pk_add_f16 v17, v17, v29
	v_pk_add_f16 v16, v16, v28
	v_pk_add_f16 v15, v15, v27
	v_pk_add_f16 v14, v14, v26
	v_pk_fma_f16 v21, v113, v29, v21
	v_pk_fma_f16 v20, v112, v28, v20
	v_pk_fma_f16 v19, v111, v27, v19
	v_pk_fma_f16 v18, v110, v26, v18
	v_pk_add_f16 v26, v58, v85
	v_pk_add_f16 v27, v59, v84
	v_pk_add_f16 v28, v60, v83
	v_pk_add_f16 v29, v61, v82
	v_exp_f16_sdwa v22, v26 dst_sel:WORD_0 dst_unused:UNUSED_PAD src0_sel:WORD_0
	v_exp_f16_sdwa v23, v27 dst_sel:WORD_0 dst_unused:UNUSED_PAD src0_sel:WORD_0
	v_exp_f16_sdwa v24, v28 dst_sel:WORD_0 dst_unused:UNUSED_PAD src0_sel:WORD_0
	v_exp_f16_sdwa v25, v29 dst_sel:WORD_0 dst_unused:UNUSED_PAD src0_sel:WORD_0
	v_exp_f16_sdwa v22, v26 dst_sel:WORD_1 dst_unused:UNUSED_PRESERVE src0_sel:WORD_1
	v_exp_f16_sdwa v23, v27 dst_sel:WORD_1 dst_unused:UNUSED_PRESERVE src0_sel:WORD_1
	v_exp_f16_sdwa v24, v28 dst_sel:WORD_1 dst_unused:UNUSED_PRESERVE src0_sel:WORD_1
	v_exp_f16_sdwa v25, v29 dst_sel:WORD_1 dst_unused:UNUSED_PRESERVE src0_sel:WORD_1
	s_nop 0

_Z7k_stageILi0ELi4EEv8AttnArgsPKDF16_PKfPDF16_iii:
	v_readfirstlane_b32 s94, v0
	s_nop 0
	s_lshr_b32 s94, s94, 6
	s_load_dwordx2 s[80:81], s[0:1], 0x70
	s_load_dwordx2 s[82:83], s[0:1], 0x88
	v_and_b32_e32 v255, 63, v0
	v_lshlrev_b32_e32 v255, 7, v255
	s_load_dwordx4 s[8:11], s[0:1], 0x70
	s_load_dwordx2 s[20:21], s[0:1], 0x80
	s_load_dwordx4 s[12:15], s[0:1], 0x88
	s_lshl_b32 s5, s2, 5
	s_waitcnt lgkmcnt(0)
	s_mul_i32 s84, s3, s83
	s_add_i32 s84, s84, s82
	s_mul_i32 s84, s84, 0x60000
	s_mul_i32 s85, s94, 0x6000
	s_add_u32 s84, s84, s85
	s_add_u32 s80, s80, s84
	s_addc_u32 s81, s81, 0
	s_and_b32 s15, s5, 0xe0
	s_lshr_b32 s5, s2, 3
	s_add_i32 s15, s15, s5
	s_and_b32 s2, s2, 56
	v_readfirstlane_b32 s4, v0
	v_and_b32_e32 v1, 15, v0
	s_cmp_lt_i32 s14, 1
	v_bfe_u32 v158, v0, 4, 2
	s_cbranch_scc1 .LBB5_79
	s_bfe_u32 s5, s4, 0x10006
	s_lshl_b32 s6, s5, 4
	s_mul_i32 s16, s3, 40
	s_mul_hi_i32 s7, s3, 40
	s_add_u32 s22, s0, s16
	s_addc_u32 s23, s1, s7
	s_load_dwordx4 s[16:19], s[22:23], 0x0
	s_load_dwordx2 s[0:1], s[22:23], 0x10
	v_or_b32_e32 v159, s6, v1
	v_lshlrev_b32_e32 v18, 5, v159
	s_waitcnt lgkmcnt(0)
	global_load_dwordx4 v[2:5], v18, s[18:19]
	global_load_dwordx4 v[6:9], v18, s[0:1]
	global_load_dwordx4 v[10:13], v18, s[18:19] offset:16
	global_load_dwordx4 v[14:17], v18, s[0:1] offset:16
	v_bfe_u32 v21, v0, 7, 1
	v_lshrrev_b32_e32 v19, 4, v0
	v_lshlrev_b16_e32 v23, 2, v21
	v_lshrrev_b32_e32 v18, 5, v0
	v_lshrrev_b32_e32 v20, 6, v0
	v_and_b32_e32 v24, 3, v19
	v_bitop3_b16 v19, v23, v19, 3 bitop3:0xf8
	s_movk_i32 s0, 0x3000
	v_and_b32_e32 v18, 4, v18
	v_and_b32_e32 v22, 4, v20
	v_lshlrev_b32_e32 v20, 12, v20
	v_lshlrev_b32_e32 v21, 11, v21
	v_and_b32_e32 v19, 0xffff, v19
	s_bitcmp1_b32 s4, 6
	v_or_b32_e32 v161, v18, v158
	v_and_or_b32 v162, s15, 56, v22
	v_bitop3_b16 v23, v23, 8, v24 bitop3:0xfe
	v_lshlrev_b32_e32 v24, 3, v22
	v_lshl_or_b32 v22, v22, 12, v21
	v_or3_b32 v163, v20, v21, s0
	v_bitop3_b32 v18, v18, v159, v158 bitop3:0x36
	v_bitop3_b32 v19, s6, v19, v1 bitop3:0x36
	s_cselect_b64 s[24:25], -1, 0
	s_and_b32 s0, s15, 0x1ffc0
	s_movk_i32 s1, 0x2000
	v_lshl_or_b32 v168, v18, 4, v22
	v_lshlrev_b32_e32 v18, 4, v19
	v_or_b32_e32 v19, s0, v162
	v_add3_u32 v170, v22, v18, s1
	v_lshl_or_b32 v18, v19, 6, s2
	v_add_u32_e32 v18, v161, v18
	v_mul_u32_u24_e32 v18, 0x600, v18
	v_and_b32_e32 v20, 0xffff, v23
	v_lshl_or_b32 v18, s5, 8, v18
	v_lshlrev_b32_e32 v160, 9, v158
	v_bitop3_b32 v20, s6, v20, v1 bitop3:0x36
	v_lshl_or_b32 v18, v1, 4, v18
	v_add_u32_e32 v164, -1, v162
	v_add_u32_e32 v165, 4, v162
	v_or3_b32 v166, v161, v24, 8
	v_or_b32_e32 v167, 0x1000, v22
	v_lshl_or_b32 v169, v20, 4, v160
	s_and_b32 s17, s17, 0xffff
	s_mov_b32 s19, 0x20000
	s_mov_b32 s18, 0x1800000
	v_add_u32_e32 v171, 0xfffe7c00, v18
	s_mov_b32 s30, s2
	s_waitcnt vmcnt(3)
	v_cvt_pk_f16_f32 v172, v2, v3
	s_waitcnt vmcnt(2)
	v_cvt_pk_f16_f32 v173, v6, v7
	v_cvt_pk_f16_f32 v174, v4, v5
	v_cvt_pk_f16_f32 v175, v8, v9
	s_waitcnt vmcnt(1)
	v_cvt_pk_f16_f32 v176, v10, v11
	s_waitcnt vmcnt(0)
	v_cvt_pk_f16_f32 v177, v14, v15
	v_cvt_pk_f16_f32 v178, v12, v13
	v_cvt_pk_f16_f32 v179, v16, v17
	s_branch .LBB5_4
.LBB5_2:
	s_waitcnt lgkmcnt(0)
	v_cvt_f16_f32_e32 v180, s7
	v_cvt_f16_f32_e32 v182, s6
	v_cvt_f16_f32_e32 v181, s28
	s_waitcnt vmcnt(3)
	v_pk_mul_f16 v183, v182, v184 op_sel_hi:[0,1]
	v_pk_mul_f16 v190, v182, v187 op_sel_hi:[0,1]
	v_pk_mul_f16 v194, v180, v187 op_sel_hi:[0,1]
	v_pk_mul_f16 v198, v181, v187 op_sel_hi:[0,1]
	v_pk_mul_f16 v188, v182, v185 op_sel_hi:[0,1]
	v_pk_mul_f16 v189, v182, v186 op_sel_hi:[0,1]
	v_pk_mul_f16 v191, v180, v184 op_sel_hi:[0,1]
	s_mov_b64 exec, s[64:65]
	buffer_load_dwordx4 v[18:21], v224, s[16:19], 0 offen
	buffer_load_dwordx4 v[6:9], v224, s[16:19], 0 offen offset:512
	s_mov_b64 exec, -1
	v_pk_mul_f16 v192, v180, v185 op_sel_hi:[0,1]
	v_pk_mul_f16 v193, v180, v186 op_sel_hi:[0,1]
	v_pk_mul_f16 v195, v181, v184 op_sel_hi:[0,1]
	v_pk_mul_f16 v196, v181, v185 op_sel_hi:[0,1]
	v_pk_mul_f16 v197, v181, v186 op_sel_hi:[0,1]
	v_pk_fma_f16 v113, v113, v187, v190
	v_pk_fma_f16 v110, v110, v184, v183
	v_pk_fma_f16 v129, v129, v187, v190
	v_pk_fma_f16 v126, v126, v184, v183
	v_pk_fma_f16 v137, v137, v187, v190
	v_pk_fma_f16 v134, v134, v184, v183
	v_pk_fma_f16 v183, v85, v187, v194
	v_pk_fma_f16 v199, v109, v187, v194
	buffer_load_dwordx4 v[30:33], v225, s[16:19], 0 offen offset:512
	buffer_load_dwordx4 v[10:13], v225, s[16:19], 0 offen offset:1024
	v_pk_fma_f16 v194, v125, v187, v194
	v_pk_fma_f16 v203, v53, v187, v198
	v_pk_fma_f16 v207, v69, v187, v198
	v_pk_fma_f16 v187, v97, v187, v198
	v_pk_maximum3_f16 v198, v113, v129, v137
	v_pk_fma_f16 v112, v112, v186, v189
	v_pk_fma_f16 v111, v111, v185, v188
	v_pk_fma_f16 v128, v128, v186, v189
	v_pk_fma_f16 v127, v127, v185, v188
	v_pk_fma_f16 v136, v136, v186, v189
	v_pk_fma_f16 v135, v135, v185, v188
	v_pk_fma_f16 v188, v84, v186, v193
	v_pk_fma_f16 v189, v83, v185, v192
	v_pk_fma_f16 v190, v82, v184, v191
	v_pk_fma_f16 v200, v108, v186, v193
	v_pk_fma_f16 v201, v107, v185, v192
	s_mov_b64 exec, s[66:67]
	buffer_load_dwordx4 v[54:57], v225, s[16:19], 0 offen offset:2048
	buffer_load_dwordx4 v[14:17], v225, s[16:19], 0 offen offset:2560
	s_mov_b64 exec, -1
	v_pk_fma_f16 v202, v106, v184, v191
	v_pk_fma_f16 v193, v124, v186, v193
	v_pk_fma_f16 v192, v123, v185, v192
	v_pk_fma_f16 v191, v122, v184, v191
	v_pk_fma_f16 v204, v52, v186, v197
	v_pk_fma_f16 v205, v51, v185, v196
	v_pk_fma_f16 v206, v50, v184, v195
	v_pk_fma_f16 v208, v68, v186, v197
	v_pk_fma_f16 v209, v67, v185, v196
	v_pk_fma_f16 v210, v66, v184, v195
	v_pk_fma_f16 v186, v96, v186, v197
	v_pk_fma_f16 v185, v95, v185, v196
	v_pk_fma_f16 v184, v94, v184, v195
	v_pk_maximum3_f16 v195, v110, v126, v134
	v_pk_maximum3_f16 v196, v111, v127, v135
	v_pk_maximum3_f16 v197, v112, v128, v136
	v_pk_maximum3_f16 v214, v183, v199, v194
	v_pk_maximum3_f16 v218, v203, v207, v187
	v_pk_maximum3_f16 v211, v190, v202, v191
	v_pk_maximum3_f16 v212, v189, v201, v192
	v_pk_maximum3_f16 v213, v188, v200, v193
	v_pk_maximum3_f16 v215, v206, v210, v184
	v_pk_maximum3_f16 v216, v205, v209, v185
	v_pk_maximum3_f16 v198, v198, v214, v218
	v_pk_maximum3_f16 v217, v204, v208, v186
	v_pk_maximum3_f16 v195, v195, v211, v215
	v_pk_maximum3_f16 v196, v196, v212, v216
	v_pk_maximum3_f16 v197, v197, v213, v217
	v_pk_add_f16 v113, v113, v198 neg_lo:[0,1] neg_hi:[0,1]
	s_mov_b64 exec, s[64:65]
	buffer_load_dwordx4 v[74:77], v226, s[16:19], 0 offen
	buffer_load_dwordx4 v[26:29], v226, s[16:19], 0 offen offset:512
	s_mov_b64 exec, -1
	v_pk_add_f16 v110, v110, v195 neg_lo:[0,1] neg_hi:[0,1]
	v_pk_add_f16 v111, v111, v196 neg_lo:[0,1] neg_hi:[0,1]
	v_pk_add_f16 v112, v112, v197 neg_lo:[0,1] neg_hi:[0,1]
	v_pk_add_f16 v126, v126, v195 neg_lo:[0,1] neg_hi:[0,1]
	v_exp_f16_sdwa v211, v110 dst_sel:WORD_0 dst_unused:UNUSED_PAD src0_sel:WORD_0
	v_exp_f16_sdwa v212, v111 dst_sel:WORD_0 dst_unused:UNUSED_PAD src0_sel:WORD_0
	v_exp_f16_sdwa v213, v112 dst_sel:WORD_0 dst_unused:UNUSED_PAD src0_sel:WORD_0
	v_exp_f16_sdwa v214, v113 dst_sel:WORD_0 dst_unused:UNUSED_PAD src0_sel:WORD_0
	v_exp_f16_sdwa v211, v110 dst_sel:WORD_1 dst_unused:UNUSED_PRESERVE src0_sel:WORD_1
	v_exp_f16_sdwa v212, v111 dst_sel:WORD_1 dst_unused:UNUSED_PRESERVE src0_sel:WORD_1
	v_exp_f16_sdwa v213, v112 dst_sel:WORD_1 dst_unused:UNUSED_PRESERVE src0_sel:WORD_1
	v_exp_f16_sdwa v214, v113 dst_sel:WORD_1 dst_unused:UNUSED_PRESERVE src0_sel:WORD_1
	v_pk_add_f16 v127, v127, v196 neg_lo:[0,1] neg_hi:[0,1]
	v_pk_add_f16 v113, v211, 0
	v_pk_fma_f16 v81, v81, v214, 0
	v_pk_add_f16 v110, v214, 0
	v_pk_add_f16 v111, v213, 0
	v_pk_add_f16 v112, v212, 0
	v_pk_fma_f16 v80, v80, v213, 0
	v_pk_fma_f16 v79, v79, v212, 0
	v_pk_fma_f16 v78, v78, v211, 0
	v_pk_add_f16 v128, v128, v197 neg_lo:[0,1] neg_hi:[0,1]
	buffer_load_dwordx4 v[98:101], v227, s[16:19], 0 offen offset:512
	buffer_load_dwordx4 v[38:41], v227, s[16:19], 0 offen offset:1024
	v_pk_add_f16 v129, v129, v198 neg_lo:[0,1] neg_hi:[0,1]
	v_exp_f16_sdwa v211, v126 dst_sel:WORD_0 dst_unused:UNUSED_PAD src0_sel:WORD_0
	v_exp_f16_sdwa v212, v127 dst_sel:WORD_0 dst_unused:UNUSED_PAD src0_sel:WORD_0
	v_exp_f16_sdwa v213, v128 dst_sel:WORD_0 dst_unused:UNUSED_PAD src0_sel:WORD_0
	v_exp_f16_sdwa v214, v129 dst_sel:WORD_0 dst_unused:UNUSED_PAD src0_sel:WORD_0
	v_exp_f16_sdwa v211, v126 dst_sel:WORD_1 dst_unused:UNUSED_PRESERVE src0_sel:WORD_1
	v_exp_f16_sdwa v212, v127 dst_sel:WORD_1 dst_unused:UNUSED_PRESERVE src0_sel:WORD_1
	v_exp_f16_sdwa v213, v128 dst_sel:WORD_1 dst_unused:UNUSED_PRESERVE src0_sel:WORD_1
	v_exp_f16_sdwa v214, v129 dst_sel:WORD_1 dst_unused:UNUSED_PRESERVE src0_sel:WORD_1
	v_pk_add_f16 v113, v113, v211
	v_pk_fma_f16 v81, v105, v214, v81
	v_pk_add_f16 v105, v137, v198 neg_lo:[0,1] neg_hi:[0,1]
	v_pk_add_f16 v112, v112, v212
	v_pk_add_f16 v111, v111, v213
	v_pk_add_f16 v110, v110, v214
	v_pk_fma_f16 v78, v102, v211, v78
	v_pk_fma_f16 v79, v103, v212, v79
	v_pk_fma_f16 v80, v104, v213, v80
	v_pk_add_f16 v102, v134, v195 neg_lo:[0,1] neg_hi:[0,1]
	v_pk_add_f16 v103, v135, v196 neg_lo:[0,1] neg_hi:[0,1]
	v_pk_add_f16 v104, v136, v197 neg_lo:[0,1] neg_hi:[0,1]
	v_exp_f16_sdwa v126, v102 dst_sel:WORD_0 dst_unused:UNUSED_PAD src0_sel:WORD_0
	v_exp_f16_sdwa v127, v103 dst_sel:WORD_0 dst_unused:UNUSED_PAD src0_sel:WORD_0
	v_exp_f16_sdwa v128, v104 dst_sel:WORD_0 dst_unused:UNUSED_PAD src0_sel:WORD_0
	v_exp_f16_sdwa v129, v105 dst_sel:WORD_0 dst_unused:UNUSED_PAD src0_sel:WORD_0
	v_exp_f16_sdwa v126, v102 dst_sel:WORD_1 dst_unused:UNUSED_PRESERVE src0_sel:WORD_1
	v_exp_f16_sdwa v127, v103 dst_sel:WORD_1 dst_unused:UNUSED_PRESERVE src0_sel:WORD_1
	v_exp_f16_sdwa v128, v104 dst_sel:WORD_1 dst_unused:UNUSED_PRESERVE src0_sel:WORD_1
	v_exp_f16_sdwa v129, v105 dst_sel:WORD_1 dst_unused:UNUSED_PRESERVE src0_sel:WORD_1
	v_pk_add_f16 v105, v113, v126
	v_pk_add_f16 v102, v110, v129
	s_mov_b64 exec, s[66:67]
	buffer_load_dwordx4 v[118:121], v227, s[16:19], 0 offen offset:2048
	buffer_load_dwordx4 v[58:61], v227, s[16:19], 0 offen offset:2560
	s_mov_b64 exec, -1
	v_pk_add_f16 v103, v111, v128
	v_pk_add_f16 v104, v112, v127
	v_pk_fma_f16 v81, v117, v129, v81
	v_pk_fma_f16 v80, v116, v128, v80
	v_pk_fma_f16 v79, v115, v127, v79
	v_pk_fma_f16 v78, v114, v126, v78
	v_pk_add_f16 v110, v190, v195 neg_lo:[0,1] neg_hi:[0,1]
	v_pk_add_f16 v111, v189, v196 neg_lo:[0,1] neg_hi:[0,1]
	v_pk_add_f16 v112, v188, v197 neg_lo:[0,1] neg_hi:[0,1]
	v_pk_add_f16 v113, v183, v198 neg_lo:[0,1] neg_hi:[0,1]
	v_exp_f16_sdwa v114, v110 dst_sel:WORD_0 dst_unused:UNUSED_PAD src0_sel:WORD_0
	v_exp_f16_sdwa v115, v111 dst_sel:WORD_0 dst_unused:UNUSED_PAD src0_sel:WORD_0
	v_exp_f16_sdwa v116, v112 dst_sel:WORD_0 dst_unused:UNUSED_PAD src0_sel:WORD_0
	v_exp_f16_sdwa v117, v113 dst_sel:WORD_0 dst_unused:UNUSED_PAD src0_sel:WORD_0
	v_exp_f16_sdwa v114, v110 dst_sel:WORD_1 dst_unused:UNUSED_PRESERVE src0_sel:WORD_1
	v_exp_f16_sdwa v115, v111 dst_sel:WORD_1 dst_unused:UNUSED_PRESERVE src0_sel:WORD_1
	v_exp_f16_sdwa v116, v112 dst_sel:WORD_1 dst_unused:UNUSED_PRESERVE src0_sel:WORD_1
	v_exp_f16_sdwa v117, v113 dst_sel:WORD_1 dst_unused:UNUSED_PRESERVE src0_sel:WORD_1
	v_pk_add_f16 v110, v202, v195 neg_lo:[0,1] neg_hi:[0,1]
	v_pk_add_f16 v105, v105, v114
	v_pk_add_f16 v104, v104, v115
	v_pk_add_f16 v103, v103, v116
	s_mov_b64 exec, s[76:77]
	buffer_load_dwordx4 v[130:133], v228, s[16:19], 0 offen
	buffer_load_dwordx4 v[70:73], v228, s[16:19], 0 offen offset:512
	s_mov_b64 exec, -1
	v_pk_add_f16 v102, v102, v117
	v_pk_fma_f16 v78, v42, v114, v78
	v_pk_fma_f16 v79, v43, v115, v79
	v_pk_fma_f16 v80, v44, v116, v80
	v_pk_fma_f16 v81, v45, v117, v81
	v_pk_add_f16 v111, v201, v196 neg_lo:[0,1] neg_hi:[0,1]
	v_pk_add_f16 v112, v200, v197 neg_lo:[0,1] neg_hi:[0,1]
	v_pk_add_f16 v113, v199, v198 neg_lo:[0,1] neg_hi:[0,1]
	v_exp_f16_sdwa v114, v110 dst_sel:WORD_0 dst_unused:UNUSED_PAD src0_sel:WORD_0
	v_exp_f16_sdwa v115, v111 dst_sel:WORD_0 dst_unused:UNUSED_PAD src0_sel:WORD_0
	v_exp_f16_sdwa v116, v112 dst_sel:WORD_0 dst_unused:UNUSED_PAD src0_sel:WORD_0
	v_exp_f16_sdwa v117, v113 dst_sel:WORD_0 dst_unused:UNUSED_PAD src0_sel:WORD_0
	v_exp_f16_sdwa v114, v110 dst_sel:WORD_1 dst_unused:UNUSED_PRESERVE src0_sel:WORD_1
	v_exp_f16_sdwa v115, v111 dst_sel:WORD_1 dst_unused:UNUSED_PRESERVE src0_sel:WORD_1
	v_exp_f16_sdwa v116, v112 dst_sel:WORD_1 dst_unused:UNUSED_PRESERVE src0_sel:WORD_1
	v_exp_f16_sdwa v117, v113 dst_sel:WORD_1 dst_unused:UNUSED_PRESERVE src0_sel:WORD_1
	v_pk_add_f16 v110, v191, v195 neg_lo:[0,1] neg_hi:[0,1]
	v_pk_add_f16 v105, v105, v114
	v_pk_add_f16 v102, v102, v117
	v_pk_add_f16 v103, v103, v116
	v_pk_add_f16 v104, v104, v115
	v_pk_fma_f16 v81, v65, v117, v81
	v_pk_fma_f16 v80, v64, v116, v80
	s_mov_b64 exec, s[70:71]
	buffer_load_dwordx4 v[138:141], v229, s[16:19], 0 offen offset:512
	buffer_load_dwordx4 v[90:93], v229, s[16:19], 0 offen offset:1024
	s_mov_b64 exec, -1
	v_pk_fma_f16 v79, v63, v115, v79
	v_pk_fma_f16 v78, v62, v114, v78
	v_pk_add_f16 v111, v192, v196 neg_lo:[0,1] neg_hi:[0,1]
	v_pk_add_f16 v112, v193, v197 neg_lo:[0,1] neg_hi:[0,1]
	v_pk_add_f16 v113, v194, v198 neg_lo:[0,1] neg_hi:[0,1]
	v_exp_f16_sdwa v114, v110 dst_sel:WORD_0 dst_unused:UNUSED_PAD src0_sel:WORD_0
	v_exp_f16_sdwa v115, v111 dst_sel:WORD_0 dst_unused:UNUSED_PAD src0_sel:WORD_0
	v_exp_f16_sdwa v116, v112 dst_sel:WORD_0 dst_unused:UNUSED_PAD src0_sel:WORD_0
	v_exp_f16_sdwa v117, v113 dst_sel:WORD_0 dst_unused:UNUSED_PAD src0_sel:WORD_0
	v_exp_f16_sdwa v114, v110 dst_sel:WORD_1 dst_unused:UNUSED_PRESERVE src0_sel:WORD_1
	v_exp_f16_sdwa v115, v111 dst_sel:WORD_1 dst_unused:UNUSED_PRESERVE src0_sel:WORD_1
	v_exp_f16_sdwa v116, v112 dst_sel:WORD_1 dst_unused:UNUSED_PRESERVE src0_sel:WORD_1
	v_exp_f16_sdwa v117, v113 dst_sel:WORD_1 dst_unused:UNUSED_PRESERVE src0_sel:WORD_1
	v_pk_add_f16 v110, v206, v195 neg_lo:[0,1] neg_hi:[0,1]
	v_pk_add_f16 v105, v105, v114
	v_pk_add_f16 v104, v104, v115
	v_pk_add_f16 v103, v103, v116
	v_pk_add_f16 v102, v102, v117
	v_pk_fma_f16 v78, v86, v114, v78
	v_pk_fma_f16 v79, v87, v115, v79
	v_pk_fma_f16 v80, v88, v116, v80
	v_pk_fma_f16 v81, v89, v117, v81
	s_mov_b64 exec, s[78:79]
	buffer_load_dwordx4 v[142:145], v229, s[16:19], 0 offen offset:2048
	buffer_load_dwordx4 v[2:5], v229, s[16:19], 0 offen offset:2560
	s_mov_b64 exec, -1
	v_pk_add_f16 v111, v205, v196 neg_lo:[0,1] neg_hi:[0,1]
	v_pk_add_f16 v112, v204, v197 neg_lo:[0,1] neg_hi:[0,1]
	v_pk_add_f16 v113, v203, v198 neg_lo:[0,1] neg_hi:[0,1]
	v_exp_f16_sdwa v114, v110 dst_sel:WORD_0 dst_unused:UNUSED_PAD src0_sel:WORD_0
	v_exp_f16_sdwa v115, v111 dst_sel:WORD_0 dst_unused:UNUSED_PAD src0_sel:WORD_0
	v_exp_f16_sdwa v116, v112 dst_sel:WORD_0 dst_unused:UNUSED_PAD src0_sel:WORD_0
	v_exp_f16_sdwa v117, v113 dst_sel:WORD_0 dst_unused:UNUSED_PAD src0_sel:WORD_0
	v_exp_f16_sdwa v114, v110 dst_sel:WORD_1 dst_unused:UNUSED_PRESERVE src0_sel:WORD_1
	v_exp_f16_sdwa v115, v111 dst_sel:WORD_1 dst_unused:UNUSED_PRESERVE src0_sel:WORD_1
	v_exp_f16_sdwa v116, v112 dst_sel:WORD_1 dst_unused:UNUSED_PRESERVE src0_sel:WORD_1
	v_exp_f16_sdwa v117, v113 dst_sel:WORD_1 dst_unused:UNUSED_PRESERVE src0_sel:WORD_1
	v_pk_add_f16 v110, v210, v195 neg_lo:[0,1] neg_hi:[0,1]
	v_pk_add_f16 v105, v105, v114
	v_pk_add_f16 v102, v102, v117
	v_pk_add_f16 v103, v103, v116
	v_pk_add_f16 v104, v104, v115
	v_pk_fma_f16 v81, v25, v117, v81
	v_pk_fma_f16 v80, v24, v116, v80
	v_pk_fma_f16 v79, v23, v115, v79
	v_pk_fma_f16 v78, v22, v114, v78
	v_pk_add_f16 v111, v209, v196 neg_lo:[0,1] neg_hi:[0,1]
	v_pk_add_f16 v112, v208, v197 neg_lo:[0,1] neg_hi:[0,1]
	v_pk_add_f16 v113, v207, v198 neg_lo:[0,1] neg_hi:[0,1]
	v_exp_f16_sdwa v114, v110 dst_sel:WORD_0 dst_unused:UNUSED_PAD src0_sel:WORD_0
	v_exp_f16_sdwa v115, v111 dst_sel:WORD_0 dst_unused:UNUSED_PAD src0_sel:WORD_0
	v_exp_f16_sdwa v116, v112 dst_sel:WORD_0 dst_unused:UNUSED_PAD src0_sel:WORD_0
	v_exp_f16_sdwa v117, v113 dst_sel:WORD_0 dst_unused:UNUSED_PAD src0_sel:WORD_0
	v_exp_f16_sdwa v114, v110 dst_sel:WORD_1 dst_unused:UNUSED_PRESERVE src0_sel:WORD_1
	v_exp_f16_sdwa v115, v111 dst_sel:WORD_1 dst_unused:UNUSED_PRESERVE src0_sel:WORD_1
	v_exp_f16_sdwa v116, v112 dst_sel:WORD_1 dst_unused:UNUSED_PRESERVE src0_sel:WORD_1
	v_exp_f16_sdwa v117, v113 dst_sel:WORD_1 dst_unused:UNUSED_PRESERVE src0_sel:WORD_1
	v_pk_add_f16 v110, v184, v195 neg_lo:[0,1] neg_hi:[0,1]
	v_pk_add_f16 v105, v105, v114
	v_pk_add_f16 v104, v104, v115
	v_pk_add_f16 v103, v103, v116
	v_pk_add_f16 v102, v102, v117
	v_pk_fma_f16 v78, v34, v114, v78
	v_pk_fma_f16 v79, v35, v115, v79
	v_pk_fma_f16 v80, v36, v116, v80
	v_pk_fma_f16 v81, v37, v117, v81
	v_pk_add_f16 v111, v185, v196 neg_lo:[0,1] neg_hi:[0,1]
	v_pk_add_f16 v112, v186, v197 neg_lo:[0,1] neg_hi:[0,1]
	v_pk_add_f16 v113, v187, v198 neg_lo:[0,1] neg_hi:[0,1]
	v_exp_f16_sdwa v114, v110 dst_sel:WORD_0 dst_unused:UNUSED_PAD src0_sel:WORD_0
	v_exp_f16_sdwa v115, v111 dst_sel:WORD_0 dst_unused:UNUSED_PAD src0_sel:WORD_0
	v_exp_f16_sdwa v116, v112 dst_sel:WORD_0 dst_unused:UNUSED_PAD src0_sel:WORD_0
	v_exp_f16_sdwa v117, v113 dst_sel:WORD_0 dst_unused:UNUSED_PAD src0_sel:WORD_0
	v_exp_f16_sdwa v114, v110 dst_sel:WORD_1 dst_unused:UNUSED_PRESERVE src0_sel:WORD_1
	v_exp_f16_sdwa v115, v111 dst_sel:WORD_1 dst_unused:UNUSED_PRESERVE src0_sel:WORD_1
	v_exp_f16_sdwa v116, v112 dst_sel:WORD_1 dst_unused:UNUSED_PRESERVE src0_sel:WORD_1
	v_exp_f16_sdwa v117, v113 dst_sel:WORD_1 dst_unused:UNUSED_PRESERVE src0_sel:WORD_1
	v_pk_add_f16 v105, v105, v114
	v_pk_add_f16 v104, v104, v115
	v_rcp_f16_e32 v110, v105
	v_rcp_f16_sdwa v105, v105 dst_sel:DWORD dst_unused:UNUSED_PAD src0_sel:WORD_1
	v_pk_add_f16 v103, v103, v116
	v_rcp_f16_e32 v111, v104
	v_rcp_f16_sdwa v104, v104 dst_sel:DWORD dst_unused:UNUSED_PAD src0_sel:WORD_1
	v_pk_add_f16 v102, v102, v117
	v_rcp_f16_e32 v112, v103
	v_rcp_f16_sdwa v103, v103 dst_sel:DWORD dst_unused:UNUSED_PAD src0_sel:WORD_1
	v_rcp_f16_e32 v113, v102
	v_rcp_f16_sdwa v102, v102 dst_sel:DWORD dst_unused:UNUSED_PAD src0_sel:WORD_1
	v_pk_fma_f16 v78, v46, v114, v78
	v_pack_b32_f16 v105, v110, v105
	v_pk_fma_f16 v79, v47, v115, v79
	v_pk_mul_f16 v110, v78, v105
	v_pack_b32_f16 v78, v111, v104
	v_pk_fma_f16 v80, v48, v116, v80
	v_pk_mul_f16 v111, v79, v78
	v_pack_b32_f16 v78, v112, v103
	v_pk_fma_f16 v81, v49, v117, v81
	v_pk_mul_f16 v112, v80, v78
	v_pack_b32_f16 v78, v113, v102
	v_pk_mul_f16 v113, v81, v78
	s_waitcnt vmcnt(12)
	v_pk_mul_f16 v78, v182, v154 op_sel_hi:[0,1]
	v_pk_mul_f16 v81, v182, v157 op_sel_hi:[0,1]
	v_pk_mul_f16 v102, v180, v154 op_sel_hi:[0,1]
	v_pk_mul_f16 v114, v181, v154 op_sel_hi:[0,1]
	v_pk_mul_f16 v79, v182, v155 op_sel_hi:[0,1]
	v_pk_mul_f16 v80, v182, v156 op_sel_hi:[0,1]
	v_pk_mul_f16 v103, v180, v155 op_sel_hi:[0,1]
	v_pk_mul_f16 v104, v180, v156 op_sel_hi:[0,1]
	v_pk_mul_f16 v105, v180, v157 op_sel_hi:[0,1]
	v_pk_mul_f16 v115, v181, v155 op_sel_hi:[0,1]
	v_pk_mul_f16 v116, v181, v156 op_sel_hi:[0,1]
	v_pk_mul_f16 v117, v181, v157 op_sel_hi:[0,1]
	v_pk_fma_f16 v85, v85, v157, v81
	v_pk_fma_f16 v82, v82, v154, v78
	v_pk_fma_f16 v109, v109, v157, v81
	v_pk_fma_f16 v106, v106, v154, v78
	v_pk_fma_f16 v81, v125, v157, v81
	v_pk_fma_f16 v78, v122, v154, v78
	v_pk_fma_f16 v125, v50, v154, v102
	v_pk_fma_f16 v129, v66, v154, v102
	v_pk_fma_f16 v102, v94, v154, v102
	v_pk_fma_f16 v137, v18, v154, v114
	v_pk_fma_f16 v186, v30, v154, v114
	v_pk_fma_f16 v114, v54, v154, v114
	v_pk_maximum3_f16 v154, v82, v106, v78
	v_pk_fma_f16 v84, v84, v156, v80
	v_pk_fma_f16 v83, v83, v155, v79
	v_pk_fma_f16 v108, v108, v156, v80
	v_pk_fma_f16 v107, v107, v155, v79
	v_pk_fma_f16 v80, v124, v156, v80
	v_pk_fma_f16 v79, v123, v155, v79
	v_pk_fma_f16 v122, v53, v157, v105
	v_pk_fma_f16 v123, v52, v156, v104
	v_pk_fma_f16 v124, v51, v155, v103
	v_pk_fma_f16 v126, v69, v157, v105
	v_pk_fma_f16 v127, v68, v156, v104
	v_pk_fma_f16 v128, v67, v155, v103
	v_pk_fma_f16 v105, v97, v157, v105
	v_pk_fma_f16 v104, v96, v156, v104
	v_pk_fma_f16 v103, v95, v155, v103
	v_pk_fma_f16 v134, v21, v157, v117
	v_pk_fma_f16 v135, v20, v156, v116
	v_pk_fma_f16 v136, v19, v155, v115
	v_pk_fma_f16 v183, v33, v157, v117
	v_pk_fma_f16 v184, v32, v156, v116
	v_pk_fma_f16 v185, v31, v155, v115
	v_pk_fma_f16 v117, v57, v157, v117
	v_pk_fma_f16 v116, v56, v156, v116
	v_pk_fma_f16 v115, v55, v155, v115
	v_pk_maximum3_f16 v155, v83, v107, v79
	v_pk_maximum3_f16 v156, v84, v108, v80
	v_pk_maximum3_f16 v157, v85, v109, v81
	v_pk_maximum3_f16 v187, v125, v129, v102
	v_pk_maximum3_f16 v191, v137, v186, v114
	v_pk_maximum3_f16 v188, v124, v128, v103
	v_pk_maximum3_f16 v189, v123, v127, v104
	v_pk_maximum3_f16 v190, v122, v126, v105
	v_pk_maximum3_f16 v192, v136, v185, v115
	v_pk_maximum3_f16 v193, v135, v184, v116
	v_pk_maximum3_f16 v154, v154, v187, v191
	v_pk_maximum3_f16 v194, v134, v183, v117
	v_pk_maximum3_f16 v155, v155, v188, v192
	v_pk_maximum3_f16 v156, v156, v189, v193
	v_pk_maximum3_f16 v157, v157, v190, v194
	v_pk_add_f16 v82, v82, v154 neg_lo:[0,1] neg_hi:[0,1]
	v_pk_add_f16 v83, v83, v155 neg_lo:[0,1] neg_hi:[0,1]
	v_pk_add_f16 v84, v84, v156 neg_lo:[0,1] neg_hi:[0,1]
	v_pk_add_f16 v85, v85, v157 neg_lo:[0,1] neg_hi:[0,1]
	v_pk_add_f16 v106, v106, v154 neg_lo:[0,1] neg_hi:[0,1]
	v_exp_f16_sdwa v187, v82 dst_sel:WORD_0 dst_unused:UNUSED_PAD src0_sel:WORD_0
	v_exp_f16_sdwa v188, v83 dst_sel:WORD_0 dst_unused:UNUSED_PAD src0_sel:WORD_0
	v_exp_f16_sdwa v189, v84 dst_sel:WORD_0 dst_unused:UNUSED_PAD src0_sel:WORD_0
	v_exp_f16_sdwa v190, v85 dst_sel:WORD_0 dst_unused:UNUSED_PAD src0_sel:WORD_0
	v_exp_f16_sdwa v187, v82 dst_sel:WORD_1 dst_unused:UNUSED_PRESERVE src0_sel:WORD_1
	v_exp_f16_sdwa v188, v83 dst_sel:WORD_1 dst_unused:UNUSED_PRESERVE src0_sel:WORD_1
	v_exp_f16_sdwa v189, v84 dst_sel:WORD_1 dst_unused:UNUSED_PRESERVE src0_sel:WORD_1
	v_exp_f16_sdwa v190, v85 dst_sel:WORD_1 dst_unused:UNUSED_PRESERVE src0_sel:WORD_1
	v_pk_add_f16 v107, v107, v155 neg_lo:[0,1] neg_hi:[0,1]
	v_pk_add_f16 v82, v190, 0
	v_pk_fma_f16 v42, v42, v187, 0
	v_pk_add_f16 v83, v189, 0
	v_pk_add_f16 v84, v188, 0
	v_pk_add_f16 v85, v187, 0
	v_pk_fma_f16 v45, v45, v190, 0
	v_pk_fma_f16 v44, v44, v189, 0
	v_pk_fma_f16 v43, v43, v188, 0
	v_pk_add_f16 v108, v108, v156 neg_lo:[0,1] neg_hi:[0,1]
	v_pk_add_f16 v109, v109, v157 neg_lo:[0,1] neg_hi:[0,1]
	v_exp_f16_sdwa v187, v106 dst_sel:WORD_0 dst_unused:UNUSED_PAD src0_sel:WORD_0
	v_exp_f16_sdwa v188, v107 dst_sel:WORD_0 dst_unused:UNUSED_PAD src0_sel:WORD_0
	v_exp_f16_sdwa v189, v108 dst_sel:WORD_0 dst_unused:UNUSED_PAD src0_sel:WORD_0
	v_exp_f16_sdwa v190, v109 dst_sel:WORD_0 dst_unused:UNUSED_PAD src0_sel:WORD_0
	v_exp_f16_sdwa v187, v106 dst_sel:WORD_1 dst_unused:UNUSED_PRESERVE src0_sel:WORD_1
	v_exp_f16_sdwa v188, v107 dst_sel:WORD_1 dst_unused:UNUSED_PRESERVE src0_sel:WORD_1
	v_exp_f16_sdwa v189, v108 dst_sel:WORD_1 dst_unused:UNUSED_PRESERVE src0_sel:WORD_1
	v_exp_f16_sdwa v190, v109 dst_sel:WORD_1 dst_unused:UNUSED_PRESERVE src0_sel:WORD_1
	s_nop 0
	v_pk_add_f16 v82, v82, v190
	v_pk_fma_f16 v42, v62, v187, v42
	v_pk_add_f16 v62, v78, v154 neg_lo:[0,1] neg_hi:[0,1]
	v_pk_add_f16 v85, v85, v187
	v_pk_add_f16 v84, v84, v188
	v_pk_add_f16 v83, v83, v189
	v_pk_fma_f16 v43, v63, v188, v43
	v_pk_fma_f16 v44, v64, v189, v44
	v_pk_fma_f16 v45, v65, v190, v45
	v_pk_add_f16 v63, v79, v155 neg_lo:[0,1] neg_hi:[0,1]
	v_pk_add_f16 v64, v80, v156 neg_lo:[0,1] neg_hi:[0,1]
	v_pk_add_f16 v65, v81, v157 neg_lo:[0,1] neg_hi:[0,1]
	v_exp_f16_sdwa v78, v62 dst_sel:WORD_0 dst_unused:UNUSED_PAD src0_sel:WORD_0
	v_exp_f16_sdwa v79, v63 dst_sel:WORD_0 dst_unused:UNUSED_PAD src0_sel:WORD_0
	v_exp_f16_sdwa v80, v64 dst_sel:WORD_0 dst_unused:UNUSED_PAD src0_sel:WORD_0
	v_exp_f16_sdwa v81, v65 dst_sel:WORD_0 dst_unused:UNUSED_PAD src0_sel:WORD_0
	v_exp_f16_sdwa v78, v62 dst_sel:WORD_1 dst_unused:UNUSED_PRESERVE src0_sel:WORD_1
	v_exp_f16_sdwa v79, v63 dst_sel:WORD_1 dst_unused:UNUSED_PRESERVE src0_sel:WORD_1
	v_exp_f16_sdwa v80, v64 dst_sel:WORD_1 dst_unused:UNUSED_PRESERVE src0_sel:WORD_1
	v_exp_f16_sdwa v81, v65 dst_sel:WORD_1 dst_unused:UNUSED_PRESERVE src0_sel:WORD_1
	s_nop 0
	v_pk_add_f16 v62, v82, v81
	v_pk_add_f16 v63, v83, v80
	v_pk_add_f16 v64, v84, v79
	v_pk_add_f16 v65, v85, v78
	v_pk_fma_f16 v45, v89, v81, v45
	v_pk_fma_f16 v44, v88, v80, v44
	v_pk_fma_f16 v43, v87, v79, v43
	v_pk_fma_f16 v42, v86, v78, v42
	v_pk_add_f16 v78, v125, v154 neg_lo:[0,1] neg_hi:[0,1]
	v_pk_add_f16 v79, v124, v155 neg_lo:[0,1] neg_hi:[0,1]
	v_pk_add_f16 v80, v123, v156 neg_lo:[0,1] neg_hi:[0,1]
	v_pk_add_f16 v81, v122, v157 neg_lo:[0,1] neg_hi:[0,1]
	v_exp_f16_sdwa v82, v78 dst_sel:WORD_0 dst_unused:UNUSED_PAD src0_sel:WORD_0
	v_exp_f16_sdwa v83, v79 dst_sel:WORD_0 dst_unused:UNUSED_PAD src0_sel:WORD_0
	v_exp_f16_sdwa v84, v80 dst_sel:WORD_0 dst_unused:UNUSED_PAD src0_sel:WORD_0
	v_exp_f16_sdwa v85, v81 dst_sel:WORD_0 dst_unused:UNUSED_PAD src0_sel:WORD_0
	v_exp_f16_sdwa v82, v78 dst_sel:WORD_1 dst_unused:UNUSED_PRESERVE src0_sel:WORD_1
	v_exp_f16_sdwa v83, v79 dst_sel:WORD_1 dst_unused:UNUSED_PRESERVE src0_sel:WORD_1
	v_exp_f16_sdwa v84, v80 dst_sel:WORD_1 dst_unused:UNUSED_PRESERVE src0_sel:WORD_1
	v_exp_f16_sdwa v85, v81 dst_sel:WORD_1 dst_unused:UNUSED_PRESERVE src0_sel:WORD_1
	v_pk_add_f16 v78, v129, v154 neg_lo:[0,1] neg_hi:[0,1]
	v_pk_add_f16 v62, v62, v85
	v_pk_add_f16 v65, v65, v82
	v_pk_add_f16 v64, v64, v83
	v_pk_add_f16 v63, v63, v84
	v_pk_fma_f16 v42, v22, v82, v42
	v_pk_fma_f16 v43, v23, v83, v43
	v_pk_fma_f16 v44, v24, v84, v44
	v_pk_fma_f16 v45, v25, v85, v45
	v_pk_add_f16 v79, v128, v155 neg_lo:[0,1] neg_hi:[0,1]
	v_pk_add_f16 v80, v127, v156 neg_lo:[0,1] neg_hi:[0,1]
	v_pk_add_f16 v81, v126, v157 neg_lo:[0,1] neg_hi:[0,1]
	v_exp_f16_sdwa v82, v78 dst_sel:WORD_0 dst_unused:UNUSED_PAD src0_sel:WORD_0
	v_exp_f16_sdwa v83, v79 dst_sel:WORD_0 dst_unused:UNUSED_PAD src0_sel:WORD_0
	v_exp_f16_sdwa v84, v80 dst_sel:WORD_0 dst_unused:UNUSED_PAD src0_sel:WORD_0
	v_exp_f16_sdwa v85, v81 dst_sel:WORD_0 dst_unused:UNUSED_PAD src0_sel:WORD_0
	v_exp_f16_sdwa v82, v78 dst_sel:WORD_1 dst_unused:UNUSED_PRESERVE src0_sel:WORD_1
	v_exp_f16_sdwa v83, v79 dst_sel:WORD_1 dst_unused:UNUSED_PRESERVE src0_sel:WORD_1
	v_exp_f16_sdwa v84, v80 dst_sel:WORD_1 dst_unused:UNUSED_PRESERVE src0_sel:WORD_1
	v_exp_f16_sdwa v85, v81 dst_sel:WORD_1 dst_unused:UNUSED_PRESERVE src0_sel:WORD_1
	v_pk_add_f16 v78, v102, v154 neg_lo:[0,1] neg_hi:[0,1]
	v_pk_add_f16 v62, v62, v85
	v_pk_add_f16 v63, v63, v84
	v_pk_add_f16 v64, v64, v83
	v_pk_add_f16 v65, v65, v82
	v_pk_fma_f16 v45, v37, v85, v45
	v_pk_fma_f16 v44, v36, v84, v44
	v_pk_fma_f16 v43, v35, v83, v43
	v_pk_fma_f16 v42, v34, v82, v42
	v_pk_add_f16 v79, v103, v155 neg_lo:[0,1] neg_hi:[0,1]
	v_pk_add_f16 v80, v104, v156 neg_lo:[0,1] neg_hi:[0,1]
	v_pk_add_f16 v81, v105, v157 neg_lo:[0,1] neg_hi:[0,1]
	v_exp_f16_sdwa v82, v78 dst_sel:WORD_0 dst_unused:UNUSED_PAD src0_sel:WORD_0
	v_exp_f16_sdwa v83, v79 dst_sel:WORD_0 dst_unused:UNUSED_PAD src0_sel:WORD_0
	v_exp_f16_sdwa v84, v80 dst_sel:WORD_0 dst_unused:UNUSED_PAD src0_sel:WORD_0
	v_exp_f16_sdwa v85, v81 dst_sel:WORD_0 dst_unused:UNUSED_PAD src0_sel:WORD_0
	v_exp_f16_sdwa v82, v78 dst_sel:WORD_1 dst_unused:UNUSED_PRESERVE src0_sel:WORD_1
	v_exp_f16_sdwa v83, v79 dst_sel:WORD_1 dst_unused:UNUSED_PRESERVE src0_sel:WORD_1
	v_exp_f16_sdwa v84, v80 dst_sel:WORD_1 dst_unused:UNUSED_PRESERVE src0_sel:WORD_1
	v_exp_f16_sdwa v85, v81 dst_sel:WORD_1 dst_unused:UNUSED_PRESERVE src0_sel:WORD_1
	v_pk_add_f16 v78, v137, v154 neg_lo:[0,1] neg_hi:[0,1]
	v_pk_add_f16 v62, v62, v85
	v_pk_add_f16 v65, v65, v82
	v_pk_add_f16 v64, v64, v83
	v_pk_add_f16 v63, v63, v84
	v_pk_fma_f16 v42, v46, v82, v42
	v_pk_fma_f16 v43, v47, v83, v43
	v_pk_fma_f16 v44, v48, v84, v44
	v_pk_fma_f16 v45, v49, v85, v45
	v_pk_add_f16 v79, v136, v155 neg_lo:[0,1] neg_hi:[0,1]
	v_pk_add_f16 v80, v135, v156 neg_lo:[0,1] neg_hi:[0,1]
	v_pk_add_f16 v81, v134, v157 neg_lo:[0,1] neg_hi:[0,1]
	v_exp_f16_sdwa v82, v78 dst_sel:WORD_0 dst_unused:UNUSED_PAD src0_sel:WORD_0
	v_exp_f16_sdwa v83, v79 dst_sel:WORD_0 dst_unused:UNUSED_PAD src0_sel:WORD_0
	v_exp_f16_sdwa v84, v80 dst_sel:WORD_0 dst_unused:UNUSED_PAD src0_sel:WORD_0
	v_exp_f16_sdwa v85, v81 dst_sel:WORD_0 dst_unused:UNUSED_PAD src0_sel:WORD_0
	v_exp_f16_sdwa v82, v78 dst_sel:WORD_1 dst_unused:UNUSED_PRESERVE src0_sel:WORD_1
	v_exp_f16_sdwa v83, v79 dst_sel:WORD_1 dst_unused:UNUSED_PRESERVE src0_sel:WORD_1
	v_exp_f16_sdwa v84, v80 dst_sel:WORD_1 dst_unused:UNUSED_PRESERVE src0_sel:WORD_1
	v_exp_f16_sdwa v85, v81 dst_sel:WORD_1 dst_unused:UNUSED_PRESERVE src0_sel:WORD_1
	v_pk_add_f16 v78, v186, v154 neg_lo:[0,1] neg_hi:[0,1]
	v_pk_add_f16 v62, v62, v85
	v_pk_add_f16 v63, v63, v84
	v_pk_add_f16 v64, v64, v83
	v_pk_add_f16 v65, v65, v82
	v_pk_fma_f16 v45, v9, v85, v45
	v_pk_fma_f16 v44, v8, v84, v44
	v_pk_fma_f16 v43, v7, v83, v43
	v_pk_fma_f16 v42, v6, v82, v42
	v_pk_add_f16 v79, v185, v155 neg_lo:[0,1] neg_hi:[0,1]
	v_pk_add_f16 v80, v184, v156 neg_lo:[0,1] neg_hi:[0,1]
	v_pk_add_f16 v81, v183, v157 neg_lo:[0,1] neg_hi:[0,1]
	v_exp_f16_sdwa v82, v78 dst_sel:WORD_0 dst_unused:UNUSED_PAD src0_sel:WORD_0
	v_exp_f16_sdwa v83, v79 dst_sel:WORD_0 dst_unused:UNUSED_PAD src0_sel:WORD_0
	v_exp_f16_sdwa v84, v80 dst_sel:WORD_0 dst_unused:UNUSED_PAD src0_sel:WORD_0
	v_exp_f16_sdwa v85, v81 dst_sel:WORD_0 dst_unused:UNUSED_PAD src0_sel:WORD_0
	v_exp_f16_sdwa v82, v78 dst_sel:WORD_1 dst_unused:UNUSED_PRESERVE src0_sel:WORD_1
	v_exp_f16_sdwa v83, v79 dst_sel:WORD_1 dst_unused:UNUSED_PRESERVE src0_sel:WORD_1
	v_exp_f16_sdwa v84, v80 dst_sel:WORD_1 dst_unused:UNUSED_PRESERVE src0_sel:WORD_1
	v_exp_f16_sdwa v85, v81 dst_sel:WORD_1 dst_unused:UNUSED_PRESERVE src0_sel:WORD_1
	v_pk_add_f16 v78, v114, v154 neg_lo:[0,1] neg_hi:[0,1]
	v_pk_add_f16 v62, v62, v85
	v_pk_add_f16 v65, v65, v82
	v_pk_add_f16 v64, v64, v83
	v_pk_add_f16 v63, v63, v84
	v_pk_fma_f16 v42, v10, v82, v42
	v_pk_fma_f16 v43, v11, v83, v43
	v_pk_fma_f16 v44, v12, v84, v44
	v_pk_fma_f16 v45, v13, v85, v45
	v_pk_add_f16 v79, v115, v155 neg_lo:[0,1] neg_hi:[0,1]
	v_pk_add_f16 v80, v116, v156 neg_lo:[0,1] neg_hi:[0,1]
	v_pk_add_f16 v81, v117, v157 neg_lo:[0,1] neg_hi:[0,1]
	v_exp_f16_sdwa v82, v78 dst_sel:WORD_0 dst_unused:UNUSED_PAD src0_sel:WORD_0
	v_exp_f16_sdwa v83, v79 dst_sel:WORD_0 dst_unused:UNUSED_PAD src0_sel:WORD_0
	v_exp_f16_sdwa v84, v80 dst_sel:WORD_0 dst_unused:UNUSED_PAD src0_sel:WORD_0
	v_exp_f16_sdwa v85, v81 dst_sel:WORD_0 dst_unused:UNUSED_PAD src0_sel:WORD_0
	v_exp_f16_sdwa v82, v78 dst_sel:WORD_1 dst_unused:UNUSED_PRESERVE src0_sel:WORD_1
	v_exp_f16_sdwa v83, v79 dst_sel:WORD_1 dst_unused:UNUSED_PRESERVE src0_sel:WORD_1
	v_exp_f16_sdwa v84, v80 dst_sel:WORD_1 dst_unused:UNUSED_PRESERVE src0_sel:WORD_1
	v_exp_f16_sdwa v85, v81 dst_sel:WORD_1 dst_unused:UNUSED_PRESERVE src0_sel:WORD_1
	s_nop 0
	v_pk_add_f16 v62, v62, v85
	v_pk_add_f16 v63, v63, v84
	v_pk_add_f16 v64, v64, v83
	v_pk_add_f16 v65, v65, v82
	v_rcp_f16_e32 v81, v62
	v_rcp_f16_sdwa v62, v62 dst_sel:DWORD dst_unused:UNUSED_PAD src0_sel:WORD_1
	v_rcp_f16_e32 v78, v65
	v_rcp_f16_sdwa v65, v65 dst_sel:DWORD dst_unused:UNUSED_PAD src0_sel:WORD_1
	v_rcp_f16_e32 v79, v64
	v_rcp_f16_sdwa v64, v64 dst_sel:DWORD dst_unused:UNUSED_PAD src0_sel:WORD_1
	v_rcp_f16_e32 v80, v63
	v_rcp_f16_sdwa v63, v63 dst_sel:DWORD dst_unused:UNUSED_PAD src0_sel:WORD_1
	v_pk_fma_f16 v45, v17, v85, v45
	v_pack_b32_f16 v62, v81, v62
	v_pk_fma_f16 v44, v16, v84, v44
	v_pk_fma_f16 v43, v15, v83, v43
	v_pk_fma_f16 v42, v14, v82, v42
	v_pack_b32_f16 v65, v78, v65
	v_pack_b32_f16 v64, v79, v64
	v_pack_b32_f16 v63, v80, v63
	v_pk_mul_f16 v45, v45, v62
	s_waitcnt vmcnt(6)
	v_pk_mul_f16 v62, v182, v150 op_sel_hi:[0,1]
	v_pk_mul_f16 v42, v42, v65
	v_pk_mul_f16 v43, v43, v64
	v_pk_mul_f16 v44, v44, v63
	v_pk_mul_f16 v63, v182, v151 op_sel_hi:[0,1]
	v_pk_mul_f16 v64, v182, v152 op_sel_hi:[0,1]
	v_pk_mul_f16 v65, v182, v153 op_sel_hi:[0,1]
	v_pk_mul_f16 v78, v180, v150 op_sel_hi:[0,1]
	v_pk_mul_f16 v82, v181, v150 op_sel_hi:[0,1]
	v_pk_fma_f16 v50, v50, v150, v62
	v_pk_fma_f16 v66, v66, v150, v62
	v_pk_fma_f16 v62, v94, v150, v62
	v_pk_mul_f16 v79, v180, v151 op_sel_hi:[0,1]
	v_pk_maximum3_f16 v114, v50, v66, v62
	v_pk_mul_f16 v80, v180, v152 op_sel_hi:[0,1]
	v_pk_mul_f16 v81, v180, v153 op_sel_hi:[0,1]
	v_pk_mul_f16 v83, v181, v151 op_sel_hi:[0,1]
	v_pk_mul_f16 v84, v181, v152 op_sel_hi:[0,1]
	v_pk_mul_f16 v85, v181, v153 op_sel_hi:[0,1]
	v_pk_fma_f16 v53, v53, v153, v65
	v_pk_fma_f16 v52, v52, v152, v64
	v_pk_fma_f16 v51, v51, v151, v63
	v_pk_fma_f16 v69, v69, v153, v65
	v_pk_fma_f16 v68, v68, v152, v64
	v_pk_fma_f16 v67, v67, v151, v63
	v_pk_fma_f16 v65, v97, v153, v65
	v_pk_fma_f16 v64, v96, v152, v64
	v_pk_fma_f16 v63, v95, v151, v63
	v_pk_fma_f16 v89, v18, v150, v78
	v_pk_fma_f16 v97, v30, v150, v78
	v_pk_fma_f16 v78, v54, v150, v78
	v_pk_fma_f16 v105, v74, v150, v82
	v_pk_fma_f16 v109, v98, v150, v82
	v_pk_fma_f16 v82, v118, v150, v82
	v_pk_maximum3_f16 v115, v51, v67, v63
	v_pk_maximum3_f16 v116, v52, v68, v64
	v_pk_maximum3_f16 v117, v53, v69, v65
	v_pk_maximum3_f16 v122, v89, v97, v78
	v_pk_fma_f16 v86, v21, v153, v81
	v_pk_maximum3_f16 v126, v105, v109, v82
	v_pk_fma_f16 v87, v20, v152, v80
	v_pk_maximum3_f16 v114, v114, v122, v126
	v_pk_fma_f16 v88, v19, v151, v79
	v_pk_fma_f16 v94, v33, v153, v81
	v_pk_fma_f16 v95, v32, v152, v80
	v_pk_fma_f16 v96, v31, v151, v79
	v_pk_fma_f16 v81, v57, v153, v81
	v_pk_fma_f16 v80, v56, v152, v80
	v_pk_fma_f16 v79, v55, v151, v79
	v_pk_fma_f16 v102, v77, v153, v85
	v_pk_fma_f16 v103, v76, v152, v84
	v_pk_fma_f16 v104, v75, v151, v83
	v_pk_fma_f16 v106, v101, v153, v85
	v_pk_fma_f16 v107, v100, v152, v84
	v_pk_fma_f16 v108, v99, v151, v83
	v_pk_fma_f16 v85, v121, v153, v85
	v_pk_fma_f16 v84, v120, v152, v84
	v_pk_fma_f16 v83, v119, v151, v83
	v_pk_maximum3_f16 v123, v88, v96, v79
	v_pk_maximum3_f16 v124, v87, v95, v80
	v_pk_maximum3_f16 v125, v86, v94, v81
	v_pk_maximum3_f16 v128, v103, v107, v84
	v_pk_maximum3_f16 v129, v102, v106, v85
	v_pk_maximum3_f16 v127, v104, v108, v83
	v_pk_maximum3_f16 v115, v115, v123, v127
	v_pk_maximum3_f16 v116, v116, v124, v128
	v_pk_maximum3_f16 v117, v117, v125, v129
	v_pk_add_f16 v50, v50, v114 neg_lo:[0,1] neg_hi:[0,1]
	v_pk_add_f16 v51, v51, v115 neg_lo:[0,1] neg_hi:[0,1]
	v_pk_add_f16 v52, v52, v116 neg_lo:[0,1] neg_hi:[0,1]
	v_pk_add_f16 v53, v53, v117 neg_lo:[0,1] neg_hi:[0,1]
	v_pk_add_f16 v66, v66, v114 neg_lo:[0,1] neg_hi:[0,1]
	v_exp_f16_sdwa v122, v50 dst_sel:WORD_0 dst_unused:UNUSED_PAD src0_sel:WORD_0
	v_exp_f16_sdwa v123, v51 dst_sel:WORD_0 dst_unused:UNUSED_PAD src0_sel:WORD_0
	v_exp_f16_sdwa v124, v52 dst_sel:WORD_0 dst_unused:UNUSED_PAD src0_sel:WORD_0
	v_exp_f16_sdwa v125, v53 dst_sel:WORD_0 dst_unused:UNUSED_PAD src0_sel:WORD_0
	v_exp_f16_sdwa v122, v50 dst_sel:WORD_1 dst_unused:UNUSED_PRESERVE src0_sel:WORD_1
	v_exp_f16_sdwa v123, v51 dst_sel:WORD_1 dst_unused:UNUSED_PRESERVE src0_sel:WORD_1
	v_exp_f16_sdwa v124, v52 dst_sel:WORD_1 dst_unused:UNUSED_PRESERVE src0_sel:WORD_1
	v_exp_f16_sdwa v125, v53 dst_sel:WORD_1 dst_unused:UNUSED_PRESERVE src0_sel:WORD_1
	v_pk_add_f16 v67, v67, v115 neg_lo:[0,1] neg_hi:[0,1]
	v_pk_add_f16 v50, v125, 0
	v_pk_fma_f16 v22, v22, v122, 0
	v_pk_add_f16 v51, v124, 0
	v_pk_add_f16 v52, v123, 0
	v_pk_add_f16 v53, v122, 0
	v_pk_fma_f16 v23, v23, v123, 0
	v_pk_fma_f16 v24, v24, v124, 0
	v_pk_fma_f16 v25, v25, v125, 0
	v_pk_add_f16 v68, v68, v116 neg_lo:[0,1] neg_hi:[0,1]
	v_pk_add_f16 v69, v69, v117 neg_lo:[0,1] neg_hi:[0,1]
	v_exp_f16_sdwa v122, v66 dst_sel:WORD_0 dst_unused:UNUSED_PAD src0_sel:WORD_0
	v_exp_f16_sdwa v123, v67 dst_sel:WORD_0 dst_unused:UNUSED_PAD src0_sel:WORD_0
	v_exp_f16_sdwa v124, v68 dst_sel:WORD_0 dst_unused:UNUSED_PAD src0_sel:WORD_0
	v_exp_f16_sdwa v125, v69 dst_sel:WORD_0 dst_unused:UNUSED_PAD src0_sel:WORD_0
	v_exp_f16_sdwa v122, v66 dst_sel:WORD_1 dst_unused:UNUSED_PRESERVE src0_sel:WORD_1
	v_exp_f16_sdwa v123, v67 dst_sel:WORD_1 dst_unused:UNUSED_PRESERVE src0_sel:WORD_1
	v_exp_f16_sdwa v124, v68 dst_sel:WORD_1 dst_unused:UNUSED_PRESERVE src0_sel:WORD_1
	v_exp_f16_sdwa v125, v69 dst_sel:WORD_1 dst_unused:UNUSED_PRESERVE src0_sel:WORD_1
	s_nop 0
	v_pk_add_f16 v50, v50, v125
	v_pk_fma_f16 v22, v34, v122, v22
	v_pk_add_f16 v34, v62, v114 neg_lo:[0,1] neg_hi:[0,1]
	v_pk_add_f16 v53, v53, v122
	v_pk_add_f16 v52, v52, v123
	v_pk_add_f16 v51, v51, v124
	v_pk_fma_f16 v25, v37, v125, v25
	v_pk_fma_f16 v24, v36, v124, v24
	v_pk_fma_f16 v23, v35, v123, v23
	v_pk_add_f16 v35, v63, v115 neg_lo:[0,1] neg_hi:[0,1]
	v_pk_add_f16 v36, v64, v116 neg_lo:[0,1] neg_hi:[0,1]
	v_pk_add_f16 v37, v65, v117 neg_lo:[0,1] neg_hi:[0,1]
	v_exp_f16_sdwa v62, v34 dst_sel:WORD_0 dst_unused:UNUSED_PAD src0_sel:WORD_0
	v_exp_f16_sdwa v63, v35 dst_sel:WORD_0 dst_unused:UNUSED_PAD src0_sel:WORD_0
	v_exp_f16_sdwa v64, v36 dst_sel:WORD_0 dst_unused:UNUSED_PAD src0_sel:WORD_0
	v_exp_f16_sdwa v65, v37 dst_sel:WORD_0 dst_unused:UNUSED_PAD src0_sel:WORD_0
	v_exp_f16_sdwa v62, v34 dst_sel:WORD_1 dst_unused:UNUSED_PRESERVE src0_sel:WORD_1
	v_exp_f16_sdwa v63, v35 dst_sel:WORD_1 dst_unused:UNUSED_PRESERVE src0_sel:WORD_1
	v_exp_f16_sdwa v64, v36 dst_sel:WORD_1 dst_unused:UNUSED_PRESERVE src0_sel:WORD_1
	v_exp_f16_sdwa v65, v37 dst_sel:WORD_1 dst_unused:UNUSED_PRESERVE src0_sel:WORD_1
	s_nop 0
	v_pk_add_f16 v34, v50, v65
	v_pk_add_f16 v35, v51, v64
	v_pk_add_f16 v36, v52, v63
	v_pk_add_f16 v37, v53, v62
	v_pk_fma_f16 v22, v46, v62, v22
	v_pk_fma_f16 v23, v47, v63, v23
	v_pk_fma_f16 v24, v48, v64, v24
	v_pk_fma_f16 v25, v49, v65, v25
	v_pk_add_f16 v46, v89, v114 neg_lo:[0,1] neg_hi:[0,1]
	v_pk_add_f16 v47, v88, v115 neg_lo:[0,1] neg_hi:[0,1]
	v_pk_add_f16 v48, v87, v116 neg_lo:[0,1] neg_hi:[0,1]
	v_pk_add_f16 v49, v86, v117 neg_lo:[0,1] neg_hi:[0,1]
	v_exp_f16_sdwa v50, v46 dst_sel:WORD_0 dst_unused:UNUSED_PAD src0_sel:WORD_0
	v_exp_f16_sdwa v51, v47 dst_sel:WORD_0 dst_unused:UNUSED_PAD src0_sel:WORD_0
	v_exp_f16_sdwa v52, v48 dst_sel:WORD_0 dst_unused:UNUSED_PAD src0_sel:WORD_0
	v_exp_f16_sdwa v53, v49 dst_sel:WORD_0 dst_unused:UNUSED_PAD src0_sel:WORD_0
	v_exp_f16_sdwa v50, v46 dst_sel:WORD_1 dst_unused:UNUSED_PRESERVE src0_sel:WORD_1
	v_exp_f16_sdwa v51, v47 dst_sel:WORD_1 dst_unused:UNUSED_PRESERVE src0_sel:WORD_1
	v_exp_f16_sdwa v52, v48 dst_sel:WORD_1 dst_unused:UNUSED_PRESERVE src0_sel:WORD_1
	v_exp_f16_sdwa v53, v49 dst_sel:WORD_1 dst_unused:UNUSED_PRESERVE src0_sel:WORD_1
	v_pk_add_f16 v46, v97, v114 neg_lo:[0,1] neg_hi:[0,1]
	v_pk_add_f16 v34, v34, v53
	v_pk_add_f16 v37, v37, v50
	v_pk_add_f16 v36, v36, v51
	v_pk_add_f16 v35, v35, v52
	v_pk_fma_f16 v25, v9, v53, v25
	v_pk_fma_f16 v24, v8, v52, v24
	v_pk_fma_f16 v23, v7, v51, v23
	v_pk_fma_f16 v22, v6, v50, v22
	v_pk_add_f16 v47, v96, v115 neg_lo:[0,1] neg_hi:[0,1]
	v_pk_add_f16 v48, v95, v116 neg_lo:[0,1] neg_hi:[0,1]
	v_pk_add_f16 v49, v94, v117 neg_lo:[0,1] neg_hi:[0,1]
	v_exp_f16_sdwa v50, v46 dst_sel:WORD_0 dst_unused:UNUSED_PAD src0_sel:WORD_0
	v_exp_f16_sdwa v51, v47 dst_sel:WORD_0 dst_unused:UNUSED_PAD src0_sel:WORD_0
	v_exp_f16_sdwa v52, v48 dst_sel:WORD_0 dst_unused:UNUSED_PAD src0_sel:WORD_0
	v_exp_f16_sdwa v53, v49 dst_sel:WORD_0 dst_unused:UNUSED_PAD src0_sel:WORD_0
	v_exp_f16_sdwa v50, v46 dst_sel:WORD_1 dst_unused:UNUSED_PRESERVE src0_sel:WORD_1
	v_exp_f16_sdwa v51, v47 dst_sel:WORD_1 dst_unused:UNUSED_PRESERVE src0_sel:WORD_1
	v_exp_f16_sdwa v52, v48 dst_sel:WORD_1 dst_unused:UNUSED_PRESERVE src0_sel:WORD_1
	v_exp_f16_sdwa v53, v49 dst_sel:WORD_1 dst_unused:UNUSED_PRESERVE src0_sel:WORD_1
	v_pk_add_f16 v46, v78, v114 neg_lo:[0,1] neg_hi:[0,1]
	v_pk_add_f16 v34, v34, v53
	v_pk_add_f16 v35, v35, v52
	v_pk_add_f16 v36, v36, v51
	v_pk_add_f16 v37, v37, v50
	v_pk_fma_f16 v22, v10, v50, v22
	v_pk_fma_f16 v23, v11, v51, v23
	v_pk_fma_f16 v24, v12, v52, v24
	v_pk_fma_f16 v25, v13, v53, v25
	v_pk_add_f16 v47, v79, v115 neg_lo:[0,1] neg_hi:[0,1]
	v_pk_add_f16 v48, v80, v116 neg_lo:[0,1] neg_hi:[0,1]
	v_pk_add_f16 v49, v81, v117 neg_lo:[0,1] neg_hi:[0,1]
	v_exp_f16_sdwa v50, v46 dst_sel:WORD_0 dst_unused:UNUSED_PAD src0_sel:WORD_0
	v_exp_f16_sdwa v51, v47 dst_sel:WORD_0 dst_unused:UNUSED_PAD src0_sel:WORD_0
	v_exp_f16_sdwa v52, v48 dst_sel:WORD_0 dst_unused:UNUSED_PAD src0_sel:WORD_0
	v_exp_f16_sdwa v53, v49 dst_sel:WORD_0 dst_unused:UNUSED_PAD src0_sel:WORD_0
	v_exp_f16_sdwa v50, v46 dst_sel:WORD_1 dst_unused:UNUSED_PRESERVE src0_sel:WORD_1
	v_exp_f16_sdwa v51, v47 dst_sel:WORD_1 dst_unused:UNUSED_PRESERVE src0_sel:WORD_1
	v_exp_f16_sdwa v52, v48 dst_sel:WORD_1 dst_unused:UNUSED_PRESERVE src0_sel:WORD_1
	v_exp_f16_sdwa v53, v49 dst_sel:WORD_1 dst_unused:UNUSED_PRESERVE src0_sel:WORD_1
	v_pk_add_f16 v46, v105, v114 neg_lo:[0,1] neg_hi:[0,1]
	v_pk_add_f16 v34, v34, v53
	v_pk_add_f16 v37, v37, v50
	v_pk_add_f16 v36, v36, v51
	v_pk_add_f16 v35, v35, v52
	v_pk_fma_f16 v25, v17, v53, v25
	v_pk_fma_f16 v24, v16, v52, v24
	v_pk_fma_f16 v23, v15, v51, v23
	v_pk_fma_f16 v22, v14, v50, v22
	v_pk_add_f16 v47, v104, v115 neg_lo:[0,1] neg_hi:[0,1]
	v_pk_add_f16 v48, v103, v116 neg_lo:[0,1] neg_hi:[0,1]
	v_pk_add_f16 v49, v102, v117 neg_lo:[0,1] neg_hi:[0,1]
	v_exp_f16_sdwa v50, v46 dst_sel:WORD_0 dst_unused:UNUSED_PAD src0_sel:WORD_0
	v_exp_f16_sdwa v51, v47 dst_sel:WORD_0 dst_unused:UNUSED_PAD src0_sel:WORD_0
	v_exp_f16_sdwa v52, v48 dst_sel:WORD_0 dst_unused:UNUSED_PAD src0_sel:WORD_0
	v_exp_f16_sdwa v53, v49 dst_sel:WORD_0 dst_unused:UNUSED_PAD src0_sel:WORD_0
	v_exp_f16_sdwa v50, v46 dst_sel:WORD_1 dst_unused:UNUSED_PRESERVE src0_sel:WORD_1
	v_exp_f16_sdwa v51, v47 dst_sel:WORD_1 dst_unused:UNUSED_PRESERVE src0_sel:WORD_1
	v_exp_f16_sdwa v52, v48 dst_sel:WORD_1 dst_unused:UNUSED_PRESERVE src0_sel:WORD_1
	v_exp_f16_sdwa v53, v49 dst_sel:WORD_1 dst_unused:UNUSED_PRESERVE src0_sel:WORD_1
	v_pk_add_f16 v46, v109, v114 neg_lo:[0,1] neg_hi:[0,1]
	v_pk_add_f16 v34, v34, v53
	v_pk_add_f16 v35, v35, v52
	v_pk_add_f16 v36, v36, v51
	v_pk_add_f16 v37, v37, v50
	v_pk_fma_f16 v22, v26, v50, v22
	v_pk_fma_f16 v23, v27, v51, v23
	v_pk_fma_f16 v24, v28, v52, v24
	v_pk_fma_f16 v25, v29, v53, v25
	v_pk_add_f16 v47, v108, v115 neg_lo:[0,1] neg_hi:[0,1]
	v_pk_add_f16 v48, v107, v116 neg_lo:[0,1] neg_hi:[0,1]
	v_pk_add_f16 v49, v106, v117 neg_lo:[0,1] neg_hi:[0,1]
	v_exp_f16_sdwa v50, v46 dst_sel:WORD_0 dst_unused:UNUSED_PAD src0_sel:WORD_0
	v_exp_f16_sdwa v51, v47 dst_sel:WORD_0 dst_unused:UNUSED_PAD src0_sel:WORD_0
	v_exp_f16_sdwa v52, v48 dst_sel:WORD_0 dst_unused:UNUSED_PAD src0_sel:WORD_0
	v_exp_f16_sdwa v53, v49 dst_sel:WORD_0 dst_unused:UNUSED_PAD src0_sel:WORD_0
	v_exp_f16_sdwa v50, v46 dst_sel:WORD_1 dst_unused:UNUSED_PRESERVE src0_sel:WORD_1
	v_exp_f16_sdwa v51, v47 dst_sel:WORD_1 dst_unused:UNUSED_PRESERVE src0_sel:WORD_1
	v_exp_f16_sdwa v52, v48 dst_sel:WORD_1 dst_unused:UNUSED_PRESERVE src0_sel:WORD_1
	v_exp_f16_sdwa v53, v49 dst_sel:WORD_1 dst_unused:UNUSED_PRESERVE src0_sel:WORD_1
	v_pk_add_f16 v46, v82, v114 neg_lo:[0,1] neg_hi:[0,1]
	v_pk_add_f16 v34, v34, v53
	v_pk_add_f16 v37, v37, v50
	v_pk_add_f16 v36, v36, v51
	v_pk_add_f16 v35, v35, v52
	v_pk_fma_f16 v25, v41, v53, v25
	v_pk_fma_f16 v24, v40, v52, v24
	v_pk_fma_f16 v23, v39, v51, v23
	v_pk_fma_f16 v22, v38, v50, v22
	v_pk_add_f16 v47, v83, v115 neg_lo:[0,1] neg_hi:[0,1]
	v_pk_add_f16 v48, v84, v116 neg_lo:[0,1] neg_hi:[0,1]
	v_pk_add_f16 v49, v85, v117 neg_lo:[0,1] neg_hi:[0,1]
	v_exp_f16_sdwa v50, v46 dst_sel:WORD_0 dst_unused:UNUSED_PAD src0_sel:WORD_0
	v_exp_f16_sdwa v51, v47 dst_sel:WORD_0 dst_unused:UNUSED_PAD src0_sel:WORD_0
	v_exp_f16_sdwa v52, v48 dst_sel:WORD_0 dst_unused:UNUSED_PAD src0_sel:WORD_0
	v_exp_f16_sdwa v53, v49 dst_sel:WORD_0 dst_unused:UNUSED_PAD src0_sel:WORD_0
	v_exp_f16_sdwa v50, v46 dst_sel:WORD_1 dst_unused:UNUSED_PRESERVE src0_sel:WORD_1
	v_exp_f16_sdwa v51, v47 dst_sel:WORD_1 dst_unused:UNUSED_PRESERVE src0_sel:WORD_1
	v_exp_f16_sdwa v52, v48 dst_sel:WORD_1 dst_unused:UNUSED_PRESERVE src0_sel:WORD_1
	v_exp_f16_sdwa v53, v49 dst_sel:WORD_1 dst_unused:UNUSED_PRESERVE src0_sel:WORD_1
	s_nop 0
	v_pk_add_f16 v34, v34, v53
	v_pk_add_f16 v35, v35, v52
	v_rcp_f16_e32 v48, v34
	v_rcp_f16_sdwa v34, v34 dst_sel:DWORD dst_unused:UNUSED_PAD src0_sel:WORD_1
	v_pk_add_f16 v36, v36, v51
	v_rcp_f16_e32 v49, v35
	v_rcp_f16_sdwa v35, v35 dst_sel:DWORD dst_unused:UNUSED_PAD src0_sel:WORD_1
	v_pk_add_f16 v37, v37, v50
	v_rcp_f16_e32 v47, v36
	v_rcp_f16_sdwa v36, v36 dst_sel:DWORD dst_unused:UNUSED_PAD src0_sel:WORD_1
	v_rcp_f16_e32 v46, v37
	v_rcp_f16_sdwa v37, v37 dst_sel:DWORD dst_unused:UNUSED_PAD src0_sel:WORD_1
	v_pk_fma_f16 v25, v61, v53, v25
	v_pack_b32_f16 v34, v48, v34
	v_pk_fma_f16 v24, v60, v52, v24
	v_pk_mul_f16 v25, v25, v34
	v_pack_b32_f16 v34, v49, v35
	v_pk_fma_f16 v23, v59, v51, v23
	v_pk_mul_f16 v24, v24, v34
	v_pack_b32_f16 v34, v47, v36
	v_pk_fma_f16 v22, v58, v50, v22
	v_pk_mul_f16 v23, v23, v34
	v_pack_b32_f16 v34, v46, v37
	v_pk_mul_f16 v22, v22, v34
	s_waitcnt vmcnt(0)
	s_mov_b64 s[86:87], s[80:81]
	global_load_dword v254, v255, s[86:87]
	s_add_u32 s86, s86, 0x2000
	s_addc_u32 s87, s87, 0
	global_load_dword v254, v255, s[86:87]
	s_add_u32 s86, s86, 0x2000
	s_addc_u32 s87, s87, 0
	global_load_dword v254, v255, s[86:87]
	s_add_u32 s86, s86, 0x2c000
	s_addc_u32 s87, s87, 0
	global_load_dword v254, v255, s[86:87]
	s_add_u32 s86, s86, 0x2000
	s_addc_u32 s87, s87, 0
	global_load_dword v254, v255, s[86:87]
	s_add_u32 s86, s86, 0x2000
	s_addc_u32 s87, s87, 0
	global_load_dword v254, v255, s[86:87]
	v_pk_mul_f16 v34, v182, v146 op_sel_hi:[0,1]
	v_pk_mul_f16 v35, v182, v147 op_sel_hi:[0,1]
	v_pk_mul_f16 v36, v182, v148 op_sel_hi:[0,1]
	v_pk_mul_f16 v37, v182, v149 op_sel_hi:[0,1]
	v_pk_mul_f16 v46, v180, v146 op_sel_hi:[0,1]
	v_pk_mul_f16 v47, v180, v147 op_sel_hi:[0,1]
	v_pk_mul_f16 v48, v180, v148 op_sel_hi:[0,1]
	v_pk_mul_f16 v49, v180, v149 op_sel_hi:[0,1]
	v_pk_mul_f16 v50, v181, v146 op_sel_hi:[0,1]
	v_pk_mul_f16 v51, v181, v147 op_sel_hi:[0,1]
	v_pk_mul_f16 v52, v181, v148 op_sel_hi:[0,1]
	v_pk_mul_f16 v53, v181, v149 op_sel_hi:[0,1]
	v_pk_fma_f16 v21, v21, v149, v37
	v_pk_fma_f16 v20, v20, v148, v36
	v_pk_fma_f16 v19, v19, v147, v35
	v_pk_fma_f16 v18, v18, v146, v34
	v_pk_fma_f16 v33, v33, v149, v37
	v_pk_fma_f16 v32, v32, v148, v36
	v_pk_fma_f16 v31, v31, v147, v35
	v_pk_fma_f16 v30, v30, v146, v34
	v_pk_fma_f16 v37, v57, v149, v37
	v_pk_fma_f16 v36, v56, v148, v36
	v_pk_fma_f16 v35, v55, v147, v35
	v_pk_fma_f16 v34, v54, v146, v34
	v_pk_maximum3_f16 v79, v19, v31, v35
	v_pk_maximum3_f16 v80, v20, v32, v36
	v_pk_maximum3_f16 v81, v21, v33, v37
	v_pk_fma_f16 v54, v77, v149, v49
	v_pk_maximum3_f16 v78, v18, v30, v34
	v_pk_fma_f16 v55, v76, v148, v48
	v_pk_fma_f16 v56, v75, v147, v47
	v_pk_fma_f16 v57, v74, v146, v46
	v_pk_fma_f16 v62, v101, v149, v49
	v_pk_fma_f16 v63, v100, v148, v48
	v_pk_fma_f16 v64, v99, v147, v47
	v_pk_fma_f16 v65, v98, v146, v46
	v_pk_fma_f16 v49, v121, v149, v49
	v_pk_fma_f16 v48, v120, v148, v48
	v_pk_fma_f16 v47, v119, v147, v47
	v_pk_fma_f16 v46, v118, v146, v46
	v_pk_fma_f16 v66, v133, v149, v53
	v_pk_fma_f16 v67, v132, v148, v52
	v_pk_fma_f16 v68, v131, v147, v51
	v_pk_fma_f16 v69, v130, v146, v50
	v_pk_fma_f16 v74, v141, v149, v53
	v_pk_fma_f16 v75, v140, v148, v52
	v_pk_fma_f16 v76, v139, v147, v51
	v_pk_fma_f16 v77, v138, v146, v50
	v_pk_fma_f16 v53, v145, v149, v53
	v_pk_fma_f16 v52, v144, v148, v52
	v_pk_fma_f16 v51, v143, v147, v51
	v_pk_fma_f16 v50, v142, v146, v50
	v_pk_maximum3_f16 v82, v57, v65, v46
	v_pk_maximum3_f16 v83, v56, v64, v47
	v_pk_maximum3_f16 v84, v55, v63, v48
	v_pk_maximum3_f16 v85, v54, v62, v49
	v_pk_maximum3_f16 v87, v68, v76, v51
	v_pk_maximum3_f16 v86, v69, v77, v50
	v_pk_maximum3_f16 v88, v67, v75, v52
	v_pk_maximum3_f16 v89, v66, v74, v53
	v_pk_maximum3_f16 v78, v78, v82, v86
	v_pk_maximum3_f16 v79, v79, v83, v87
	v_pk_maximum3_f16 v80, v80, v84, v88
	v_pk_maximum3_f16 v81, v81, v85, v89
	s_nop 0
	v_pk_add_f16 v18, v18, v78 neg_lo:[0,1] neg_hi:[0,1]
	v_pk_add_f16 v19, v19, v79 neg_lo:[0,1] neg_hi:[0,1]
	v_pk_add_f16 v20, v20, v80 neg_lo:[0,1] neg_hi:[0,1]
	v_pk_add_f16 v21, v21, v81 neg_lo:[0,1] neg_hi:[0,1]
	v_pk_add_f16 v30, v30, v78 neg_lo:[0,1] neg_hi:[0,1]
	v_exp_f16_sdwa v82, v18 dst_sel:WORD_0 dst_unused:UNUSED_PAD src0_sel:WORD_0
	v_exp_f16_sdwa v83, v19 dst_sel:WORD_0 dst_unused:UNUSED_PAD src0_sel:WORD_0
	v_exp_f16_sdwa v84, v20 dst_sel:WORD_0 dst_unused:UNUSED_PAD src0_sel:WORD_0
	v_exp_f16_sdwa v85, v21 dst_sel:WORD_0 dst_unused:UNUSED_PAD src0_sel:WORD_0
	v_exp_f16_sdwa v82, v18 dst_sel:WORD_1 dst_unused:UNUSED_PRESERVE src0_sel:WORD_1
	v_exp_f16_sdwa v83, v19 dst_sel:WORD_1 dst_unused:UNUSED_PRESERVE src0_sel:WORD_1
	v_exp_f16_sdwa v84, v20 dst_sel:WORD_1 dst_unused:UNUSED_PRESERVE src0_sel:WORD_1
	v_exp_f16_sdwa v85, v21 dst_sel:WORD_1 dst_unused:UNUSED_PRESERVE src0_sel:WORD_1
	v_pk_add_f16 v31, v31, v79 neg_lo:[0,1] neg_hi:[0,1]
	v_pk_add_f16 v18, v82, 0
	v_pk_add_f16 v19, v83, 0
	v_pk_add_f16 v20, v84, 0
	v_pk_add_f16 v21, v85, 0
	v_pk_fma_f16 v6, v6, v82, 0
	v_pk_fma_f16 v7, v7, v83, 0
	v_pk_fma_f16 v8, v8, v84, 0
	v_pk_fma_f16 v9, v9, v85, 0
	v_pk_add_f16 v32, v32, v80 neg_lo:[0,1] neg_hi:[0,1]
	v_pk_add_f16 v33, v33, v81 neg_lo:[0,1] neg_hi:[0,1]
	v_exp_f16_sdwa v82, v30 dst_sel:WORD_0 dst_unused:UNUSED_PAD src0_sel:WORD_0
	v_exp_f16_sdwa v83, v31 dst_sel:WORD_0 dst_unused:UNUSED_PAD src0_sel:WORD_0
	v_exp_f16_sdwa v84, v32 dst_sel:WORD_0 dst_unused:UNUSED_PAD src0_sel:WORD_0
	v_exp_f16_sdwa v85, v33 dst_sel:WORD_0 dst_unused:UNUSED_PAD src0_sel:WORD_0
	v_exp_f16_sdwa v82, v30 dst_sel:WORD_1 dst_unused:UNUSED_PRESERVE src0_sel:WORD_1
	v_exp_f16_sdwa v83, v31 dst_sel:WORD_1 dst_unused:UNUSED_PRESERVE src0_sel:WORD_1
	v_exp_f16_sdwa v84, v32 dst_sel:WORD_1 dst_unused:UNUSED_PRESERVE src0_sel:WORD_1
	v_exp_f16_sdwa v85, v33 dst_sel:WORD_1 dst_unused:UNUSED_PRESERVE src0_sel:WORD_1
	s_nop 0
	v_pk_add_f16 v21, v21, v85
	v_pk_add_f16 v20, v20, v84
	v_pk_add_f16 v19, v19, v83
	v_pk_add_f16 v18, v18, v82
	v_pk_fma_f16 v9, v13, v85, v9
	v_pk_fma_f16 v8, v12, v84, v8
	v_pk_fma_f16 v7, v11, v83, v7
	v_pk_fma_f16 v6, v10, v82, v6
	v_pk_add_f16 v10, v34, v78 neg_lo:[0,1] neg_hi:[0,1]
	v_pk_add_f16 v11, v35, v79 neg_lo:[0,1] neg_hi:[0,1]
	v_pk_add_f16 v12, v36, v80 neg_lo:[0,1] neg_hi:[0,1]
	v_pk_add_f16 v13, v37, v81 neg_lo:[0,1] neg_hi:[0,1]
	v_exp_f16_sdwa v30, v10 dst_sel:WORD_0 dst_unused:UNUSED_PAD src0_sel:WORD_0
	v_exp_f16_sdwa v31, v11 dst_sel:WORD_0 dst_unused:UNUSED_PAD src0_sel:WORD_0
	v_exp_f16_sdwa v32, v12 dst_sel:WORD_0 dst_unused:UNUSED_PAD src0_sel:WORD_0
	v_exp_f16_sdwa v33, v13 dst_sel:WORD_0 dst_unused:UNUSED_PAD src0_sel:WORD_0
	v_exp_f16_sdwa v30, v10 dst_sel:WORD_1 dst_unused:UNUSED_PRESERVE src0_sel:WORD_1
	v_exp_f16_sdwa v31, v11 dst_sel:WORD_1 dst_unused:UNUSED_PRESERVE src0_sel:WORD_1
	v_exp_f16_sdwa v32, v12 dst_sel:WORD_1 dst_unused:UNUSED_PRESERVE src0_sel:WORD_1
	v_exp_f16_sdwa v33, v13 dst_sel:WORD_1 dst_unused:UNUSED_PRESERVE src0_sel:WORD_1
	v_pk_add_f16 v10, v18, v30
	v_pk_add_f16 v11, v19, v31
	v_pk_add_f16 v12, v20, v32
	v_pk_add_f16 v13, v21, v33
	v_pk_fma_f16 v6, v14, v30, v6
	v_pk_fma_f16 v7, v15, v31, v7
	v_pk_fma_f16 v8, v16, v32, v8
	v_pk_fma_f16 v9, v17, v33, v9
	v_pk_add_f16 v14, v57, v78 neg_lo:[0,1] neg_hi:[0,1]
	v_pk_add_f16 v15, v56, v79 neg_lo:[0,1] neg_hi:[0,1]
	v_pk_add_f16 v16, v55, v80 neg_lo:[0,1] neg_hi:[0,1]
	v_pk_add_f16 v17, v54, v81 neg_lo:[0,1] neg_hi:[0,1]
	v_exp_f16_sdwa v18, v14 dst_sel:WORD_0 dst_unused:UNUSED_PAD src0_sel:WORD_0
	v_exp_f16_sdwa v19, v15 dst_sel:WORD_0 dst_unused:UNUSED_PAD src0_sel:WORD_0
	v_exp_f16_sdwa v20, v16 dst_sel:WORD_0 dst_unused:UNUSED_PAD src0_sel:WORD_0
	v_exp_f16_sdwa v21, v17 dst_sel:WORD_0 dst_unused:UNUSED_PAD src0_sel:WORD_0
	v_exp_f16_sdwa v18, v14 dst_sel:WORD_1 dst_unused:UNUSED_PRESERVE src0_sel:WORD_1
	v_exp_f16_sdwa v19, v15 dst_sel:WORD_1 dst_unused:UNUSED_PRESERVE src0_sel:WORD_1
	v_exp_f16_sdwa v20, v16 dst_sel:WORD_1 dst_unused:UNUSED_PRESERVE src0_sel:WORD_1
	v_exp_f16_sdwa v21, v17 dst_sel:WORD_1 dst_unused:UNUSED_PRESERVE src0_sel:WORD_1
	v_pk_add_f16 v14, v65, v78 neg_lo:[0,1] neg_hi:[0,1]
	v_pk_add_f16 v13, v13, v21
	v_pk_add_f16 v12, v12, v20
	v_pk_add_f16 v11, v11, v19
	v_pk_add_f16 v10, v10, v18
	v_pk_fma_f16 v9, v29, v21, v9
	v_pk_fma_f16 v8, v28, v20, v8
	v_pk_fma_f16 v7, v27, v19, v7
	v_pk_fma_f16 v6, v26, v18, v6
	v_pk_add_f16 v15, v64, v79 neg_lo:[0,1] neg_hi:[0,1]
	v_pk_add_f16 v16, v63, v80 neg_lo:[0,1] neg_hi:[0,1]
	v_pk_add_f16 v17, v62, v81 neg_lo:[0,1] neg_hi:[0,1]
	v_exp_f16_sdwa v18, v14 dst_sel:WORD_0 dst_unused:UNUSED_PAD src0_sel:WORD_0
	v_exp_f16_sdwa v19, v15 dst_sel:WORD_0 dst_unused:UNUSED_PAD src0_sel:WORD_0
	v_exp_f16_sdwa v20, v16 dst_sel:WORD_0 dst_unused:UNUSED_PAD src0_sel:WORD_0
	v_exp_f16_sdwa v21, v17 dst_sel:WORD_0 dst_unused:UNUSED_PAD src0_sel:WORD_0
	v_exp_f16_sdwa v18, v14 dst_sel:WORD_1 dst_unused:UNUSED_PRESERVE src0_sel:WORD_1
	v_exp_f16_sdwa v19, v15 dst_sel:WORD_1 dst_unused:UNUSED_PRESERVE src0_sel:WORD_1
	v_exp_f16_sdwa v20, v16 dst_sel:WORD_1 dst_unused:UNUSED_PRESERVE src0_sel:WORD_1
	v_exp_f16_sdwa v21, v17 dst_sel:WORD_1 dst_unused:UNUSED_PRESERVE src0_sel:WORD_1
	v_pk_add_f16 v14, v46, v78 neg_lo:[0,1] neg_hi:[0,1]
	v_pk_add_f16 v10, v10, v18
	v_pk_add_f16 v11, v11, v19
	v_pk_add_f16 v12, v12, v20
	v_pk_add_f16 v13, v13, v21
	v_pk_fma_f16 v6, v38, v18, v6
	v_pk_fma_f16 v7, v39, v19, v7
	v_pk_fma_f16 v8, v40, v20, v8
	v_pk_fma_f16 v9, v41, v21, v9
	v_pk_add_f16 v15, v47, v79 neg_lo:[0,1] neg_hi:[0,1]
	v_pk_add_f16 v16, v48, v80 neg_lo:[0,1] neg_hi:[0,1]
	v_pk_add_f16 v17, v49, v81 neg_lo:[0,1] neg_hi:[0,1]
	v_exp_f16_sdwa v18, v14 dst_sel:WORD_0 dst_unused:UNUSED_PAD src0_sel:WORD_0
	v_exp_f16_sdwa v19, v15 dst_sel:WORD_0 dst_unused:UNUSED_PAD src0_sel:WORD_0
	v_exp_f16_sdwa v20, v16 dst_sel:WORD_0 dst_unused:UNUSED_PAD src0_sel:WORD_0
	v_exp_f16_sdwa v21, v17 dst_sel:WORD_0 dst_unused:UNUSED_PAD src0_sel:WORD_0
	v_exp_f16_sdwa v18, v14 dst_sel:WORD_1 dst_unused:UNUSED_PRESERVE src0_sel:WORD_1
	v_exp_f16_sdwa v19, v15 dst_sel:WORD_1 dst_unused:UNUSED_PRESERVE src0_sel:WORD_1
	v_exp_f16_sdwa v20, v16 dst_sel:WORD_1 dst_unused:UNUSED_PRESERVE src0_sel:WORD_1
	v_exp_f16_sdwa v21, v17 dst_sel:WORD_1 dst_unused:UNUSED_PRESERVE src0_sel:WORD_1
	v_pk_add_f16 v14, v69, v78 neg_lo:[0,1] neg_hi:[0,1]
	v_pk_add_f16 v13, v13, v21
	v_pk_add_f16 v12, v12, v20
	v_pk_add_f16 v11, v11, v19
	v_pk_add_f16 v10, v10, v18
	v_pk_fma_f16 v9, v61, v21, v9
	v_pk_fma_f16 v8, v60, v20, v8
	v_pk_fma_f16 v7, v59, v19, v7
	v_pk_fma_f16 v6, v58, v18, v6
	v_pk_add_f16 v15, v68, v79 neg_lo:[0,1] neg_hi:[0,1]
	v_pk_add_f16 v16, v67, v80 neg_lo:[0,1] neg_hi:[0,1]
	v_pk_add_f16 v17, v66, v81 neg_lo:[0,1] neg_hi:[0,1]
	v_exp_f16_sdwa v18, v14 dst_sel:WORD_0 dst_unused:UNUSED_PAD src0_sel:WORD_0
	v_exp_f16_sdwa v19, v15 dst_sel:WORD_0 dst_unused:UNUSED_PAD src0_sel:WORD_0
	v_exp_f16_sdwa v20, v16 dst_sel:WORD_0 dst_unused:UNUSED_PAD src0_sel:WORD_0
	v_exp_f16_sdwa v21, v17 dst_sel:WORD_0 dst_unused:UNUSED_PAD src0_sel:WORD_0
	v_exp_f16_sdwa v18, v14 dst_sel:WORD_1 dst_unused:UNUSED_PRESERVE src0_sel:WORD_1
	v_exp_f16_sdwa v19, v15 dst_sel:WORD_1 dst_unused:UNUSED_PRESERVE src0_sel:WORD_1
	v_exp_f16_sdwa v20, v16 dst_sel:WORD_1 dst_unused:UNUSED_PRESERVE src0_sel:WORD_1
	v_exp_f16_sdwa v21, v17 dst_sel:WORD_1 dst_unused:UNUSED_PRESERVE src0_sel:WORD_1
	v_pk_add_f16 v10, v10, v18
	v_pk_add_f16 v11, v11, v19
	v_pk_add_f16 v12, v12, v20
	v_pk_add_f16 v13, v13, v21
	v_pk_fma_f16 v14, v70, v18, v6
	v_pk_fma_f16 v15, v71, v19, v7
	v_pk_fma_f16 v16, v72, v20, v8
	v_pk_fma_f16 v17, v73, v21, v9
	v_pk_add_f16 v6, v77, v78 neg_lo:[0,1] neg_hi:[0,1]
	v_pk_add_f16 v7, v76, v79 neg_lo:[0,1] neg_hi:[0,1]
	v_pk_add_f16 v8, v75, v80 neg_lo:[0,1] neg_hi:[0,1]
	v_pk_add_f16 v9, v74, v81 neg_lo:[0,1] neg_hi:[0,1]
	v_exp_f16_sdwa v18, v6 dst_sel:WORD_0 dst_unused:UNUSED_PAD src0_sel:WORD_0
	v_exp_f16_sdwa v19, v7 dst_sel:WORD_0 dst_unused:UNUSED_PAD src0_sel:WORD_0
	v_exp_f16_sdwa v20, v8 dst_sel:WORD_0 dst_unused:UNUSED_PAD src0_sel:WORD_0
	v_exp_f16_sdwa v21, v9 dst_sel:WORD_0 dst_unused:UNUSED_PAD src0_sel:WORD_0
	v_exp_f16_sdwa v18, v6 dst_sel:WORD_1 dst_unused:UNUSED_PRESERVE src0_sel:WORD_1
	v_exp_f16_sdwa v19, v7 dst_sel:WORD_1 dst_unused:UNUSED_PRESERVE src0_sel:WORD_1
	v_exp_f16_sdwa v20, v8 dst_sel:WORD_1 dst_unused:UNUSED_PRESERVE src0_sel:WORD_1
	v_exp_f16_sdwa v21, v9 dst_sel:WORD_1 dst_unused:UNUSED_PRESERVE src0_sel:WORD_1
	s_nop 0
	v_pk_add_f16 v9, v13, v21
	v_pk_add_f16 v8, v12, v20
	v_pk_add_f16 v7, v11, v19
	v_pk_add_f16 v6, v10, v18
	v_pk_fma_f16 v13, v93, v21, v17
	v_pk_fma_f16 v12, v92, v20, v16
	v_pk_fma_f16 v11, v91, v19, v15
	v_pk_fma_f16 v10, v90, v18, v14
	v_pk_add_f16 v18, v50, v78 neg_lo:[0,1] neg_hi:[0,1]
	v_pk_add_f16 v19, v51, v79 neg_lo:[0,1] neg_hi:[0,1]
	v_pk_add_f16 v20, v52, v80 neg_lo:[0,1] neg_hi:[0,1]
	v_pk_add_f16 v21, v53, v81 neg_lo:[0,1] neg_hi:[0,1]
	v_exp_f16_sdwa v14, v18 dst_sel:WORD_0 dst_unused:UNUSED_PAD src0_sel:WORD_0
	v_exp_f16_sdwa v17, v19 dst_sel:WORD_0 dst_unused:UNUSED_PAD src0_sel:WORD_0
	v_exp_f16_sdwa v15, v20 dst_sel:WORD_0 dst_unused:UNUSED_PAD src0_sel:WORD_0
	v_exp_f16_sdwa v16, v21 dst_sel:WORD_0 dst_unused:UNUSED_PAD src0_sel:WORD_0
	v_exp_f16_sdwa v14, v18 dst_sel:WORD_1 dst_unused:UNUSED_PRESERVE src0_sel:WORD_1
	v_exp_f16_sdwa v17, v19 dst_sel:WORD_1 dst_unused:UNUSED_PRESERVE src0_sel:WORD_1
	v_exp_f16_sdwa v15, v20 dst_sel:WORD_1 dst_unused:UNUSED_PRESERVE src0_sel:WORD_1
	v_exp_f16_sdwa v16, v21 dst_sel:WORD_1 dst_unused:UNUSED_PRESERVE src0_sel:WORD_1
	s_nop 0

.LBB5_4:
	v_add_u32_e32 v182, s30, v161
	v_add_u32_e32 v181, -1, v182
	v_or_b32_e32 v2, v181, v164
	v_add_u32_e32 v180, 0x18400, v171
	v_cmp_gt_u32_e64 s[0:1], 64, v2
	s_mov_b64 s[4:5], -1
	s_and_b64 vcc, exec, s[24:25]
	s_cbranch_vccz .LBB5_42
	s_load_dwordx2 s[4:5], s[22:23], 0x20
	s_waitcnt lgkmcnt(0)
	s_load_dwordx2 s[26:27], s[4:5], 0x0
	s_load_dword s31, s[4:5], 0x8
	v_cmp_lt_u32_e64 s[64:65], 0, v182
	v_cmp_gt_u32_e64 s[66:67], 63, v182
	v_cmp_lt_u32_e64 s[68:69], 0, v162
	v_cmp_gt_u32_e64 s[70:71], 60, v162
	buffer_load_dwordx4 v[186:189], v180, s[16:19], 0 offen
	s_and_b64 s[72:73], s[68:69], s[64:65]
	s_and_b64 s[74:75], s[68:69], s[66:67]
	s_and_b64 s[76:77], s[70:71], s[64:65]
	s_and_b64 s[78:79], s[70:71], s[66:67]
	v_mov_b32_e32 v110, v172
	v_mov_b32_e32 v111, v174
	v_mov_b32_e32 v112, v176
	v_mov_b32_e32 v113, v178
	v_mov_b32_e32 v70, v173
	v_mov_b32_e32 v71, v175
	v_mov_b32_e32 v72, v177
	v_mov_b32_e32 v73, v179
	v_mov_b32_e32 v126, v172
	v_mov_b32_e32 v127, v174
	v_mov_b32_e32 v128, v176
	v_mov_b32_e32 v129, v178
	v_mov_b32_e32 v98, v173
	v_mov_b32_e32 v99, v175
	v_mov_b32_e32 v100, v177
	v_mov_b32_e32 v101, v179
	v_mov_b32_e32 v134, v172
	v_mov_b32_e32 v135, v174
	v_mov_b32_e32 v136, v176
	v_mov_b32_e32 v137, v178
	v_mov_b32_e32 v114, v173
	v_mov_b32_e32 v115, v175
	v_mov_b32_e32 v116, v177
	v_mov_b32_e32 v117, v179
	v_mov_b32_e32 v82, v172
	v_mov_b32_e32 v83, v174
	v_mov_b32_e32 v84, v176
	v_mov_b32_e32 v85, v178
	v_mov_b32_e32 v42, v173
	v_mov_b32_e32 v43, v175
	v_mov_b32_e32 v44, v177
	v_mov_b32_e32 v45, v179
	v_mov_b32_e32 v122, v172
	v_mov_b32_e32 v123, v174
	v_mov_b32_e32 v124, v176
	v_mov_b32_e32 v125, v178
	v_mov_b32_e32 v86, v173
	v_mov_b32_e32 v87, v175
	v_mov_b32_e32 v88, v177
	v_mov_b32_e32 v89, v179
	v_mov_b32_e32 v50, v172
	v_mov_b32_e32 v51, v174
	v_mov_b32_e32 v52, v176
	v_mov_b32_e32 v53, v178
	v_mov_b32_e32 v22, v173
	v_mov_b32_e32 v23, v175
	v_mov_b32_e32 v24, v177
	v_mov_b32_e32 v25, v179
	v_mov_b32_e32 v94, v172
	v_mov_b32_e32 v95, v174
	v_mov_b32_e32 v96, v176
	v_mov_b32_e32 v97, v178
	v_mov_b32_e32 v46, v173
	v_mov_b32_e32 v47, v175
	v_mov_b32_e32 v48, v177
	v_mov_b32_e32 v49, v179
	v_mov_b32_e32 v18, v172
	v_mov_b32_e32 v19, v174
	v_mov_b32_e32 v20, v176
	v_mov_b32_e32 v21, v178
	v_mov_b32_e32 v6, v173
	v_mov_b32_e32 v7, v175
	v_mov_b32_e32 v8, v177
	v_mov_b32_e32 v9, v179
	v_mov_b32_e32 v54, v172
	v_mov_b32_e32 v55, v174
	v_mov_b32_e32 v56, v176
	v_mov_b32_e32 v57, v178
	v_mov_b32_e32 v14, v173
	v_mov_b32_e32 v15, v175
	v_mov_b32_e32 v16, v177
	v_mov_b32_e32 v17, v179
	v_mov_b32_e32 v74, v172
	v_mov_b32_e32 v75, v174
	v_mov_b32_e32 v76, v176
	v_mov_b32_e32 v77, v178
	v_mov_b32_e32 v26, v173
	v_mov_b32_e32 v27, v175
	v_mov_b32_e32 v28, v177
	v_mov_b32_e32 v29, v179
	v_mov_b32_e32 v118, v172
	v_mov_b32_e32 v119, v174
	v_mov_b32_e32 v120, v176
	v_mov_b32_e32 v121, v178
	v_mov_b32_e32 v58, v173
	v_mov_b32_e32 v59, v175
	v_mov_b32_e32 v60, v177
	v_mov_b32_e32 v61, v179
	v_mov_b32_e32 v130, v172
	v_mov_b32_e32 v131, v174
	v_mov_b32_e32 v132, v176
	v_mov_b32_e32 v133, v178
	v_mov_b32_e32 v78, v173
	v_mov_b32_e32 v79, v175
	v_mov_b32_e32 v80, v177
	v_mov_b32_e32 v81, v179
	v_mov_b32_e32 v138, v172
	v_mov_b32_e32 v139, v174
	v_mov_b32_e32 v140, v176
	v_mov_b32_e32 v141, v178
	v_mov_b32_e32 v90, v173
	v_mov_b32_e32 v91, v175
	v_mov_b32_e32 v92, v177
	v_mov_b32_e32 v93, v179
	v_mov_b32_e32 v142, v172
	v_mov_b32_e32 v143, v174
	v_mov_b32_e32 v144, v176
	v_mov_b32_e32 v145, v178
	v_mov_b32_e32 v2, v173
	v_mov_b32_e32 v3, v175
	v_mov_b32_e32 v4, v177
	v_mov_b32_e32 v5, v179
	v_add_u32_e32 v224, 0xfffe7c00, v180
	v_add_u32_e32 v225, 0xfffe8000, v180
	s_mov_b64 exec, s[72:73]
	buffer_load_dwordx4 v[110:113], v224, s[16:19], 0 offen
	buffer_load_dwordx4 v[70:73], v224, s[16:19], 0 offen offset:512
	s_mov_b64 exec, -1
	s_mov_b64 exec, s[68:69]
	buffer_load_dwordx4 v[126:129], v225, s[16:19], 0 offen offset:512
	buffer_load_dwordx4 v[98:101], v225, s[16:19], 0 offen offset:1024
	s_mov_b64 exec, -1
	s_mov_b64 exec, s[74:75]
	buffer_load_dwordx4 v[134:137], v225, s[16:19], 0 offen offset:2048
	buffer_load_dwordx4 v[114:117], v225, s[16:19], 0 offen offset:2560
	s_mov_b64 exec, -1
	v_add_u32_e32 v224, 0xfffffc00, v180
	s_mov_b64 exec, s[64:65]
	buffer_load_dwordx4 v[82:85], v224, s[16:19], 0 offen
	buffer_load_dwordx4 v[42:45], v224, s[16:19], 0 offen offset:512
	s_mov_b64 exec, -1
	buffer_load_dwordx4 v[106:109], v180, s[16:19], 0 offen offset:512
	buffer_load_dwordx4 v[62:65], v180, s[16:19], 0 offen offset:1024
	s_mov_b64 exec, s[66:67]
	buffer_load_dwordx4 v[122:125], v180, s[16:19], 0 offen offset:2048
	buffer_load_dwordx4 v[86:89], v180, s[16:19], 0 offen offset:2560
	s_mov_b64 exec, -1
	v_add_u32_e32 v224, 0x17c00, v180
	v_add_u32_e32 v225, 0x18000, v180
	s_mov_b64 exec, s[64:65]
	buffer_load_dwordx4 v[50:53], v224, s[16:19], 0 offen
	buffer_load_dwordx4 v[22:25], v224, s[16:19], 0 offen offset:512
	s_mov_b64 exec, -1
	buffer_load_dwordx4 v[66:69], v225, s[16:19], 0 offen offset:512
	buffer_load_dwordx4 v[30:33], v225, s[16:19], 0 offen offset:1024
	s_mov_b64 exec, s[66:67]
	buffer_load_dwordx4 v[94:97], v225, s[16:19], 0 offen offset:2048
	buffer_load_dwordx4 v[46:49], v225, s[16:19], 0 offen offset:2560
	s_mov_b64 exec, -1
	v_add_u32_e32 v224, 0x18000, v180
	buffer_load_dwordx4 v[154:157], v224, s[16:19], 0 offen
	v_add_u32_e32 v225, 0x30000, v180
	buffer_load_dwordx4 v[150:153], v225, s[16:19], 0 offen
	v_add_u32_e32 v224, 0x48000, v180
	buffer_load_dwordx4 v[146:149], v224, s[16:19], 0 offen
	v_add_u32_e32 v224, 0x2fc00, v180
	v_add_u32_e32 v225, 0x30000, v180
	v_add_u32_e32 v226, 0x47c00, v180
	v_add_u32_e32 v227, 0x48000, v180
	v_add_u32_e32 v228, 0x5fc00, v180
	v_add_u32_e32 v229, 0x60000, v180
	s_waitcnt lgkmcnt(0)
	v_cvt_f16_f32_e32 v183, s27
	v_cvt_f16_f32_e32 v185, s26
	v_cvt_f16_f32_e32 v184, s31
	s_mov_b64 s[4:5], 0
	s_waitcnt vmcnt(3)
	v_pk_mul_f16 v193, v185, v189 op_sel_hi:[0,1]
	v_pk_mul_f16 v197, v183, v189 op_sel_hi:[0,1]
	v_pk_mul_f16 v201, v184, v189 op_sel_hi:[0,1]
	v_pk_mul_f16 v190, v185, v186 op_sel_hi:[0,1]
	v_pk_mul_f16 v191, v185, v187 op_sel_hi:[0,1]
	v_pk_mul_f16 v192, v185, v188 op_sel_hi:[0,1]
	v_pk_mul_f16 v194, v183, v186 op_sel_hi:[0,1]
	s_mov_b64 exec, s[64:65]
	buffer_load_dwordx4 v[18:21], v224, s[16:19], 0 offen
	buffer_load_dwordx4 v[6:9], v224, s[16:19], 0 offen offset:512
	s_mov_b64 exec, -1
	v_pk_mul_f16 v195, v183, v187 op_sel_hi:[0,1]
	v_pk_mul_f16 v196, v183, v188 op_sel_hi:[0,1]
	v_pk_mul_f16 v198, v184, v186 op_sel_hi:[0,1]
	v_pk_mul_f16 v199, v184, v187 op_sel_hi:[0,1]
	v_pk_mul_f16 v200, v184, v188 op_sel_hi:[0,1]
	v_pk_fma_f16 v113, v113, v189, v193
	v_pk_fma_f16 v129, v129, v189, v197
	v_pk_fma_f16 v137, v137, v189, v201
	v_pk_fma_f16 v202, v85, v189, v193
	v_pk_fma_f16 v206, v109, v189, v197
	v_pk_fma_f16 v210, v125, v189, v201
	v_pk_fma_f16 v193, v53, v189, v193
	v_pk_fma_f16 v197, v69, v189, v197
	buffer_load_dwordx4 v[34:37], v225, s[16:19], 0 offen offset:512
	buffer_load_dwordx4 v[10:13], v225, s[16:19], 0 offen offset:1024
	v_pk_fma_f16 v189, v97, v189, v201
	v_pk_maximum3_f16 v201, v113, v129, v137
	v_pk_fma_f16 v112, v112, v188, v192
	v_pk_fma_f16 v111, v111, v187, v191
	v_pk_fma_f16 v110, v110, v186, v190
	v_pk_fma_f16 v128, v128, v188, v196
	v_pk_fma_f16 v127, v127, v187, v195
	v_pk_fma_f16 v126, v126, v186, v194
	v_pk_fma_f16 v136, v136, v188, v200
	v_pk_fma_f16 v135, v135, v187, v199
	v_pk_fma_f16 v134, v134, v186, v198
	v_pk_fma_f16 v203, v84, v188, v192
	v_pk_fma_f16 v204, v83, v187, v191
	v_pk_fma_f16 v205, v82, v186, v190
	v_pk_fma_f16 v207, v108, v188, v196
	v_pk_fma_f16 v208, v107, v187, v195
	s_mov_b64 exec, s[66:67]
	buffer_load_dwordx4 v[54:57], v225, s[16:19], 0 offen offset:2048
	buffer_load_dwordx4 v[14:17], v225, s[16:19], 0 offen offset:2560
	s_mov_b64 exec, -1
	v_pk_fma_f16 v209, v106, v186, v194
	v_pk_fma_f16 v211, v124, v188, v200
	v_pk_fma_f16 v212, v123, v187, v199
	v_pk_fma_f16 v213, v122, v186, v198
	v_pk_fma_f16 v192, v52, v188, v192
	v_pk_fma_f16 v191, v51, v187, v191
	v_pk_fma_f16 v190, v50, v186, v190
	v_pk_fma_f16 v196, v68, v188, v196
	v_pk_fma_f16 v195, v67, v187, v195
	v_pk_fma_f16 v194, v66, v186, v194
	v_pk_fma_f16 v188, v96, v188, v200
	v_pk_fma_f16 v187, v95, v187, v199
	v_pk_fma_f16 v186, v94, v186, v198
	v_pk_maximum3_f16 v198, v110, v126, v134
	v_pk_maximum3_f16 v199, v111, v127, v135
	v_pk_maximum3_f16 v200, v112, v128, v136
	v_pk_maximum3_f16 v217, v202, v206, v210
	v_pk_maximum3_f16 v221, v193, v197, v189
	v_pk_maximum3_f16 v214, v205, v209, v213
	v_pk_maximum3_f16 v215, v204, v208, v212
	v_pk_maximum3_f16 v216, v203, v207, v211
	v_pk_maximum3_f16 v218, v190, v194, v186
	v_pk_maximum3_f16 v219, v191, v195, v187
	v_pk_maximum3_f16 v201, v201, v217, v221
	v_pk_maximum3_f16 v220, v192, v196, v188
	v_pk_maximum3_f16 v198, v198, v214, v218
	v_pk_maximum3_f16 v199, v199, v215, v219
	v_pk_maximum3_f16 v200, v200, v216, v220
	v_pk_add_f16 v113, v113, v201 neg_lo:[0,1] neg_hi:[0,1]
	s_mov_b64 exec, s[64:65]
	buffer_load_dwordx4 v[74:77], v226, s[16:19], 0 offen
	buffer_load_dwordx4 v[26:29], v226, s[16:19], 0 offen offset:512
	s_mov_b64 exec, -1
	v_pk_add_f16 v110, v110, v198 neg_lo:[0,1] neg_hi:[0,1]
	v_pk_add_f16 v111, v111, v199 neg_lo:[0,1] neg_hi:[0,1]
	v_pk_add_f16 v112, v112, v200 neg_lo:[0,1] neg_hi:[0,1]
	v_pk_add_f16 v126, v126, v198 neg_lo:[0,1] neg_hi:[0,1]
	v_exp_f16_sdwa v214, v110 dst_sel:WORD_0 dst_unused:UNUSED_PAD src0_sel:WORD_0
	v_exp_f16_sdwa v215, v111 dst_sel:WORD_0 dst_unused:UNUSED_PAD src0_sel:WORD_0
	v_exp_f16_sdwa v216, v112 dst_sel:WORD_0 dst_unused:UNUSED_PAD src0_sel:WORD_0
	v_exp_f16_sdwa v217, v113 dst_sel:WORD_0 dst_unused:UNUSED_PAD src0_sel:WORD_0
	v_exp_f16_sdwa v214, v110 dst_sel:WORD_1 dst_unused:UNUSED_PRESERVE src0_sel:WORD_1
	v_exp_f16_sdwa v215, v111 dst_sel:WORD_1 dst_unused:UNUSED_PRESERVE src0_sel:WORD_1
	v_exp_f16_sdwa v216, v112 dst_sel:WORD_1 dst_unused:UNUSED_PRESERVE src0_sel:WORD_1
	v_exp_f16_sdwa v217, v113 dst_sel:WORD_1 dst_unused:UNUSED_PRESERVE src0_sel:WORD_1
	v_pk_add_f16 v127, v127, v199 neg_lo:[0,1] neg_hi:[0,1]
	v_pk_add_f16 v113, v214, 0
	v_pk_fma_f16 v73, v73, v217, 0
	v_pk_add_f16 v110, v217, 0
	v_pk_add_f16 v111, v216, 0
	v_pk_add_f16 v112, v215, 0
	v_pk_fma_f16 v72, v72, v216, 0
	v_pk_fma_f16 v71, v71, v215, 0
	v_pk_fma_f16 v70, v70, v214, 0
	v_pk_add_f16 v128, v128, v200 neg_lo:[0,1] neg_hi:[0,1]
	buffer_load_dwordx4 v[102:105], v227, s[16:19], 0 offen offset:512
	buffer_load_dwordx4 v[38:41], v227, s[16:19], 0 offen offset:1024
	v_pk_add_f16 v129, v129, v201 neg_lo:[0,1] neg_hi:[0,1]
	v_exp_f16_sdwa v214, v126 dst_sel:WORD_0 dst_unused:UNUSED_PAD src0_sel:WORD_0
	v_exp_f16_sdwa v215, v127 dst_sel:WORD_0 dst_unused:UNUSED_PAD src0_sel:WORD_0
	v_exp_f16_sdwa v216, v128 dst_sel:WORD_0 dst_unused:UNUSED_PAD src0_sel:WORD_0
	v_exp_f16_sdwa v217, v129 dst_sel:WORD_0 dst_unused:UNUSED_PAD src0_sel:WORD_0
	v_exp_f16_sdwa v214, v126 dst_sel:WORD_1 dst_unused:UNUSED_PRESERVE src0_sel:WORD_1
	v_exp_f16_sdwa v215, v127 dst_sel:WORD_1 dst_unused:UNUSED_PRESERVE src0_sel:WORD_1
	v_exp_f16_sdwa v216, v128 dst_sel:WORD_1 dst_unused:UNUSED_PRESERVE src0_sel:WORD_1
	v_exp_f16_sdwa v217, v129 dst_sel:WORD_1 dst_unused:UNUSED_PRESERVE src0_sel:WORD_1
	v_pk_add_f16 v113, v113, v214
	v_pk_fma_f16 v73, v101, v217, v73
	v_pk_add_f16 v101, v137, v201 neg_lo:[0,1] neg_hi:[0,1]
	v_pk_add_f16 v112, v112, v215
	v_pk_add_f16 v111, v111, v216
	v_pk_add_f16 v110, v110, v217
	v_pk_fma_f16 v70, v98, v214, v70
	v_pk_fma_f16 v71, v99, v215, v71
	v_pk_fma_f16 v72, v100, v216, v72
	v_pk_add_f16 v98, v134, v198 neg_lo:[0,1] neg_hi:[0,1]
	v_pk_add_f16 v99, v135, v199 neg_lo:[0,1] neg_hi:[0,1]
	v_pk_add_f16 v100, v136, v200 neg_lo:[0,1] neg_hi:[0,1]
	v_exp_f16_sdwa v126, v98 dst_sel:WORD_0 dst_unused:UNUSED_PAD src0_sel:WORD_0
	v_exp_f16_sdwa v127, v99 dst_sel:WORD_0 dst_unused:UNUSED_PAD src0_sel:WORD_0
	v_exp_f16_sdwa v128, v100 dst_sel:WORD_0 dst_unused:UNUSED_PAD src0_sel:WORD_0
	v_exp_f16_sdwa v129, v101 dst_sel:WORD_0 dst_unused:UNUSED_PAD src0_sel:WORD_0
	v_exp_f16_sdwa v126, v98 dst_sel:WORD_1 dst_unused:UNUSED_PRESERVE src0_sel:WORD_1
	v_exp_f16_sdwa v127, v99 dst_sel:WORD_1 dst_unused:UNUSED_PRESERVE src0_sel:WORD_1
	v_exp_f16_sdwa v128, v100 dst_sel:WORD_1 dst_unused:UNUSED_PRESERVE src0_sel:WORD_1
	v_exp_f16_sdwa v129, v101 dst_sel:WORD_1 dst_unused:UNUSED_PRESERVE src0_sel:WORD_1
	v_pk_add_f16 v101, v113, v126
	v_pk_add_f16 v98, v110, v129
	s_mov_b64 exec, s[66:67]
	buffer_load_dwordx4 v[118:121], v227, s[16:19], 0 offen offset:2048
	buffer_load_dwordx4 v[58:61], v227, s[16:19], 0 offen offset:2560
	s_mov_b64 exec, -1
	v_pk_add_f16 v99, v111, v128
	v_pk_add_f16 v100, v112, v127
	v_pk_fma_f16 v73, v117, v129, v73
	v_pk_fma_f16 v72, v116, v128, v72
	v_pk_fma_f16 v71, v115, v127, v71
	v_pk_fma_f16 v70, v114, v126, v70
	v_pk_add_f16 v110, v205, v198 neg_lo:[0,1] neg_hi:[0,1]
	v_pk_add_f16 v111, v204, v199 neg_lo:[0,1] neg_hi:[0,1]
	v_pk_add_f16 v112, v203, v200 neg_lo:[0,1] neg_hi:[0,1]
	v_pk_add_f16 v113, v202, v201 neg_lo:[0,1] neg_hi:[0,1]
	v_exp_f16_sdwa v114, v110 dst_sel:WORD_0 dst_unused:UNUSED_PAD src0_sel:WORD_0
	v_exp_f16_sdwa v115, v111 dst_sel:WORD_0 dst_unused:UNUSED_PAD src0_sel:WORD_0
	v_exp_f16_sdwa v116, v112 dst_sel:WORD_0 dst_unused:UNUSED_PAD src0_sel:WORD_0
	v_exp_f16_sdwa v117, v113 dst_sel:WORD_0 dst_unused:UNUSED_PAD src0_sel:WORD_0
	v_exp_f16_sdwa v114, v110 dst_sel:WORD_1 dst_unused:UNUSED_PRESERVE src0_sel:WORD_1
	v_exp_f16_sdwa v115, v111 dst_sel:WORD_1 dst_unused:UNUSED_PRESERVE src0_sel:WORD_1
	v_exp_f16_sdwa v116, v112 dst_sel:WORD_1 dst_unused:UNUSED_PRESERVE src0_sel:WORD_1
	v_exp_f16_sdwa v117, v113 dst_sel:WORD_1 dst_unused:UNUSED_PRESERVE src0_sel:WORD_1
	v_pk_add_f16 v110, v209, v198 neg_lo:[0,1] neg_hi:[0,1]
	v_pk_add_f16 v101, v101, v114
	v_pk_add_f16 v100, v100, v115
	v_pk_add_f16 v99, v99, v116
	s_mov_b64 exec, s[76:77]
	buffer_load_dwordx4 v[130:133], v228, s[16:19], 0 offen
	buffer_load_dwordx4 v[78:81], v228, s[16:19], 0 offen offset:512
	s_mov_b64 exec, -1
	v_pk_add_f16 v98, v98, v117
	v_pk_fma_f16 v70, v42, v114, v70
	v_pk_fma_f16 v71, v43, v115, v71
	v_pk_fma_f16 v72, v44, v116, v72
	v_pk_fma_f16 v73, v45, v117, v73
	v_pk_add_f16 v111, v208, v199 neg_lo:[0,1] neg_hi:[0,1]
	v_pk_add_f16 v112, v207, v200 neg_lo:[0,1] neg_hi:[0,1]
	v_pk_add_f16 v113, v206, v201 neg_lo:[0,1] neg_hi:[0,1]
	v_exp_f16_sdwa v114, v110 dst_sel:WORD_0 dst_unused:UNUSED_PAD src0_sel:WORD_0
	v_exp_f16_sdwa v115, v111 dst_sel:WORD_0 dst_unused:UNUSED_PAD src0_sel:WORD_0
	v_exp_f16_sdwa v116, v112 dst_sel:WORD_0 dst_unused:UNUSED_PAD src0_sel:WORD_0
	v_exp_f16_sdwa v117, v113 dst_sel:WORD_0 dst_unused:UNUSED_PAD src0_sel:WORD_0
	v_exp_f16_sdwa v114, v110 dst_sel:WORD_1 dst_unused:UNUSED_PRESERVE src0_sel:WORD_1
	v_exp_f16_sdwa v115, v111 dst_sel:WORD_1 dst_unused:UNUSED_PRESERVE src0_sel:WORD_1
	v_exp_f16_sdwa v116, v112 dst_sel:WORD_1 dst_unused:UNUSED_PRESERVE src0_sel:WORD_1
	v_exp_f16_sdwa v117, v113 dst_sel:WORD_1 dst_unused:UNUSED_PRESERVE src0_sel:WORD_1
	v_pk_add_f16 v110, v213, v198 neg_lo:[0,1] neg_hi:[0,1]
	v_pk_add_f16 v101, v101, v114
	v_pk_add_f16 v98, v98, v117
	v_pk_add_f16 v99, v99, v116
	v_pk_add_f16 v100, v100, v115
	v_pk_fma_f16 v73, v65, v117, v73
	v_pk_fma_f16 v72, v64, v116, v72
	s_mov_b64 exec, s[70:71]
	buffer_load_dwordx4 v[138:141], v229, s[16:19], 0 offen offset:512
	buffer_load_dwordx4 v[90:93], v229, s[16:19], 0 offen offset:1024
	s_mov_b64 exec, -1
	v_pk_fma_f16 v71, v63, v115, v71
	v_pk_fma_f16 v70, v62, v114, v70
	v_pk_add_f16 v111, v212, v199 neg_lo:[0,1] neg_hi:[0,1]
	v_pk_add_f16 v112, v211, v200 neg_lo:[0,1] neg_hi:[0,1]
	v_pk_add_f16 v113, v210, v201 neg_lo:[0,1] neg_hi:[0,1]
	v_exp_f16_sdwa v114, v110 dst_sel:WORD_0 dst_unused:UNUSED_PAD src0_sel:WORD_0
	v_exp_f16_sdwa v115, v111 dst_sel:WORD_0 dst_unused:UNUSED_PAD src0_sel:WORD_0
	v_exp_f16_sdwa v116, v112 dst_sel:WORD_0 dst_unused:UNUSED_PAD src0_sel:WORD_0
	v_exp_f16_sdwa v117, v113 dst_sel:WORD_0 dst_unused:UNUSED_PAD src0_sel:WORD_0
	v_exp_f16_sdwa v114, v110 dst_sel:WORD_1 dst_unused:UNUSED_PRESERVE src0_sel:WORD_1
	v_exp_f16_sdwa v115, v111 dst_sel:WORD_1 dst_unused:UNUSED_PRESERVE src0_sel:WORD_1
	v_exp_f16_sdwa v116, v112 dst_sel:WORD_1 dst_unused:UNUSED_PRESERVE src0_sel:WORD_1
	v_exp_f16_sdwa v117, v113 dst_sel:WORD_1 dst_unused:UNUSED_PRESERVE src0_sel:WORD_1
	v_pk_add_f16 v110, v190, v198 neg_lo:[0,1] neg_hi:[0,1]
	v_pk_add_f16 v101, v101, v114
	v_pk_add_f16 v100, v100, v115
	v_pk_add_f16 v99, v99, v116
	v_pk_add_f16 v98, v98, v117
	v_pk_fma_f16 v70, v86, v114, v70
	v_pk_fma_f16 v71, v87, v115, v71
	v_pk_fma_f16 v72, v88, v116, v72
	v_pk_fma_f16 v73, v89, v117, v73
	s_mov_b64 exec, s[78:79]
	buffer_load_dwordx4 v[142:145], v229, s[16:19], 0 offen offset:2048
	buffer_load_dwordx4 v[2:5], v229, s[16:19], 0 offen offset:2560
	s_mov_b64 exec, -1
	v_pk_add_f16 v111, v191, v199 neg_lo:[0,1] neg_hi:[0,1]
	v_pk_add_f16 v112, v192, v200 neg_lo:[0,1] neg_hi:[0,1]
	v_pk_add_f16 v113, v193, v201 neg_lo:[0,1] neg_hi:[0,1]
	v_exp_f16_sdwa v114, v110 dst_sel:WORD_0 dst_unused:UNUSED_PAD src0_sel:WORD_0
	v_exp_f16_sdwa v115, v111 dst_sel:WORD_0 dst_unused:UNUSED_PAD src0_sel:WORD_0
	v_exp_f16_sdwa v116, v112 dst_sel:WORD_0 dst_unused:UNUSED_PAD src0_sel:WORD_0
	v_exp_f16_sdwa v117, v113 dst_sel:WORD_0 dst_unused:UNUSED_PAD src0_sel:WORD_0
	v_exp_f16_sdwa v114, v110 dst_sel:WORD_1 dst_unused:UNUSED_PRESERVE src0_sel:WORD_1
	v_exp_f16_sdwa v115, v111 dst_sel:WORD_1 dst_unused:UNUSED_PRESERVE src0_sel:WORD_1
	v_exp_f16_sdwa v116, v112 dst_sel:WORD_1 dst_unused:UNUSED_PRESERVE src0_sel:WORD_1
	v_exp_f16_sdwa v117, v113 dst_sel:WORD_1 dst_unused:UNUSED_PRESERVE src0_sel:WORD_1
	v_pk_add_f16 v110, v194, v198 neg_lo:[0,1] neg_hi:[0,1]
	v_pk_add_f16 v101, v101, v114
	v_pk_add_f16 v98, v98, v117
	v_pk_add_f16 v99, v99, v116
	v_pk_add_f16 v100, v100, v115
	v_pk_fma_f16 v73, v25, v117, v73
	v_pk_fma_f16 v72, v24, v116, v72
	v_pk_fma_f16 v71, v23, v115, v71
	v_pk_fma_f16 v70, v22, v114, v70
	v_pk_add_f16 v111, v195, v199 neg_lo:[0,1] neg_hi:[0,1]
	v_pk_add_f16 v112, v196, v200 neg_lo:[0,1] neg_hi:[0,1]
	v_pk_add_f16 v113, v197, v201 neg_lo:[0,1] neg_hi:[0,1]
	v_exp_f16_sdwa v114, v110 dst_sel:WORD_0 dst_unused:UNUSED_PAD src0_sel:WORD_0
	v_exp_f16_sdwa v115, v111 dst_sel:WORD_0 dst_unused:UNUSED_PAD src0_sel:WORD_0
	v_exp_f16_sdwa v116, v112 dst_sel:WORD_0 dst_unused:UNUSED_PAD src0_sel:WORD_0
	v_exp_f16_sdwa v117, v113 dst_sel:WORD_0 dst_unused:UNUSED_PAD src0_sel:WORD_0
	v_exp_f16_sdwa v114, v110 dst_sel:WORD_1 dst_unused:UNUSED_PRESERVE src0_sel:WORD_1
	v_exp_f16_sdwa v115, v111 dst_sel:WORD_1 dst_unused:UNUSED_PRESERVE src0_sel:WORD_1
	v_exp_f16_sdwa v116, v112 dst_sel:WORD_1 dst_unused:UNUSED_PRESERVE src0_sel:WORD_1
	v_exp_f16_sdwa v117, v113 dst_sel:WORD_1 dst_unused:UNUSED_PRESERVE src0_sel:WORD_1
	v_pk_add_f16 v110, v186, v198 neg_lo:[0,1] neg_hi:[0,1]
	v_pk_add_f16 v101, v101, v114
	v_pk_add_f16 v100, v100, v115
	v_pk_add_f16 v99, v99, v116
	v_pk_add_f16 v98, v98, v117
	v_pk_fma_f16 v70, v30, v114, v70
	v_pk_fma_f16 v71, v31, v115, v71
	v_pk_fma_f16 v72, v32, v116, v72
	v_pk_fma_f16 v73, v33, v117, v73
	v_pk_add_f16 v111, v187, v199 neg_lo:[0,1] neg_hi:[0,1]
	v_pk_add_f16 v112, v188, v200 neg_lo:[0,1] neg_hi:[0,1]
	v_pk_add_f16 v113, v189, v201 neg_lo:[0,1] neg_hi:[0,1]
	v_exp_f16_sdwa v114, v110 dst_sel:WORD_0 dst_unused:UNUSED_PAD src0_sel:WORD_0
	v_exp_f16_sdwa v115, v111 dst_sel:WORD_0 dst_unused:UNUSED_PAD src0_sel:WORD_0
	v_exp_f16_sdwa v116, v112 dst_sel:WORD_0 dst_unused:UNUSED_PAD src0_sel:WORD_0
	v_exp_f16_sdwa v117, v113 dst_sel:WORD_0 dst_unused:UNUSED_PAD src0_sel:WORD_0
	v_exp_f16_sdwa v114, v110 dst_sel:WORD_1 dst_unused:UNUSED_PRESERVE src0_sel:WORD_1
	v_exp_f16_sdwa v115, v111 dst_sel:WORD_1 dst_unused:UNUSED_PRESERVE src0_sel:WORD_1
	v_exp_f16_sdwa v116, v112 dst_sel:WORD_1 dst_unused:UNUSED_PRESERVE src0_sel:WORD_1
	v_exp_f16_sdwa v117, v113 dst_sel:WORD_1 dst_unused:UNUSED_PRESERVE src0_sel:WORD_1
	v_pk_add_f16 v101, v101, v114
	v_pk_add_f16 v100, v100, v115
	v_rcp_f16_e32 v110, v101
	v_rcp_f16_sdwa v101, v101 dst_sel:DWORD dst_unused:UNUSED_PAD src0_sel:WORD_1
	v_pk_add_f16 v99, v99, v116
	v_rcp_f16_e32 v111, v100
	v_rcp_f16_sdwa v100, v100 dst_sel:DWORD dst_unused:UNUSED_PAD src0_sel:WORD_1
	v_pk_add_f16 v98, v98, v117
	v_rcp_f16_e32 v112, v99
	v_rcp_f16_sdwa v99, v99 dst_sel:DWORD dst_unused:UNUSED_PAD src0_sel:WORD_1
	v_rcp_f16_e32 v113, v98
	v_rcp_f16_sdwa v98, v98 dst_sel:DWORD dst_unused:UNUSED_PAD src0_sel:WORD_1
	v_pk_fma_f16 v70, v46, v114, v70
	v_pack_b32_f16 v101, v110, v101
	v_pk_fma_f16 v71, v47, v115, v71
	v_pk_mul_f16 v110, v70, v101
	v_pack_b32_f16 v70, v111, v100
	v_pk_fma_f16 v72, v48, v116, v72
	v_pk_mul_f16 v111, v71, v70
	v_pack_b32_f16 v70, v112, v99
	v_pk_fma_f16 v73, v49, v117, v73
	v_pk_mul_f16 v112, v72, v70
	v_pack_b32_f16 v70, v113, v98
	v_pk_mul_f16 v113, v73, v70
	s_waitcnt vmcnt(12)
	v_pk_mul_f16 v70, v185, v154 op_sel_hi:[0,1]
	v_pk_mul_f16 v98, v183, v154 op_sel_hi:[0,1]
	v_pk_mul_f16 v114, v184, v154 op_sel_hi:[0,1]
	v_pk_mul_f16 v71, v185, v155 op_sel_hi:[0,1]
	v_pk_mul_f16 v72, v185, v156 op_sel_hi:[0,1]
	v_pk_mul_f16 v73, v185, v157 op_sel_hi:[0,1]
	v_pk_mul_f16 v99, v183, v155 op_sel_hi:[0,1]
	v_pk_mul_f16 v100, v183, v156 op_sel_hi:[0,1]
	v_pk_mul_f16 v101, v183, v157 op_sel_hi:[0,1]
	v_pk_mul_f16 v115, v184, v155 op_sel_hi:[0,1]
	v_pk_mul_f16 v116, v184, v156 op_sel_hi:[0,1]
	v_pk_mul_f16 v117, v184, v157 op_sel_hi:[0,1]
	v_pk_fma_f16 v82, v82, v154, v70
	v_pk_fma_f16 v106, v106, v154, v98
	v_pk_fma_f16 v122, v122, v154, v114
	v_pk_fma_f16 v129, v50, v154, v70
	v_pk_fma_f16 v137, v66, v154, v98
	v_pk_fma_f16 v189, v94, v154, v114
	v_pk_fma_f16 v70, v18, v154, v70
	v_pk_fma_f16 v98, v34, v154, v98
	v_pk_fma_f16 v114, v54, v154, v114
	v_pk_maximum3_f16 v154, v82, v106, v122
	v_pk_fma_f16 v85, v85, v157, v73
	v_pk_fma_f16 v84, v84, v156, v72
	v_pk_fma_f16 v83, v83, v155, v71
	v_pk_fma_f16 v109, v109, v157, v101
	v_pk_fma_f16 v108, v108, v156, v100
	v_pk_fma_f16 v107, v107, v155, v99
	v_pk_fma_f16 v125, v125, v157, v117
	v_pk_fma_f16 v124, v124, v156, v116
	v_pk_fma_f16 v123, v123, v155, v115
	v_pk_fma_f16 v126, v53, v157, v73
	v_pk_fma_f16 v127, v52, v156, v72
	v_pk_fma_f16 v128, v51, v155, v71
	v_pk_fma_f16 v134, v69, v157, v101
	v_pk_fma_f16 v135, v68, v156, v100
	v_pk_fma_f16 v136, v67, v155, v99
	v_pk_fma_f16 v186, v97, v157, v117
	v_pk_fma_f16 v187, v96, v156, v116
	v_pk_fma_f16 v188, v95, v155, v115
	v_pk_fma_f16 v73, v21, v157, v73
	v_pk_fma_f16 v72, v20, v156, v72
	v_pk_fma_f16 v71, v19, v155, v71
	v_pk_fma_f16 v101, v37, v157, v101
	v_pk_fma_f16 v100, v36, v156, v100
	v_pk_fma_f16 v99, v35, v155, v99
	v_pk_fma_f16 v117, v57, v157, v117
	v_pk_fma_f16 v116, v56, v156, v116
	v_pk_fma_f16 v115, v55, v155, v115
	v_pk_maximum3_f16 v155, v83, v107, v123
	v_pk_maximum3_f16 v156, v84, v108, v124
	v_pk_maximum3_f16 v157, v85, v109, v125
	v_pk_maximum3_f16 v190, v129, v137, v189
	v_pk_maximum3_f16 v194, v70, v98, v114
	v_pk_maximum3_f16 v191, v128, v136, v188
	v_pk_maximum3_f16 v192, v127, v135, v187
	v_pk_maximum3_f16 v193, v126, v134, v186
	v_pk_maximum3_f16 v195, v71, v99, v115
	v_pk_maximum3_f16 v196, v72, v100, v116
	v_pk_maximum3_f16 v154, v154, v190, v194
	v_pk_maximum3_f16 v197, v73, v101, v117
	v_pk_maximum3_f16 v155, v155, v191, v195
	v_pk_maximum3_f16 v156, v156, v192, v196
	v_pk_maximum3_f16 v157, v157, v193, v197
	v_pk_add_f16 v82, v82, v154 neg_lo:[0,1] neg_hi:[0,1]
	v_pk_add_f16 v83, v83, v155 neg_lo:[0,1] neg_hi:[0,1]
	v_pk_add_f16 v84, v84, v156 neg_lo:[0,1] neg_hi:[0,1]
	v_pk_add_f16 v85, v85, v157 neg_lo:[0,1] neg_hi:[0,1]
	v_pk_add_f16 v106, v106, v154 neg_lo:[0,1] neg_hi:[0,1]
	v_exp_f16_sdwa v190, v82 dst_sel:WORD_0 dst_unused:UNUSED_PAD src0_sel:WORD_0
	v_exp_f16_sdwa v191, v83 dst_sel:WORD_0 dst_unused:UNUSED_PAD src0_sel:WORD_0
	v_exp_f16_sdwa v192, v84 dst_sel:WORD_0 dst_unused:UNUSED_PAD src0_sel:WORD_0
	v_exp_f16_sdwa v193, v85 dst_sel:WORD_0 dst_unused:UNUSED_PAD src0_sel:WORD_0
	v_exp_f16_sdwa v190, v82 dst_sel:WORD_1 dst_unused:UNUSED_PRESERVE src0_sel:WORD_1
	v_exp_f16_sdwa v191, v83 dst_sel:WORD_1 dst_unused:UNUSED_PRESERVE src0_sel:WORD_1
	v_exp_f16_sdwa v192, v84 dst_sel:WORD_1 dst_unused:UNUSED_PRESERVE src0_sel:WORD_1
	v_exp_f16_sdwa v193, v85 dst_sel:WORD_1 dst_unused:UNUSED_PRESERVE src0_sel:WORD_1
	v_pk_add_f16 v107, v107, v155 neg_lo:[0,1] neg_hi:[0,1]
	v_pk_add_f16 v82, v193, 0
	v_pk_fma_f16 v42, v42, v190, 0
	v_pk_add_f16 v83, v192, 0
	v_pk_add_f16 v84, v191, 0
	v_pk_add_f16 v85, v190, 0
	v_pk_fma_f16 v45, v45, v193, 0
	v_pk_fma_f16 v44, v44, v192, 0
	v_pk_fma_f16 v43, v43, v191, 0
	v_pk_add_f16 v108, v108, v156 neg_lo:[0,1] neg_hi:[0,1]
	v_pk_add_f16 v109, v109, v157 neg_lo:[0,1] neg_hi:[0,1]
	v_pk_add_f16 v70, v70, v154 neg_lo:[0,1] neg_hi:[0,1]
	v_exp_f16_sdwa v190, v106 dst_sel:WORD_0 dst_unused:UNUSED_PAD src0_sel:WORD_0
	v_exp_f16_sdwa v191, v107 dst_sel:WORD_0 dst_unused:UNUSED_PAD src0_sel:WORD_0
	v_exp_f16_sdwa v192, v108 dst_sel:WORD_0 dst_unused:UNUSED_PAD src0_sel:WORD_0
	v_exp_f16_sdwa v193, v109 dst_sel:WORD_0 dst_unused:UNUSED_PAD src0_sel:WORD_0
	v_exp_f16_sdwa v190, v106 dst_sel:WORD_1 dst_unused:UNUSED_PRESERVE src0_sel:WORD_1
	v_exp_f16_sdwa v191, v107 dst_sel:WORD_1 dst_unused:UNUSED_PRESERVE src0_sel:WORD_1
	v_exp_f16_sdwa v192, v108 dst_sel:WORD_1 dst_unused:UNUSED_PRESERVE src0_sel:WORD_1
	v_exp_f16_sdwa v193, v109 dst_sel:WORD_1 dst_unused:UNUSED_PRESERVE src0_sel:WORD_1
	v_pk_add_f16 v71, v71, v155 neg_lo:[0,1] neg_hi:[0,1]
	v_pk_add_f16 v82, v82, v193
	v_pk_fma_f16 v42, v62, v190, v42
	v_pk_add_f16 v62, v122, v154 neg_lo:[0,1] neg_hi:[0,1]
	v_pk_add_f16 v85, v85, v190
	v_pk_add_f16 v84, v84, v191
	v_pk_add_f16 v83, v83, v192
	v_pk_fma_f16 v43, v63, v191, v43
	v_pk_fma_f16 v44, v64, v192, v44
	v_pk_fma_f16 v45, v65, v193, v45
	v_pk_add_f16 v63, v123, v155 neg_lo:[0,1] neg_hi:[0,1]
	v_pk_add_f16 v64, v124, v156 neg_lo:[0,1] neg_hi:[0,1]
	v_pk_add_f16 v65, v125, v157 neg_lo:[0,1] neg_hi:[0,1]
	v_pk_add_f16 v72, v72, v156 neg_lo:[0,1] neg_hi:[0,1]
	v_exp_f16_sdwa v106, v62 dst_sel:WORD_0 dst_unused:UNUSED_PAD src0_sel:WORD_0
	v_exp_f16_sdwa v107, v63 dst_sel:WORD_0 dst_unused:UNUSED_PAD src0_sel:WORD_0
	v_exp_f16_sdwa v108, v64 dst_sel:WORD_0 dst_unused:UNUSED_PAD src0_sel:WORD_0
	v_exp_f16_sdwa v109, v65 dst_sel:WORD_0 dst_unused:UNUSED_PAD src0_sel:WORD_0
	v_exp_f16_sdwa v106, v62 dst_sel:WORD_1 dst_unused:UNUSED_PRESERVE src0_sel:WORD_1
	v_exp_f16_sdwa v107, v63 dst_sel:WORD_1 dst_unused:UNUSED_PRESERVE src0_sel:WORD_1
	v_exp_f16_sdwa v108, v64 dst_sel:WORD_1 dst_unused:UNUSED_PRESERVE src0_sel:WORD_1
	v_exp_f16_sdwa v109, v65 dst_sel:WORD_1 dst_unused:UNUSED_PRESERVE src0_sel:WORD_1
	v_pk_add_f16 v73, v73, v157 neg_lo:[0,1] neg_hi:[0,1]
	v_pk_add_f16 v62, v82, v109
	v_pk_add_f16 v63, v83, v108
	v_pk_add_f16 v64, v84, v107
	v_pk_add_f16 v65, v85, v106
	v_pk_fma_f16 v45, v89, v109, v45
	v_pk_fma_f16 v44, v88, v108, v44
	v_pk_fma_f16 v43, v87, v107, v43
	v_pk_fma_f16 v42, v86, v106, v42
	v_pk_add_f16 v82, v129, v154 neg_lo:[0,1] neg_hi:[0,1]
	v_pk_add_f16 v83, v128, v155 neg_lo:[0,1] neg_hi:[0,1]
	v_pk_add_f16 v84, v127, v156 neg_lo:[0,1] neg_hi:[0,1]
	v_pk_add_f16 v85, v126, v157 neg_lo:[0,1] neg_hi:[0,1]
	v_exp_f16_sdwa v86, v82 dst_sel:WORD_0 dst_unused:UNUSED_PAD src0_sel:WORD_0
	v_exp_f16_sdwa v87, v83 dst_sel:WORD_0 dst_unused:UNUSED_PAD src0_sel:WORD_0
	v_exp_f16_sdwa v88, v84 dst_sel:WORD_0 dst_unused:UNUSED_PAD src0_sel:WORD_0
	v_exp_f16_sdwa v89, v85 dst_sel:WORD_0 dst_unused:UNUSED_PAD src0_sel:WORD_0
	v_exp_f16_sdwa v86, v82 dst_sel:WORD_1 dst_unused:UNUSED_PRESERVE src0_sel:WORD_1
	v_exp_f16_sdwa v87, v83 dst_sel:WORD_1 dst_unused:UNUSED_PRESERVE src0_sel:WORD_1
	v_exp_f16_sdwa v88, v84 dst_sel:WORD_1 dst_unused:UNUSED_PRESERVE src0_sel:WORD_1
	v_exp_f16_sdwa v89, v85 dst_sel:WORD_1 dst_unused:UNUSED_PRESERVE src0_sel:WORD_1
	v_pk_add_f16 v82, v137, v154 neg_lo:[0,1] neg_hi:[0,1]
	v_pk_add_f16 v62, v62, v89
	v_pk_add_f16 v65, v65, v86
	v_pk_add_f16 v64, v64, v87
	v_pk_add_f16 v63, v63, v88
	v_pk_fma_f16 v42, v22, v86, v42
	v_pk_fma_f16 v43, v23, v87, v43
	v_pk_fma_f16 v44, v24, v88, v44
	v_pk_fma_f16 v45, v25, v89, v45
	v_pk_add_f16 v83, v136, v155 neg_lo:[0,1] neg_hi:[0,1]
	v_pk_add_f16 v84, v135, v156 neg_lo:[0,1] neg_hi:[0,1]
	v_pk_add_f16 v85, v134, v157 neg_lo:[0,1] neg_hi:[0,1]
	v_exp_f16_sdwa v86, v82 dst_sel:WORD_0 dst_unused:UNUSED_PAD src0_sel:WORD_0
	v_exp_f16_sdwa v87, v83 dst_sel:WORD_0 dst_unused:UNUSED_PAD src0_sel:WORD_0
	v_exp_f16_sdwa v88, v84 dst_sel:WORD_0 dst_unused:UNUSED_PAD src0_sel:WORD_0
	v_exp_f16_sdwa v89, v85 dst_sel:WORD_0 dst_unused:UNUSED_PAD src0_sel:WORD_0
	v_exp_f16_sdwa v86, v82 dst_sel:WORD_1 dst_unused:UNUSED_PRESERVE src0_sel:WORD_1
	v_exp_f16_sdwa v87, v83 dst_sel:WORD_1 dst_unused:UNUSED_PRESERVE src0_sel:WORD_1
	v_exp_f16_sdwa v88, v84 dst_sel:WORD_1 dst_unused:UNUSED_PRESERVE src0_sel:WORD_1
	v_exp_f16_sdwa v89, v85 dst_sel:WORD_1 dst_unused:UNUSED_PRESERVE src0_sel:WORD_1
	v_pk_add_f16 v82, v189, v154 neg_lo:[0,1] neg_hi:[0,1]
	v_pk_add_f16 v62, v62, v89
	v_pk_add_f16 v63, v63, v88
	v_pk_add_f16 v64, v64, v87
	v_pk_add_f16 v65, v65, v86
	v_pk_fma_f16 v45, v33, v89, v45
	v_pk_fma_f16 v44, v32, v88, v44
	v_pk_fma_f16 v43, v31, v87, v43
	v_pk_fma_f16 v42, v30, v86, v42
	v_pk_add_f16 v83, v188, v155 neg_lo:[0,1] neg_hi:[0,1]
	v_pk_add_f16 v84, v187, v156 neg_lo:[0,1] neg_hi:[0,1]
	v_pk_add_f16 v85, v186, v157 neg_lo:[0,1] neg_hi:[0,1]
	v_exp_f16_sdwa v86, v82 dst_sel:WORD_0 dst_unused:UNUSED_PAD src0_sel:WORD_0
	v_exp_f16_sdwa v87, v83 dst_sel:WORD_0 dst_unused:UNUSED_PAD src0_sel:WORD_0
	v_exp_f16_sdwa v88, v84 dst_sel:WORD_0 dst_unused:UNUSED_PAD src0_sel:WORD_0
	v_exp_f16_sdwa v89, v85 dst_sel:WORD_0 dst_unused:UNUSED_PAD src0_sel:WORD_0
	v_exp_f16_sdwa v86, v82 dst_sel:WORD_1 dst_unused:UNUSED_PRESERVE src0_sel:WORD_1
	v_exp_f16_sdwa v87, v83 dst_sel:WORD_1 dst_unused:UNUSED_PRESERVE src0_sel:WORD_1
	v_exp_f16_sdwa v88, v84 dst_sel:WORD_1 dst_unused:UNUSED_PRESERVE src0_sel:WORD_1
	v_exp_f16_sdwa v89, v85 dst_sel:WORD_1 dst_unused:UNUSED_PRESERVE src0_sel:WORD_1
	v_exp_f16_sdwa v82, v70 dst_sel:WORD_0 dst_unused:UNUSED_PAD src0_sel:WORD_0
	v_exp_f16_sdwa v83, v71 dst_sel:WORD_0 dst_unused:UNUSED_PAD src0_sel:WORD_0
	v_exp_f16_sdwa v84, v72 dst_sel:WORD_0 dst_unused:UNUSED_PAD src0_sel:WORD_0
	v_exp_f16_sdwa v85, v73 dst_sel:WORD_0 dst_unused:UNUSED_PAD src0_sel:WORD_0
	v_exp_f16_sdwa v82, v70 dst_sel:WORD_1 dst_unused:UNUSED_PRESERVE src0_sel:WORD_1
	v_exp_f16_sdwa v83, v71 dst_sel:WORD_1 dst_unused:UNUSED_PRESERVE src0_sel:WORD_1
	v_exp_f16_sdwa v84, v72 dst_sel:WORD_1 dst_unused:UNUSED_PRESERVE src0_sel:WORD_1
	v_exp_f16_sdwa v85, v73 dst_sel:WORD_1 dst_unused:UNUSED_PRESERVE src0_sel:WORD_1
	v_pk_add_f16 v70, v98, v154 neg_lo:[0,1] neg_hi:[0,1]
	v_pk_add_f16 v62, v62, v89
	v_pk_add_f16 v65, v65, v86
	v_pk_add_f16 v64, v64, v87
	v_pk_add_f16 v63, v63, v88
	v_pk_fma_f16 v42, v46, v86, v42
	v_pk_fma_f16 v43, v47, v87, v43
	v_pk_fma_f16 v44, v48, v88, v44
	v_pk_fma_f16 v45, v49, v89, v45
	v_pk_add_f16 v62, v62, v85
	v_pk_add_f16 v63, v63, v84
	v_pk_add_f16 v64, v64, v83
	v_pk_add_f16 v65, v65, v82
	v_pk_fma_f16 v45, v9, v85, v45
	v_pk_fma_f16 v44, v8, v84, v44
	v_pk_fma_f16 v43, v7, v83, v43
	v_pk_fma_f16 v42, v6, v82, v42
	v_pk_add_f16 v71, v99, v155 neg_lo:[0,1] neg_hi:[0,1]
	v_pk_add_f16 v72, v100, v156 neg_lo:[0,1] neg_hi:[0,1]
	v_pk_add_f16 v73, v101, v157 neg_lo:[0,1] neg_hi:[0,1]
	v_exp_f16_sdwa v82, v70 dst_sel:WORD_0 dst_unused:UNUSED_PAD src0_sel:WORD_0
	v_exp_f16_sdwa v83, v71 dst_sel:WORD_0 dst_unused:UNUSED_PAD src0_sel:WORD_0
	v_exp_f16_sdwa v84, v72 dst_sel:WORD_0 dst_unused:UNUSED_PAD src0_sel:WORD_0
	v_exp_f16_sdwa v85, v73 dst_sel:WORD_0 dst_unused:UNUSED_PAD src0_sel:WORD_0
	v_exp_f16_sdwa v82, v70 dst_sel:WORD_1 dst_unused:UNUSED_PRESERVE src0_sel:WORD_1
	v_exp_f16_sdwa v83, v71 dst_sel:WORD_1 dst_unused:UNUSED_PRESERVE src0_sel:WORD_1
	v_exp_f16_sdwa v84, v72 dst_sel:WORD_1 dst_unused:UNUSED_PRESERVE src0_sel:WORD_1
	v_exp_f16_sdwa v85, v73 dst_sel:WORD_1 dst_unused:UNUSED_PRESERVE src0_sel:WORD_1
	v_pk_add_f16 v70, v114, v154 neg_lo:[0,1] neg_hi:[0,1]
	v_pk_add_f16 v62, v62, v85
	v_pk_add_f16 v65, v65, v82
	v_pk_add_f16 v64, v64, v83
	v_pk_add_f16 v63, v63, v84
	v_pk_fma_f16 v42, v10, v82, v42
	v_pk_fma_f16 v43, v11, v83, v43
	v_pk_fma_f16 v44, v12, v84, v44
	v_pk_fma_f16 v45, v13, v85, v45
	v_pk_add_f16 v71, v115, v155 neg_lo:[0,1] neg_hi:[0,1]
	v_pk_add_f16 v72, v116, v156 neg_lo:[0,1] neg_hi:[0,1]
	v_pk_add_f16 v73, v117, v157 neg_lo:[0,1] neg_hi:[0,1]
	v_exp_f16_sdwa v82, v70 dst_sel:WORD_0 dst_unused:UNUSED_PAD src0_sel:WORD_0
	v_exp_f16_sdwa v83, v71 dst_sel:WORD_0 dst_unused:UNUSED_PAD src0_sel:WORD_0
	v_exp_f16_sdwa v84, v72 dst_sel:WORD_0 dst_unused:UNUSED_PAD src0_sel:WORD_0
	v_exp_f16_sdwa v85, v73 dst_sel:WORD_0 dst_unused:UNUSED_PAD src0_sel:WORD_0
	v_exp_f16_sdwa v82, v70 dst_sel:WORD_1 dst_unused:UNUSED_PRESERVE src0_sel:WORD_1
	v_exp_f16_sdwa v83, v71 dst_sel:WORD_1 dst_unused:UNUSED_PRESERVE src0_sel:WORD_1
	v_exp_f16_sdwa v84, v72 dst_sel:WORD_1 dst_unused:UNUSED_PRESERVE src0_sel:WORD_1
	v_exp_f16_sdwa v85, v73 dst_sel:WORD_1 dst_unused:UNUSED_PRESERVE src0_sel:WORD_1
	s_nop 0
	v_pk_add_f16 v62, v62, v85
	v_pk_add_f16 v63, v63, v84
	v_pk_add_f16 v64, v64, v83
	v_pk_add_f16 v65, v65, v82
	v_rcp_f16_e32 v73, v62
	v_rcp_f16_sdwa v62, v62 dst_sel:DWORD dst_unused:UNUSED_PAD src0_sel:WORD_1
	v_rcp_f16_e32 v70, v65
	v_rcp_f16_sdwa v65, v65 dst_sel:DWORD dst_unused:UNUSED_PAD src0_sel:WORD_1
	v_rcp_f16_e32 v71, v64
	v_rcp_f16_sdwa v64, v64 dst_sel:DWORD dst_unused:UNUSED_PAD src0_sel:WORD_1
	v_rcp_f16_e32 v72, v63
	v_rcp_f16_sdwa v63, v63 dst_sel:DWORD dst_unused:UNUSED_PAD src0_sel:WORD_1
	v_pk_fma_f16 v45, v17, v85, v45
	v_pack_b32_f16 v62, v73, v62
	v_pk_fma_f16 v44, v16, v84, v44
	v_pk_fma_f16 v43, v15, v83, v43
	v_pk_fma_f16 v42, v14, v82, v42
	v_pack_b32_f16 v65, v70, v65
	v_pack_b32_f16 v64, v71, v64
	v_pack_b32_f16 v63, v72, v63
	v_pk_mul_f16 v45, v45, v62
	s_waitcnt vmcnt(6)
	v_pk_mul_f16 v62, v185, v150 op_sel_hi:[0,1]
	v_pk_mul_f16 v70, v183, v150 op_sel_hi:[0,1]
	v_pk_mul_f16 v82, v184, v150 op_sel_hi:[0,1]
	v_pk_mul_f16 v42, v42, v65
	v_pk_mul_f16 v43, v43, v64
	v_pk_mul_f16 v44, v44, v63
	v_pk_mul_f16 v63, v185, v151 op_sel_hi:[0,1]
	v_pk_mul_f16 v64, v185, v152 op_sel_hi:[0,1]
	v_pk_mul_f16 v65, v185, v153 op_sel_hi:[0,1]
	v_pk_mul_f16 v71, v183, v151 op_sel_hi:[0,1]
	v_pk_mul_f16 v72, v183, v152 op_sel_hi:[0,1]
	v_pk_mul_f16 v73, v183, v153 op_sel_hi:[0,1]
	v_pk_mul_f16 v83, v184, v151 op_sel_hi:[0,1]
	v_pk_mul_f16 v84, v184, v152 op_sel_hi:[0,1]
	v_pk_mul_f16 v85, v184, v153 op_sel_hi:[0,1]
	v_pk_fma_f16 v50, v50, v150, v62
	v_pk_fma_f16 v66, v66, v150, v70
	v_pk_fma_f16 v89, v94, v150, v82
	v_pk_fma_f16 v53, v53, v153, v65
	v_pk_maximum3_f16 v114, v50, v66, v89
	v_pk_fma_f16 v52, v52, v152, v64
	v_pk_fma_f16 v51, v51, v151, v63
	v_pk_fma_f16 v69, v69, v153, v73
	v_pk_fma_f16 v68, v68, v152, v72
	v_pk_fma_f16 v67, v67, v151, v71
	v_pk_fma_f16 v86, v97, v153, v85
	v_pk_fma_f16 v87, v96, v152, v84
	v_pk_fma_f16 v88, v95, v151, v83
	v_pk_fma_f16 v97, v18, v150, v62
	v_pk_fma_f16 v101, v34, v150, v70
	v_pk_fma_f16 v109, v54, v150, v82
	v_pk_fma_f16 v62, v74, v150, v62
	v_pk_fma_f16 v70, v102, v150, v70
	v_pk_fma_f16 v82, v118, v150, v82
	v_pk_maximum3_f16 v115, v51, v67, v88
	v_pk_maximum3_f16 v116, v52, v68, v87
	v_pk_maximum3_f16 v117, v53, v69, v86
	v_pk_maximum3_f16 v122, v97, v101, v109
	v_pk_fma_f16 v94, v21, v153, v65
	v_pk_maximum3_f16 v126, v62, v70, v82
	v_pk_fma_f16 v95, v20, v152, v64
	v_pk_maximum3_f16 v114, v114, v122, v126
	v_pk_fma_f16 v96, v19, v151, v63
	v_pk_fma_f16 v98, v37, v153, v73
	v_pk_fma_f16 v99, v36, v152, v72
	v_pk_fma_f16 v100, v35, v151, v71
	v_pk_fma_f16 v106, v57, v153, v85
	v_pk_fma_f16 v107, v56, v152, v84
	v_pk_fma_f16 v108, v55, v151, v83
	v_pk_fma_f16 v65, v77, v153, v65
	v_pk_fma_f16 v64, v76, v152, v64
	v_pk_fma_f16 v63, v75, v151, v63
	v_pk_fma_f16 v73, v105, v153, v73
	v_pk_fma_f16 v72, v104, v152, v72
	v_pk_fma_f16 v71, v103, v151, v71
	v_pk_fma_f16 v85, v121, v153, v85
	v_pk_fma_f16 v84, v120, v152, v84
	v_pk_fma_f16 v83, v119, v151, v83
	v_pk_maximum3_f16 v123, v96, v100, v108
	v_pk_maximum3_f16 v124, v95, v99, v107
	v_pk_maximum3_f16 v125, v94, v98, v106
	v_pk_maximum3_f16 v128, v64, v72, v84
	v_pk_maximum3_f16 v129, v65, v73, v85
	v_pk_maximum3_f16 v127, v63, v71, v83
	v_pk_maximum3_f16 v115, v115, v123, v127
	v_pk_maximum3_f16 v116, v116, v124, v128
	v_pk_maximum3_f16 v117, v117, v125, v129
	v_pk_add_f16 v50, v50, v114 neg_lo:[0,1] neg_hi:[0,1]
	v_pk_add_f16 v51, v51, v115 neg_lo:[0,1] neg_hi:[0,1]
	v_pk_add_f16 v52, v52, v116 neg_lo:[0,1] neg_hi:[0,1]
	v_pk_add_f16 v53, v53, v117 neg_lo:[0,1] neg_hi:[0,1]
	v_pk_add_f16 v66, v66, v114 neg_lo:[0,1] neg_hi:[0,1]
	v_exp_f16_sdwa v122, v50 dst_sel:WORD_0 dst_unused:UNUSED_PAD src0_sel:WORD_0
	v_exp_f16_sdwa v123, v51 dst_sel:WORD_0 dst_unused:UNUSED_PAD src0_sel:WORD_0
	v_exp_f16_sdwa v124, v52 dst_sel:WORD_0 dst_unused:UNUSED_PAD src0_sel:WORD_0
	v_exp_f16_sdwa v125, v53 dst_sel:WORD_0 dst_unused:UNUSED_PAD src0_sel:WORD_0
	v_exp_f16_sdwa v122, v50 dst_sel:WORD_1 dst_unused:UNUSED_PRESERVE src0_sel:WORD_1
	v_exp_f16_sdwa v123, v51 dst_sel:WORD_1 dst_unused:UNUSED_PRESERVE src0_sel:WORD_1
	v_exp_f16_sdwa v124, v52 dst_sel:WORD_1 dst_unused:UNUSED_PRESERVE src0_sel:WORD_1
	v_exp_f16_sdwa v125, v53 dst_sel:WORD_1 dst_unused:UNUSED_PRESERVE src0_sel:WORD_1
	v_pk_add_f16 v67, v67, v115 neg_lo:[0,1] neg_hi:[0,1]
	v_pk_add_f16 v50, v125, 0
	v_pk_fma_f16 v22, v22, v122, 0
	v_pk_add_f16 v51, v124, 0
	v_pk_add_f16 v52, v123, 0
	v_pk_add_f16 v53, v122, 0
	v_pk_fma_f16 v23, v23, v123, 0
	v_pk_fma_f16 v24, v24, v124, 0
	v_pk_fma_f16 v25, v25, v125, 0
	v_pk_add_f16 v68, v68, v116 neg_lo:[0,1] neg_hi:[0,1]
	v_pk_add_f16 v69, v69, v117 neg_lo:[0,1] neg_hi:[0,1]
	v_exp_f16_sdwa v122, v66 dst_sel:WORD_0 dst_unused:UNUSED_PAD src0_sel:WORD_0
	v_exp_f16_sdwa v123, v67 dst_sel:WORD_0 dst_unused:UNUSED_PAD src0_sel:WORD_0
	v_exp_f16_sdwa v124, v68 dst_sel:WORD_0 dst_unused:UNUSED_PAD src0_sel:WORD_0
	v_exp_f16_sdwa v125, v69 dst_sel:WORD_0 dst_unused:UNUSED_PAD src0_sel:WORD_0
	v_exp_f16_sdwa v122, v66 dst_sel:WORD_1 dst_unused:UNUSED_PRESERVE src0_sel:WORD_1
	v_exp_f16_sdwa v123, v67 dst_sel:WORD_1 dst_unused:UNUSED_PRESERVE src0_sel:WORD_1
	v_exp_f16_sdwa v124, v68 dst_sel:WORD_1 dst_unused:UNUSED_PRESERVE src0_sel:WORD_1
	v_exp_f16_sdwa v125, v69 dst_sel:WORD_1 dst_unused:UNUSED_PRESERVE src0_sel:WORD_1
	s_nop 0
	v_pk_add_f16 v50, v50, v125
	v_pk_fma_f16 v22, v30, v122, v22
	v_pk_add_f16 v30, v89, v114 neg_lo:[0,1] neg_hi:[0,1]
	v_pk_add_f16 v53, v53, v122
	v_pk_add_f16 v52, v52, v123
	v_pk_add_f16 v51, v51, v124
	v_pk_fma_f16 v25, v33, v125, v25
	v_pk_fma_f16 v24, v32, v124, v24
	v_pk_fma_f16 v23, v31, v123, v23
	v_pk_add_f16 v31, v88, v115 neg_lo:[0,1] neg_hi:[0,1]
	v_pk_add_f16 v32, v87, v116 neg_lo:[0,1] neg_hi:[0,1]
	v_pk_add_f16 v33, v86, v117 neg_lo:[0,1] neg_hi:[0,1]
	v_exp_f16_sdwa v66, v30 dst_sel:WORD_0 dst_unused:UNUSED_PAD src0_sel:WORD_0
	v_exp_f16_sdwa v67, v31 dst_sel:WORD_0 dst_unused:UNUSED_PAD src0_sel:WORD_0
	v_exp_f16_sdwa v68, v32 dst_sel:WORD_0 dst_unused:UNUSED_PAD src0_sel:WORD_0
	v_exp_f16_sdwa v69, v33 dst_sel:WORD_0 dst_unused:UNUSED_PAD src0_sel:WORD_0
	v_exp_f16_sdwa v66, v30 dst_sel:WORD_1 dst_unused:UNUSED_PRESERVE src0_sel:WORD_1
	v_exp_f16_sdwa v67, v31 dst_sel:WORD_1 dst_unused:UNUSED_PRESERVE src0_sel:WORD_1
	v_exp_f16_sdwa v68, v32 dst_sel:WORD_1 dst_unused:UNUSED_PRESERVE src0_sel:WORD_1
	v_exp_f16_sdwa v69, v33 dst_sel:WORD_1 dst_unused:UNUSED_PRESERVE src0_sel:WORD_1
	s_nop 0
	v_pk_add_f16 v30, v50, v69
	v_pk_add_f16 v31, v51, v68
	v_pk_add_f16 v32, v52, v67
	v_pk_add_f16 v33, v53, v66
	v_pk_fma_f16 v22, v46, v66, v22
	v_pk_fma_f16 v23, v47, v67, v23
	v_pk_fma_f16 v24, v48, v68, v24
	v_pk_fma_f16 v25, v49, v69, v25
	v_pk_add_f16 v46, v97, v114 neg_lo:[0,1] neg_hi:[0,1]
	v_pk_add_f16 v47, v96, v115 neg_lo:[0,1] neg_hi:[0,1]
	v_pk_add_f16 v48, v95, v116 neg_lo:[0,1] neg_hi:[0,1]
	v_pk_add_f16 v49, v94, v117 neg_lo:[0,1] neg_hi:[0,1]
	v_exp_f16_sdwa v50, v46 dst_sel:WORD_0 dst_unused:UNUSED_PAD src0_sel:WORD_0
	v_exp_f16_sdwa v51, v47 dst_sel:WORD_0 dst_unused:UNUSED_PAD src0_sel:WORD_0
	v_exp_f16_sdwa v52, v48 dst_sel:WORD_0 dst_unused:UNUSED_PAD src0_sel:WORD_0
	v_exp_f16_sdwa v53, v49 dst_sel:WORD_0 dst_unused:UNUSED_PAD src0_sel:WORD_0
	v_exp_f16_sdwa v50, v46 dst_sel:WORD_1 dst_unused:UNUSED_PRESERVE src0_sel:WORD_1
	v_exp_f16_sdwa v51, v47 dst_sel:WORD_1 dst_unused:UNUSED_PRESERVE src0_sel:WORD_1
	v_exp_f16_sdwa v52, v48 dst_sel:WORD_1 dst_unused:UNUSED_PRESERVE src0_sel:WORD_1
	v_exp_f16_sdwa v53, v49 dst_sel:WORD_1 dst_unused:UNUSED_PRESERVE src0_sel:WORD_1
	v_pk_add_f16 v46, v101, v114 neg_lo:[0,1] neg_hi:[0,1]
	v_pk_add_f16 v30, v30, v53
	v_pk_add_f16 v33, v33, v50
	v_pk_add_f16 v32, v32, v51
	v_pk_add_f16 v31, v31, v52
	v_pk_fma_f16 v25, v9, v53, v25
	v_pk_fma_f16 v24, v8, v52, v24
	v_pk_fma_f16 v23, v7, v51, v23
	v_pk_fma_f16 v22, v6, v50, v22
	v_pk_add_f16 v47, v100, v115 neg_lo:[0,1] neg_hi:[0,1]
	v_pk_add_f16 v48, v99, v116 neg_lo:[0,1] neg_hi:[0,1]
	v_pk_add_f16 v49, v98, v117 neg_lo:[0,1] neg_hi:[0,1]
	v_exp_f16_sdwa v50, v46 dst_sel:WORD_0 dst_unused:UNUSED_PAD src0_sel:WORD_0
	v_exp_f16_sdwa v51, v47 dst_sel:WORD_0 dst_unused:UNUSED_PAD src0_sel:WORD_0
	v_exp_f16_sdwa v52, v48 dst_sel:WORD_0 dst_unused:UNUSED_PAD src0_sel:WORD_0
	v_exp_f16_sdwa v53, v49 dst_sel:WORD_0 dst_unused:UNUSED_PAD src0_sel:WORD_0
	v_exp_f16_sdwa v50, v46 dst_sel:WORD_1 dst_unused:UNUSED_PRESERVE src0_sel:WORD_1
	v_exp_f16_sdwa v51, v47 dst_sel:WORD_1 dst_unused:UNUSED_PRESERVE src0_sel:WORD_1
	v_exp_f16_sdwa v52, v48 dst_sel:WORD_1 dst_unused:UNUSED_PRESERVE src0_sel:WORD_1
	v_exp_f16_sdwa v53, v49 dst_sel:WORD_1 dst_unused:UNUSED_PRESERVE src0_sel:WORD_1
	v_pk_add_f16 v46, v109, v114 neg_lo:[0,1] neg_hi:[0,1]
	v_pk_add_f16 v30, v30, v53
	v_pk_add_f16 v31, v31, v52
	v_pk_add_f16 v32, v32, v51
	v_pk_add_f16 v33, v33, v50
	v_pk_fma_f16 v22, v10, v50, v22
	v_pk_fma_f16 v23, v11, v51, v23
	v_pk_fma_f16 v24, v12, v52, v24
	v_pk_fma_f16 v25, v13, v53, v25
	v_pk_add_f16 v47, v108, v115 neg_lo:[0,1] neg_hi:[0,1]
	v_pk_add_f16 v48, v107, v116 neg_lo:[0,1] neg_hi:[0,1]
	v_pk_add_f16 v49, v106, v117 neg_lo:[0,1] neg_hi:[0,1]
	v_exp_f16_sdwa v50, v46 dst_sel:WORD_0 dst_unused:UNUSED_PAD src0_sel:WORD_0
	v_exp_f16_sdwa v51, v47 dst_sel:WORD_0 dst_unused:UNUSED_PAD src0_sel:WORD_0
	v_exp_f16_sdwa v52, v48 dst_sel:WORD_0 dst_unused:UNUSED_PAD src0_sel:WORD_0
	v_exp_f16_sdwa v53, v49 dst_sel:WORD_0 dst_unused:UNUSED_PAD src0_sel:WORD_0
	v_exp_f16_sdwa v50, v46 dst_sel:WORD_1 dst_unused:UNUSED_PRESERVE src0_sel:WORD_1
	v_exp_f16_sdwa v51, v47 dst_sel:WORD_1 dst_unused:UNUSED_PRESERVE src0_sel:WORD_1
	v_exp_f16_sdwa v52, v48 dst_sel:WORD_1 dst_unused:UNUSED_PRESERVE src0_sel:WORD_1
	v_exp_f16_sdwa v53, v49 dst_sel:WORD_1 dst_unused:UNUSED_PRESERVE src0_sel:WORD_1
	v_pk_add_f16 v46, v62, v114 neg_lo:[0,1] neg_hi:[0,1]
	v_pk_add_f16 v30, v30, v53
	v_pk_add_f16 v33, v33, v50
	v_pk_add_f16 v32, v32, v51
	v_pk_add_f16 v31, v31, v52
	v_pk_fma_f16 v25, v17, v53, v25
	v_pk_fma_f16 v24, v16, v52, v24
	v_pk_fma_f16 v23, v15, v51, v23
	v_pk_fma_f16 v22, v14, v50, v22
	v_pk_add_f16 v47, v63, v115 neg_lo:[0,1] neg_hi:[0,1]
	v_pk_add_f16 v48, v64, v116 neg_lo:[0,1] neg_hi:[0,1]
	v_pk_add_f16 v49, v65, v117 neg_lo:[0,1] neg_hi:[0,1]
	v_exp_f16_sdwa v50, v46 dst_sel:WORD_0 dst_unused:UNUSED_PAD src0_sel:WORD_0
	v_exp_f16_sdwa v51, v47 dst_sel:WORD_0 dst_unused:UNUSED_PAD src0_sel:WORD_0
	v_exp_f16_sdwa v52, v48 dst_sel:WORD_0 dst_unused:UNUSED_PAD src0_sel:WORD_0
	v_exp_f16_sdwa v53, v49 dst_sel:WORD_0 dst_unused:UNUSED_PAD src0_sel:WORD_0
	v_exp_f16_sdwa v50, v46 dst_sel:WORD_1 dst_unused:UNUSED_PRESERVE src0_sel:WORD_1
	v_exp_f16_sdwa v51, v47 dst_sel:WORD_1 dst_unused:UNUSED_PRESERVE src0_sel:WORD_1
	v_exp_f16_sdwa v52, v48 dst_sel:WORD_1 dst_unused:UNUSED_PRESERVE src0_sel:WORD_1
	v_exp_f16_sdwa v53, v49 dst_sel:WORD_1 dst_unused:UNUSED_PRESERVE src0_sel:WORD_1
	v_pk_add_f16 v46, v70, v114 neg_lo:[0,1] neg_hi:[0,1]
	v_pk_add_f16 v30, v30, v53
	v_pk_add_f16 v31, v31, v52
	v_pk_add_f16 v32, v32, v51
	v_pk_add_f16 v33, v33, v50
	v_pk_fma_f16 v22, v26, v50, v22
	v_pk_fma_f16 v23, v27, v51, v23
	v_pk_fma_f16 v24, v28, v52, v24
	v_pk_fma_f16 v25, v29, v53, v25
	v_pk_add_f16 v47, v71, v115 neg_lo:[0,1] neg_hi:[0,1]
	v_pk_add_f16 v48, v72, v116 neg_lo:[0,1] neg_hi:[0,1]
	v_pk_add_f16 v49, v73, v117 neg_lo:[0,1] neg_hi:[0,1]
	v_exp_f16_sdwa v50, v46 dst_sel:WORD_0 dst_unused:UNUSED_PAD src0_sel:WORD_0
	v_exp_f16_sdwa v51, v47 dst_sel:WORD_0 dst_unused:UNUSED_PAD src0_sel:WORD_0
	v_exp_f16_sdwa v52, v48 dst_sel:WORD_0 dst_unused:UNUSED_PAD src0_sel:WORD_0
	v_exp_f16_sdwa v53, v49 dst_sel:WORD_0 dst_unused:UNUSED_PAD src0_sel:WORD_0
	v_exp_f16_sdwa v50, v46 dst_sel:WORD_1 dst_unused:UNUSED_PRESERVE src0_sel:WORD_1
	v_exp_f16_sdwa v51, v47 dst_sel:WORD_1 dst_unused:UNUSED_PRESERVE src0_sel:WORD_1
	v_exp_f16_sdwa v52, v48 dst_sel:WORD_1 dst_unused:UNUSED_PRESERVE src0_sel:WORD_1
	v_exp_f16_sdwa v53, v49 dst_sel:WORD_1 dst_unused:UNUSED_PRESERVE src0_sel:WORD_1
	v_pk_add_f16 v46, v82, v114 neg_lo:[0,1] neg_hi:[0,1]
	v_pk_add_f16 v30, v30, v53
	v_pk_add_f16 v33, v33, v50
	v_pk_add_f16 v32, v32, v51
	v_pk_add_f16 v31, v31, v52
	v_pk_fma_f16 v25, v41, v53, v25
	v_pk_fma_f16 v24, v40, v52, v24
	v_pk_fma_f16 v23, v39, v51, v23
	v_pk_fma_f16 v22, v38, v50, v22
	v_pk_add_f16 v47, v83, v115 neg_lo:[0,1] neg_hi:[0,1]
	v_pk_add_f16 v48, v84, v116 neg_lo:[0,1] neg_hi:[0,1]
	v_pk_add_f16 v49, v85, v117 neg_lo:[0,1] neg_hi:[0,1]
	v_exp_f16_sdwa v50, v46 dst_sel:WORD_0 dst_unused:UNUSED_PAD src0_sel:WORD_0
	v_exp_f16_sdwa v51, v47 dst_sel:WORD_0 dst_unused:UNUSED_PAD src0_sel:WORD_0
	v_exp_f16_sdwa v52, v48 dst_sel:WORD_0 dst_unused:UNUSED_PAD src0_sel:WORD_0
	v_exp_f16_sdwa v53, v49 dst_sel:WORD_0 dst_unused:UNUSED_PAD src0_sel:WORD_0
	v_exp_f16_sdwa v50, v46 dst_sel:WORD_1 dst_unused:UNUSED_PRESERVE src0_sel:WORD_1
	v_exp_f16_sdwa v51, v47 dst_sel:WORD_1 dst_unused:UNUSED_PRESERVE src0_sel:WORD_1
	v_exp_f16_sdwa v52, v48 dst_sel:WORD_1 dst_unused:UNUSED_PRESERVE src0_sel:WORD_1
	v_exp_f16_sdwa v53, v49 dst_sel:WORD_1 dst_unused:UNUSED_PRESERVE src0_sel:WORD_1
	s_nop 0
	v_pk_add_f16 v30, v30, v53
	v_pk_add_f16 v31, v31, v52
	v_rcp_f16_e32 v48, v30
	v_rcp_f16_sdwa v30, v30 dst_sel:DWORD dst_unused:UNUSED_PAD src0_sel:WORD_1
	v_pk_add_f16 v32, v32, v51
	v_rcp_f16_e32 v49, v31
	v_rcp_f16_sdwa v31, v31 dst_sel:DWORD dst_unused:UNUSED_PAD src0_sel:WORD_1
	v_pk_add_f16 v33, v33, v50
	v_rcp_f16_e32 v47, v32
	v_rcp_f16_sdwa v32, v32 dst_sel:DWORD dst_unused:UNUSED_PAD src0_sel:WORD_1
	v_rcp_f16_e32 v46, v33
	v_rcp_f16_sdwa v33, v33 dst_sel:DWORD dst_unused:UNUSED_PAD src0_sel:WORD_1
	v_pk_fma_f16 v25, v61, v53, v25
	v_pack_b32_f16 v30, v48, v30
	v_pk_fma_f16 v24, v60, v52, v24
	v_pk_mul_f16 v25, v25, v30
	v_pack_b32_f16 v30, v49, v31
	v_pk_fma_f16 v23, v59, v51, v23
	v_pk_mul_f16 v24, v24, v30
	v_pack_b32_f16 v30, v47, v32
	v_pk_fma_f16 v22, v58, v50, v22
	v_pk_mul_f16 v23, v23, v30
	v_pack_b32_f16 v30, v46, v33
	v_pk_mul_f16 v22, v22, v30
	s_waitcnt vmcnt(0)
	s_mov_b64 s[86:87], s[80:81]
	global_load_dword v254, v255, s[86:87]
	s_add_u32 s86, s86, 0x2000
	s_addc_u32 s87, s87, 0
	global_load_dword v254, v255, s[86:87]
	s_add_u32 s86, s86, 0x2000
	s_addc_u32 s87, s87, 0
	global_load_dword v254, v255, s[86:87]
	s_add_u32 s86, s86, 0x2c000
	s_addc_u32 s87, s87, 0
	global_load_dword v254, v255, s[86:87]
	s_add_u32 s86, s86, 0x2000
	s_addc_u32 s87, s87, 0
	global_load_dword v254, v255, s[86:87]
	s_add_u32 s86, s86, 0x2000
	s_addc_u32 s87, s87, 0
	global_load_dword v254, v255, s[86:87]
	v_pk_mul_f16 v30, v185, v146 op_sel_hi:[0,1]
	v_pk_mul_f16 v31, v185, v147 op_sel_hi:[0,1]
	v_pk_mul_f16 v32, v185, v148 op_sel_hi:[0,1]
	v_pk_mul_f16 v33, v185, v149 op_sel_hi:[0,1]
	v_pk_mul_f16 v46, v183, v146 op_sel_hi:[0,1]
	v_pk_mul_f16 v47, v183, v147 op_sel_hi:[0,1]
	v_pk_mul_f16 v48, v183, v148 op_sel_hi:[0,1]
	v_pk_mul_f16 v49, v183, v149 op_sel_hi:[0,1]
	v_pk_mul_f16 v50, v184, v146 op_sel_hi:[0,1]
	v_pk_mul_f16 v51, v184, v147 op_sel_hi:[0,1]
	v_pk_mul_f16 v52, v184, v148 op_sel_hi:[0,1]
	v_pk_mul_f16 v53, v184, v149 op_sel_hi:[0,1]
	v_pk_fma_f16 v21, v21, v149, v33
	v_pk_fma_f16 v20, v20, v148, v32
	v_pk_fma_f16 v19, v19, v147, v31
	v_pk_fma_f16 v18, v18, v146, v30
	v_pk_fma_f16 v37, v37, v149, v49
	v_pk_fma_f16 v36, v36, v148, v48
	v_pk_fma_f16 v35, v35, v147, v47
	v_pk_fma_f16 v34, v34, v146, v46
	v_pk_fma_f16 v57, v57, v149, v53
	v_pk_fma_f16 v56, v56, v148, v52
	v_pk_fma_f16 v55, v55, v147, v51
	v_pk_fma_f16 v54, v54, v146, v50
	v_pk_fma_f16 v62, v77, v149, v33
	v_pk_fma_f16 v63, v76, v148, v32
	v_pk_fma_f16 v64, v75, v147, v31
	v_pk_fma_f16 v65, v74, v146, v30
	v_pk_maximum3_f16 v74, v18, v34, v54
	v_pk_maximum3_f16 v75, v19, v35, v55
	v_pk_maximum3_f16 v76, v20, v36, v56
	v_pk_maximum3_f16 v77, v21, v37, v57
	v_pk_fma_f16 v66, v105, v149, v49
	v_pk_fma_f16 v67, v104, v148, v48
	v_pk_fma_f16 v68, v103, v147, v47
	v_pk_fma_f16 v69, v102, v146, v46
	v_pk_fma_f16 v70, v121, v149, v53
	v_pk_fma_f16 v71, v120, v148, v52
	v_pk_fma_f16 v72, v119, v147, v51
	v_pk_fma_f16 v73, v118, v146, v50
	v_pk_fma_f16 v33, v133, v149, v33
	v_pk_fma_f16 v32, v132, v148, v32
	v_pk_fma_f16 v31, v131, v147, v31
	v_pk_fma_f16 v30, v130, v146, v30
	v_pk_fma_f16 v49, v141, v149, v49
	v_pk_fma_f16 v48, v140, v148, v48
	v_pk_fma_f16 v47, v139, v147, v47
	v_pk_fma_f16 v46, v138, v146, v46
	v_pk_fma_f16 v53, v145, v149, v53
	v_pk_fma_f16 v52, v144, v148, v52
	v_pk_fma_f16 v51, v143, v147, v51
	v_pk_fma_f16 v50, v142, v146, v50
	v_pk_maximum3_f16 v82, v65, v69, v73
	v_pk_maximum3_f16 v83, v64, v68, v72
	v_pk_maximum3_f16 v84, v63, v67, v71
	v_pk_maximum3_f16 v85, v62, v66, v70
	v_pk_maximum3_f16 v87, v31, v47, v51
	v_pk_maximum3_f16 v86, v30, v46, v50
	v_pk_maximum3_f16 v88, v32, v48, v52
	v_pk_maximum3_f16 v89, v33, v49, v53
	v_pk_maximum3_f16 v74, v74, v82, v86
	v_pk_maximum3_f16 v75, v75, v83, v87
	v_pk_maximum3_f16 v76, v76, v84, v88
	v_pk_maximum3_f16 v77, v77, v85, v89
	s_nop 0
	v_pk_add_f16 v18, v18, v74 neg_lo:[0,1] neg_hi:[0,1]
	v_pk_add_f16 v19, v19, v75 neg_lo:[0,1] neg_hi:[0,1]
	v_pk_add_f16 v20, v20, v76 neg_lo:[0,1] neg_hi:[0,1]
	v_pk_add_f16 v21, v21, v77 neg_lo:[0,1] neg_hi:[0,1]
	v_pk_add_f16 v34, v34, v74 neg_lo:[0,1] neg_hi:[0,1]
	v_exp_f16_sdwa v82, v18 dst_sel:WORD_0 dst_unused:UNUSED_PAD src0_sel:WORD_0
	v_exp_f16_sdwa v83, v19 dst_sel:WORD_0 dst_unused:UNUSED_PAD src0_sel:WORD_0
	v_exp_f16_sdwa v84, v20 dst_sel:WORD_0 dst_unused:UNUSED_PAD src0_sel:WORD_0
	v_exp_f16_sdwa v85, v21 dst_sel:WORD_0 dst_unused:UNUSED_PAD src0_sel:WORD_0
	v_exp_f16_sdwa v82, v18 dst_sel:WORD_1 dst_unused:UNUSED_PRESERVE src0_sel:WORD_1
	v_exp_f16_sdwa v83, v19 dst_sel:WORD_1 dst_unused:UNUSED_PRESERVE src0_sel:WORD_1
	v_exp_f16_sdwa v84, v20 dst_sel:WORD_1 dst_unused:UNUSED_PRESERVE src0_sel:WORD_1
	v_exp_f16_sdwa v85, v21 dst_sel:WORD_1 dst_unused:UNUSED_PRESERVE src0_sel:WORD_1
	v_pk_add_f16 v35, v35, v75 neg_lo:[0,1] neg_hi:[0,1]
	v_pk_add_f16 v18, v82, 0
	v_pk_add_f16 v19, v83, 0
	v_pk_add_f16 v20, v84, 0
	v_pk_add_f16 v21, v85, 0
	v_pk_fma_f16 v6, v6, v82, 0
	v_pk_fma_f16 v7, v7, v83, 0
	v_pk_fma_f16 v8, v8, v84, 0
	v_pk_fma_f16 v9, v9, v85, 0
	v_pk_add_f16 v36, v36, v76 neg_lo:[0,1] neg_hi:[0,1]
	v_pk_add_f16 v37, v37, v77 neg_lo:[0,1] neg_hi:[0,1]
	v_exp_f16_sdwa v82, v34 dst_sel:WORD_0 dst_unused:UNUSED_PAD src0_sel:WORD_0
	v_exp_f16_sdwa v83, v35 dst_sel:WORD_0 dst_unused:UNUSED_PAD src0_sel:WORD_0
	v_exp_f16_sdwa v84, v36 dst_sel:WORD_0 dst_unused:UNUSED_PAD src0_sel:WORD_0
	v_exp_f16_sdwa v85, v37 dst_sel:WORD_0 dst_unused:UNUSED_PAD src0_sel:WORD_0
	v_exp_f16_sdwa v82, v34 dst_sel:WORD_1 dst_unused:UNUSED_PRESERVE src0_sel:WORD_1
	v_exp_f16_sdwa v83, v35 dst_sel:WORD_1 dst_unused:UNUSED_PRESERVE src0_sel:WORD_1
	v_exp_f16_sdwa v84, v36 dst_sel:WORD_1 dst_unused:UNUSED_PRESERVE src0_sel:WORD_1
	v_exp_f16_sdwa v85, v37 dst_sel:WORD_1 dst_unused:UNUSED_PRESERVE src0_sel:WORD_1
	s_nop 0
	v_pk_add_f16 v21, v21, v85
	v_pk_add_f16 v20, v20, v84
	v_pk_add_f16 v19, v19, v83
	v_pk_add_f16 v18, v18, v82
	v_pk_fma_f16 v9, v13, v85, v9
	v_pk_fma_f16 v8, v12, v84, v8
	v_pk_fma_f16 v7, v11, v83, v7
	v_pk_fma_f16 v6, v10, v82, v6
	v_pk_add_f16 v10, v54, v74 neg_lo:[0,1] neg_hi:[0,1]
	v_pk_add_f16 v11, v55, v75 neg_lo:[0,1] neg_hi:[0,1]
	v_pk_add_f16 v12, v56, v76 neg_lo:[0,1] neg_hi:[0,1]
	v_pk_add_f16 v13, v57, v77 neg_lo:[0,1] neg_hi:[0,1]
	v_exp_f16_sdwa v34, v10 dst_sel:WORD_0 dst_unused:UNUSED_PAD src0_sel:WORD_0
	v_exp_f16_sdwa v35, v11 dst_sel:WORD_0 dst_unused:UNUSED_PAD src0_sel:WORD_0
	v_exp_f16_sdwa v36, v12 dst_sel:WORD_0 dst_unused:UNUSED_PAD src0_sel:WORD_0
	v_exp_f16_sdwa v37, v13 dst_sel:WORD_0 dst_unused:UNUSED_PAD src0_sel:WORD_0
	v_exp_f16_sdwa v34, v10 dst_sel:WORD_1 dst_unused:UNUSED_PRESERVE src0_sel:WORD_1
	v_exp_f16_sdwa v35, v11 dst_sel:WORD_1 dst_unused:UNUSED_PRESERVE src0_sel:WORD_1
	v_exp_f16_sdwa v36, v12 dst_sel:WORD_1 dst_unused:UNUSED_PRESERVE src0_sel:WORD_1
	v_exp_f16_sdwa v37, v13 dst_sel:WORD_1 dst_unused:UNUSED_PRESERVE src0_sel:WORD_1
	v_pk_add_f16 v10, v18, v34
	v_pk_add_f16 v11, v19, v35
	v_pk_add_f16 v12, v20, v36
	v_pk_add_f16 v13, v21, v37
	v_pk_fma_f16 v6, v14, v34, v6
	v_pk_fma_f16 v7, v15, v35, v7
	v_pk_fma_f16 v8, v16, v36, v8
	v_pk_fma_f16 v9, v17, v37, v9
	v_pk_add_f16 v14, v65, v74 neg_lo:[0,1] neg_hi:[0,1]
	v_pk_add_f16 v15, v64, v75 neg_lo:[0,1] neg_hi:[0,1]
	v_pk_add_f16 v16, v63, v76 neg_lo:[0,1] neg_hi:[0,1]
	v_pk_add_f16 v17, v62, v77 neg_lo:[0,1] neg_hi:[0,1]
	v_exp_f16_sdwa v18, v14 dst_sel:WORD_0 dst_unused:UNUSED_PAD src0_sel:WORD_0
	v_exp_f16_sdwa v19, v15 dst_sel:WORD_0 dst_unused:UNUSED_PAD src0_sel:WORD_0
	v_exp_f16_sdwa v20, v16 dst_sel:WORD_0 dst_unused:UNUSED_PAD src0_sel:WORD_0
	v_exp_f16_sdwa v21, v17 dst_sel:WORD_0 dst_unused:UNUSED_PAD src0_sel:WORD_0
	v_exp_f16_sdwa v18, v14 dst_sel:WORD_1 dst_unused:UNUSED_PRESERVE src0_sel:WORD_1
	v_exp_f16_sdwa v19, v15 dst_sel:WORD_1 dst_unused:UNUSED_PRESERVE src0_sel:WORD_1
	v_exp_f16_sdwa v20, v16 dst_sel:WORD_1 dst_unused:UNUSED_PRESERVE src0_sel:WORD_1
	v_exp_f16_sdwa v21, v17 dst_sel:WORD_1 dst_unused:UNUSED_PRESERVE src0_sel:WORD_1
	v_pk_add_f16 v14, v69, v74 neg_lo:[0,1] neg_hi:[0,1]
	v_pk_add_f16 v13, v13, v21
	v_pk_add_f16 v12, v12, v20
	v_pk_add_f16 v11, v11, v19
	v_pk_add_f16 v10, v10, v18
	v_pk_fma_f16 v9, v29, v21, v9
	v_pk_fma_f16 v8, v28, v20, v8
	v_pk_fma_f16 v7, v27, v19, v7
	v_pk_fma_f16 v6, v26, v18, v6
	v_pk_add_f16 v15, v68, v75 neg_lo:[0,1] neg_hi:[0,1]
	v_pk_add_f16 v16, v67, v76 neg_lo:[0,1] neg_hi:[0,1]
	v_pk_add_f16 v17, v66, v77 neg_lo:[0,1] neg_hi:[0,1]
	v_exp_f16_sdwa v18, v14 dst_sel:WORD_0 dst_unused:UNUSED_PAD src0_sel:WORD_0
	v_exp_f16_sdwa v19, v15 dst_sel:WORD_0 dst_unused:UNUSED_PAD src0_sel:WORD_0
	v_exp_f16_sdwa v20, v16 dst_sel:WORD_0 dst_unused:UNUSED_PAD src0_sel:WORD_0
	v_exp_f16_sdwa v21, v17 dst_sel:WORD_0 dst_unused:UNUSED_PAD src0_sel:WORD_0
	v_exp_f16_sdwa v18, v14 dst_sel:WORD_1 dst_unused:UNUSED_PRESERVE src0_sel:WORD_1
	v_exp_f16_sdwa v19, v15 dst_sel:WORD_1 dst_unused:UNUSED_PRESERVE src0_sel:WORD_1
	v_exp_f16_sdwa v20, v16 dst_sel:WORD_1 dst_unused:UNUSED_PRESERVE src0_sel:WORD_1
	v_exp_f16_sdwa v21, v17 dst_sel:WORD_1 dst_unused:UNUSED_PRESERVE src0_sel:WORD_1
	v_pk_add_f16 v14, v73, v74 neg_lo:[0,1] neg_hi:[0,1]
	v_pk_add_f16 v10, v10, v18
	v_pk_add_f16 v11, v11, v19
	v_pk_add_f16 v12, v12, v20
	v_pk_add_f16 v13, v13, v21
	v_pk_fma_f16 v6, v38, v18, v6
	v_pk_fma_f16 v7, v39, v19, v7
	v_pk_fma_f16 v8, v40, v20, v8
	v_pk_fma_f16 v9, v41, v21, v9
	v_pk_add_f16 v15, v72, v75 neg_lo:[0,1] neg_hi:[0,1]
	v_pk_add_f16 v16, v71, v76 neg_lo:[0,1] neg_hi:[0,1]
	v_pk_add_f16 v17, v70, v77 neg_lo:[0,1] neg_hi:[0,1]
	v_exp_f16_sdwa v18, v14 dst_sel:WORD_0 dst_unused:UNUSED_PAD src0_sel:WORD_0
	v_exp_f16_sdwa v19, v15 dst_sel:WORD_0 dst_unused:UNUSED_PAD src0_sel:WORD_0
	v_exp_f16_sdwa v20, v16 dst_sel:WORD_0 dst_unused:UNUSED_PAD src0_sel:WORD_0
	v_exp_f16_sdwa v21, v17 dst_sel:WORD_0 dst_unused:UNUSED_PAD src0_sel:WORD_0
	v_exp_f16_sdwa v18, v14 dst_sel:WORD_1 dst_unused:UNUSED_PRESERVE src0_sel:WORD_1
	v_exp_f16_sdwa v19, v15 dst_sel:WORD_1 dst_unused:UNUSED_PRESERVE src0_sel:WORD_1
	v_exp_f16_sdwa v20, v16 dst_sel:WORD_1 dst_unused:UNUSED_PRESERVE src0_sel:WORD_1
	v_exp_f16_sdwa v21, v17 dst_sel:WORD_1 dst_unused:UNUSED_PRESERVE src0_sel:WORD_1
	v_pk_add_f16 v14, v30, v74 neg_lo:[0,1] neg_hi:[0,1]
	v_pk_add_f16 v13, v13, v21
	v_pk_add_f16 v12, v12, v20
	v_pk_add_f16 v11, v11, v19
	v_pk_add_f16 v10, v10, v18
	v_pk_fma_f16 v9, v61, v21, v9
	v_pk_fma_f16 v8, v60, v20, v8
	v_pk_fma_f16 v7, v59, v19, v7
	v_pk_fma_f16 v6, v58, v18, v6
	v_pk_add_f16 v15, v31, v75 neg_lo:[0,1] neg_hi:[0,1]
	v_pk_add_f16 v16, v32, v76 neg_lo:[0,1] neg_hi:[0,1]
	v_pk_add_f16 v17, v33, v77 neg_lo:[0,1] neg_hi:[0,1]
	v_exp_f16_sdwa v18, v14 dst_sel:WORD_0 dst_unused:UNUSED_PAD src0_sel:WORD_0
	v_exp_f16_sdwa v19, v15 dst_sel:WORD_0 dst_unused:UNUSED_PAD src0_sel:WORD_0
	v_exp_f16_sdwa v20, v16 dst_sel:WORD_0 dst_unused:UNUSED_PAD src0_sel:WORD_0
	v_exp_f16_sdwa v21, v17 dst_sel:WORD_0 dst_unused:UNUSED_PAD src0_sel:WORD_0
	v_exp_f16_sdwa v18, v14 dst_sel:WORD_1 dst_unused:UNUSED_PRESERVE src0_sel:WORD_1
	v_exp_f16_sdwa v19, v15 dst_sel:WORD_1 dst_unused:UNUSED_PRESERVE src0_sel:WORD_1
	v_exp_f16_sdwa v20, v16 dst_sel:WORD_1 dst_unused:UNUSED_PRESERVE src0_sel:WORD_1
	v_exp_f16_sdwa v21, v17 dst_sel:WORD_1 dst_unused:UNUSED_PRESERVE src0_sel:WORD_1
	v_pk_add_f16 v10, v10, v18
	v_pk_add_f16 v11, v11, v19
	v_pk_add_f16 v12, v12, v20
	v_pk_add_f16 v13, v13, v21
	v_pk_fma_f16 v14, v78, v18, v6
	v_pk_fma_f16 v15, v79, v19, v7
	v_pk_fma_f16 v16, v80, v20, v8
	v_pk_fma_f16 v17, v81, v21, v9
	v_pk_add_f16 v6, v46, v74 neg_lo:[0,1] neg_hi:[0,1]
	v_pk_add_f16 v7, v47, v75 neg_lo:[0,1] neg_hi:[0,1]
	v_pk_add_f16 v8, v48, v76 neg_lo:[0,1] neg_hi:[0,1]
	v_pk_add_f16 v9, v49, v77 neg_lo:[0,1] neg_hi:[0,1]
	v_exp_f16_sdwa v18, v6 dst_sel:WORD_0 dst_unused:UNUSED_PAD src0_sel:WORD_0
	v_exp_f16_sdwa v19, v7 dst_sel:WORD_0 dst_unused:UNUSED_PAD src0_sel:WORD_0
	v_exp_f16_sdwa v20, v8 dst_sel:WORD_0 dst_unused:UNUSED_PAD src0_sel:WORD_0
	v_exp_f16_sdwa v21, v9 dst_sel:WORD_0 dst_unused:UNUSED_PAD src0_sel:WORD_0
	v_exp_f16_sdwa v18, v6 dst_sel:WORD_1 dst_unused:UNUSED_PRESERVE src0_sel:WORD_1
	v_exp_f16_sdwa v19, v7 dst_sel:WORD_1 dst_unused:UNUSED_PRESERVE src0_sel:WORD_1
	v_exp_f16_sdwa v20, v8 dst_sel:WORD_1 dst_unused:UNUSED_PRESERVE src0_sel:WORD_1
	v_exp_f16_sdwa v21, v9 dst_sel:WORD_1 dst_unused:UNUSED_PRESERVE src0_sel:WORD_1
	s_nop 0
	v_pk_add_f16 v9, v13, v21
	v_pk_add_f16 v8, v12, v20
	v_pk_add_f16 v7, v11, v19
	v_pk_add_f16 v6, v10, v18
	v_pk_fma_f16 v13, v93, v21, v17
	v_pk_fma_f16 v12, v92, v20, v16
	v_pk_fma_f16 v11, v91, v19, v15
	v_pk_fma_f16 v10, v90, v18, v14
	v_pk_add_f16 v18, v50, v74 neg_lo:[0,1] neg_hi:[0,1]
	v_pk_add_f16 v19, v51, v75 neg_lo:[0,1] neg_hi:[0,1]
	v_pk_add_f16 v20, v52, v76 neg_lo:[0,1] neg_hi:[0,1]
	v_pk_add_f16 v21, v53, v77 neg_lo:[0,1] neg_hi:[0,1]
	v_exp_f16_sdwa v14, v18 dst_sel:WORD_0 dst_unused:UNUSED_PAD src0_sel:WORD_0
	v_exp_f16_sdwa v17, v19 dst_sel:WORD_0 dst_unused:UNUSED_PAD src0_sel:WORD_0
	v_exp_f16_sdwa v15, v20 dst_sel:WORD_0 dst_unused:UNUSED_PAD src0_sel:WORD_0
	v_exp_f16_sdwa v16, v21 dst_sel:WORD_0 dst_unused:UNUSED_PAD src0_sel:WORD_0
	v_exp_f16_sdwa v14, v18 dst_sel:WORD_1 dst_unused:UNUSED_PRESERVE src0_sel:WORD_1
	v_exp_f16_sdwa v17, v19 dst_sel:WORD_1 dst_unused:UNUSED_PRESERVE src0_sel:WORD_1
	v_exp_f16_sdwa v15, v20 dst_sel:WORD_1 dst_unused:UNUSED_PRESERVE src0_sel:WORD_1
	v_exp_f16_sdwa v16, v21 dst_sel:WORD_1 dst_unused:UNUSED_PRESERVE src0_sel:WORD_1
	s_nop 0

.Lmystag5_3:
	global_load_dwordx4 v[82:85], v[58:59], off
	global_load_dwordx4 v[86:89], v[58:59], off offset:1024
	global_load_dwordx4 v[90:93], v[58:59], off offset:2048
	v_add_lshl_u32 v52, v150, v0, 4
	v_mad_u64_u32 v[50:51], s[8:9], v61, s5, v[52:53]
	v_or_b32_e32 v1, 0x200, v0
	v_mad_u32_u24 v51, v60, s4, v52
	v_mul_u32_u24_e32 v52, 0x556, v1
	v_lshrrev_b32_e32 v53, 16, v52
	v_mul_lo_u32 v52, v53, s7
	v_add_lshl_u32 v52, v52, v1, 4
	v_lshlrev_b32_e32 v1, 3, v53
	s_movk_i32 s8, 0xc7
	ds_read_b128 v[60:63], v51 offset:32768
	v_bitop3_b32 v1, v1, s8, v53 bitop3:0xc8
	v_or_b32_e32 v1, s6, v1
	v_mad_u32_u24 v81, v53, s4, v52
	v_mad_u64_u32 v[52:53], s[8:9], v1, s5, v[52:53]
	v_or_b32_e32 v1, 0x400, v0
	v_mul_u32_u24_e32 v53, 0x556, v1
	v_lshrrev_b32_e32 v53, 16, v53
	ds_read_b128 v[94:97], v81 offset:32768
	s_waitcnt lgkmcnt(1)
	buffer_store_dwordx4 v[60:63], v50, s[0:3], 0 offen sc1
	s_waitcnt lgkmcnt(0)
	buffer_store_dwordx4 v[94:97], v52, s[0:3], 0 offen sc1
	v_lshlrev_b32_e32 v61, 3, v53
	v_mul_lo_u32 v60, v53, s7
	v_bitop3_b32 v61, v61, s10, v53 bitop3:0xc8
	v_or_b32_e32 v61, s6, v61
	v_add_lshl_u32 v62, v60, v1, 4
	v_mad_u64_u32 v[60:61], s[8:9], v61, s5, v[62:63]
	v_or_b32_e32 v1, 0x600, v0
	v_mad_u32_u24 v53, v53, s4, v62
	v_mul_u32_u24_e32 v61, 0x556, v1
	ds_read_b128 v[62:65], v53 offset:32768
	v_lshrrev_b32_e32 v67, 16, v61
	v_mul_lo_u32 v94, v67, s7
	v_add_lshl_u32 v98, v94, v1, 4
	v_lshrrev_b32_e32 v1, 13, v61
	v_mad_u32_u24 v160, v67, s4, v98
	v_and_b32_e32 v1, 0x1c0, v1
	v_bfe_u32 v61, v61, 16, 3
	ds_read_b128 v[94:97], v160 offset:32768
	v_or3_b32 v1, s6, v61, v1
	s_waitcnt lgkmcnt(1)
	buffer_store_dwordx4 v[62:65], v60, s[0:3], 0 offen sc1
	s_nop 1
	v_mad_u64_u32 v[62:63], s[8:9], v1, s5, v[98:99]
	v_or_b32_e32 v1, 0x800, v0
	v_mul_u32_u24_e32 v61, 0xaab, v1
	v_lshrrev_b32_e32 v61, 17, v61
	v_mul_lo_u32 v63, v61, s7
	v_lshlrev_b32_e32 v64, 3, v61
	s_waitcnt lgkmcnt(0)
	buffer_store_dwordx4 v[94:97], v62, s[0:3], 0 offen sc1
	v_bitop3_b32 v64, v64, s10, v61 bitop3:0xc8
	v_or_b32_e32 v64, s6, v64
	v_add_lshl_u32 v94, v63, v1, 4
	v_mad_u32_u24 v61, v61, s4, v94
	v_or_b32_e32 v0, 0xa00, v0
	v_mad_u64_u32 v[64:65], s[8:9], v64, s5, v[94:95]
	ds_read_b128 v[94:97], v61 offset:32768
	v_mul_u32_u24_e32 v1, 0xaab, v0
	v_lshrrev_b32_e32 v63, 17, v1
	v_mul_lo_u32 v65, v63, s7
	v_add_lshl_u32 v0, v65, v0, 4
	v_mad_u32_u24 v63, v63, s4, v0
	ds_read_b128 v[98:101], v63 offset:32768
	s_waitcnt lgkmcnt(1)
	buffer_store_dwordx4 v[94:97], v64, s[0:3], 0 offen sc1
	ds_read_b128 v[94:97], v66
	ds_read_b128 v[102:105], v66 offset:8192
	ds_read_b128 v[106:109], v66 offset:16384
	ds_read_b128 v[110:113], v66 offset:24576
	v_lshrrev_b32_e32 v65, 14, v1
	v_and_b32_e32 v65, 0x1c0, v65
	v_bfe_u32 v1, v1, 17, 3
	v_or3_b32 v1, s6, v1, v65
	v_mad_u64_u32 v[66:67], s[4:5], v1, s5, v[0:1]
	s_waitcnt lgkmcnt(4)
	buffer_store_dwordx4 v[98:101], v66, s[0:3], 0 offen sc1
	s_waitcnt lgkmcnt(3)
	s_nop 0
	v_mfma_f32_16x16x32_f16 v[98:101], v[34:37], v[94:97], 0
	s_waitcnt lgkmcnt(2)
	v_mfma_f32_16x16x32_f16 v[114:117], v[34:37], v[102:105], 0
	s_waitcnt lgkmcnt(1)
	v_mfma_f32_16x16x32_f16 v[118:121], v[34:37], v[106:109], 0
	s_waitcnt lgkmcnt(0)
	v_mfma_f32_16x16x32_f16 v[34:37], v[34:37], v[110:113], 0
	v_mfma_f32_16x16x32_f16 v[122:125], v[26:29], v[94:97], 0
	v_mfma_f32_16x16x32_f16 v[126:129], v[26:29], v[102:105], 0
	v_mfma_f32_16x16x32_f16 v[130:133], v[26:29], v[106:109], 0
	v_mfma_f32_16x16x32_f16 v[26:29], v[26:29], v[110:113], 0
	v_mfma_f32_16x16x32_f16 v[94:97], v[22:25], v[94:97], 0
	v_mfma_f32_16x16x32_f16 v[102:105], v[22:25], v[102:105], 0
	v_mfma_f32_16x16x32_f16 v[106:109], v[22:25], v[106:109], 0
	v_mfma_f32_16x16x32_f16 v[22:25], v[22:25], v[110:113], 0
	s_mov_b32 s4, 0x34000
	v_add_co_u32_e32 v158, vcc, s4, v54
	s_mov_b32 s4, 0x35000
	s_nop 0
	v_addc_co_u32_e32 v159, vcc, 0, v55, vcc
	v_add_co_u32_e32 v54, vcc, s4, v54
	s_nop 1
	v_addc_co_u32_e32 v55, vcc, 0, v55, vcc
	global_load_dwordx4 v[110:113], v[54:55], off offset:-4096
	global_load_dwordx4 v[134:137], v[58:59], off offset:3072
	global_load_dwordx4 v[138:141], v[158:159], off offset:1024
	ds_read_b128 v[142:145], v72
	ds_read_b128 v[146:149], v72 offset:8192
	ds_read_b128 v[150:153], v72 offset:16384
	ds_read_b128 v[154:157], v72 offset:24576
	s_waitcnt lgkmcnt(3)
	v_mfma_f32_16x16x32_f16 v[98:101], v[14:17], v[142:145], v[98:101]
	s_waitcnt lgkmcnt(2)
	v_mfma_f32_16x16x32_f16 v[114:117], v[14:17], v[146:149], v[114:117]
	s_waitcnt lgkmcnt(1)
	v_mfma_f32_16x16x32_f16 v[118:121], v[14:17], v[150:153], v[118:121]
	s_waitcnt lgkmcnt(0)
	v_mfma_f32_16x16x32_f16 v[14:17], v[14:17], v[154:157], v[34:37]
	v_mfma_f32_16x16x32_f16 v[34:37], v[6:9], v[142:145], v[122:125]
	v_mfma_f32_16x16x32_f16 v[122:125], v[6:9], v[146:149], v[126:129]
	v_mfma_f32_16x16x32_f16 v[126:129], v[6:9], v[150:153], v[130:133]
	v_mfma_f32_16x16x32_f16 v[6:9], v[6:9], v[154:157], v[26:29]
	v_mfma_f32_16x16x32_f16 v[26:29], v[2:5], v[142:145], v[94:97]
	v_mfma_f32_16x16x32_f16 v[94:97], v[2:5], v[146:149], v[102:105]
	v_mfma_f32_16x16x32_f16 v[102:105], v[2:5], v[150:153], v[106:109]
	v_mfma_f32_16x16x32_f16 v[0:3], v[2:5], v[154:157], v[22:25]
	s_nop 2
	global_load_dwordx4 v[22:25], v[158:159], off offset:2048
	global_load_dwordx4 v[106:109], v[158:159], off offset:3072
	global_load_dwordx4 v[130:133], v[54:55], off
	ds_read_b128 v[142:145], v74
	ds_read_b128 v[146:149], v74 offset:8192
	ds_read_b128 v[150:153], v74 offset:16384
	ds_read_b128 v[154:157], v74 offset:24576
	s_waitcnt lgkmcnt(3)
	v_mfma_f32_16x16x32_f16 v[98:101], v[18:21], v[142:145], v[98:101]
	s_waitcnt lgkmcnt(2)
	v_mfma_f32_16x16x32_f16 v[114:117], v[18:21], v[146:149], v[114:117]
	s_waitcnt lgkmcnt(1)
	v_mfma_f32_16x16x32_f16 v[118:121], v[18:21], v[150:153], v[118:121]
	s_waitcnt lgkmcnt(0)
	v_mfma_f32_16x16x32_f16 v[14:17], v[18:21], v[154:157], v[14:17]
	v_mfma_f32_16x16x32_f16 v[18:21], v[10:13], v[142:145], v[34:37]
	v_mfma_f32_16x16x32_f16 v[34:37], v[10:13], v[146:149], v[122:125]
	v_mfma_f32_16x16x32_f16 v[122:125], v[10:13], v[150:153], v[126:129]
	v_mfma_f32_16x16x32_f16 v[4:7], v[10:13], v[154:157], v[6:9]
	v_mfma_f32_16x16x32_f16 v[8:11], v[30:33], v[142:145], v[26:29]
	v_mfma_f32_16x16x32_f16 v[26:29], v[30:33], v[146:149], v[94:97]
	v_mfma_f32_16x16x32_f16 v[94:97], v[30:33], v[150:153], v[102:105]
	v_mfma_f32_16x16x32_f16 v[0:3], v[30:33], v[154:157], v[0:3]
	global_load_dwordx4 v[30:33], v[54:55], off offset:1024
	s_nop 0
	global_load_dwordx4 v[102:105], v[54:55], off offset:2048
	global_load_dwordx4 v[126:129], v[54:55], off offset:3072
	ds_read_b128 v[142:145], v75
	ds_read_b128 v[146:149], v75 offset:8192
	ds_read_b128 v[150:153], v75 offset:16384
	ds_read_b128 v[154:157], v75 offset:24576
	s_waitcnt lgkmcnt(3)
	v_mfma_f32_16x16x32_f16 v[98:101], v[46:49], v[142:145], v[98:101]
	s_waitcnt lgkmcnt(2)
	v_mfma_f32_16x16x32_f16 v[114:117], v[46:49], v[146:149], v[114:117]
	s_waitcnt lgkmcnt(1)
	v_mfma_f32_16x16x32_f16 v[118:121], v[46:49], v[150:153], v[118:121]
	s_waitcnt lgkmcnt(0)
	v_mfma_f32_16x16x32_f16 v[12:15], v[46:49], v[154:157], v[14:17]
	v_mfma_f32_16x16x32_f16 v[16:19], v[42:45], v[142:145], v[18:21]
	v_mfma_f32_16x16x32_f16 v[34:37], v[42:45], v[146:149], v[34:37]
	v_mfma_f32_16x16x32_f16 v[46:49], v[42:45], v[150:153], v[122:125]
	v_mfma_f32_16x16x32_f16 v[4:7], v[42:45], v[154:157], v[4:7]
	v_mfma_f32_16x16x32_f16 v[8:11], v[38:41], v[142:145], v[8:11]
	v_mfma_f32_16x16x32_f16 v[26:29], v[38:41], v[146:149], v[26:29]
	v_mfma_f32_16x16x32_f16 v[42:45], v[38:41], v[150:153], v[94:97]
	v_mfma_f32_16x16x32_f16 v[0:3], v[38:41], v[154:157], v[0:3]
	ds_read_b128 v[38:41], v76
	s_nop 0
	ds_read_b128 v[94:97], v76 offset:8192
	ds_read_b128 v[122:125], v76 offset:16384
	ds_read_b128 v[142:145], v76 offset:24576
	s_waitcnt vmcnt(17) lgkmcnt(3)
	v_mfma_f32_16x16x32_f16 v[98:101], v[82:85], v[38:41], v[98:101]
	s_waitcnt lgkmcnt(2)
	v_mfma_f32_16x16x32_f16 v[114:117], v[82:85], v[94:97], v[114:117]
	s_waitcnt lgkmcnt(1)
	v_mfma_f32_16x16x32_f16 v[118:121], v[82:85], v[122:125], v[118:121]
	s_waitcnt lgkmcnt(0)
	v_mfma_f32_16x16x32_f16 v[12:15], v[82:85], v[142:145], v[12:15]
	s_waitcnt vmcnt(16)
	v_mfma_f32_16x16x32_f16 v[16:19], v[86:89], v[38:41], v[16:19]
	v_mfma_f32_16x16x32_f16 v[34:37], v[86:89], v[94:97], v[34:37]
	v_mfma_f32_16x16x32_f16 v[46:49], v[86:89], v[122:125], v[46:49]
	v_mfma_f32_16x16x32_f16 v[4:7], v[86:89], v[142:145], v[4:7]
	s_waitcnt vmcnt(15)
	v_mfma_f32_16x16x32_f16 v[8:11], v[90:93], v[38:41], v[8:11]
	v_mfma_f32_16x16x32_f16 v[26:29], v[90:93], v[94:97], v[26:29]
	v_mfma_f32_16x16x32_f16 v[38:41], v[90:93], v[122:125], v[42:45]
	v_mfma_f32_16x16x32_f16 v[0:3], v[90:93], v[142:145], v[0:3]
	s_nop 1
	ds_read_b128 v[42:45], v77
	ds_read_b128 v[82:85], v77 offset:8192
	ds_read_b128 v[86:89], v77 offset:16384
	ds_read_b128 v[74:77], v77 offset:24576
	s_waitcnt vmcnt(7) lgkmcnt(3)
	v_mfma_f32_16x16x32_f16 v[90:93], v[134:137], v[42:45], v[98:101]
	s_waitcnt lgkmcnt(2)
	v_mfma_f32_16x16x32_f16 v[94:97], v[134:137], v[82:85], v[114:117]
	s_waitcnt lgkmcnt(1)
	v_mfma_f32_16x16x32_f16 v[98:101], v[134:137], v[86:89], v[118:121]
	s_waitcnt lgkmcnt(0)
	v_mfma_f32_16x16x32_f16 v[12:15], v[134:137], v[74:77], v[12:15]
	v_mfma_f32_16x16x32_f16 v[16:19], v[110:113], v[42:45], v[16:19]
	v_mfma_f32_16x16x32_f16 v[34:37], v[110:113], v[82:85], v[34:37]
	v_mfma_f32_16x16x32_f16 v[46:49], v[110:113], v[86:89], v[46:49]
	v_mfma_f32_16x16x32_f16 v[4:7], v[110:113], v[74:77], v[4:7]
	s_waitcnt vmcnt(6)
	v_mfma_f32_16x16x32_f16 v[8:11], v[138:141], v[42:45], v[8:11]
	v_mfma_f32_16x16x32_f16 v[26:29], v[138:141], v[82:85], v[26:29]
	v_mfma_f32_16x16x32_f16 v[38:41], v[138:141], v[86:89], v[38:41]
	v_mfma_f32_16x16x32_f16 v[0:3], v[138:141], v[74:77], v[0:3]
	ds_read_b128 v[42:45], v78
	ds_read_b128 v[74:77], v78 offset:8192
	ds_read_b128 v[82:85], v78 offset:16384
	ds_read_b128 v[86:89], v78 offset:24576
	s_waitcnt vmcnt(5) lgkmcnt(3)
	v_mfma_f32_16x16x32_f16 v[90:93], v[22:25], v[42:45], v[90:93]
	s_waitcnt lgkmcnt(2)
	v_mfma_f32_16x16x32_f16 v[94:97], v[22:25], v[74:77], v[94:97]
	s_waitcnt lgkmcnt(1)
	v_mfma_f32_16x16x32_f16 v[98:101], v[22:25], v[82:85], v[98:101]
	s_waitcnt lgkmcnt(0)
	v_mfma_f32_16x16x32_f16 v[12:15], v[22:25], v[86:89], v[12:15]
	s_waitcnt vmcnt(4)
	v_mfma_f32_16x16x32_f16 v[16:19], v[106:109], v[42:45], v[16:19]
	v_mfma_f32_16x16x32_f16 v[20:23], v[106:109], v[74:77], v[34:37]
	v_mfma_f32_16x16x32_f16 v[34:37], v[106:109], v[82:85], v[46:49]
	v_mfma_f32_16x16x32_f16 v[4:7], v[106:109], v[86:89], v[4:7]
	s_waitcnt vmcnt(3)
	v_mfma_f32_16x16x32_f16 v[8:11], v[130:133], v[42:45], v[8:11]
	v_mfma_f32_16x16x32_f16 v[24:27], v[130:133], v[74:77], v[26:29]
	v_mfma_f32_16x16x32_f16 v[38:41], v[130:133], v[82:85], v[38:41]
	v_mfma_f32_16x16x32_f16 v[0:3], v[130:133], v[86:89], v[0:3]
	ds_read_b128 v[42:45], v79
	ds_read_b128 v[46:49], v79 offset:8192
	ds_read_b128 v[74:77], v79 offset:16384
	ds_read_b128 v[82:85], v79 offset:24576
	s_waitcnt vmcnt(2) lgkmcnt(3)
	v_mfma_f32_16x16x32_f16 v[86:89], v[30:33], v[42:45], v[90:93]
	s_waitcnt lgkmcnt(2)
	v_mfma_f32_16x16x32_f16 v[90:93], v[30:33], v[46:49], v[94:97]
	s_waitcnt lgkmcnt(1)
	v_mfma_f32_16x16x32_f16 v[94:97], v[30:33], v[74:77], v[98:101]
	s_waitcnt lgkmcnt(0)
	v_mfma_f32_16x16x32_f16 v[12:15], v[30:33], v[82:85], v[12:15]
	s_waitcnt vmcnt(1)
	v_mfma_f32_16x16x32_f16 v[16:19], v[102:105], v[42:45], v[16:19]
	v_mfma_f32_16x16x32_f16 v[20:23], v[102:105], v[46:49], v[20:23]
	v_mfma_f32_16x16x32_f16 v[28:31], v[102:105], v[74:77], v[34:37]
	v_mfma_f32_16x16x32_f16 v[4:7], v[102:105], v[82:85], v[4:7]
	s_waitcnt vmcnt(0)
	s_mov_b64 s[86:87], s[80:81]
	global_load_dword v254, v255, s[86:87]
	s_add_u32 s86, s86, 0x2000
	s_addc_u32 s87, s87, 0
	global_load_dword v254, v255, s[86:87]
	s_add_u32 s86, s86, 0x2000
	s_addc_u32 s87, s87, 0
	global_load_dword v254, v255, s[86:87]
	s_add_u32 s86, s86, 0x2c000
	s_addc_u32 s87, s87, 0
	global_load_dword v254, v255, s[86:87]
	s_add_u32 s86, s86, 0x2000
	s_addc_u32 s87, s87, 0
	global_load_dword v254, v255, s[86:87]
	s_add_u32 s86, s86, 0x2000
	s_addc_u32 s87, s87, 0
	global_load_dword v254, v255, s[86:87]
	v_mfma_f32_16x16x32_f16 v[8:11], v[126:129], v[42:45], v[8:11]
	v_mfma_f32_16x16x32_f16 v[24:27], v[126:129], v[46:49], v[24:27]
	v_mfma_f32_16x16x32_f16 v[32:35], v[126:129], v[74:77], v[38:41]
	v_mfma_f32_16x16x32_f16 v[0:3], v[126:129], v[82:85], v[0:3]
	s_nop 1
	global_load_dwordx4 v[36:39], v[56:57], off offset:1536
	global_load_dwordx4 v[40:43], v[56:57], off offset:1600
	global_load_dwordx4 v[44:47], v[56:57], off offset:1664
	v_mov_b32_e32 v58, v21
	v_mov_b32_e32 v59, v22
	v_mov_b32_e32 v74, v29
	v_mov_b32_e32 v56, v13
	v_mov_b32_e32 v57, v14
	v_mov_b32_e32 v75, v30
	v_mov_b32_e32 v48, v91
	v_mov_b32_e32 v49, v92
	v_mov_b32_e32 v54, v95
	v_mov_b32_e32 v55, v96
	v_mov_b32_e32 v76, v5
	v_mov_b32_e32 v77, v6
	s_barrier
	s_waitcnt vmcnt(2)
	v_pk_add_f32 v[78:79], v[86:87], v[36:37]
	v_pk_add_f32 v[82:83], v[88:89], v[38:39]
	v_add_f32_e32 v21, v90, v36
	v_pk_mov_b32 v[84:85], v[36:37], v[38:39] op_sel:[1,0]
	v_add_f32_e32 v22, v93, v39
	v_add_f32_e32 v29, v94, v36
	v_add_f32_e32 v36, v12, v36
	v_add_f32_e32 v37, v15, v39
	s_waitcnt vmcnt(1)
	v_add_f32_e32 v38, v20, v40
	v_add_f32_e32 v23, v23, v43
	v_add_f32_e32 v30, v97, v39
	v_pk_add_f32 v[12:13], v[16:17], v[40:41]
	v_pk_add_f32 v[14:15], v[18:19], v[42:43]
	v_pk_mov_b32 v[16:17], v[40:41], v[42:43] op_sel:[1,0]
	v_add_f32_e32 v28, v28, v40
	v_add_f32_e32 v31, v31, v43
	v_add_f32_e32 v39, v4, v40
	v_add_f32_e32 v40, v7, v43
	v_cvt_f16_f32_e32 v41, v21
	v_cvt_f16_f32_e32 v42, v22
	v_cvt_f16_f32_e32 v36, v36
	v_cvt_f16_f32_e32 v37, v37
	v_cvt_f16_f32_e32 v38, v38
	v_cvt_f16_f32_e32 v43, v23
	v_cvt_f16_f32_e32 v29, v29
	v_cvt_f16_f32_e32 v30, v30
	v_cvt_f16_f32_e32 v28, v28
	v_cvt_f16_f32_e32 v31, v31
	v_cvt_f16_f32_e32 v39, v39
	v_cvt_f16_f32_e32 v40, v40
	s_waitcnt vmcnt(0)
	v_pk_add_f32 v[4:5], v[8:9], v[44:45]
	v_pk_add_f32 v[6:7], v[10:11], v[46:47]
	v_pk_add_f32 v[10:11], v[48:49], v[84:85]
	v_pk_add_f32 v[20:21], v[56:57], v[84:85]
	v_cvt_pk_f16_f32 v12, v12, v13
	v_cvt_pk_f16_f32 v13, v14, v15
	v_pk_add_f32 v[14:15], v[58:59], v[16:17]
	v_cvt_pk_f16_f32 v8, v78, v79
	v_cvt_pk_f16_f32 v9, v82, v83
	v_pk_add_f32 v[18:19], v[54:55], v[84:85]
	v_pk_add_f32 v[22:23], v[74:75], v[16:17]
	v_pk_add_f32 v[16:17], v[76:77], v[16:17]
	v_cvt_pk_f16_f32 v4, v4, v5
	v_cvt_pk_f16_f32 v5, v6, v7
	v_cvt_pk_f16_f32 v6, v10, v11
	v_cvt_pk_f16_f32 v10, v20, v21
	v_cvt_pk_f16_f32 v11, v14, v15
	v_cvt_pk_f16_f32 v7, v18, v19
	v_cvt_pk_f16_f32 v14, v22, v23
	v_cvt_pk_f16_f32 v15, v16, v17
	ds_write2_b64 v73, v[8:9], v[12:13] offset1:4
	ds_write_b64 v69, v[4:5] offset:32832
	v_pack_b32_f16 v4, v41, v6
	v_alignbit_b32 v5, v42, v6, 16
	v_pack_b32_f16 v8, v36, v10
	v_alignbit_b32 v9, v37, v10, 16
	v_pack_b32_f16 v10, v38, v11
	v_alignbit_b32 v11, v43, v11, 16
	v_add_f32_e32 v24, v24, v44
	v_pack_b32_f16 v6, v29, v7
	v_alignbit_b32 v7, v30, v7, 16
	v_pack_b32_f16 v12, v28, v14
	v_alignbit_b32 v13, v31, v14, 16
	v_pack_b32_f16 v14, v39, v15
	v_alignbit_b32 v15, v40, v15, 16
	ds_write2_b64 v70, v[4:5], v[10:11] offset0:32 offset1:36
	ds_write2_b64 v71, v[6:7], v[12:13] offset0:64 offset1:68
	ds_write2_b64 v80, v[8:9], v[14:15] offset1:4
	v_add_f32_e32 v8, v27, v47
	v_cvt_f16_f32_e32 v24, v24
	v_cvt_f16_f32_e32 v8, v8
	v_mov_b32_e32 v4, v25
	v_mov_b32_e32 v5, v26
	v_pk_mov_b32 v[6:7], v[44:45], v[46:47] op_sel:[1,0]
	v_add_f32_e32 v9, v35, v47
	v_pk_add_f32 v[4:5], v[4:5], v[6:7]
	v_cvt_f16_f32_e32 v9, v9
	v_cvt_pk_f16_f32 v5, v4, v5
	v_pack_b32_f16 v4, v24, v5
	v_alignbit_b32 v5, v8, v5, 16
	ds_write_b64 v69, v[4:5] offset:45376
	v_add_f32_e32 v4, v32, v44
	v_cvt_f16_f32_e32 v8, v4
	v_mov_b32_e32 v4, v33
	v_mov_b32_e32 v5, v34
	v_pk_add_f32 v[4:5], v[4:5], v[6:7]
	v_add_f32_e32 v0, v0, v44
	v_cvt_pk_f16_f32 v5, v4, v5
	v_pack_b32_f16 v4, v8, v5
	v_alignbit_b32 v5, v9, v5, 16
	ds_write_b64 v69, v[4:5] offset:57920
	v_cvt_f16_f32_e32 v4, v0
	v_mov_b32_e32 v0, v1
	v_mov_b32_e32 v1, v2
	v_add_f32_e32 v2, v3, v47
	v_cvt_f16_f32_e32 v2, v2
	v_pk_add_f32 v[0:1], v[0:1], v[6:7]
	s_nop 0
	v_cvt_pk_f16_f32 v1, v0, v1
	v_pack_b32_f16 v0, v4, v1
	v_alignbit_b32 v1, v2, v1, 16
	ds_write_b64 v68, v[0:1] offset:32832
	s_waitcnt lgkmcnt(0)
	s_barrier
	ds_read_b128 v[0:3], v51 offset:32768
	ds_read_b128 v[4:7], v81 offset:32768
	s_waitcnt lgkmcnt(1)
	buffer_store_dwordx4 v[0:3], v50, s[0:3], 0 offen offset:768 sc1
	ds_read_b128 v[0:3], v53 offset:32768
	ds_read_b128 v[8:11], v160 offset:32768
	ds_read_b128 v[12:15], v61 offset:32768
	ds_read_b128 v[16:19], v63 offset:32768
	s_waitcnt lgkmcnt(4)
	buffer_store_dwordx4 v[4:7], v52, s[0:3], 0 offen offset:768 sc1
	s_waitcnt lgkmcnt(3)
	buffer_store_dwordx4 v[0:3], v60, s[0:3], 0 offen offset:768 sc1
	s_waitcnt lgkmcnt(2)
	buffer_store_dwordx4 v[8:11], v62, s[0:3], 0 offen offset:768 sc1
	s_waitcnt lgkmcnt(1)
	buffer_store_dwordx4 v[12:15], v64, s[0:3], 0 offen offset:768 sc1
	s_waitcnt lgkmcnt(0)
	buffer_store_dwordx4 v[16:19], v66, s[0:3], 0 offen offset:768 sc1
	s_endpgm
	.p2alignl 8, 3212836864
